# bit-trick f32-to-bf16 roundings replaced by v_cvt_pk_bf16_f32 across the layer loop (wait states re-derived and padded)
# speedup vs baseline: 1.0390x; 1.0094x over previous
; __device__ __forceinline__ f32x4 bf4(u32x2 v) { return (f32x4){lo_bf(v.x), hi_bf(v.x), lo_bf(v.y), hi_bf(v.y)}; }
; __device__ __forceinline__ void ph_prep_conv(CArgs& a, int l, LAS unsigned char* lds, int bid, int nblk) {
;     ...
;     for (int it = bid + (l == DEPTH - 1 ? 64 : 0); it < 576; it += nblk) {
;         const Chunk c = chunk_of(it);
;         const int tb = c.t0 + tg * 8;
;         const bf16* pb = P + (size_t)(c.row0 + tg * 8) * D_INP;
;         f32x4 x1[10], vv[10], mm[10];
; #pragma unroll
;         for (int r = 0; r < 10; ++r) { const int t = tb + r - 1, tc = min(max(t, c.lo), c.hi - 1); const float ok = (t == tc) ? 1.f : 0.f; const bf16* p = pb + (ptrdiff_t)(tc - tb) * D_INP;
;             x1[r] = ok * bf4(*(const u32x2*)(p + HY0 + 256 + c4)); vv[r] = ok * bf4(*(const u32x2*)(p + HY0 + 512 + c4));
;             mm[r] = ok * bf4(*(const u32x2*)(p + SC0 + 256 + c4)) * bf4(*(const u32x2*)(p + SC0 + 512 + c4)); }
.LBB0_266:
	v_add_u32_e32 v59, s28, v1
	v_add_u32_e32 v56, s11, v1
	v_mov_b64_e32 v[52:53], s[14:15]
	v_mad_i64_i32 v[78:79], s[16:17], v56, s65, v[52:53]
	v_max_i32_e32 v52, s10, v59
	v_min_u32_e32 v60, s9, v52
	v_sub_u32_e32 v52, v60, v59
	v_add_u32_e32 v58, -1, v59
	v_mad_i64_i32 v[52:53], s[16:17], v52, s65, v[78:79]
	v_lshl_add_u64 v[54:55], v[52:53], 0, v[34:35]
	v_max_i32_e32 v52, s10, v58
	v_min_u32_e32 v64, s9, v52
	v_sub_u32_e32 v52, v64, v59
	v_mad_i64_i32 v[52:53], s[16:17], v52, s65, v[78:79]
	v_or_b32_e32 v65, 1, v59
	v_lshl_add_u64 v[62:63], v[52:53], 0, v[34:35]
	v_max_i32_e32 v52, s10, v65
	v_min_u32_e32 v66, s9, v52
	v_sub_u32_e32 v52, v66, v59
	global_load_dwordx2 v[68:69], v[54:55], off offset:2048
	global_load_dwordx2 v[70:71], v[54:55], off offset:2560
	v_mad_i64_i32 v[52:53], s[16:17], v52, s65, v[78:79]
	v_lshl_add_u64 v[86:87], v[52:53], 0, v[34:35]
	global_load_dwordx2 v[82:83], v[62:63], off offset:2048
	global_load_dwordx2 v[84:85], v[62:63], off offset:2560
	global_load_dwordx2 v[88:89], v[86:87], off offset:2048
	global_load_dwordx2 v[90:91], v[86:87], off offset:2560
	v_lshl_add_u64 v[52:53], v[78:79], 0, v[34:35]
	global_load_dwordx2 v[92:93], v[52:53], off offset:1536
	v_or_b32_e32 v61, 2, v59
	v_max_i32_e32 v67, s10, v61
	v_cmp_eq_u32_e32 vcc, v60, v59
	v_min_u32_e32 v73, s9, v67
	v_or_b32_e32 v137, 3, v59
	v_cndmask_b32_e64 v60, 0, 1.0, vcc
	v_cmp_eq_u32_e32 vcc, v58, v64
	v_sub_u32_e32 v64, v73, v59
	v_or_b32_e32 v212, 4, v59
	v_cndmask_b32_e64 v72, 0, 1.0, vcc
	v_cmp_eq_u32_e32 vcc, v65, v66
	v_mad_i64_i32 v[64:65], s[16:17], v64, s65, v[78:79]
	global_load_dwordx2 v[74:75], v[54:55], off offset:512
	global_load_dwordx2 v[66:67], v[54:55], off offset:1024
	v_cndmask_b32_e64 v58, 0, 1.0, vcc
	v_lshl_add_u64 v[98:99], v[64:65], 0, v[34:35]
	global_load_dwordx2 v[80:81], v[62:63], off offset:512
	global_load_dwordx2 v[76:77], v[62:63], off offset:1024
	global_load_dwordx2 v[64:65], v[86:87], off offset:512
	s_nop 0
	global_load_dwordx2 v[62:63], v[86:87], off offset:1024
	v_or_b32_e32 v214, 5, v59
	v_or_b32_e32 v216, 6, v59
	v_or_b32_e32 v211, 7, v59
	v_add_u32_e32 v209, 8, v59
	v_ashrrev_i32_e32 v57, 31, v56
	v_lshlrev_b64 v[56:57], 11, v[56:57]
	v_lshl_add_u64 v[56:57], s[2:3], 0, v[56:57]
	v_lshl_add_u64 v[56:57], v[56:57], 0, v[34:35]
	s_lshl_b32 s78, s30, 1
	s_mov_b32 s29, s79
	s_add_i32 s0, s0, s68
	s_waitcnt vmcnt(0)
	v_lshlrev_b32_e32 v54, 16, v68
	v_and_b32_e32 v55, 0xffff0000, v68
	v_lshlrev_b32_e32 v68, 16, v69
	v_and_b32_e32 v69, 0xffff0000, v69
	v_lshlrev_b32_e32 v86, 16, v70
	v_and_b32_e32 v87, 0xffff0000, v70
	v_lshlrev_b32_e32 v70, 16, v71
	v_and_b32_e32 v71, 0xffff0000, v71
	v_lshlrev_b32_e32 v94, 16, v82
	v_and_b32_e32 v95, 0xffff0000, v82
	v_lshlrev_b32_e32 v82, 16, v83
	v_and_b32_e32 v83, 0xffff0000, v83
	v_pk_mul_f32 v[54:55], v[60:61], v[54:55] op_sel_hi:[0,1]
	v_pk_mul_f32 v[68:69], v[60:61], v[68:69] op_sel_hi:[0,1]
	v_lshlrev_b32_e32 v102, 16, v88
	v_and_b32_e32 v103, 0xffff0000, v88
	v_lshlrev_b32_e32 v88, 16, v89
	v_and_b32_e32 v89, 0xffff0000, v89
	v_lshlrev_b32_e32 v96, 16, v84
	v_and_b32_e32 v97, 0xffff0000, v84
	v_lshlrev_b32_e32 v100, 16, v85
	v_and_b32_e32 v101, 0xffff0000, v85
	v_lshlrev_b32_e32 v104, 16, v90
	v_and_b32_e32 v105, 0xffff0000, v90
	v_lshlrev_b32_e32 v90, 16, v91
	v_and_b32_e32 v91, 0xffff0000, v91
	v_pk_mul_f32 v[82:83], v[72:73], v[82:83] op_sel_hi:[0,1]
	v_pk_mul_f32 v[94:95], v[72:73], v[94:95] op_sel_hi:[0,1]
	v_pk_mul_f32 v[84:85], v[68:69], v[70:71]
	v_pk_mul_f32 v[86:87], v[54:55], v[86:87]
	v_pk_mul_f32 v[54:55], v[58:59], v[102:103] op_sel_hi:[0,1]
	v_pk_mul_f32 v[68:69], v[58:59], v[88:89] op_sel_hi:[0,1]
	v_pk_mul_f32 v[94:95], v[94:95], v[96:97]
	v_pk_mul_f32 v[96:97], v[82:83], v[100:101]
	v_pk_mul_f32 v[68:69], v[68:69], v[90:91]
	v_pk_mul_f32 v[70:71], v[54:55], v[104:105]
	global_load_dwordx2 v[82:83], v[98:99], off offset:512
	global_load_dwordx2 v[54:55], v[98:99], off offset:1024
	global_load_dwordx2 v[90:91], v[98:99], off offset:2048
	global_load_dwordx2 v[88:89], v[98:99], off offset:2560
	v_max_i32_e32 v98, s10, v137
	v_min_u32_e32 v142, s9, v98
	v_sub_u32_e32 v98, v142, v59
	v_mad_i64_i32 v[98:99], s[16:17], v98, s65, v[78:79]
	v_lshl_add_u64 v[98:99], v[98:99], 0, v[34:35]
	global_load_dwordx2 v[120:121], v[98:99], off offset:512
	global_load_dwordx2 v[118:119], v[98:99], off offset:1024
	global_load_dwordx2 v[124:125], v[98:99], off offset:2048
	global_load_dwordx2 v[122:123], v[98:99], off offset:2560
	v_max_i32_e32 v98, s10, v212
	v_min_u32_e32 v213, s9, v98
	v_sub_u32_e32 v98, v213, v59
	v_mad_i64_i32 v[98:99], s[16:17], v98, s65, v[78:79]
	v_lshl_add_u64 v[98:99], v[98:99], 0, v[34:35]
	global_load_dwordx2 v[174:175], v[98:99], off offset:512
	global_load_dwordx2 v[172:173], v[98:99], off offset:1024
	global_load_dwordx2 v[170:171], v[98:99], off offset:2048
	global_load_dwordx2 v[162:163], v[98:99], off offset:2560
	v_max_i32_e32 v98, s10, v214
	v_min_u32_e32 v215, s9, v98
	v_sub_u32_e32 v98, v215, v59
	v_mad_i64_i32 v[98:99], s[16:17], v98, s65, v[78:79]
	v_lshl_add_u64 v[98:99], v[98:99], 0, v[34:35]
	global_load_dwordx2 v[160:161], v[98:99], off offset:512
	global_load_dwordx2 v[158:159], v[98:99], off offset:1024
	global_load_dwordx2 v[128:129], v[98:99], off offset:2048
	global_load_dwordx2 v[126:127], v[98:99], off offset:2560
	v_max_i32_e32 v98, s10, v216
	v_min_u32_e32 v217, s9, v98
	v_sub_u32_e32 v98, v217, v59
	v_mad_i64_i32 v[98:99], s[16:17], v98, s65, v[78:79]
	v_lshl_add_u64 v[98:99], v[98:99], 0, v[34:35]
	global_load_dwordx2 v[156:157], v[98:99], off offset:512
	global_load_dwordx2 v[116:117], v[98:99], off offset:1024
; #define LAS __attribute__((address_space(3)))
; __device__ __forceinline__ unsigned pk2(float lo, float hi) { return f2bf(lo) | (f2bf(hi) << 16); }
; __device__ __forceinline__ f32x4 bf4(u32x2 v) { return (f32x4){lo_bf(v.x), hi_bf(v.x), lo_bf(v.y), hi_bf(v.y)}; }
; __device__ __forceinline__ void ph_prep_conv(CArgs& a, int l, LAS unsigned char* lds, int bid, int nblk) {
;     ...
; #pragma unroll
;         for (int tt = 0; tt < 8; ++tt) {
;             const f32x4 xx = wx[0] * x1[tt] + wx[1] * x1[tt + 1] + wx[2] * x1[tt + 2] + bx, v2 = wv[0] * vv[tt] + wv[1] * vv[tt + 1] + wv[2] * vv[tt + 2] + bv, z = xx * v2;
;             u32x2 zo; zo.x = pk2(z[0], z[1]); zo.y = pk2(z[2], z[3]); *(LAS u32x2*)(zt + (tg * 8 + tt) * 264 + c4) = zo;
;             const f32x4 bg = bf4(*(const u32x2*)(pb + (size_t)tt * D_INP + SC0 + c4));
;             const f32x4 y = bg * (ws3[0] * mm[tt] + ws3[1] * mm[tt + 1] + ws3[2] * mm[tt + 2]);
;             u32x2 yo; yo.x = pk2(y[0], y[1]); yo.y = pk2(y[2], y[3]); *(u32x2*)(YMIX + (size_t)(c.row0 + tg * 8 + tt) * D + 256 + c4) = yo;
	global_load_dwordx2 v[114:115], v[98:99], off offset:2048
	global_load_dwordx2 v[112:113], v[98:99], off offset:2560
	v_max_i32_e32 v98, s10, v211
	v_min_u32_e32 v218, s9, v98
	v_sub_u32_e32 v98, v218, v59
	v_mad_i64_i32 v[98:99], s[16:17], v98, s65, v[78:79]
	v_lshl_add_u64 v[98:99], v[98:99], 0, v[34:35]
	v_pk_mul_f32 v[132:133], v[14:15], v[86:87]
	global_load_dwordx2 v[110:111], v[98:99], off offset:512
	global_load_dwordx2 v[108:109], v[98:99], off offset:1024
	global_load_dwordx2 v[106:107], v[98:99], off offset:2048
	global_load_dwordx2 v[104:105], v[98:99], off offset:2560
	v_max_i32_e32 v98, s10, v209
	v_pk_fma_f32 v[94:95], v[10:11], v[94:95], v[132:133]
	v_min_u32_e32 v210, s9, v98
	v_lshlrev_b32_e32 v130, 16, v92
	v_and_b32_e32 v131, 0xffff0000, v92
	v_pk_fma_f32 v[94:95], v[36:37], v[70:71], v[94:95]
	v_sub_u32_e32 v59, v210, v59
	v_pk_mul_f32 v[134:135], v[16:17], v[84:85]
	v_pk_mul_f32 v[94:95], v[94:95], v[130:131]
	v_mad_i64_i32 v[78:79], s[10:11], v59, s65, v[78:79]
	v_pk_fma_f32 v[96:97], v[12:13], v[96:97], v[134:135]
	v_lshlrev_b32_e32 v92, 16, v93
	v_and_b32_e32 v93, 0xffff0000, v93
	v_pk_fma_f32 v[96:97], v[38:39], v[68:69], v[96:97]
	v_pk_mul_f32 v[92:93], v[96:97], v[92:93]
	v_cvt_pk_bf16_f32 v94, v94, v95
	s_mov_b32 s9, 0x2dc00000
	v_add_co_u32_e32 v96, vcc, s9, v56
	s_nop 1
	v_addc_co_u32_e32 v97, vcc, 0, v57, vcc
	s_movk_i32 s9, 0x2000
	v_lshl_add_u64 v[78:79], v[78:79], 0, v[34:35]
	v_cvt_pk_bf16_f32 v95, v92, v93
	v_add_co_u32_e32 v92, vcc, s9, v52
	global_load_dwordx2 v[102:103], v[78:79], off offset:512
	global_load_dwordx2 v[100:101], v[78:79], off offset:1024
	global_load_dwordx2 v[98:99], v[78:79], off offset:2048
	s_nop 0
	global_load_dwordx2 v[78:79], v[78:79], off offset:2560
	v_addc_co_u32_e32 v93, vcc, 0, v53, vcc
	global_store_dwordx2 v[96:97], v[94:95], off offset:512
	global_load_dwordx2 v[130:131], v[92:93], off offset:512
	v_add_co_u32_e32 v232, vcc, 0x3000, v52
	s_nop 1
	v_addc_co_u32_e32 v233, vcc, 0, v53, vcc
	global_load_dwordx2 v[220:221], v[232:233], off offset:3584
	v_add_co_u32_e32 v232, vcc, 0x5000, v52
	s_nop 1
	v_addc_co_u32_e32 v233, vcc, 0, v53, vcc
	global_load_dwordx2 v[222:223], v[232:233], off offset:2560
	v_add_co_u32_e32 v232, vcc, 0x7000, v52
	s_nop 1
	v_addc_co_u32_e32 v233, vcc, 0, v53, vcc
	global_load_dwordx2 v[224:225], v[232:233], off offset:1536
	v_add_co_u32_e32 v232, vcc, 0x9000, v52
	s_nop 1
	v_addc_co_u32_e32 v233, vcc, 0, v53, vcc
	global_load_dwordx2 v[226:227], v[232:233], off offset:512
	v_add_co_u32_e32 v232, vcc, 0xa000, v52
	s_nop 1
	v_addc_co_u32_e32 v233, vcc, 0, v53, vcc
	global_load_dwordx2 v[228:229], v[232:233], off offset:3584
	v_add_co_u32_e32 v232, vcc, 0xc000, v52
	s_nop 1
	v_addc_co_u32_e32 v233, vcc, 0, v53, vcc
	global_load_dwordx2 v[230:231], v[232:233], off offset:2560
	v_cmp_eq_u32_e32 vcc, v61, v73
	s_waitcnt vmcnt(27)
	v_lshlrev_b32_e32 v92, 16, v90
	v_and_b32_e32 v93, 0xffff0000, v90
	v_cndmask_b32_e64 v136, 0, 1.0, vcc
	v_lshlrev_b32_e32 v90, 16, v91
	v_and_b32_e32 v91, 0xffff0000, v91
	v_pk_mul_f32 v[90:91], v[136:137], v[90:91] op_sel_hi:[0,1]
	s_waitcnt vmcnt(26)
	v_lshlrev_b32_e32 v132, 16, v88
	v_and_b32_e32 v133, 0xffff0000, v88
	v_lshlrev_b32_e32 v88, 16, v89
	v_and_b32_e32 v89, 0xffff0000, v89
	v_pk_mul_f32 v[94:95], v[136:137], v[92:93] op_sel_hi:[0,1]
	v_pk_mul_f32 v[92:93], v[90:91], v[88:89]
	v_pk_mul_f32 v[94:95], v[94:95], v[132:133]
	v_pk_mul_f32 v[132:133], v[16:17], v[68:69]
	s_movk_i32 s9, 0x3000
	v_pk_fma_f32 v[84:85], v[12:13], v[84:85], v[132:133]
	s_waitcnt vmcnt(0)
	v_lshlrev_b32_e32 v88, 16, v130
	v_and_b32_e32 v89, 0xffff0000, v130
	v_lshlrev_b32_e32 v90, 16, v131
	v_and_b32_e32 v91, 0xffff0000, v131
	v_pk_mul_f32 v[130:131], v[14:15], v[70:71]
	v_pk_fma_f32 v[84:85], v[38:39], v[92:93], v[84:85]
	v_pk_fma_f32 v[86:87], v[10:11], v[86:87], v[130:131]
	v_pk_mul_f32 v[84:85], v[84:85], v[90:91]
	v_pk_fma_f32 v[86:87], v[36:37], v[94:95], v[86:87]
	s_nop 0
	v_pk_mul_f32 v[86:87], v[86:87], v[88:89]
	s_nop 0
	v_cvt_pk_bf16_f32 v86, v86, v87
	v_bfe_u32 v59, v84, 16, 1
	v_add3_u32 v59, v84, v59, s81
	v_bfe_u32 v61, v85, 16, 1
	v_lshrrev_b32_e32 v59, 16, v59
	v_add3_u32 v61, v85, v61, s81
	v_and_or_b32 v87, v61, s80, v59
	global_store_dwordx2 v[96:97], v[86:87], off offset:2560
	s_nop 0
	v_lshlrev_b32_e32 v86, 16, v80
	v_and_b32_e32 v87, 0xffff0000, v80
	v_lshlrev_b32_e32 v80, 16, v81
	v_and_b32_e32 v81, 0xffff0000, v81
	v_pk_mul_f32 v[176:177], v[72:73], v[80:81] op_sel_hi:[0,1]
	v_lshlrev_b32_e32 v80, 16, v76
	v_and_b32_e32 v81, 0xffff0000, v76
	v_lshlrev_b32_e32 v76, 16, v77
	v_and_b32_e32 v77, 0xffff0000, v77
	v_pk_mul_f32 v[178:179], v[72:73], v[86:87] op_sel_hi:[0,1]
	v_pk_mul_f32 v[152:153], v[72:73], v[76:77] op_sel_hi:[0,1]
	v_pk_mul_f32 v[154:155], v[72:73], v[80:81] op_sel_hi:[0,1]
	v_lshlrev_b32_e32 v72, 16, v74
	v_and_b32_e32 v73, 0xffff0000, v74
	v_lshlrev_b32_e32 v74, 16, v75
	v_and_b32_e32 v75, 0xffff0000, v75
	v_pk_mul_f32 v[148:149], v[60:61], v[72:73] op_sel_hi:[0,1]
	v_lshlrev_b32_e32 v72, 16, v66
	v_and_b32_e32 v73, 0xffff0000, v66
	v_lshlrev_b32_e32 v66, 16, v67
	v_and_b32_e32 v67, 0xffff0000, v67
	v_pk_mul_f32 v[150:151], v[60:61], v[74:75] op_sel_hi:[0,1]
	v_pk_mul_f32 v[144:145], v[60:61], v[72:73] op_sel_hi:[0,1]
	v_pk_mul_f32 v[146:147], v[60:61], v[66:67] op_sel_hi:[0,1]
	v_lshlrev_b32_e32 v60, 16, v64
	v_and_b32_e32 v61, 0xffff0000, v64
	v_lshlrev_b32_e32 v64, 16, v65
	v_and_b32_e32 v65, 0xffff0000, v65
	v_pk_mul_f32 v[138:139], v[58:59], v[60:61] op_sel_hi:[0,1]
	v_lshlrev_b32_e32 v60, 16, v62
	v_and_b32_e32 v61, 0xffff0000, v62
	v_lshlrev_b32_e32 v62, 16, v63
	v_and_b32_e32 v63, 0xffff0000, v63
; #define LAS __attribute__((address_space(3)))
; __device__ __forceinline__ unsigned pk2(float lo, float hi) { return f2bf(lo) | (f2bf(hi) << 16); }
; __device__ __forceinline__ f32x4 bf4(u32x2 v) { return (f32x4){lo_bf(v.x), hi_bf(v.x), lo_bf(v.y), hi_bf(v.y)}; }
; __device__ __forceinline__ void ph_prep_conv(CArgs& a, int l, LAS unsigned char* lds, int bid, int nblk) {
;     ...
; #pragma unroll
;         for (int tt = 0; tt < 8; ++tt) {
;             const f32x4 xx = wx[0] * x1[tt] + wx[1] * x1[tt + 1] + wx[2] * x1[tt + 2] + bx, v2 = wv[0] * vv[tt] + wv[1] * vv[tt + 1] + wv[2] * vv[tt + 2] + bv, z = xx * v2;
;             u32x2 zo; zo.x = pk2(z[0], z[1]); zo.y = pk2(z[2], z[3]); *(LAS u32x2*)(zt + (tg * 8 + tt) * 264 + c4) = zo;
;             const f32x4 bg = bf4(*(const u32x2*)(pb + (size_t)tt * D_INP + SC0 + c4));
;             const f32x4 y = bg * (ws3[0] * mm[tt] + ws3[1] * mm[tt + 1] + ws3[2] * mm[tt + 2]);
;             u32x2 yo; yo.x = pk2(y[0], y[1]); yo.y = pk2(y[2], y[3]); *(u32x2*)(YMIX + (size_t)(c.row0 + tg * 8 + tt) * D + 256 + c4) = yo;
	v_pk_mul_f32 v[140:141], v[58:59], v[64:65] op_sel_hi:[0,1]
	v_pk_mul_f32 v[130:131], v[58:59], v[60:61] op_sel_hi:[0,1]
	v_pk_mul_f32 v[132:133], v[58:59], v[62:63] op_sel_hi:[0,1]
	v_lshlrev_b32_e32 v58, 16, v82
	v_and_b32_e32 v59, 0xffff0000, v82
	v_cmp_eq_u32_e32 vcc, v137, v142
	v_pk_mul_f32 v[72:73], v[136:137], v[58:59] op_sel_hi:[0,1]
	v_lshlrev_b32_e32 v62, 16, v124
	v_cndmask_b32_e64 v58, 0, 1.0, vcc
	v_and_b32_e32 v63, 0xffff0000, v124
	v_pk_mul_f32 v[62:63], v[58:59], v[62:63] op_sel_hi:[0,1]
	v_lshlrev_b32_e32 v66, 16, v122
	v_and_b32_e32 v67, 0xffff0000, v122
	v_pk_mul_f32 v[182:183], v[62:63], v[66:67]
	v_pk_mul_f32 v[66:67], v[14:15], v[94:95]
	v_lshlrev_b32_e32 v64, 16, v125
	v_and_b32_e32 v65, 0xffff0000, v125
	v_pk_fma_f32 v[66:67], v[10:11], v[70:71], v[66:67]
	v_pk_mul_f32 v[64:65], v[58:59], v[64:65] op_sel_hi:[0,1]
	v_lshlrev_b32_e32 v74, 16, v123
	v_and_b32_e32 v75, 0xffff0000, v123
	v_pk_fma_f32 v[66:67], v[36:37], v[182:183], v[66:67]
	v_pk_mul_f32 v[180:181], v[64:65], v[74:75]
	v_pk_mul_f32 v[74:75], v[16:17], v[92:93]
	s_mov_b32 s9, 0x2dc01000
	v_pk_fma_f32 v[68:69], v[12:13], v[68:69], v[74:75]
	v_lshlrev_b32_e32 v60, 16, v83
	v_pk_fma_f32 v[68:69], v[38:39], v[180:181], v[68:69]
	v_and_b32_e32 v61, 0xffff0000, v83
	v_pk_mul_f32 v[142:143], v[136:137], v[60:61] op_sel_hi:[0,1]
	v_lshlrev_b32_e32 v60, 16, v54
	v_and_b32_e32 v61, 0xffff0000, v54
	v_lshlrev_b32_e32 v54, 16, v55
	v_and_b32_e32 v55, 0xffff0000, v55
	v_pk_mul_f32 v[134:135], v[136:137], v[60:61] op_sel_hi:[0,1]
	v_pk_mul_f32 v[136:137], v[136:137], v[54:55] op_sel_hi:[0,1]
	v_lshlrev_b32_e32 v54, 16, v120
	v_and_b32_e32 v55, 0xffff0000, v120
	v_lshlrev_b32_e32 v60, 16, v121
	v_and_b32_e32 v61, 0xffff0000, v121
	v_lshlrev_b32_e32 v74, 16, v129
	v_and_b32_e32 v75, 0xffff0000, v129
	v_lshlrev_b32_e32 v76, 16, v127
	v_and_b32_e32 v77, 0xffff0000, v127
	v_pk_mul_f32 v[82:83], v[16:17], v[180:181]
	v_lshlrev_b32_e32 v96, 16, v109
	v_lshlrev_b32_e32 v62, 16, v220
	v_and_b32_e32 v63, 0xffff0000, v220
	v_pk_mul_f32 v[62:63], v[66:67], v[62:63]
	v_lshlrev_b32_e32 v64, 16, v221
	v_and_b32_e32 v65, 0xffff0000, v221
	v_pk_mul_f32 v[64:65], v[68:69], v[64:65]
	v_cvt_pk_bf16_f32 v62, v62, v63
	v_bfe_u32 v59, v64, 16, 1
	v_add3_u32 v59, v64, v59, s81
	v_bfe_u32 v63, v65, 16, 1
	v_lshrrev_b32_e32 v59, 16, v59
	v_add3_u32 v63, v65, v63, s81
	v_add_co_u32_e32 v68, vcc, s9, v56
	v_and_or_b32 v63, v63, s80, v59
	s_nop 0
	v_addc_co_u32_e32 v69, vcc, 0, v57, vcc
	s_movk_i32 s9, 0x5000
	global_store_dwordx2 v[68:69], v[62:63], off offset:512
	v_pk_mul_f32 v[122:123], v[58:59], v[54:55] op_sel_hi:[0,1]
	s_nop 0
	v_pk_mul_f32 v[124:125], v[58:59], v[60:61] op_sel_hi:[0,1]
	v_lshlrev_b32_e32 v54, 16, v118
	v_and_b32_e32 v55, 0xffff0000, v118
	v_lshlrev_b32_e32 v60, 16, v119
	v_and_b32_e32 v61, 0xffff0000, v119
	v_cmp_eq_u32_e32 vcc, v212, v213
	v_pk_mul_f32 v[118:119], v[58:59], v[54:55] op_sel_hi:[0,1]
	v_pk_mul_f32 v[120:121], v[58:59], v[60:61] op_sel_hi:[0,1]
	v_cndmask_b32_e64 v54, 0, 1.0, vcc
	v_lshlrev_b32_e32 v58, 16, v174
	v_and_b32_e32 v59, 0xffff0000, v174
	v_lshlrev_b32_e32 v60, 16, v175
	v_and_b32_e32 v61, 0xffff0000, v175
	v_pk_mul_f32 v[88:89], v[54:55], v[58:59] op_sel_hi:[0,1]
	v_pk_mul_f32 v[90:91], v[54:55], v[60:61] op_sel_hi:[0,1]
	v_lshlrev_b32_e32 v58, 16, v172
	v_and_b32_e32 v59, 0xffff0000, v172
	v_lshlrev_b32_e32 v60, 16, v173
	v_and_b32_e32 v61, 0xffff0000, v173
	v_pk_mul_f32 v[84:85], v[54:55], v[58:59] op_sel_hi:[0,1]
	v_pk_mul_f32 v[86:87], v[54:55], v[60:61] op_sel_hi:[0,1]
	v_lshlrev_b32_e32 v58, 16, v170
	v_and_b32_e32 v59, 0xffff0000, v170
	v_lshlrev_b32_e32 v60, 16, v171
	v_and_b32_e32 v61, 0xffff0000, v171
	v_pk_mul_f32 v[58:59], v[54:55], v[58:59] op_sel_hi:[0,1]
	v_pk_mul_f32 v[54:55], v[54:55], v[60:61] op_sel_hi:[0,1]
	v_lshlrev_b32_e32 v60, 16, v162
	v_and_b32_e32 v61, 0xffff0000, v162
	v_lshlrev_b32_e32 v62, 16, v163
	v_and_b32_e32 v63, 0xffff0000, v163
	v_cmp_eq_u32_e32 vcc, v214, v215
	v_pk_mul_f32 v[162:163], v[54:55], v[62:63]
	v_pk_mul_f32 v[170:171], v[58:59], v[60:61]
	v_cndmask_b32_e64 v54, 0, 1.0, vcc
	v_lshlrev_b32_e32 v58, 16, v160
	v_and_b32_e32 v59, 0xffff0000, v160
	v_lshlrev_b32_e32 v60, 16, v161
	v_and_b32_e32 v61, 0xffff0000, v161
	v_pk_mul_f32 v[64:65], v[54:55], v[58:59] op_sel_hi:[0,1]
	v_lshlrev_b32_e32 v58, 16, v158
	v_and_b32_e32 v59, 0xffff0000, v158
	v_pk_mul_f32 v[66:67], v[54:55], v[60:61] op_sel_hi:[0,1]
	v_lshlrev_b32_e32 v62, 16, v159
	v_and_b32_e32 v63, 0xffff0000, v159
	v_pk_mul_f32 v[60:61], v[54:55], v[58:59] op_sel_hi:[0,1]
	v_lshlrev_b32_e32 v58, 16, v128
	v_and_b32_e32 v59, 0xffff0000, v128
	v_pk_mul_f32 v[62:63], v[54:55], v[62:63] op_sel_hi:[0,1]
	v_pk_mul_f32 v[58:59], v[54:55], v[58:59] op_sel_hi:[0,1]
	v_pk_mul_f32 v[54:55], v[54:55], v[74:75] op_sel_hi:[0,1]
	v_lshlrev_b32_e32 v74, 16, v126
	v_and_b32_e32 v75, 0xffff0000, v126
	v_pk_mul_f32 v[126:127], v[54:55], v[76:77]
	v_pk_mul_f32 v[76:77], v[14:15], v[182:183]
	v_pk_mul_f32 v[128:129], v[58:59], v[74:75]
	v_pk_fma_f32 v[76:77], v[10:11], v[94:95], v[76:77]
	v_pk_fma_f32 v[82:83], v[12:13], v[92:93], v[82:83]
	v_pk_fma_f32 v[76:77], v[36:37], v[170:171], v[76:77]
	v_pk_fma_f32 v[82:83], v[38:39], v[162:163], v[82:83]
	v_cmp_eq_u32_e32 vcc, v216, v217
	s_movk_i32 s9, 0x7000
	v_lshlrev_b32_e32 v54, 16, v156
	v_cndmask_b32_e64 v80, 0, 1.0, vcc
	v_and_b32_e32 v55, 0xffff0000, v156
	v_lshlrev_b32_e32 v58, 16, v157
	v_and_b32_e32 v59, 0xffff0000, v157
	v_pk_mul_f32 v[158:159], v[14:15], v[170:171]
	v_pk_mul_f32 v[160:161], v[16:17], v[162:163]
	v_pk_fma_f32 v[158:159], v[10:11], v[182:183], v[158:159]
	v_pk_fma_f32 v[160:161], v[12:13], v[180:181], v[160:161]
; #define LAS __attribute__((address_space(3)))
; __device__ __forceinline__ unsigned pk2(float lo, float hi) { return f2bf(lo) | (f2bf(hi) << 16); }
; __device__ __forceinline__ f32x4 bf4(u32x2 v) { return (f32x4){lo_bf(v.x), hi_bf(v.x), lo_bf(v.y), hi_bf(v.y)}; }
; __device__ __forceinline__ void ph_prep_conv(CArgs& a, int l, LAS unsigned char* lds, int bid, int nblk) {
;     ...
; #pragma unroll
;         for (int tt = 0; tt < 8; ++tt) {
;             const f32x4 xx = wx[0] * x1[tt] + wx[1] * x1[tt + 1] + wx[2] * x1[tt + 2] + bx, v2 = wv[0] * vv[tt] + wv[1] * vv[tt + 1] + wv[2] * vv[tt + 2] + bv, z = xx * v2;
;             u32x2 zo; zo.x = pk2(z[0], z[1]); zo.y = pk2(z[2], z[3]); *(LAS u32x2*)(zt + (tg * 8 + tt) * 264 + c4) = zo;
;             const f32x4 bg = bf4(*(const u32x2*)(pb + (size_t)tt * D_INP + SC0 + c4));
;             const f32x4 y = bg * (ws3[0] * mm[tt] + ws3[1] * mm[tt + 1] + ws3[2] * mm[tt + 2]);
;             u32x2 yo; yo.x = pk2(y[0], y[1]); yo.y = pk2(y[2], y[3]); *(u32x2*)(YMIX + (size_t)(c.row0 + tg * 8 + tt) * D + 256 + c4) = yo;
	v_pk_fma_f32 v[158:159], v[36:37], v[128:129], v[158:159]
	v_pk_fma_f32 v[160:161], v[38:39], v[126:127], v[160:161]
	v_pk_mul_f32 v[54:55], v[80:81], v[54:55] op_sel_hi:[0,1]
	v_pk_mul_f32 v[58:59], v[80:81], v[58:59] op_sel_hi:[0,1]
	v_lshlrev_b32_e32 v92, 16, v111
	v_and_b32_e32 v93, 0xffff0000, v111
	v_and_b32_e32 v97, 0xffff0000, v109
	v_lshlrev_b32_e32 v74, 16, v222
	v_and_b32_e32 v75, 0xffff0000, v222
	v_pk_mul_f32 v[74:75], v[76:77], v[74:75]
	v_lshlrev_b32_e32 v70, 16, v223
	v_and_b32_e32 v71, 0xffff0000, v223
	v_pk_mul_f32 v[70:71], v[82:83], v[70:71]
	v_cvt_pk_bf16_f32 v74, v74, v75
	v_cvt_pk_bf16_f32 v75, v70, v71
	global_store_dwordx2 v[68:69], v[74:75], off offset:2560
	v_lshlrev_b32_e32 v70, 16, v117
	s_nop 0
	v_lshlrev_b32_e32 v68, 16, v116
	v_and_b32_e32 v69, 0xffff0000, v116
	v_and_b32_e32 v71, 0xffff0000, v117
	v_pk_mul_f32 v[74:75], v[80:81], v[68:69] op_sel_hi:[0,1]
	v_pk_mul_f32 v[76:77], v[80:81], v[70:71] op_sel_hi:[0,1]
	v_lshlrev_b32_e32 v68, 16, v114
	v_and_b32_e32 v69, 0xffff0000, v114
	v_lshlrev_b32_e32 v70, 16, v115
	v_and_b32_e32 v71, 0xffff0000, v115
	v_pk_mul_f32 v[82:83], v[80:81], v[68:69] op_sel_hi:[0,1]
	v_pk_mul_f32 v[68:69], v[80:81], v[70:71] op_sel_hi:[0,1]
	v_lshlrev_b32_e32 v70, 16, v112
	v_and_b32_e32 v71, 0xffff0000, v112
	v_lshlrev_b32_e32 v80, 16, v113
	v_and_b32_e32 v81, 0xffff0000, v113
	v_cmp_eq_u32_e32 vcc, v211, v218
	v_pk_mul_f32 v[68:69], v[68:69], v[80:81]
	v_pk_mul_f32 v[70:71], v[82:83], v[70:71]
	v_cndmask_b32_e64 v80, 0, 1.0, vcc
	v_lshlrev_b32_e32 v82, 16, v110
	v_and_b32_e32 v83, 0xffff0000, v110
	v_cmp_eq_u32_e32 vcc, v209, v210
	s_mov_b32 s9, 0x2dc02000
	v_pk_mul_f32 v[94:95], v[80:81], v[82:83] op_sel_hi:[0,1]
	v_lshlrev_b32_e32 v82, 16, v108
	v_and_b32_e32 v83, 0xffff0000, v108
	v_cndmask_b32_e64 v108, 0, 1.0, vcc
	v_pk_mul_f32 v[110:111], v[80:81], v[92:93] op_sel_hi:[0,1]
	v_pk_mul_f32 v[92:93], v[80:81], v[82:83] op_sel_hi:[0,1]
	v_lshlrev_b32_e32 v82, 16, v106
	v_and_b32_e32 v83, 0xffff0000, v106
	v_lshlrev_b32_e32 v106, 16, v107
	v_and_b32_e32 v107, 0xffff0000, v107
	v_pk_mul_f32 v[96:97], v[80:81], v[96:97] op_sel_hi:[0,1]
	v_pk_mul_f32 v[82:83], v[80:81], v[82:83] op_sel_hi:[0,1]
	v_pk_mul_f32 v[80:81], v[80:81], v[106:107] op_sel_hi:[0,1]
	v_lshlrev_b32_e32 v106, 16, v104
	v_and_b32_e32 v107, 0xffff0000, v104
	v_lshlrev_b32_e32 v104, 16, v105
	v_and_b32_e32 v105, 0xffff0000, v105
	v_pk_mul_f32 v[80:81], v[80:81], v[104:105]
	v_lshlrev_b32_e32 v104, 16, v102
	v_and_b32_e32 v105, 0xffff0000, v102
	v_pk_mul_f32 v[82:83], v[82:83], v[106:107]
	v_lshlrev_b32_e32 v106, 16, v103
	v_and_b32_e32 v107, 0xffff0000, v103
	v_pk_mul_f32 v[102:103], v[108:109], v[104:105] op_sel_hi:[0,1]
	v_lshlrev_b32_e32 v104, 16, v100
	v_and_b32_e32 v105, 0xffff0000, v100
	v_lshlrev_b32_e32 v112, 16, v101
	v_and_b32_e32 v113, 0xffff0000, v101
	v_pk_mul_f32 v[100:101], v[108:109], v[104:105] op_sel_hi:[0,1]
	v_pk_mul_f32 v[104:105], v[108:109], v[112:113] op_sel_hi:[0,1]
	v_lshlrev_b32_e32 v112, 16, v98
	v_and_b32_e32 v113, 0xffff0000, v98
	v_lshlrev_b32_e32 v98, 16, v99
	v_and_b32_e32 v99, 0xffff0000, v99
	v_pk_mul_f32 v[106:107], v[108:109], v[106:107] op_sel_hi:[0,1]
	v_pk_mul_f32 v[112:113], v[108:109], v[112:113] op_sel_hi:[0,1]
	v_pk_mul_f32 v[98:99], v[108:109], v[98:99] op_sel_hi:[0,1]
	v_lshlrev_b32_e32 v108, 16, v78
	v_and_b32_e32 v109, 0xffff0000, v78
	v_lshlrev_b32_e32 v78, 16, v79
	v_and_b32_e32 v79, 0xffff0000, v79
	v_pk_mul_f32 v[78:79], v[98:99], v[78:79]
	v_pk_mul_f32 v[98:99], v[112:113], v[108:109]
	v_pk_mul_f32 v[112:113], v[26:27], v[148:149]
	v_pk_mul_f32 v[108:109], v[28:29], v[150:151]
	v_pk_fma_f32 v[112:113], v[2:3], v[178:179], v[112:113]
	v_pk_mul_f32 v[114:115], v[20:21], v[146:147]
	v_pk_fma_f32 v[108:109], v[4:5], v[176:177], v[108:109]
	v_pk_fma_f32 v[112:113], v[22:23], v[138:139], v[112:113]
	v_pk_fma_f32 v[114:115], v[8:9], v[152:153], v[114:115]
	v_pk_fma_f32 v[108:109], v[24:25], v[140:141], v[108:109]
	v_pk_add_f32 v[112:113], v[40:41], v[112:113]
	v_pk_fma_f32 v[114:115], v[32:33], v[132:133], v[114:115]
	v_pk_add_f32 v[108:109], v[42:43], v[108:109]
	v_pk_add_f32 v[114:115], v[46:47], v[114:115]
	v_lshlrev_b32_e32 v116, 16, v224
	v_and_b32_e32 v117, 0xffff0000, v224
	v_pk_mul_f32 v[116:117], v[158:159], v[116:117]
	v_lshlrev_b32_e32 v156, 16, v225
	v_and_b32_e32 v157, 0xffff0000, v225
	v_pk_mul_f32 v[156:157], v[160:161], v[156:157]
	v_cvt_pk_bf16_f32 v116, v116, v117
	v_cvt_pk_bf16_f32 v117, v156, v157
	v_add_co_u32_e32 v156, vcc, s9, v56
	s_mov_b32 s9, 0x9000
	s_nop 0
	v_addc_co_u32_e32 v157, vcc, 0, v57, vcc
	global_store_dwordx2 v[156:157], v[116:117], off offset:512
	v_pk_mul_f32 v[158:159], v[18:19], v[144:145]
	s_nop 0
	v_pk_fma_f32 v[154:155], v[6:7], v[154:155], v[158:159]
	v_pk_mul_f32 v[108:109], v[108:109], v[114:115]
	v_pk_fma_f32 v[152:153], v[30:31], v[130:131], v[154:155]
	s_mov_b32 s9, 0xa000
	v_pk_add_f32 v[152:153], v[44:45], v[152:153]
	s_nop 0
	v_pk_mul_f32 v[112:113], v[112:113], v[152:153]
	s_nop 0
	v_cvt_pk_bf16_f32 v112, v112, v113
	v_cvt_pk_bf16_f32 v113, v108, v109
	v_pk_mul_f32 v[108:109], v[28:29], v[140:141]
	v_pk_mul_f32 v[114:115], v[26:27], v[138:139]
	v_pk_fma_f32 v[108:109], v[4:5], v[150:151], v[108:109]
	v_pk_mul_f32 v[150:151], v[18:19], v[130:131]
	v_pk_fma_f32 v[114:115], v[2:3], v[148:149], v[114:115]
	v_pk_fma_f32 v[144:145], v[6:7], v[144:145], v[150:151]
	v_pk_fma_f32 v[114:115], v[22:23], v[72:73], v[114:115]
	v_pk_fma_f32 v[144:145], v[30:31], v[134:135], v[144:145]
	v_pk_add_f32 v[114:115], v[40:41], v[114:115]
	v_pk_mul_f32 v[148:149], v[20:21], v[132:133]
	v_pk_add_f32 v[144:145], v[44:45], v[144:145]
; #define LAS __attribute__((address_space(3)))
; __device__ __forceinline__ unsigned pk2(float lo, float hi) { return f2bf(lo) | (f2bf(hi) << 16); }
; __device__ __forceinline__ f32x4 bf4(u32x2 v) { return (f32x4){lo_bf(v.x), hi_bf(v.x), lo_bf(v.y), hi_bf(v.y)}; }
; __device__ __forceinline__ void ph_prep_conv(CArgs& a, int l, LAS unsigned char* lds, int bid, int nblk) {
;     ...
; #pragma unroll
;         for (int tt = 0; tt < 8; ++tt) {
;             const f32x4 xx = wx[0] * x1[tt] + wx[1] * x1[tt + 1] + wx[2] * x1[tt + 2] + bx, v2 = wv[0] * vv[tt] + wv[1] * vv[tt + 1] + wv[2] * vv[tt + 2] + bv, z = xx * v2;
;             u32x2 zo; zo.x = pk2(z[0], z[1]); zo.y = pk2(z[2], z[3]); *(LAS u32x2*)(zt + (tg * 8 + tt) * 264 + c4) = zo;
;             const f32x4 bg = bf4(*(const u32x2*)(pb + (size_t)tt * D_INP + SC0 + c4));
;             const f32x4 y = bg * (ws3[0] * mm[tt] + ws3[1] * mm[tt + 1] + ws3[2] * mm[tt + 2]);
;             u32x2 yo; yo.x = pk2(y[0], y[1]); yo.y = pk2(y[2], y[3]); *(u32x2*)(YMIX + (size_t)(c.row0 + tg * 8 + tt) * D + 256 + c4) = yo;
	v_pk_fma_f32 v[146:147], v[8:9], v[146:147], v[148:149]
	v_pk_mul_f32 v[114:115], v[114:115], v[144:145]
	v_pk_fma_f32 v[108:109], v[24:25], v[142:143], v[108:109]
	v_pk_fma_f32 v[146:147], v[32:33], v[136:137], v[146:147]
	v_bfe_u32 v144, v114, 16, 1
	v_pk_add_f32 v[108:109], v[42:43], v[108:109]
	v_pk_add_f32 v[146:147], v[46:47], v[146:147]
	v_add3_u32 v114, v114, v144, s81
	v_bfe_u32 v144, v115, 16, 1
	v_pk_mul_f32 v[108:109], v[108:109], v[146:147]
	v_lshrrev_b32_e32 v114, 16, v114
	v_add3_u32 v115, v115, v144, s81
	v_and_or_b32 v114, v115, s80, v114
	v_cvt_pk_bf16_f32 v115, v108, v109
	ds_write2_b64 v185, v[112:113], v[114:115] offset1:66
	v_pk_mul_f32 v[112:113], v[26:27], v[72:73]
	v_pk_mul_f32 v[108:109], v[28:29], v[142:143]
	v_pk_fma_f32 v[112:113], v[2:3], v[138:139], v[112:113]
	v_pk_mul_f32 v[138:139], v[18:19], v[134:135]
	v_pk_mul_f32 v[114:115], v[20:21], v[136:137]
	v_pk_fma_f32 v[130:131], v[6:7], v[130:131], v[138:139]
	v_pk_fma_f32 v[108:109], v[4:5], v[140:141], v[108:109]
	v_pk_fma_f32 v[112:113], v[22:23], v[122:123], v[112:113]
	v_pk_fma_f32 v[114:115], v[8:9], v[132:133], v[114:115]
	v_pk_fma_f32 v[130:131], v[30:31], v[118:119], v[130:131]
	v_pk_fma_f32 v[108:109], v[24:25], v[124:125], v[108:109]
	v_pk_add_f32 v[112:113], v[40:41], v[112:113]
	v_pk_fma_f32 v[114:115], v[32:33], v[120:121], v[114:115]
	v_pk_add_f32 v[130:131], v[44:45], v[130:131]
	v_pk_add_f32 v[108:109], v[42:43], v[108:109]
	v_pk_add_f32 v[114:115], v[46:47], v[114:115]
	v_pk_mul_f32 v[112:113], v[112:113], v[130:131]
	v_pk_mul_f32 v[108:109], v[108:109], v[114:115]
	v_pk_mul_f32 v[130:131], v[14:15], v[128:129]
	v_pk_fma_f32 v[130:131], v[10:11], v[170:171], v[130:131]
	v_pk_fma_f32 v[130:131], v[36:37], v[70:71], v[130:131]
	v_cvt_pk_bf16_f32 v112, v112, v113
	v_lshlrev_b32_e32 v114, 16, v226
	v_and_b32_e32 v115, 0xffff0000, v226
	v_pk_mul_f32 v[132:133], v[16:17], v[126:127]
	v_pk_mul_f32 v[114:115], v[130:131], v[114:115]
	v_pk_fma_f32 v[132:133], v[12:13], v[162:163], v[132:133]
	v_lshlrev_b32_e32 v116, 16, v227
	v_and_b32_e32 v117, 0xffff0000, v227
	v_pk_fma_f32 v[132:133], v[38:39], v[68:69], v[132:133]
	v_pk_mul_f32 v[116:117], v[132:133], v[116:117]
	v_cvt_pk_bf16_f32 v114, v114, v115
	v_cvt_pk_bf16_f32 v115, v116, v117
	global_store_dwordx2 v[156:157], v[114:115], off offset:2560
	s_nop 0
	v_pk_mul_f32 v[116:117], v[26:27], v[122:123]
	v_pk_mul_f32 v[130:131], v[18:19], v[118:119]
	v_cvt_pk_bf16_f32 v113, v108, v109
	v_pk_mul_f32 v[108:109], v[28:29], v[124:125]
	v_pk_fma_f32 v[72:73], v[2:3], v[72:73], v[116:117]
	v_pk_mul_f32 v[116:117], v[20:21], v[120:121]
	v_pk_fma_f32 v[130:131], v[6:7], v[134:135], v[130:131]
	v_pk_fma_f32 v[108:109], v[4:5], v[142:143], v[108:109]
	v_pk_fma_f32 v[72:73], v[22:23], v[88:89], v[72:73]
	v_pk_fma_f32 v[116:117], v[8:9], v[136:137], v[116:117]
	v_pk_fma_f32 v[130:131], v[30:31], v[84:85], v[130:131]
	v_pk_fma_f32 v[108:109], v[24:25], v[90:91], v[108:109]
	v_pk_add_f32 v[72:73], v[40:41], v[72:73]
	v_pk_fma_f32 v[116:117], v[32:33], v[86:87], v[116:117]
	v_pk_add_f32 v[130:131], v[44:45], v[130:131]
	v_pk_add_f32 v[108:109], v[42:43], v[108:109]
	v_pk_add_f32 v[116:117], v[46:47], v[116:117]
	v_pk_mul_f32 v[72:73], v[72:73], v[130:131]
	v_pk_mul_f32 v[108:109], v[108:109], v[116:117]
	v_cvt_pk_bf16_f32 v72, v72, v73
	v_cvt_pk_bf16_f32 v73, v108, v109
	v_pk_mul_f32 v[108:109], v[26:27], v[88:89]
	v_pk_mul_f32 v[116:117], v[18:19], v[84:85]
	ds_write2_b64 v185, v[112:113], v[72:73] offset0:132 offset1:198
	v_pk_mul_f32 v[72:73], v[28:29], v[90:91]
	v_pk_fma_f32 v[108:109], v[2:3], v[122:123], v[108:109]
	v_pk_mul_f32 v[112:113], v[20:21], v[86:87]
	v_pk_fma_f32 v[116:117], v[6:7], v[118:119], v[116:117]
	v_pk_fma_f32 v[72:73], v[4:5], v[124:125], v[72:73]
	v_pk_fma_f32 v[108:109], v[22:23], v[64:65], v[108:109]
	v_pk_fma_f32 v[112:113], v[8:9], v[120:121], v[112:113]
	v_pk_fma_f32 v[116:117], v[30:31], v[60:61], v[116:117]
	v_pk_fma_f32 v[72:73], v[24:25], v[66:67], v[72:73]
	v_pk_add_f32 v[108:109], v[40:41], v[108:109]
	v_pk_fma_f32 v[112:113], v[32:33], v[62:63], v[112:113]
	v_pk_add_f32 v[116:117], v[44:45], v[116:117]
	v_pk_add_f32 v[72:73], v[42:43], v[72:73]
	v_pk_add_f32 v[112:113], v[46:47], v[112:113]
	v_pk_mul_f32 v[108:109], v[108:109], v[116:117]
	v_pk_mul_f32 v[72:73], v[72:73], v[112:113]
	v_cvt_pk_bf16_f32 v108, v108, v109
	v_cvt_pk_bf16_f32 v109, v72, v73
	v_pk_mul_f32 v[72:73], v[28:29], v[66:67]
	v_pk_mul_f32 v[112:113], v[26:27], v[64:65]
	v_pk_fma_f32 v[72:73], v[4:5], v[90:91], v[72:73]
	v_pk_fma_f32 v[88:89], v[2:3], v[88:89], v[112:113]
	v_pk_mul_f32 v[90:91], v[20:21], v[62:63]
	v_pk_mul_f32 v[112:113], v[18:19], v[60:61]
	v_pk_fma_f32 v[86:87], v[8:9], v[86:87], v[90:91]
	v_pk_fma_f32 v[84:85], v[6:7], v[84:85], v[112:113]
	v_pk_mul_f32 v[116:117], v[16:17], v[68:69]
	s_mov_b32 s9, 0x2dc03000
	v_pk_fma_f32 v[116:117], v[12:13], v[126:127], v[116:117]
	v_add_co_u32_e32 v56, vcc, s9, v56
	v_pk_fma_f32 v[116:117], v[38:39], v[80:81], v[116:117]
	s_nop 0
	v_addc_co_u32_e32 v57, vcc, 0, v57, vcc
	v_lshlrev_b32_e32 v90, 16, v228
	v_and_b32_e32 v91, 0xffff0000, v228
	v_lshlrev_b32_e32 v112, 16, v229
	v_and_b32_e32 v113, 0xffff0000, v229
	v_pk_mul_f32 v[114:115], v[14:15], v[70:71]
	v_pk_mul_f32 v[112:113], v[116:117], v[112:113]
	v_pk_fma_f32 v[114:115], v[10:11], v[128:129], v[114:115]
	s_mov_b32 s9, 0xc000
	v_pk_fma_f32 v[114:115], v[36:37], v[82:83], v[114:115]
	v_pk_mul_f32 v[90:91], v[114:115], v[90:91]
	s_nop 0
	v_bfe_u32 v114, v90, 16, 1
	v_add3_u32 v90, v90, v114, s81
	v_bfe_u32 v114, v91, 16, 1
	v_lshrrev_b32_e32 v90, 16, v90
	v_add3_u32 v91, v91, v114, s81
; #define LAS __attribute__((address_space(3)))
; __device__ __forceinline__ unsigned pk2(float lo, float hi) { return f2bf(lo) | (f2bf(hi) << 16); }
; __device__ __forceinline__ f32x4 bf4(u32x2 v) { return (f32x4){lo_bf(v.x), hi_bf(v.x), lo_bf(v.y), hi_bf(v.y)}; }
; __device__ __forceinline__ void ph_prep_conv(CArgs& a, int l, LAS unsigned char* lds, int bid, int nblk) {
;     ...
; #pragma unroll
;         for (int tt = 0; tt < 8; ++tt) {
;             const f32x4 xx = wx[0] * x1[tt] + wx[1] * x1[tt + 1] + wx[2] * x1[tt + 2] + bx, v2 = wv[0] * vv[tt] + wv[1] * vv[tt + 1] + wv[2] * vv[tt + 2] + bv, z = xx * v2;
;             u32x2 zo; zo.x = pk2(z[0], z[1]); zo.y = pk2(z[2], z[3]); *(LAS u32x2*)(zt + (tg * 8 + tt) * 264 + c4) = zo;
;             const f32x4 bg = bf4(*(const u32x2*)(pb + (size_t)tt * D_INP + SC0 + c4));
;             const f32x4 y = bg * (ws3[0] * mm[tt] + ws3[1] * mm[tt + 1] + ws3[2] * mm[tt + 2]);
;             u32x2 yo; yo.x = pk2(y[0], y[1]); yo.y = pk2(y[2], y[3]); *(u32x2*)(YMIX + (size_t)(c.row0 + tg * 8 + tt) * D + 256 + c4) = yo;
;         }
;         __syncthreads();
;         { const int ch = tid & 255, g0 = (tid >> 8) * 4;
;           const int soff = c.L == CTXL ? 0 : CTXL;
; #pragma unroll
;           for (int g = 0; g < 4; ++g) { const int t8 = (g0 + g) * 8; unsigned short e[8];
; #pragma unroll
;               for (int j = 0; j < 8; ++j) e[j] = zt[(t8 + j) * 264 + ch];
;               u32x4 o; o.x = e[0] | ((unsigned)e[1] << 16); o.y = e[2] | ((unsigned)e[3] << 16); o.z = e[4] | ((unsigned)e[5] << 16); o.w = e[6] | ((unsigned)e[7] << 16);
;               *(u32x4*)(ZT + ((size_t)(ch * 16 + c.b)) * 2304 + soff + c.t0 + t8) = o; } }
;         __syncthreads();
	v_and_or_b32 v90, v91, s80, v90
	v_bfe_u32 v91, v112, 16, 1
	v_add3_u32 v91, v112, v91, s81
	v_bfe_u32 v112, v113, 16, 1
	v_lshrrev_b32_e32 v91, 16, v91
	v_add3_u32 v112, v113, v112, s81
	v_and_or_b32 v91, v112, s80, v91
	global_store_dwordx2 v[56:57], v[90:91], off offset:512
	v_pk_fma_f32 v[88:89], v[22:23], v[54:55], v[88:89]
	v_pk_fma_f32 v[84:85], v[30:31], v[74:75], v[84:85]
	v_pk_fma_f32 v[72:73], v[24:25], v[58:59], v[72:73]
	v_pk_add_f32 v[88:89], v[40:41], v[88:89]
	v_pk_fma_f32 v[86:87], v[32:33], v[76:77], v[86:87]
	v_pk_add_f32 v[84:85], v[44:45], v[84:85]
	v_pk_add_f32 v[72:73], v[42:43], v[72:73]
	v_pk_add_f32 v[86:87], v[46:47], v[86:87]
	v_pk_mul_f32 v[84:85], v[88:89], v[84:85]
	v_pk_mul_f32 v[72:73], v[72:73], v[86:87]
	v_bfe_u32 v86, v84, 16, 1
	v_add3_u32 v84, v84, v86, s81
	v_bfe_u32 v86, v85, 16, 1
	v_lshrrev_b32_e32 v84, 16, v84
	v_add3_u32 v85, v85, v86, s81
	v_and_or_b32 v84, v85, s80, v84
	v_cvt_pk_bf16_f32 v85, v72, v73
	v_add_u32_e32 v72, 0x800, v185
	ds_write2_b64 v72, v[108:109], v[84:85] offset0:8 offset1:74
	v_pk_mul_f32 v[84:85], v[26:27], v[54:55]
	v_pk_mul_f32 v[72:73], v[28:29], v[58:59]
	v_pk_fma_f32 v[64:65], v[2:3], v[64:65], v[84:85]
	v_pk_mul_f32 v[84:85], v[18:19], v[74:75]
	v_pk_fma_f32 v[64:65], v[22:23], v[94:95], v[64:65]
	v_pk_fma_f32 v[60:61], v[6:7], v[60:61], v[84:85]
	v_pk_fma_f32 v[66:67], v[4:5], v[66:67], v[72:73]
	v_pk_fma_f32 v[60:61], v[30:31], v[92:93], v[60:61]
	v_pk_add_f32 v[64:65], v[40:41], v[64:65]
	v_pk_mul_f32 v[72:73], v[20:21], v[76:77]
	v_pk_add_f32 v[60:61], v[44:45], v[60:61]
	v_pk_fma_f32 v[62:63], v[8:9], v[62:63], v[72:73]
	v_pk_mul_f32 v[60:61], v[64:65], v[60:61]
	v_pk_fma_f32 v[66:67], v[24:25], v[110:111], v[66:67]
	v_pk_fma_f32 v[62:63], v[32:33], v[96:97], v[62:63]
	v_pk_add_f32 v[66:67], v[42:43], v[66:67]
	v_pk_add_f32 v[62:63], v[46:47], v[62:63]
	v_pk_mul_f32 v[62:63], v[66:67], v[62:63]
	v_cvt_pk_bf16_f32 v60, v60, v61
	v_cvt_pk_bf16_f32 v61, v62, v63
	v_pk_mul_f32 v[62:63], v[26:27], v[94:95]
	ds_write_b64 v185, v[60:61] offset:3168
	v_pk_mul_f32 v[60:61], v[28:29], v[110:111]
	v_pk_fma_f32 v[54:55], v[2:3], v[54:55], v[62:63]
	v_pk_mul_f32 v[62:63], v[18:19], v[92:93]
	v_pk_fma_f32 v[58:59], v[4:5], v[58:59], v[60:61]
	v_pk_mul_f32 v[60:61], v[20:21], v[96:97]
	v_pk_fma_f32 v[62:63], v[6:7], v[74:75], v[62:63]
	v_pk_fma_f32 v[54:55], v[22:23], v[102:103], v[54:55]
	v_pk_fma_f32 v[60:61], v[8:9], v[76:77], v[60:61]
	v_pk_fma_f32 v[62:63], v[30:31], v[100:101], v[62:63]
	v_pk_fma_f32 v[58:59], v[24:25], v[106:107], v[58:59]
	v_pk_add_f32 v[54:55], v[40:41], v[54:55]
	v_pk_fma_f32 v[60:61], v[32:33], v[104:105], v[60:61]
	v_pk_add_f32 v[62:63], v[44:45], v[62:63]
	v_pk_add_f32 v[58:59], v[42:43], v[58:59]
	v_pk_add_f32 v[60:61], v[46:47], v[60:61]
	v_pk_mul_f32 v[54:55], v[54:55], v[62:63]
	v_pk_mul_f32 v[58:59], v[58:59], v[60:61]
	v_cvt_pk_bf16_f32 v54, v54, v55
	v_cvt_pk_bf16_f32 v55, v58, v59
	v_pk_mul_f32 v[58:59], v[14:15], v[82:83]
	ds_write_b64 v186, v[54:55]
	v_pk_fma_f32 v[58:59], v[10:11], v[70:71], v[58:59]
	v_lshlrev_b32_e32 v54, 16, v230
	v_and_b32_e32 v55, 0xffff0000, v230
	v_pk_fma_f32 v[58:59], v[36:37], v[98:99], v[58:59]
	v_pk_mul_f32 v[60:61], v[16:17], v[80:81]
	v_pk_mul_f32 v[54:55], v[58:59], v[54:55]
	v_pk_fma_f32 v[60:61], v[12:13], v[68:69], v[60:61]
	v_lshlrev_b32_e32 v52, 16, v231
	v_and_b32_e32 v53, 0xffff0000, v231
	v_pk_fma_f32 v[60:61], v[38:39], v[78:79], v[60:61]
	v_pk_mul_f32 v[52:53], v[60:61], v[52:53]
	v_cvt_pk_bf16_f32 v54, v54, v55
	v_cvt_pk_bf16_f32 v55, v52, v53
	global_store_dwordx2 v[56:57], v[54:55], off offset:2560
	v_add_u32_e32 v54, s8, v184
	v_mov_b64_e32 v[52:53], s[26:27]
	s_movk_i32 s8, 0x1200
	s_waitcnt lgkmcnt(0)
	s_barrier
	v_mad_i64_i32 v[52:53], s[8:9], v54, s8, v[52:53]
	ds_read_u16 v58, v187
	ds_read_u16 v59, v187 offset:528
	ds_read_u16 v60, v187 offset:1056
	ds_read_u16 v61, v187 offset:1584
	ds_read_u16 v54, v187 offset:2112
	ds_read_u16 v62, v187 offset:2640
	ds_read_u16 v55, v187 offset:3168
	ds_read_u16 v63, v187 offset:3696
	v_lshl_add_u64 v[52:53], v[52:53], 0, s[78:79]
	v_lshl_add_u64 v[56:57], s[28:29], 1, v[52:53]
	s_mov_b32 s8, 0x5040100
	s_waitcnt lgkmcnt(2)
	v_perm_b32 v54, v62, v54, s8
	s_waitcnt lgkmcnt(0)
	v_perm_b32 v55, v63, v55, s8
	v_perm_b32 v53, v61, v60, s8
	v_perm_b32 v52, v59, v58, s8
	v_lshl_add_u64 v[58:59], v[50:51], 1, v[56:57]
	global_store_dwordx4 v[58:59], v[52:55], off
	ds_read_u16 v52, v187 offset:4752
	ds_read_u16 v53, v187 offset:5280
	ds_read_u16 v54, v187 offset:7392
	ds_read_u16 v55, v187 offset:7920
	ds_read_u16 v60, v187 offset:5808
	ds_read_u16 v61, v187 offset:6336
	ds_read_u16 v62, v187 offset:8976
	ds_read_u16 v63, v187 offset:6864
	ds_read_u16 v64, v188
	ds_read_u16 v65, v188 offset:4224
	ds_read_u16 v66, v187 offset:9504
	ds_read_u16 v67, v187 offset:10032
	ds_read_u16 v68, v187 offset:10560
	ds_read_u16 v69, v187 offset:11088
	ds_read_u16 v70, v187 offset:11616
	ds_read_u16 v71, v187 offset:12144
	s_waitcnt lgkmcnt(12)
	v_perm_b32 v55, v55, v54, s8
	s_waitcnt lgkmcnt(11)
	v_perm_b32 v53, v60, v53, s8
	s_waitcnt lgkmcnt(7)
	v_perm_b32 v52, v52, v64, s8
	v_perm_b32 v54, v63, v61, s8
	global_store_dwordx4 v[58:59], v[52:55], off offset:16
	v_lshl_add_u64 v[56:57], v[48:49], 1, v[56:57]
	s_waitcnt lgkmcnt(0)
	v_perm_b32 v55, v71, v70, s8
	ds_read_u16 v60, v189
	ds_read_u16 v61, v202
	ds_read_u16 v63, v203
	ds_read_u16 v64, v204
	ds_read_u16 v70, v205
	ds_read_u16 v71, v206
	ds_read_u16 v72, v207
	ds_read_u16 v73, v208
	v_perm_b32 v54, v69, v68, s8
	v_perm_b32 v53, v67, v66, s8
	v_perm_b32 v52, v62, v65, s8
	global_store_dwordx4 v[58:59], v[52:55], off offset:32
	s_waitcnt lgkmcnt(0)
	s_nop 0
	v_perm_b32 v55, v73, v72, s8
	v_perm_b32 v54, v71, v70, s8
	v_perm_b32 v53, v64, v63, s8
	v_perm_b32 v52, v61, v60, s8
	v_readlane_b32 s8, v252, 57
	s_add_i32 s1, s1, s8
	s_cmpk_lt_i32 s0, 0x240
	global_store_dwordx4 v[56:57], v[52:55], off
	s_barrier
	s_cbranch_scc0 .LBB0_271

; #define LAS __attribute__((address_space(3)))
; __device__ __forceinline__ float bf2f(unsigned v) { return __uint_as_float(v << 16); }
; __device__ __forceinline__ float rdlane_f(float v, int l) { return __builtin_bit_cast(float, __builtin_amdgcn_readlane(__builtin_bit_cast(int, v), l)); }
; __device__ __forceinline__ void ph_prep_tok(CArgs& a, int l, LAS unsigned char* lds, int gw, int ngw) {
;     ...
;     for (int row0 = gw * 4; row0 < NTOK; row0 += ngw * 4) {
;         int z = 0; asm volatile("" : "+v"(z));
;         const LAS float* wa = swa + z; const LAS float* cw = scw + z;
;         const bf16* pr0 = P + (size_t)row0 * D_INP;
;         int tpos, lo, hi;
;         if (row0 < NTOK_C) { tpos = row0 & 255; lo = 0; hi = CTXL; } else { tpos = (row0 - NTOK_C) & 2047; lo = tpos & ~63; hi = lo + 64; }
;         bf16 avb[4]; u32x2 xr[3][6]; bf16 gb4[4];
; #pragma unroll
;         for (int r = 0; r < 4; ++r) avb[r] = pr0[(size_t)r * D_INP + GLA0 + 768 + (lane & 31)];
; #pragma unroll
;         for (int g = 0; g < 3; ++g)
; #pragma unroll
;             for (int r = 0; r < 6; ++r) { const int tc = min(max(tpos + r - 1, lo), hi - 1); xr[g][r] = *(const u32x2*)(pr0 + (ptrdiff_t)(tc - tpos) * D_INP + GDN0 + g * 256 + 4 * lane); }
; #pragma unroll
;         for (int i = 0; i < 4; ++i) gb4[i] = pr0[(size_t)gr * D_INP + GDN0 + 1024 + 4 * i + gh];
;         float av[4], s[4][4];
; #pragma unroll
;         for (int r = 0; r < 4; ++r) { av[r] = bf2f(avb[r]); s[r][0] = sba[lane]; s[r][1] = sba[64 + lane]; s[r][2] = sba[128 + lane]; s[r][3] = sba[192 + lane]; }
; #pragma unroll
;         for (int i = 0; i < 16; ++i) { const float w0 = wa[i * 128 + lane], w1 = wa[i * 128 + 64 + lane], w2 = wa[2048 + i * 128 + lane], w3 = wa[2048 + i * 128 + 64 + lane];
; #pragma unroll
;             for (int r = 0; r < 4; ++r) { const float af = rdlane_f(av[r], i), ab = rdlane_f(av[r], 16 + i); s[r][0] += af * w0; s[r][1] += af * w1; s[r][2] += ab * w2; s[r][3] += ab * w3; } }
.LBB0_302:
	s_and_b32 s4, s0, 0x7c0
	s_add_i32 s1, s4, 64
	s_cmpk_lt_i32 s0, 0x1000
	s_movk_i32 s5, 0x7fc
	s_cselect_b32 s5, 0xfc, s5
	s_cselect_b32 s1, 0x100, s1
	s_cselect_b32 s8, 0, s4
	s_and_b32 s9, s5, s0
	s_add_i32 s4, s9, -1
	s_add_i32 s6, s1, -1
	s_max_i32 s4, s4, s8
	s_min_u32 s4, s4, s6
	s_sub_i32 s4, s4, s9
	s_mul_hi_i32 s5, s4, 0x1c00
	s_mulk_i32 s4, 0x1c00
	v_mov_b32_e32 v2, v35
	s_add_u32 s4, s2, s4
	s_addc_u32 s5, s3, s5
	v_lshl_add_u32 v52, v2, 2, 0
	v_lshl_add_u64 v[2:3], s[4:5], 0, v[26:27]
	s_max_u32 s4, s9, s8
	s_min_u32 s4, s4, s6
	s_sub_i32 s4, s4, s9
	s_mulk_i32 s4, 0x1c00
	s_ashr_i32 s5, s4, 31
	s_add_u32 s4, s2, s4
	s_addc_u32 s5, s3, s5
	v_lshl_add_u64 v[4:5], s[4:5], 0, v[26:27]
	s_or_b32 s4, s9, 1
	s_max_u32 s4, s4, s8
	s_min_u32 s4, s4, s6
	s_sub_i32 s4, s4, s9
	s_mulk_i32 s4, 0x1c00
	s_ashr_i32 s5, s4, 31
	s_add_u32 s4, s2, s4
	s_addc_u32 s5, s3, s5
	v_lshl_add_u64 v[6:7], s[4:5], 0, v[26:27]
	s_or_b32 s4, s9, 2
	s_max_u32 s4, s4, s8
	s_min_u32 s4, s4, s6
	s_sub_i32 s4, s4, s9
	s_mulk_i32 s4, 0x1c00
	s_ashr_i32 s5, s4, 31
	s_add_u32 s4, s2, s4
	s_mov_b32 s7, 0x1e001000
	s_addc_u32 s5, s3, s5
	s_or_b32 s10, s9, 3
	v_add_co_u32_e32 v2, vcc, s7, v2
	v_lshl_add_u64 v[8:9], s[4:5], 0, v[26:27]
	s_max_u32 s4, s10, s8
	v_addc_co_u32_e32 v3, vcc, 0, v3, vcc
	s_min_u32 s4, s4, s6
	v_add_co_u32_e32 v4, vcc, s7, v4
	s_sub_i32 s4, s4, s9
	s_nop 0
	v_addc_co_u32_e32 v5, vcc, 0, v5, vcc
	s_mulk_i32 s4, 0x1c00
	v_add_co_u32_e32 v6, vcc, s7, v6
	s_ashr_i32 s5, s4, 31
	s_nop 0
	v_addc_co_u32_e32 v7, vcc, 0, v7, vcc
	s_add_u32 s4, s2, s4
	v_add_co_u32_e32 v44, vcc, s7, v8
	s_addc_u32 s5, s3, s5
	s_nop 0
	v_addc_co_u32_e32 v45, vcc, 0, v9, vcc
	v_lshl_add_u64 v[8:9], s[4:5], 0, v[26:27]
	s_add_i32 s4, s9, 4
	s_max_u32 s4, s4, s8
	s_min_u32 s4, s4, s6
	s_sub_i32 s4, s4, s9
	s_mulk_i32 s4, 0x1c00
	s_ashr_i32 s5, s4, 31
	s_add_u32 s4, s2, s4
	v_add_co_u32_e32 v46, vcc, s7, v8
	s_addc_u32 s5, s3, s5
	s_nop 0
	v_addc_co_u32_e32 v47, vcc, 0, v9, vcc
	v_lshl_add_u64 v[8:9], s[4:5], 0, v[26:27]
	v_add_co_u32_e32 v50, vcc, s7, v8
	global_load_dwordx2 v[40:41], v[2:3], off offset:576
	global_load_dwordx2 v[38:39], v[4:5], off offset:576
	global_load_dwordx2 v[42:43], v[6:7], off offset:576
	global_load_dwordx2 v[32:33], v[44:45], off offset:576
	v_addc_co_u32_e32 v51, vcc, 0, v9, vcc
	global_load_dwordx2 v[36:37], v[46:47], off offset:576
	global_load_dwordx2 v[30:31], v[50:51], off offset:576
	global_load_dwordx2 v[66:67], v[2:3], off offset:1088
	global_load_dwordx2 v[64:65], v[4:5], off offset:1088
	global_load_dwordx2 v[62:63], v[6:7], off offset:1088
	global_load_dwordx2 v[60:61], v[44:45], off offset:1088
	global_load_dwordx2 v[58:59], v[46:47], off offset:1088
	global_load_dwordx2 v[56:57], v[50:51], off offset:1088
	global_load_dwordx2 v[12:13], v[2:3], off offset:1600
	global_load_dwordx2 v[10:11], v[4:5], off offset:1600
	global_load_dwordx2 v[8:9], v[6:7], off offset:1600
	s_nop 0
	global_load_dwordx2 v[6:7], v[44:45], off offset:1600
	global_load_dwordx2 v[4:5], v[46:47], off offset:1600
	global_load_dwordx2 v[2:3], v[50:51], off offset:1600
	v_lshl_add_u64 v[44:45], s[2:3], 0, v[24:25]
	s_mov_b32 s4, 0x1e000000
	v_add_co_u32_e32 v44, vcc, s4, v44
	v_lshl_add_u64 v[48:49], s[2:3], 0, v[28:29]
	s_nop 0
	v_addc_co_u32_e32 v45, vcc, 0, v45, vcc
	v_add_co_u32_e32 v50, vcc, s7, v48
	global_load_ushort v34, v[44:45], off
	global_load_ushort v113, v[44:45], off offset:8
	global_load_ushort v114, v[44:45], off offset:16
	global_load_ushort v115, v[44:45], off offset:24
	v_addc_co_u32_e32 v51, vcc, 0, v49, vcc
	ds_read2st64_b32 v[46:47], v110 offset0:224 offset1:225
	ds_read2st64_b32 v[44:45], v110 offset0:226 offset1:227
	global_load_ushort v50, v[50:51], off offset:512
	s_mov_b32 s4, 0x1e002000
	v_lshl_add_u32 v79, v108, 2, v52
	s_mov_b32 s6, 0x7f800000
	s_mov_b32 s7, 0x52800000
	s_mov_b32 s11, 0x53c00000
	s_cmp_le_u32 s9, s8
	v_lshl_add_u32 v117, v109, 2, v52
	v_add_u32_e32 v116, 0xfc00, v52
	s_waitcnt vmcnt(0)
	v_lshlrev_b32_e32 v71, 16, v50
	v_add_co_u32_e32 v50, vcc, s4, v48
	s_mov_b32 s4, 0x1e004000
	s_nop 0
	v_addc_co_u32_e32 v51, vcc, 0, v49, vcc
	global_load_ushort v50, v[50:51], off offset:3584
	v_readlane_b32 s5, v71, 16
	s_waitcnt vmcnt(0)
	v_lshlrev_b32_e32 v72, 16, v50
	v_add_co_u32_e32 v50, vcc, s4, v48
	s_mov_b32 s4, 0x1e006000
	s_nop 0
	v_addc_co_u32_e32 v51, vcc, 0, v49, vcc
	v_add_co_u32_e32 v48, vcc, s4, v48
	global_load_ushort v50, v[50:51], off offset:2560
	s_nop 0
	v_addc_co_u32_e32 v49, vcc, 0, v49, vcc
	global_load_ushort v48, v[48:49], off offset:1536
	v_readlane_b32 s4, v71, 0
	s_waitcnt vmcnt(1)
	v_lshlrev_b32_e32 v73, 16, v50
	s_waitcnt vmcnt(0)
	v_lshlrev_b32_e32 v76, 16, v48
	ds_read2st64_b32 v[48:49], v79 offset0:160 offset1:161
	ds_read2st64_b32 v[80:81], v79 offset0:192 offset1:193
	s_waitcnt lgkmcnt(1)
	v_fma_f32 v78, s4, v48, v46
	v_fma_f32 v77, s4, v49, v47
	s_waitcnt lgkmcnt(0)
	v_fma_f32 v75, s5, v80, v44
	v_fma_f32 v74, s5, v81, v45
	v_readlane_b32 s4, v72, 0
	v_readlane_b32 s5, v72, 16
	s_nop 0
	v_fma_f32 v70, s4, v48, v46
	v_fma_f32 v51, s4, v49, v47
	v_fma_f32 v50, s5, v80, v44
	v_fma_f32 v69, s5, v81, v45
	v_readlane_b32 s4, v73, 0
	v_readlane_b32 s5, v73, 16
	s_nop 0
	v_fma_f32 v68, s4, v48, v46
	v_fma_f32 v55, s4, v49, v47
	v_fma_f32 v54, s5, v80, v44
	v_fma_f32 v53, s5, v81, v45
	v_readlane_b32 s4, v76, 0
	v_readlane_b32 s5, v76, 16
	s_nop 0
	v_fma_f32 v46, s4, v48, v46
	v_fmac_f32_e32 v47, s4, v49
	v_fma_f32 v44, s5, v80, v44
	v_fmac_f32_e32 v45, s5, v81
	ds_read2st64_b32 v[48:49], v79 offset0:162 offset1:163
	ds_read2st64_b32 v[80:81], v79 offset0:194 offset1:195
	v_readlane_b32 s4, v71, 1
	v_readlane_b32 s5, v71, 17
	s_waitcnt lgkmcnt(1)
; __device__ __forceinline__ float rdlane_f(float v, int l) { return __builtin_bit_cast(float, __builtin_amdgcn_readlane(__builtin_bit_cast(int, v), l)); }
; __device__ __forceinline__ void ph_prep_tok(CArgs& a, int l, LAS unsigned char* lds, int gw, int ngw) {
;     ...
;         for (int i = 0; i < 16; ++i) { const float w0 = wa[i * 128 + lane], w1 = wa[i * 128 + 64 + lane], w2 = wa[2048 + i * 128 + lane], w3 = wa[2048 + i * 128 + 64 + lane];
; #pragma unroll
;             for (int r = 0; r < 4; ++r) { const float af = rdlane_f(av[r], i), ab = rdlane_f(av[r], 16 + i); s[r][0] += af * w0; s[r][1] += af * w1; s[r][2] += ab * w2; s[r][3] += ab * w3; } }
	v_fmac_f32_e32 v78, s4, v48
	v_fmac_f32_e32 v77, s4, v49
	s_waitcnt lgkmcnt(0)
	v_fmac_f32_e32 v75, s5, v80
	v_fmac_f32_e32 v74, s5, v81
	v_readlane_b32 s4, v72, 1
	v_readlane_b32 s5, v72, 17
	s_nop 0
	v_fmac_f32_e32 v70, s4, v48
	v_fmac_f32_e32 v51, s4, v49
	v_fmac_f32_e32 v50, s5, v80
	v_fmac_f32_e32 v69, s5, v81
	v_readlane_b32 s4, v73, 1
	v_readlane_b32 s5, v73, 17
	s_nop 0
	v_fmac_f32_e32 v68, s4, v48
	v_fmac_f32_e32 v55, s4, v49
	v_fmac_f32_e32 v54, s5, v80
	v_fmac_f32_e32 v53, s5, v81
	v_readlane_b32 s4, v76, 1
	v_readlane_b32 s5, v76, 17
	s_nop 0
	v_fmac_f32_e32 v46, s4, v48
	v_fmac_f32_e32 v47, s4, v49
	v_fmac_f32_e32 v44, s5, v80
	v_fmac_f32_e32 v45, s5, v81
	ds_read2st64_b32 v[48:49], v79 offset0:164 offset1:165
	ds_read2st64_b32 v[80:81], v79 offset0:196 offset1:197
	v_readlane_b32 s4, v71, 2
	v_readlane_b32 s5, v71, 18
	s_waitcnt lgkmcnt(1)
	v_fmac_f32_e32 v78, s4, v48
	v_fmac_f32_e32 v77, s4, v49
	s_waitcnt lgkmcnt(0)
	v_fmac_f32_e32 v75, s5, v80
	v_fmac_f32_e32 v74, s5, v81
	v_readlane_b32 s4, v72, 2
	v_readlane_b32 s5, v72, 18
	s_nop 0
	v_fmac_f32_e32 v70, s4, v48
	v_fmac_f32_e32 v51, s4, v49
	v_fmac_f32_e32 v50, s5, v80
	v_fmac_f32_e32 v69, s5, v81
	v_readlane_b32 s4, v73, 2
	v_readlane_b32 s5, v73, 18
	s_nop 0
	v_fmac_f32_e32 v68, s4, v48
	v_fmac_f32_e32 v55, s4, v49
	v_fmac_f32_e32 v54, s5, v80
	v_fmac_f32_e32 v53, s5, v81
	v_readlane_b32 s4, v76, 2
	v_readlane_b32 s5, v76, 18
	s_nop 0
	v_fmac_f32_e32 v46, s4, v48
	v_fmac_f32_e32 v47, s4, v49
	v_fmac_f32_e32 v44, s5, v80
	v_fmac_f32_e32 v45, s5, v81
	ds_read2st64_b32 v[48:49], v79 offset0:166 offset1:167
	ds_read2st64_b32 v[80:81], v79 offset0:198 offset1:199
	v_readlane_b32 s4, v71, 3
	v_readlane_b32 s5, v71, 19
	s_waitcnt lgkmcnt(1)
	v_fmac_f32_e32 v78, s4, v48
	v_fmac_f32_e32 v77, s4, v49
	s_waitcnt lgkmcnt(0)
	v_fmac_f32_e32 v75, s5, v80
	v_fmac_f32_e32 v74, s5, v81
	v_readlane_b32 s4, v72, 3
	v_readlane_b32 s5, v72, 19
	s_nop 0
	v_fmac_f32_e32 v70, s4, v48
	v_fmac_f32_e32 v51, s4, v49
	v_fmac_f32_e32 v50, s5, v80
	v_fmac_f32_e32 v69, s5, v81
	v_readlane_b32 s4, v73, 3
	v_readlane_b32 s5, v73, 19
	s_nop 0
	v_fmac_f32_e32 v68, s4, v48
	v_fmac_f32_e32 v55, s4, v49
	v_fmac_f32_e32 v54, s5, v80
	v_fmac_f32_e32 v53, s5, v81
	v_readlane_b32 s4, v76, 3
	v_readlane_b32 s5, v76, 19
	s_nop 0
	v_fmac_f32_e32 v46, s4, v48
	v_fmac_f32_e32 v47, s4, v49
	v_fmac_f32_e32 v44, s5, v80
	v_fmac_f32_e32 v45, s5, v81
	ds_read2st64_b32 v[48:49], v79 offset0:168 offset1:169
	ds_read2st64_b32 v[80:81], v79 offset0:200 offset1:201
	v_readlane_b32 s4, v71, 4
	v_readlane_b32 s5, v71, 20
	s_waitcnt lgkmcnt(1)
	v_fmac_f32_e32 v78, s4, v48
	v_fmac_f32_e32 v77, s4, v49
	s_waitcnt lgkmcnt(0)
	v_fmac_f32_e32 v75, s5, v80
	v_fmac_f32_e32 v74, s5, v81
	v_readlane_b32 s4, v72, 4
	v_readlane_b32 s5, v72, 20
	s_nop 0
	v_fmac_f32_e32 v70, s4, v48
	v_fmac_f32_e32 v51, s4, v49
	v_fmac_f32_e32 v50, s5, v80
	v_fmac_f32_e32 v69, s5, v81
	v_readlane_b32 s4, v73, 4
	v_readlane_b32 s5, v73, 20
	s_nop 0
	v_fmac_f32_e32 v68, s4, v48
	v_fmac_f32_e32 v55, s4, v49
	v_fmac_f32_e32 v54, s5, v80
	v_fmac_f32_e32 v53, s5, v81
	v_readlane_b32 s4, v76, 4
	v_readlane_b32 s5, v76, 20
	s_nop 0
	v_fmac_f32_e32 v46, s4, v48
	v_fmac_f32_e32 v47, s4, v49
	v_fmac_f32_e32 v44, s5, v80
	v_fmac_f32_e32 v45, s5, v81
	ds_read2st64_b32 v[48:49], v79 offset0:170 offset1:171
	ds_read2st64_b32 v[80:81], v79 offset0:202 offset1:203
	v_readlane_b32 s4, v71, 5
	v_readlane_b32 s5, v71, 21
	s_waitcnt lgkmcnt(1)
	v_fmac_f32_e32 v78, s4, v48
	v_fmac_f32_e32 v77, s4, v49
	s_waitcnt lgkmcnt(0)
	v_fmac_f32_e32 v75, s5, v80
	v_fmac_f32_e32 v74, s5, v81
	v_readlane_b32 s4, v72, 5
	v_readlane_b32 s5, v72, 21
	s_nop 0
	v_fmac_f32_e32 v70, s4, v48
	v_fmac_f32_e32 v51, s4, v49
	v_fmac_f32_e32 v50, s5, v80
	v_fmac_f32_e32 v69, s5, v81
	v_readlane_b32 s4, v73, 5
	v_readlane_b32 s5, v73, 21
	s_nop 0
	v_fmac_f32_e32 v68, s4, v48
	v_fmac_f32_e32 v55, s4, v49
	v_fmac_f32_e32 v54, s5, v80
	v_fmac_f32_e32 v53, s5, v81
	v_readlane_b32 s4, v76, 5
	v_readlane_b32 s5, v76, 21
	s_nop 0
	v_fmac_f32_e32 v46, s4, v48
	v_fmac_f32_e32 v47, s4, v49
	v_fmac_f32_e32 v44, s5, v80
	v_fmac_f32_e32 v45, s5, v81
	ds_read2st64_b32 v[48:49], v79 offset0:172 offset1:173
	ds_read2st64_b32 v[80:81], v79 offset0:204 offset1:205
	v_readlane_b32 s4, v71, 6
	v_readlane_b32 s5, v71, 22
	s_waitcnt lgkmcnt(1)
	v_fmac_f32_e32 v78, s4, v48
	v_fmac_f32_e32 v77, s4, v49
	s_waitcnt lgkmcnt(0)
	v_fmac_f32_e32 v75, s5, v80
	v_fmac_f32_e32 v74, s5, v81
	v_readlane_b32 s4, v72, 6
	v_readlane_b32 s5, v72, 22
	s_nop 0
	v_fmac_f32_e32 v70, s4, v48
	v_fmac_f32_e32 v51, s4, v49
	v_fmac_f32_e32 v50, s5, v80
	v_fmac_f32_e32 v69, s5, v81
	v_readlane_b32 s4, v73, 6
	v_readlane_b32 s5, v73, 22
	s_nop 0
	v_fmac_f32_e32 v68, s4, v48
	v_fmac_f32_e32 v55, s4, v49
	v_fmac_f32_e32 v54, s5, v80
	v_fmac_f32_e32 v53, s5, v81
	v_readlane_b32 s4, v76, 6
	v_readlane_b32 s5, v76, 22
	s_nop 0
	v_fmac_f32_e32 v46, s4, v48
	v_fmac_f32_e32 v47, s4, v49
	v_fmac_f32_e32 v44, s5, v80
	v_fmac_f32_e32 v45, s5, v81
	ds_read2st64_b32 v[48:49], v79 offset0:174 offset1:175
	ds_read2st64_b32 v[80:81], v79 offset0:206 offset1:207
	v_readlane_b32 s4, v71, 7
	v_readlane_b32 s5, v71, 23
	s_waitcnt lgkmcnt(1)
	v_fmac_f32_e32 v78, s4, v48
	v_fmac_f32_e32 v77, s4, v49
	s_waitcnt lgkmcnt(0)
; __device__ __forceinline__ float rdlane_f(float v, int l) { return __builtin_bit_cast(float, __builtin_amdgcn_readlane(__builtin_bit_cast(int, v), l)); }
; __device__ __forceinline__ void ph_prep_tok(CArgs& a, int l, LAS unsigned char* lds, int gw, int ngw) {
;     ...
;         for (int i = 0; i < 16; ++i) { const float w0 = wa[i * 128 + lane], w1 = wa[i * 128 + 64 + lane], w2 = wa[2048 + i * 128 + lane], w3 = wa[2048 + i * 128 + 64 + lane];
; #pragma unroll
;             for (int r = 0; r < 4; ++r) { const float af = rdlane_f(av[r], i), ab = rdlane_f(av[r], 16 + i); s[r][0] += af * w0; s[r][1] += af * w1; s[r][2] += ab * w2; s[r][3] += ab * w3; } }
	v_fmac_f32_e32 v75, s5, v80
	v_fmac_f32_e32 v74, s5, v81
	v_readlane_b32 s4, v72, 7
	v_readlane_b32 s5, v72, 23
	s_nop 0
	v_fmac_f32_e32 v70, s4, v48
	v_fmac_f32_e32 v51, s4, v49
	v_fmac_f32_e32 v50, s5, v80
	v_fmac_f32_e32 v69, s5, v81
	v_readlane_b32 s4, v73, 7
	v_readlane_b32 s5, v73, 23
	s_nop 0
	v_fmac_f32_e32 v68, s4, v48
	v_fmac_f32_e32 v55, s4, v49
	v_fmac_f32_e32 v54, s5, v80
	v_fmac_f32_e32 v53, s5, v81
	v_readlane_b32 s4, v76, 7
	v_readlane_b32 s5, v76, 23
	s_nop 0
	v_fmac_f32_e32 v46, s4, v48
	v_fmac_f32_e32 v47, s4, v49
	v_fmac_f32_e32 v44, s5, v80
	v_fmac_f32_e32 v45, s5, v81
	ds_read2st64_b32 v[48:49], v79 offset0:176 offset1:177
	ds_read2st64_b32 v[80:81], v79 offset0:208 offset1:209
	v_readlane_b32 s4, v71, 8
	v_readlane_b32 s5, v71, 24
	s_waitcnt lgkmcnt(1)
	v_fmac_f32_e32 v78, s4, v48
	v_fmac_f32_e32 v77, s4, v49
	s_waitcnt lgkmcnt(0)
	v_fmac_f32_e32 v75, s5, v80
	v_fmac_f32_e32 v74, s5, v81
	v_readlane_b32 s4, v72, 8
	v_readlane_b32 s5, v72, 24
	s_nop 0
	v_fmac_f32_e32 v70, s4, v48
	v_fmac_f32_e32 v51, s4, v49
	v_fmac_f32_e32 v50, s5, v80
	v_fmac_f32_e32 v69, s5, v81
	v_readlane_b32 s4, v73, 8
	v_readlane_b32 s5, v73, 24
	s_nop 0
	v_fmac_f32_e32 v68, s4, v48
	v_fmac_f32_e32 v55, s4, v49
	v_fmac_f32_e32 v54, s5, v80
	v_fmac_f32_e32 v53, s5, v81
	v_readlane_b32 s4, v76, 8
	v_readlane_b32 s5, v76, 24
	s_nop 0
	v_fmac_f32_e32 v46, s4, v48
	v_fmac_f32_e32 v47, s4, v49
	v_fmac_f32_e32 v44, s5, v80
	v_fmac_f32_e32 v45, s5, v81
	ds_read2st64_b32 v[48:49], v79 offset0:178 offset1:179
	ds_read2st64_b32 v[80:81], v79 offset0:210 offset1:211
	v_readlane_b32 s4, v71, 9
	v_readlane_b32 s5, v71, 25
	s_waitcnt lgkmcnt(1)
	v_fmac_f32_e32 v78, s4, v48
	v_fmac_f32_e32 v77, s4, v49
	s_waitcnt lgkmcnt(0)
	v_fmac_f32_e32 v75, s5, v80
	v_fmac_f32_e32 v74, s5, v81
	v_readlane_b32 s4, v72, 9
	v_readlane_b32 s5, v72, 25
	s_nop 0
	v_fmac_f32_e32 v70, s4, v48
	v_fmac_f32_e32 v51, s4, v49
	v_fmac_f32_e32 v50, s5, v80
	v_fmac_f32_e32 v69, s5, v81
	v_readlane_b32 s4, v73, 9
	v_readlane_b32 s5, v73, 25
	s_nop 0
	v_fmac_f32_e32 v68, s4, v48
	v_fmac_f32_e32 v55, s4, v49
	v_fmac_f32_e32 v54, s5, v80
	v_fmac_f32_e32 v53, s5, v81
	v_readlane_b32 s4, v76, 9
	v_readlane_b32 s5, v76, 25
	s_nop 0
	v_fmac_f32_e32 v46, s4, v48
	v_fmac_f32_e32 v47, s4, v49
	v_fmac_f32_e32 v44, s5, v80
	v_fmac_f32_e32 v45, s5, v81
	ds_read2st64_b32 v[48:49], v79 offset0:180 offset1:181
	ds_read2st64_b32 v[80:81], v79 offset0:212 offset1:213
	v_readlane_b32 s4, v71, 10
	v_readlane_b32 s5, v71, 26
	s_waitcnt lgkmcnt(1)
	v_fmac_f32_e32 v78, s4, v48
	v_fmac_f32_e32 v77, s4, v49
	s_waitcnt lgkmcnt(0)
	v_fmac_f32_e32 v75, s5, v80
	v_fmac_f32_e32 v74, s5, v81
	v_readlane_b32 s4, v72, 10
	v_readlane_b32 s5, v72, 26
	s_nop 0
	v_fmac_f32_e32 v70, s4, v48
	v_fmac_f32_e32 v51, s4, v49
	v_fmac_f32_e32 v50, s5, v80
	v_fmac_f32_e32 v69, s5, v81
	v_readlane_b32 s4, v73, 10
	v_readlane_b32 s5, v73, 26
	s_nop 0
	v_fmac_f32_e32 v68, s4, v48
	v_fmac_f32_e32 v55, s4, v49
	v_fmac_f32_e32 v54, s5, v80
	v_fmac_f32_e32 v53, s5, v81
	v_readlane_b32 s4, v76, 10
	v_readlane_b32 s5, v76, 26
	s_nop 0
	v_fmac_f32_e32 v46, s4, v48
	v_fmac_f32_e32 v47, s4, v49
	v_fmac_f32_e32 v44, s5, v80
	v_fmac_f32_e32 v45, s5, v81
	ds_read2st64_b32 v[48:49], v79 offset0:182 offset1:183
	ds_read2st64_b32 v[80:81], v79 offset0:214 offset1:215
	v_readlane_b32 s4, v71, 11
	v_readlane_b32 s5, v71, 27
	s_waitcnt lgkmcnt(1)
	v_fmac_f32_e32 v78, s4, v48
	v_fmac_f32_e32 v77, s4, v49
	s_waitcnt lgkmcnt(0)
	v_fmac_f32_e32 v75, s5, v80
	v_fmac_f32_e32 v74, s5, v81
	v_readlane_b32 s4, v72, 11
	v_readlane_b32 s5, v72, 27
	s_nop 0
	v_fmac_f32_e32 v70, s4, v48
	v_fmac_f32_e32 v51, s4, v49
	v_fmac_f32_e32 v50, s5, v80
	v_fmac_f32_e32 v69, s5, v81
	v_readlane_b32 s4, v73, 11
	v_readlane_b32 s5, v73, 27
	s_nop 0
	v_fmac_f32_e32 v68, s4, v48
	v_fmac_f32_e32 v55, s4, v49
	v_fmac_f32_e32 v54, s5, v80
	v_fmac_f32_e32 v53, s5, v81
	v_readlane_b32 s4, v76, 11
	v_readlane_b32 s5, v76, 27
	s_nop 0
	v_fmac_f32_e32 v46, s4, v48
	v_fmac_f32_e32 v47, s4, v49
	v_fmac_f32_e32 v44, s5, v80
	v_fmac_f32_e32 v45, s5, v81
	ds_read2st64_b32 v[48:49], v79 offset0:184 offset1:185
	ds_read2st64_b32 v[80:81], v79 offset0:216 offset1:217
	v_readlane_b32 s4, v71, 12
	v_readlane_b32 s5, v71, 28
	s_waitcnt lgkmcnt(1)
	v_fmac_f32_e32 v78, s4, v48
	v_fmac_f32_e32 v77, s4, v49
	s_waitcnt lgkmcnt(0)
	v_fmac_f32_e32 v75, s5, v80
	v_fmac_f32_e32 v74, s5, v81
	v_readlane_b32 s4, v72, 12
	v_readlane_b32 s5, v72, 28
	s_nop 0
	v_fmac_f32_e32 v70, s4, v48
	v_fmac_f32_e32 v51, s4, v49
	v_fmac_f32_e32 v50, s5, v80
	v_fmac_f32_e32 v69, s5, v81
	v_readlane_b32 s4, v73, 12
	v_readlane_b32 s5, v73, 28
	s_nop 0
	v_fmac_f32_e32 v68, s4, v48
	v_fmac_f32_e32 v55, s4, v49
	v_fmac_f32_e32 v54, s5, v80
	v_fmac_f32_e32 v53, s5, v81
	v_readlane_b32 s4, v76, 12
	v_readlane_b32 s5, v76, 28
	s_nop 0
	v_fmac_f32_e32 v46, s4, v48
	v_fmac_f32_e32 v47, s4, v49
	v_fmac_f32_e32 v44, s5, v80
	v_fmac_f32_e32 v45, s5, v81
	ds_read2st64_b32 v[48:49], v79 offset0:186 offset1:187
	ds_read2st64_b32 v[80:81], v79 offset0:218 offset1:219
	v_readlane_b32 s4, v71, 13
	v_readlane_b32 s5, v71, 29
	s_waitcnt lgkmcnt(1)
	v_fmac_f32_e32 v78, s4, v48
	v_fmac_f32_e32 v77, s4, v49
	s_waitcnt lgkmcnt(0)
	v_fmac_f32_e32 v75, s5, v80
	v_fmac_f32_e32 v74, s5, v81
	v_readlane_b32 s4, v72, 13
	v_readlane_b32 s5, v72, 29
	s_nop 0
	v_fmac_f32_e32 v70, s4, v48
	v_fmac_f32_e32 v51, s4, v49
	v_fmac_f32_e32 v50, s5, v80
	v_fmac_f32_e32 v69, s5, v81
	v_readlane_b32 s4, v73, 13
	v_readlane_b32 s5, v73, 29
	s_nop 0
	v_fmac_f32_e32 v68, s4, v48
	v_fmac_f32_e32 v55, s4, v49
	v_fmac_f32_e32 v54, s5, v80
	v_fmac_f32_e32 v53, s5, v81
	v_readlane_b32 s4, v76, 13
	v_readlane_b32 s5, v76, 29
	s_nop 0
	v_fmac_f32_e32 v46, s4, v48
	v_fmac_f32_e32 v47, s4, v49
	v_fmac_f32_e32 v44, s5, v80
	v_fmac_f32_e32 v45, s5, v81
	ds_read2st64_b32 v[48:49], v79 offset0:188 offset1:189
	ds_read2st64_b32 v[80:81], v79 offset0:220 offset1:221
	v_readlane_b32 s4, v71, 14
	v_readlane_b32 s5, v71, 30
	s_waitcnt lgkmcnt(1)
; __device__ __forceinline__ unsigned f2bf(float f) { unsigned u = __float_as_uint(f); return (u + 0x7fffu + ((u >> 16) & 1u)) >> 16; }
; __device__ __forceinline__ float logsigmoidf_(float x) { return fminf(x, 0.f) - __logf(1.f + __expf(-fabsf(x))); }
; __device__ __forceinline__ float rdlane_f(float v, int l) { return __builtin_bit_cast(float, __builtin_amdgcn_readlane(__builtin_bit_cast(int, v), l)); }
; __device__ __forceinline__ void ph_prep_tok(CArgs& a, int l, LAS unsigned char* lds, int gw, int ngw) {
;     ...
;             for (int r = 0; r < 4; ++r) { const float af = rdlane_f(av[r], i), ab = rdlane_f(av[r], 16 + i); s[r][0] += af * w0; s[r][1] += af * w1; s[r][2] += ab * w2; s[r][3] += ab * w3; } }
; #pragma unroll
;         for (int r = 0; r < 4; ++r) { const size_t o = (size_t)(row0 + r) * 128;
;             ((bf16*)GDF)[o + lane] = (bf16)f2bf(logsigmoidf_(s[r][0]) * 0.0625f); ((bf16*)GDF)[o + 64 + lane] = (bf16)f2bf(logsigmoidf_(s[r][1]) * 0.0625f);
;             ((bf16*)GDB)[o + lane] = (bf16)f2bf(logsigmoidf_(s[r][2]) * 0.0625f); ((bf16*)GDB)[o + 64 + lane] = (bf16)f2bf(logsigmoidf_(s[r][3]) * 0.0625f); }
	v_fmac_f32_e32 v78, s4, v48
	v_fmac_f32_e32 v77, s4, v49
	s_waitcnt lgkmcnt(0)
	v_fmac_f32_e32 v75, s5, v80
	v_fmac_f32_e32 v74, s5, v81
	v_readlane_b32 s4, v72, 14
	v_readlane_b32 s5, v72, 30
	s_nop 0
	v_fmac_f32_e32 v70, s4, v48
	v_fmac_f32_e32 v51, s4, v49
	v_fmac_f32_e32 v50, s5, v80
	v_fmac_f32_e32 v69, s5, v81
	v_readlane_b32 s4, v73, 14
	v_readlane_b32 s5, v73, 30
	s_nop 0
	v_fmac_f32_e32 v68, s4, v48
	v_fmac_f32_e32 v55, s4, v49
	v_fmac_f32_e32 v54, s5, v80
	v_fmac_f32_e32 v53, s5, v81
	v_readlane_b32 s4, v76, 14
	v_readlane_b32 s5, v76, 30
	s_nop 0
	v_fmac_f32_e32 v46, s4, v48
	v_fmac_f32_e32 v47, s4, v49
	v_fmac_f32_e32 v44, s5, v80
	v_fmac_f32_e32 v45, s5, v81
	ds_read2st64_b32 v[48:49], v79 offset0:190 offset1:191
	ds_read2st64_b32 v[80:81], v79 offset0:222 offset1:223
	v_readlane_b32 s4, v71, 15
	v_readlane_b32 s5, v71, 31
	s_waitcnt lgkmcnt(1)
	v_fmac_f32_e32 v78, s4, v48
	v_fmac_f32_e32 v77, s4, v49
	v_readlane_b32 s4, v72, 15
	s_waitcnt lgkmcnt(0)
	v_fmac_f32_e32 v75, s5, v80
	v_fmac_f32_e32 v74, s5, v81
	v_fmac_f32_e32 v70, s4, v48
	v_fmac_f32_e32 v51, s4, v49
	v_readlane_b32 s4, v73, 15
	v_readlane_b32 s5, v72, 31
	s_nop 0
	v_fmac_f32_e32 v68, s4, v48
	v_fmac_f32_e32 v55, s4, v49
	v_readlane_b32 s4, v76, 15
	v_fmac_f32_e32 v50, s5, v80
	v_fmac_f32_e32 v69, s5, v81
	v_fmac_f32_e32 v46, s4, v48
	v_fmac_f32_e32 v47, s4, v49
	s_mov_b32 s4, 0xbfb8aa3b
	v_mul_f32_e64 v49, |v78|, s4
	v_exp_f32_e32 v49, v49
	v_readlane_b32 s5, v73, 31
	v_min_f32_e32 v48, 0, v78
	v_add_f32_e32 v49, 1.0, v49
	v_cmp_gt_f32_e32 vcc, s21, v49
	v_fmac_f32_e32 v54, s5, v80
	v_fmac_f32_e32 v53, s5, v81
	v_cndmask_b32_e64 v71, 0, 32, vcc
	v_ldexp_f32 v49, v49, v71
	v_log_f32_e32 v49, v49
	v_readlane_b32 s5, v76, 31
	v_mul_f32_e64 v76, |v77|, s4
	v_exp_f32_e32 v76, v76
	v_fmac_f32_e32 v44, s5, v80
	v_fmac_f32_e32 v45, s5, v81
	v_mul_f32_e32 v71, 0x3f317217, v49
	s_mov_b32 s5, 0x3f317217
	v_fma_f32 v71, v49, s5, -v71
	v_fmac_f32_e32 v71, 0x3377d1cf, v49
	v_fmac_f32_e32 v71, 0x3f317217, v49
	v_cmp_lt_f32_e64 s[40:41], |v49|, s6
	v_add_f32_e32 v76, 1.0, v76
	s_nop 0
	v_cndmask_b32_e64 v49, v49, v71, s[40:41]
	v_cndmask_b32_e32 v71, 0, v193, vcc
	v_sub_f32_e32 v49, v49, v71
	v_sub_f32_e32 v48, v48, v49
	v_mul_f32_e32 v48, 0x3d800000, v48
	v_cvt_pk_bf16_f32 v71, v48, v48
	v_lshl_add_u64 v[48:49], s[2:3], 0, v[22:23]
	v_add_co_u32_e32 v72, vcc, s7, v48
	s_nop 1
	v_addc_co_u32_e32 v73, vcc, 0, v49, vcc
	v_cmp_gt_f32_e32 vcc, s21, v76
	global_store_short v[72:73], v71, off
	v_min_f32_e32 v71, 0, v77
	v_cndmask_b32_e64 v77, 0, 32, vcc
	v_ldexp_f32 v76, v76, v77
	v_log_f32_e32 v76, v76
	s_nop 0
	v_mul_f32_e32 v77, 0x3f317217, v76
	v_fma_f32 v77, v76, s5, -v77
	v_fmac_f32_e32 v77, 0x3377d1cf, v76
	v_fmac_f32_e32 v77, 0x3f317217, v76
	v_cmp_lt_f32_e64 s[40:41], |v76|, s6
	s_nop 1
	v_cndmask_b32_e64 v76, v76, v77, s[40:41]
	v_cndmask_b32_e32 v77, 0, v193, vcc
	v_sub_f32_e32 v76, v76, v77
	v_sub_f32_e32 v71, v71, v76
	v_mul_f32_e32 v71, 0x3d800000, v71
	v_cvt_pk_bf16_f32 v71, v71, v71
	global_store_short v[72:73], v71, off offset:128
	v_mul_f32_e64 v72, |v75|, s4
	v_exp_f32_e32 v72, v72
	v_min_f32_e32 v71, 0, v75
	v_add_f32_e32 v72, 1.0, v72
	v_cmp_gt_f32_e32 vcc, s21, v72
	s_nop 1
	v_cndmask_b32_e64 v73, 0, 32, vcc
	v_ldexp_f32 v72, v72, v73
	v_log_f32_e32 v72, v72
	s_nop 0
	v_mul_f32_e32 v73, 0x3f317217, v72
	v_fma_f32 v73, v72, s5, -v73
	v_fmac_f32_e32 v73, 0x3377d1cf, v72
	v_fmac_f32_e32 v73, 0x3f317217, v72
	v_cmp_lt_f32_e64 s[40:41], |v72|, s6
	s_nop 1
	v_cndmask_b32_e64 v72, v72, v73, s[40:41]
	v_cndmask_b32_e32 v73, 0, v193, vcc
	v_sub_f32_e32 v72, v72, v73
	v_sub_f32_e32 v71, v71, v72
	v_mul_f32_e32 v71, 0x3d800000, v71
	v_cvt_pk_bf16_f32 v71, v71, v71
	v_mul_f32_e64 v72, |v74|, s4
	v_exp_f32_e32 v72, v72
	v_add_co_u32_e32 v48, vcc, s11, v48
	v_add_f32_e32 v72, 1.0, v72
	s_nop 0
	v_addc_co_u32_e32 v49, vcc, 0, v49, vcc
	v_cmp_gt_f32_e32 vcc, s21, v72
	global_store_short v[48:49], v71, off
	v_min_f32_e32 v71, 0, v74
	v_cndmask_b32_e64 v73, 0, 32, vcc
	v_ldexp_f32 v72, v72, v73
	v_log_f32_e32 v72, v72
	s_nop 0
	v_mul_f32_e32 v73, 0x3f317217, v72
	v_fma_f32 v73, v72, s5, -v73
	v_fmac_f32_e32 v73, 0x3377d1cf, v72
	v_fmac_f32_e32 v73, 0x3f317217, v72
	v_cmp_lt_f32_e64 s[40:41], |v72|, s6
	s_nop 1
	v_cndmask_b32_e64 v72, v72, v73, s[40:41]
	v_cndmask_b32_e32 v73, 0, v193, vcc
	v_sub_f32_e32 v72, v72, v73
	v_sub_f32_e32 v71, v71, v72
	v_mul_f32_e32 v71, 0x3d800000, v71
	v_cvt_pk_bf16_f32 v71, v71, v71
	global_store_short v[48:49], v71, off offset:128
	v_mul_f32_e64 v49, |v70|, s4
	v_exp_f32_e32 v49, v49
	v_min_f32_e32 v48, 0, v70
	v_add_f32_e32 v49, 1.0, v49
	v_cmp_gt_f32_e32 vcc, s21, v49
	s_nop 1
	v_cndmask_b32_e64 v70, 0, 32, vcc
	v_ldexp_f32 v49, v49, v70
	v_log_f32_e32 v49, v49
	s_nop 0
	v_mul_f32_e32 v70, 0x3f317217, v49
	v_fma_f32 v70, v49, s5, -v70
	v_fmac_f32_e32 v70, 0x3377d1cf, v49
	v_fmac_f32_e32 v70, 0x3f317217, v49
	v_cmp_lt_f32_e64 s[40:41], |v49|, s6
	s_nop 1
	v_cndmask_b32_e64 v49, v49, v70, s[40:41]
	v_cndmask_b32_e32 v70, 0, v193, vcc
	v_sub_f32_e32 v49, v49, v70
	v_sub_f32_e32 v48, v48, v49
	v_mul_f32_e32 v48, 0x3d800000, v48
	v_lshl_add_u64 v[70:71], s[2:3], 0, v[18:19]
	v_cvt_pk_bf16_f32 v72, v48, v48
	v_add_co_u32_e32 v48, vcc, s7, v70
	s_nop 1
	v_addc_co_u32_e32 v49, vcc, 0, v71, vcc
	global_store_short v[48:49], v72, off offset:256
	v_min_f32_e32 v72, 0, v51
	v_mul_f32_e64 v51, |v51|, s4
	v_exp_f32_e32 v51, v51
	s_nop 0
	v_add_f32_e32 v51, 1.0, v51
	v_cmp_gt_f32_e32 vcc, s21, v51
	s_nop 1
	v_cndmask_b32_e64 v73, 0, 32, vcc
	v_ldexp_f32 v51, v51, v73
	v_log_f32_e32 v51, v51
	s_nop 0
	v_mul_f32_e32 v73, 0x3f317217, v51
	v_fma_f32 v73, v51, s5, -v73
; __device__ __forceinline__ unsigned f2bf(float f) { unsigned u = __float_as_uint(f); return (u + 0x7fffu + ((u >> 16) & 1u)) >> 16; }
; __device__ __forceinline__ float logsigmoidf_(float x) { return fminf(x, 0.f) - __logf(1.f + __expf(-fabsf(x))); }
; __device__ __forceinline__ void ph_prep_tok(CArgs& a, int l, LAS unsigned char* lds, int gw, int ngw) {
;     ...
;         for (int r = 0; r < 4; ++r) { const size_t o = (size_t)(row0 + r) * 128;
;             ((bf16*)GDF)[o + lane] = (bf16)f2bf(logsigmoidf_(s[r][0]) * 0.0625f); ((bf16*)GDF)[o + 64 + lane] = (bf16)f2bf(logsigmoidf_(s[r][1]) * 0.0625f);
;             ((bf16*)GDB)[o + lane] = (bf16)f2bf(logsigmoidf_(s[r][2]) * 0.0625f); ((bf16*)GDB)[o + 64 + lane] = (bf16)f2bf(logsigmoidf_(s[r][3]) * 0.0625f); }
	v_fmac_f32_e32 v73, 0x3377d1cf, v51
	v_fmac_f32_e32 v73, 0x3f317217, v51
	v_cmp_lt_f32_e64 s[40:41], |v51|, s6
	s_nop 1
	v_cndmask_b32_e64 v51, v51, v73, s[40:41]
	v_cndmask_b32_e32 v73, 0, v193, vcc
	v_sub_f32_e32 v51, v51, v73
	v_sub_f32_e32 v51, v72, v51
	v_mul_f32_e32 v51, 0x3d800000, v51
	v_cvt_pk_bf16_f32 v51, v51, v51
	global_store_short v[48:49], v51, off offset:384
	v_min_f32_e32 v51, 0, v50
	v_mul_f32_e64 v50, |v50|, s4
	v_exp_f32_e32 v50, v50
	s_nop 0
	v_add_f32_e32 v50, 1.0, v50
	v_cmp_gt_f32_e32 vcc, s21, v50
	s_nop 1
	v_cndmask_b32_e64 v72, 0, 32, vcc
	v_ldexp_f32 v50, v50, v72
	v_log_f32_e32 v50, v50
	s_nop 0
	v_mul_f32_e32 v72, 0x3f317217, v50
	v_fma_f32 v72, v50, s5, -v72
	v_fmac_f32_e32 v72, 0x3377d1cf, v50
	v_fmac_f32_e32 v72, 0x3f317217, v50
	v_cmp_lt_f32_e64 s[40:41], |v50|, s6
	s_nop 1
	v_cndmask_b32_e64 v50, v50, v72, s[40:41]
	v_cndmask_b32_e32 v72, 0, v193, vcc
	v_sub_f32_e32 v50, v50, v72
	v_sub_f32_e32 v50, v51, v50
	v_mul_f32_e32 v50, 0x3d800000, v50
	v_cvt_pk_bf16_f32 v72, v50, v50
	v_add_co_u32_e32 v50, vcc, s11, v70
	v_min_f32_e32 v70, 0, v69
	v_mul_f32_e64 v69, |v69|, s4
	v_exp_f32_e32 v69, v69
	v_addc_co_u32_e32 v51, vcc, 0, v71, vcc
	global_store_short v[50:51], v72, off offset:256
	v_add_f32_e32 v69, 1.0, v69
	v_cmp_gt_f32_e32 vcc, s21, v69
	s_nop 1
	v_cndmask_b32_e64 v71, 0, 32, vcc
	v_ldexp_f32 v69, v69, v71
	v_log_f32_e32 v69, v69
	s_nop 0
	v_mul_f32_e32 v71, 0x3f317217, v69
	v_fma_f32 v71, v69, s5, -v71
	v_fmac_f32_e32 v71, 0x3377d1cf, v69
	v_fmac_f32_e32 v71, 0x3f317217, v69
	v_cmp_lt_f32_e64 s[40:41], |v69|, s6
	s_nop 1
	v_cndmask_b32_e64 v69, v69, v71, s[40:41]
	v_cndmask_b32_e32 v71, 0, v193, vcc
	v_sub_f32_e32 v69, v69, v71
	v_sub_f32_e32 v69, v70, v69
	v_mul_f32_e32 v69, 0x3d800000, v69
	v_cvt_pk_bf16_f32 v69, v69, v69
	global_store_short v[50:51], v69, off offset:384
	v_min_f32_e32 v69, 0, v68
	v_mul_f32_e64 v68, |v68|, s4
	v_exp_f32_e32 v68, v68
	s_nop 0
	v_add_f32_e32 v68, 1.0, v68
	v_cmp_gt_f32_e32 vcc, s21, v68
	s_nop 1
	v_cndmask_b32_e64 v70, 0, 32, vcc
	v_ldexp_f32 v68, v68, v70
	v_log_f32_e32 v68, v68
	s_nop 0
	v_mul_f32_e32 v70, 0x3f317217, v68
	v_fma_f32 v70, v68, s5, -v70
	v_fmac_f32_e32 v70, 0x3377d1cf, v68
	v_fmac_f32_e32 v70, 0x3f317217, v68
	v_cmp_lt_f32_e64 s[40:41], |v68|, s6
	s_nop 1
	v_cndmask_b32_e64 v68, v68, v70, s[40:41]
	v_cndmask_b32_e32 v70, 0, v193, vcc
	v_sub_f32_e32 v68, v68, v70
	v_sub_f32_e32 v68, v69, v68
	v_mul_f32_e32 v68, 0x3d800000, v68
	v_cvt_pk_bf16_f32 v68, v68, v68
	global_store_short v[48:49], v68, off offset:512
	v_min_f32_e32 v68, 0, v55
	v_mul_f32_e64 v55, |v55|, s4
	v_exp_f32_e32 v55, v55
	s_nop 0
	v_add_f32_e32 v55, 1.0, v55
	v_cmp_gt_f32_e32 vcc, s21, v55
	s_nop 1
	v_cndmask_b32_e64 v69, 0, 32, vcc
	v_ldexp_f32 v55, v55, v69
	v_log_f32_e32 v55, v55
	s_nop 0
	v_mul_f32_e32 v69, 0x3f317217, v55
	v_fma_f32 v69, v55, s5, -v69
	v_fmac_f32_e32 v69, 0x3377d1cf, v55
	v_fmac_f32_e32 v69, 0x3f317217, v55
	v_cmp_lt_f32_e64 s[40:41], |v55|, s6
	s_nop 1
	v_cndmask_b32_e64 v55, v55, v69, s[40:41]
	v_cndmask_b32_e32 v69, 0, v193, vcc
	v_sub_f32_e32 v55, v55, v69
	v_sub_f32_e32 v55, v68, v55
	v_mul_f32_e32 v55, 0x3d800000, v55
	v_cvt_pk_bf16_f32 v55, v55, v55
	global_store_short v[48:49], v55, off offset:640
	v_min_f32_e32 v55, 0, v54
	v_mul_f32_e64 v54, |v54|, s4
	v_exp_f32_e32 v54, v54
	s_nop 0
	v_add_f32_e32 v54, 1.0, v54
	v_cmp_gt_f32_e32 vcc, s21, v54
	s_nop 1
	v_cndmask_b32_e64 v68, 0, 32, vcc
	v_ldexp_f32 v54, v54, v68
	v_log_f32_e32 v54, v54
	s_nop 0
	v_mul_f32_e32 v68, 0x3f317217, v54
	v_fma_f32 v68, v54, s5, -v68
	v_fmac_f32_e32 v68, 0x3377d1cf, v54
	v_fmac_f32_e32 v68, 0x3f317217, v54
	v_cmp_lt_f32_e64 s[40:41], |v54|, s6
	s_nop 1
	v_cndmask_b32_e64 v54, v54, v68, s[40:41]
	v_cndmask_b32_e32 v68, 0, v193, vcc
	v_sub_f32_e32 v54, v54, v68
	v_sub_f32_e32 v54, v55, v54
	v_mul_f32_e32 v54, 0x3d800000, v54
	v_cvt_pk_bf16_f32 v54, v54, v54
	global_store_short v[50:51], v54, off offset:512
	v_min_f32_e32 v54, 0, v53
	v_mul_f32_e64 v53, |v53|, s4
	v_exp_f32_e32 v53, v53
	s_nop 0
	v_add_f32_e32 v53, 1.0, v53
	v_cmp_gt_f32_e32 vcc, s21, v53
	s_nop 1
	v_cndmask_b32_e64 v55, 0, 32, vcc
	v_ldexp_f32 v53, v53, v55
	v_log_f32_e32 v53, v53
	s_nop 0
	v_mul_f32_e32 v55, 0x3f317217, v53
	v_fma_f32 v55, v53, s5, -v55
	v_fmac_f32_e32 v55, 0x3377d1cf, v53
	v_fmac_f32_e32 v55, 0x3f317217, v53
	v_cmp_lt_f32_e64 s[40:41], |v53|, s6
	s_nop 1
	v_cndmask_b32_e64 v53, v53, v55, s[40:41]
	v_cndmask_b32_e32 v55, 0, v193, vcc
	v_sub_f32_e32 v53, v53, v55
	v_sub_f32_e32 v53, v54, v53
	v_mul_f32_e32 v53, 0x3d800000, v53
	v_cvt_pk_bf16_f32 v53, v53, v53
	global_store_short v[50:51], v53, off offset:640
	v_min_f32_e32 v53, 0, v46
	v_mul_f32_e64 v46, |v46|, s4
	v_exp_f32_e32 v46, v46
	s_nop 0
	v_add_f32_e32 v46, 1.0, v46
	v_cmp_gt_f32_e32 vcc, s21, v46
	s_nop 1
	v_cndmask_b32_e64 v54, 0, 32, vcc
	v_ldexp_f32 v46, v46, v54
	v_log_f32_e32 v46, v46
	s_nop 0
	v_mul_f32_e32 v54, 0x3f317217, v46
	v_fma_f32 v54, v46, s5, -v54
	v_fmac_f32_e32 v54, 0x3377d1cf, v46
	v_fmac_f32_e32 v54, 0x3f317217, v46
	v_cmp_lt_f32_e64 s[40:41], |v46|, s6
	s_nop 1
	v_cndmask_b32_e64 v46, v46, v54, s[40:41]
	v_cndmask_b32_e32 v54, 0, v193, vcc
	v_sub_f32_e32 v46, v46, v54
	v_sub_f32_e32 v46, v53, v46
	v_mul_f32_e32 v46, 0x3d800000, v46
	v_cvt_pk_bf16_f32 v46, v46, v46
	global_store_short v[48:49], v46, off offset:768
	v_min_f32_e32 v46, 0, v47
	v_mul_f32_e64 v47, |v47|, s4
	v_exp_f32_e32 v47, v47
	s_nop 0
	v_add_f32_e32 v47, 1.0, v47
	v_cmp_gt_f32_e32 vcc, s21, v47
	s_nop 1
	v_cndmask_b32_e64 v53, 0, 32, vcc
	v_ldexp_f32 v47, v47, v53
	v_log_f32_e32 v47, v47
	s_nop 0
	v_mul_f32_e32 v53, 0x3f317217, v47
; #define LAS __attribute__((address_space(3)))
; __device__ __forceinline__ unsigned f2bf(float f) { unsigned u = __float_as_uint(f); return (u + 0x7fffu + ((u >> 16) & 1u)) >> 16; }
; __device__ __forceinline__ float logsigmoidf_(float x) { return fminf(x, 0.f) - __logf(1.f + __expf(-fabsf(x))); }
; __device__ __forceinline__ f32x4 bf4(u32x2 v) { return (f32x4){lo_bf(v.x), hi_bf(v.x), lo_bf(v.y), hi_bf(v.y)}; }
; __device__ __forceinline__ void ph_prep_tok(CArgs& a, int l, LAS unsigned char* lds, int gw, int ngw) {
;     ...
;         for (int r = 0; r < 4; ++r) { const size_t o = (size_t)(row0 + r) * 128;
;             ((bf16*)GDF)[o + lane] = (bf16)f2bf(logsigmoidf_(s[r][0]) * 0.0625f); ((bf16*)GDF)[o + 64 + lane] = (bf16)f2bf(logsigmoidf_(s[r][1]) * 0.0625f);
;             ((bf16*)GDB)[o + lane] = (bf16)f2bf(logsigmoidf_(s[r][2]) * 0.0625f); ((bf16*)GDB)[o + 64 + lane] = (bf16)f2bf(logsigmoidf_(s[r][3]) * 0.0625f); }
;         float sq[4] = {0.f, 0.f, 0.f, 0.f}, sk[4] = {0.f, 0.f, 0.f, 0.f}; f32x4 qv[4], kv[4];
; #pragma unroll
;         for (int g = 0; g < 3; ++g) { const int col = g * 256 + 4 * lane;
;             f32x4 x[6];
; #pragma unroll
;             for (int r = 0; r < 6; ++r) { const int t = tpos + r - 1; x[r] = (t >= lo && t < hi) ? bf4(xr[g][r]) : (f32x4){0.f, 0.f, 0.f, 0.f}; }
;             const f32x4 w0 = *(const LAS f32x4*)(cw + col), w1 = *(const LAS f32x4*)(cw + 768 + col), w2 = *(const LAS f32x4*)(cw + 1536 + col);
; #pragma unroll
;             for (int r = 0; r < 4; ++r) { f32x4 y = w0 * x[r] + w1 * x[r + 1] + w2 * x[r + 2];
	v_fma_f32 v53, v47, s5, -v53
	v_fmac_f32_e32 v53, 0x3377d1cf, v47
	v_fmac_f32_e32 v53, 0x3f317217, v47
	v_cmp_lt_f32_e64 s[40:41], |v47|, s6
	s_nop 1
	v_cndmask_b32_e64 v47, v47, v53, s[40:41]
	v_cndmask_b32_e32 v53, 0, v193, vcc
	v_sub_f32_e32 v47, v47, v53
	v_sub_f32_e32 v46, v46, v47
	v_mul_f32_e32 v46, 0x3d800000, v46
	v_cvt_pk_bf16_f32 v46, v46, v46
	global_store_short v[48:49], v46, off offset:896
	v_min_f32_e32 v46, 0, v44
	v_mul_f32_e64 v44, |v44|, s4
	v_exp_f32_e32 v44, v44
	v_and_b32_e32 v48, 0xffff0000, v39
	v_add_f32_e32 v44, 1.0, v44
	v_cmp_gt_f32_e32 vcc, s21, v44
	s_nop 1
	v_cndmask_b32_e64 v47, 0, 32, vcc
	v_ldexp_f32 v44, v44, v47
	v_log_f32_e32 v44, v44
	s_nop 0
	v_mul_f32_e32 v47, 0x3f317217, v44
	v_fma_f32 v47, v44, s5, -v47
	v_fmac_f32_e32 v47, 0x3377d1cf, v44
	v_fmac_f32_e32 v47, 0x3f317217, v44
	v_cmp_lt_f32_e64 s[40:41], |v44|, s6
	s_nop 1
	v_cndmask_b32_e64 v44, v44, v47, s[40:41]
	v_cndmask_b32_e32 v47, 0, v193, vcc
	v_sub_f32_e32 v44, v44, v47
	v_sub_f32_e32 v44, v46, v44
	v_mul_f32_e32 v44, 0x3d800000, v44
	v_cvt_pk_bf16_f32 v44, v44, v44
	global_store_short v[50:51], v44, off offset:768
	v_min_f32_e32 v44, 0, v45
	v_mul_f32_e64 v45, |v45|, s4
	v_exp_f32_e32 v45, v45
	v_lshlrev_b32_e32 v47, 16, v39
	v_add_f32_e32 v45, 1.0, v45
	v_cmp_gt_f32_e32 vcc, s21, v45
	s_nop 1
	v_cndmask_b32_e64 v46, 0, 32, vcc
	v_ldexp_f32 v45, v45, v46
	v_log_f32_e32 v45, v45
	s_nop 0
	v_mul_f32_e32 v46, 0x3f317217, v45
	v_fma_f32 v46, v45, s5, -v46
	s_cselect_b64 s[4:5], -1, 0
	s_cmp_gt_u32 s9, s1
	v_cmp_lt_f32_e64 s[40:41], |v45|, s6
	s_cselect_b64 s[6:7], -1, 0
	v_fmac_f32_e32 v46, 0x3377d1cf, v45
	s_or_b64 s[6:7], s[4:5], s[6:7]
	v_fmac_f32_e32 v46, 0x3f317217, v45
	s_cmp_lt_u32 s9, s8
	v_cndmask_b32_e64 v45, v45, v46, s[40:41]
	v_cndmask_b32_e32 v46, 0, v193, vcc
	s_cselect_b64 s[4:5], -1, 0
	s_cmp_ge_u32 s9, s1
	v_sub_f32_e32 v45, v45, v46
	s_cselect_b64 s[14:15], -1, 0
	v_sub_f32_e32 v44, v44, v45
	s_or_b64 s[4:5], s[4:5], s[14:15]
	v_mul_f32_e32 v44, 0x3d800000, v44
	s_cmp_le_u32 s10, s8
	s_cselect_b64 s[14:15], -1, 0
	s_cmp_gt_u32 s10, s1
	v_cvt_pk_bf16_f32 v44, v44, v44
	s_cselect_b64 s[10:11], -1, 0
	global_store_short v[50:51], v44, off offset:896
	v_lshlrev_b32_e32 v46, 16, v38
	v_and_b32_e32 v38, 0xffff0000, v38
	s_or_b64 s[14:15], s[14:15], s[10:11]
	s_add_i32 s10, s9, 5
	v_cndmask_b32_e64 v39, v38, 0, s[4:5]
	v_cndmask_b32_e64 v38, v46, 0, s[4:5]
	v_lshlrev_b32_e32 v46, 16, v42
	v_and_b32_e32 v42, 0xffff0000, v42
	s_cmp_le_u32 s10, s8
	ds_read_b128 v[74:77], v117 offset:58368
	ds_read_b128 v[78:81], v117 offset:61440
	ds_read_b128 v[82:85], v117 offset:64512
	v_cndmask_b32_e64 v49, v48, 0, s[4:5]
	v_cndmask_b32_e64 v48, v47, 0, s[4:5]
	v_lshlrev_b32_e32 v47, 16, v43
	v_and_b32_e32 v43, 0xffff0000, v43
	v_cndmask_b32_e64 v87, v42, 0, s[4:5]
	v_cndmask_b32_e64 v86, v46, 0, s[4:5]
	v_lshlrev_b32_e32 v42, 16, v32
	v_and_b32_e32 v32, 0xffff0000, v32
	v_lshlrev_b32_e32 v46, 16, v33
	s_cselect_b64 s[8:9], -1, 0
	s_cmp_gt_u32 s10, s1
	v_cndmask_b32_e64 v89, v43, 0, s[4:5]
	v_and_b32_e32 v43, 0xffff0000, v33
	v_cndmask_b32_e64 v33, v32, 0, s[14:15]
	v_cndmask_b32_e64 v32, v42, 0, s[14:15]
	v_cndmask_b32_e64 v42, v46, 0, s[14:15]
	v_lshlrev_b32_e32 v46, 16, v36
	s_cselect_b64 s[10:11], -1, 0
	v_lshlrev_b32_e32 v44, 16, v40
	v_and_b32_e32 v45, 0xffff0000, v40
	v_cndmask_b32_e64 v88, v47, 0, s[4:5]
	v_and_b32_e32 v36, 0xffff0000, v36
	v_lshlrev_b32_e32 v47, 16, v37
	v_and_b32_e32 v37, 0xffff0000, v37
	v_cndmask_b32_e64 v68, v46, 0, s[4:5]
	s_or_b64 s[26:27], s[8:9], s[10:11]
	v_and_b32_e32 v46, 0xffff0000, v31
	v_lshlrev_b32_e32 v40, 16, v41
	v_and_b32_e32 v41, 0xffff0000, v41
	v_cndmask_b32_e64 v45, v45, 0, s[6:7]
	v_cndmask_b32_e64 v44, v44, 0, s[6:7]
	v_cndmask_b32_e64 v69, v36, 0, s[4:5]
	v_cndmask_b32_e64 v71, v37, 0, s[4:5]
	v_cndmask_b32_e64 v70, v47, 0, s[4:5]
	v_lshlrev_b32_e32 v36, 16, v30
	v_and_b32_e32 v30, 0xffff0000, v30
	v_lshlrev_b32_e32 v37, 16, v31
	v_cndmask_b32_e64 v73, v46, 0, s[26:27]
	s_waitcnt lgkmcnt(1)
	v_pk_mul_f32 v[46:47], v[38:39], v[78:79]
	v_cndmask_b32_e64 v41, v41, 0, s[6:7]
	v_cndmask_b32_e64 v40, v40, 0, s[6:7]
	v_cndmask_b32_e64 v31, v30, 0, s[26:27]
	v_cndmask_b32_e64 v30, v36, 0, s[26:27]
	v_cndmask_b32_e64 v72, v37, 0, s[26:27]
	v_pk_mul_f32 v[36:37], v[48:49], v[80:81]
	v_pk_fma_f32 v[44:45], v[44:45], v[74:75], v[46:47]
	v_pk_fma_f32 v[36:37], v[40:41], v[76:77], v[36:37]
	s_waitcnt lgkmcnt(0)
; #define LAS __attribute__((address_space(3)))
; __device__ __forceinline__ float siluf_(float x) { return x / (1.f + __expf(-x)); }
; __device__ __forceinline__ f32x4 bf4(u32x2 v) { return (f32x4){lo_bf(v.x), hi_bf(v.x), lo_bf(v.y), hi_bf(v.y)}; }
; __device__ __forceinline__ void ph_prep_tok(CArgs& a, int l, LAS unsigned char* lds, int gw, int ngw) {
;     ...
;         for (int g = 0; g < 3; ++g) { const int col = g * 256 + 4 * lane;
;             f32x4 x[6];
; #pragma unroll
;             for (int r = 0; r < 6; ++r) { const int t = tpos + r - 1; x[r] = (t >= lo && t < hi) ? bf4(xr[g][r]) : (f32x4){0.f, 0.f, 0.f, 0.f}; }
;             const f32x4 w0 = *(const LAS f32x4*)(cw + col), w1 = *(const LAS f32x4*)(cw + 768 + col), w2 = *(const LAS f32x4*)(cw + 1536 + col);
; #pragma unroll
;             for (int r = 0; r < 4; ++r) { f32x4 y = w0 * x[r] + w1 * x[r + 1] + w2 * x[r + 2];
;                 y[0] = siluf_(y[0]); y[1] = siluf_(y[1]); y[2] = siluf_(y[2]); y[3] = siluf_(y[3]);
;                 if (g == 0) { qv[r] = y; sq[r] = (y[0] * y[0] + y[1] * y[1]) + (y[2] * y[2] + y[3] * y[3]); }
;                 else if (g == 1) { kv[r] = y; sk[r] = (y[0] * y[0] + y[1] * y[1]) + (y[2] * y[2] + y[3] * y[3]); }
	v_pk_fma_f32 v[40:41], v[86:87], v[82:83], v[44:45]
	v_pk_fma_f32 v[36:37], v[88:89], v[84:85], v[36:37]
	v_mul_f32_e32 v44, 0xbfb8aa3b, v40
	v_mul_f32_e32 v45, 0xbfb8aa3b, v41
	v_exp_f32_e32 v44, v44
	v_exp_f32_e32 v45, v45
	v_cndmask_b32_e64 v43, v43, 0, s[14:15]
	s_mov_b32 s1, 0x5e000000
	v_pk_add_f32 v[44:45], v[44:45], 1.0 op_sel_hi:[1,0]
	s_nop 0
	v_div_scale_f32 v46, s[8:9], v45, v45, v41
	v_rcp_f32_e32 v47, v46
	s_nop 0
	v_fma_f32 v50, -v46, v47, 1.0
	v_fmac_f32_e32 v47, v50, v47
	v_div_scale_f32 v50, vcc, v41, v45, v41
	v_mul_f32_e32 v51, v50, v47
	v_fma_f32 v52, -v46, v51, v50
	v_fmac_f32_e32 v51, v52, v47
	v_fma_f32 v46, -v46, v51, v50
	v_div_fmas_f32 v46, v46, v47, v51
	v_div_fixup_f32 v47, v46, v45, v41
	v_div_scale_f32 v41, s[8:9], v44, v44, v40
	v_rcp_f32_e32 v45, v41
	s_nop 0
	v_fma_f32 v46, -v41, v45, 1.0
	v_fmac_f32_e32 v45, v46, v45
	v_div_scale_f32 v46, vcc, v40, v44, v40
	v_mul_f32_e32 v50, v46, v45
	v_fma_f32 v51, -v41, v50, v46
	v_fmac_f32_e32 v50, v51, v45
	v_fma_f32 v41, -v41, v50, v46
	v_div_fmas_f32 v41, v41, v45, v50
	v_div_fixup_f32 v46, v41, v44, v40
	v_mul_f32_e32 v40, 0xbfb8aa3b, v36
	v_mul_f32_e32 v41, 0xbfb8aa3b, v37
	v_exp_f32_e32 v40, v40
	v_exp_f32_e32 v41, v41
	s_nop 0
	v_pk_add_f32 v[40:41], v[40:41], 1.0 op_sel_hi:[1,0]
	s_nop 0
	v_div_scale_f32 v44, s[8:9], v41, v41, v37
	v_rcp_f32_e32 v45, v44
	s_nop 0
	v_fma_f32 v50, -v44, v45, 1.0
	v_fmac_f32_e32 v45, v50, v45
	v_div_scale_f32 v50, vcc, v37, v41, v37
	v_mul_f32_e32 v51, v50, v45
	v_fma_f32 v52, -v44, v51, v50
	v_fmac_f32_e32 v51, v52, v45
	v_fma_f32 v44, -v44, v51, v50
	v_div_fmas_f32 v44, v44, v45, v51
	v_div_fixup_f32 v51, v44, v41, v37
	v_div_scale_f32 v37, s[8:9], v40, v40, v36
	v_rcp_f32_e32 v41, v37
	s_nop 0
	v_fma_f32 v44, -v37, v41, 1.0
	v_fmac_f32_e32 v41, v44, v41
	v_div_scale_f32 v44, vcc, v36, v40, v36
	v_mul_f32_e32 v45, v44, v41
	v_fma_f32 v50, -v37, v45, v44
	v_fmac_f32_e32 v45, v50, v41
	v_fma_f32 v37, -v37, v45, v44
	v_div_fmas_f32 v37, v37, v41, v45
	v_div_fixup_f32 v50, v37, v40, v36
	v_mov_b32_e32 v40, v47
	v_mov_b32_e32 v41, v51
	v_mov_b32_e32 v36, v46
	v_mov_b32_e32 v37, v50
	v_pk_mul_f32 v[40:41], v[40:41], v[40:41]
	s_nop 0
	v_pk_fma_f32 v[54:55], v[36:37], v[36:37], v[40:41]
	v_pk_mul_f32 v[40:41], v[86:87], v[78:79]
	v_pk_mul_f32 v[36:37], v[88:89], v[80:81]
	v_pk_fma_f32 v[38:39], v[38:39], v[74:75], v[40:41]
	v_pk_fma_f32 v[36:37], v[48:49], v[76:77], v[36:37]
	v_pk_fma_f32 v[38:39], v[32:33], v[82:83], v[38:39]
	v_pk_fma_f32 v[36:37], v[42:43], v[84:85], v[36:37]
	v_mul_f32_e32 v40, 0xbfb8aa3b, v38
	v_mul_f32_e32 v41, 0xbfb8aa3b, v39
	v_exp_f32_e32 v40, v40
	v_exp_f32_e32 v41, v41
	s_nop 0
	v_pk_add_f32 v[40:41], v[40:41], 1.0 op_sel_hi:[1,0]
	s_nop 0
	v_div_scale_f32 v44, s[8:9], v41, v41, v39
	v_rcp_f32_e32 v45, v44
	s_nop 0
	v_fma_f32 v48, -v44, v45, 1.0
	v_fmac_f32_e32 v45, v48, v45
	v_div_scale_f32 v48, vcc, v39, v41, v39
	v_mul_f32_e32 v49, v48, v45
	v_fma_f32 v52, -v44, v49, v48
	v_fmac_f32_e32 v49, v52, v45
	v_fma_f32 v44, -v44, v49, v48
	v_div_fmas_f32 v44, v44, v45, v49
	v_div_fixup_f32 v41, v44, v41, v39
	v_div_scale_f32 v39, s[8:9], v40, v40, v38
	v_rcp_f32_e32 v44, v39
	s_nop 0
	v_fma_f32 v45, -v39, v44, 1.0
	v_fmac_f32_e32 v44, v45, v44
	v_div_scale_f32 v45, vcc, v38, v40, v38
	v_mul_f32_e32 v48, v45, v44
	v_fma_f32 v49, -v39, v48, v45
	v_fmac_f32_e32 v48, v49, v44
	v_fma_f32 v39, -v39, v48, v45
	v_div_fmas_f32 v39, v39, v44, v48
	v_div_fixup_f32 v40, v39, v40, v38
	v_mul_f32_e32 v38, 0xbfb8aa3b, v36
	v_mul_f32_e32 v39, 0xbfb8aa3b, v37
	v_exp_f32_e32 v38, v38
	v_exp_f32_e32 v39, v39
	s_nop 0
	v_pk_add_f32 v[38:39], v[38:39], 1.0 op_sel_hi:[1,0]
	s_nop 0
	v_div_scale_f32 v44, s[8:9], v39, v39, v37
	v_rcp_f32_e32 v45, v44
	s_nop 0
	v_fma_f32 v48, -v44, v45, 1.0
	v_fmac_f32_e32 v45, v48, v45
	v_div_scale_f32 v48, vcc, v37, v39, v37
	v_mul_f32_e32 v49, v48, v45
	v_fma_f32 v52, -v44, v49, v48
	v_fmac_f32_e32 v49, v52, v45
	v_fma_f32 v44, -v44, v49, v48
	v_div_fmas_f32 v44, v44, v45, v49
	v_div_fixup_f32 v45, v44, v39, v37
	v_div_scale_f32 v37, s[8:9], v38, v38, v36
	v_rcp_f32_e32 v39, v37
	s_nop 0
	v_fma_f32 v44, -v37, v39, 1.0
	v_fmac_f32_e32 v39, v44, v39
	v_div_scale_f32 v44, vcc, v36, v38, v36
	v_mul_f32_e32 v48, v44, v39
	v_fma_f32 v49, -v37, v48, v44
	v_fmac_f32_e32 v48, v49, v39
	v_fma_f32 v37, -v37, v48, v44
	v_div_fmas_f32 v37, v37, v39, v48
	v_div_fixup_f32 v44, v37, v38, v36
	v_mov_b32_e32 v38, v41
	v_mov_b32_e32 v39, v45
	v_mov_b32_e32 v36, v40
	v_mov_b32_e32 v37, v44
	v_pk_mul_f32 v[38:39], v[38:39], v[38:39]
	s_nop 0
	v_pk_fma_f32 v[52:53], v[36:37], v[36:37], v[38:39]
	v_pk_mul_f32 v[36:37], v[42:43], v[80:81]
	v_pk_mul_f32 v[38:39], v[32:33], v[78:79]
	v_pk_fma_f32 v[36:37], v[88:89], v[76:77], v[36:37]
	v_pk_fma_f32 v[38:39], v[86:87], v[74:75], v[38:39]
	v_pk_fma_f32 v[48:49], v[70:71], v[84:85], v[36:37]
	v_pk_fma_f32 v[36:37], v[68:69], v[82:83], v[38:39]
	v_pk_mul_f32 v[68:69], v[68:69], v[78:79]
	v_mul_f32_e32 v38, 0xbfb8aa3b, v36
	v_mul_f32_e32 v39, 0xbfb8aa3b, v37
	v_exp_f32_e32 v38, v38
	v_exp_f32_e32 v39, v39
	v_pk_fma_f32 v[32:33], v[32:33], v[74:75], v[68:69]
	v_pk_mul_f32 v[70:71], v[70:71], v[80:81]
	v_pk_fma_f32 v[30:31], v[30:31], v[82:83], v[32:33]
	v_pk_add_f32 v[38:39], v[38:39], 1.0 op_sel_hi:[1,0]
	v_mul_f32_e32 v32, 0xbfb8aa3b, v30
	v_div_scale_f32 v86, s[8:9], v39, v39, v37
	v_rcp_f32_e32 v87, v86
	v_mul_f32_e32 v33, 0xbfb8aa3b, v31
	v_exp_f32_e32 v32, v32
	v_exp_f32_e32 v33, v33
	v_fma_f32 v88, -v86, v87, 1.0
	v_fmac_f32_e32 v87, v88, v87
	v_div_scale_f32 v88, vcc, v37, v39, v37
	v_mul_f32_e32 v89, v88, v87
	v_fma_f32 v90, -v86, v89, v88
	v_fmac_f32_e32 v89, v90, v87
; #define LAS __attribute__((address_space(3)))
; __device__ __forceinline__ float siluf_(float x) { return x / (1.f + __expf(-x)); }
; __device__ __forceinline__ f32x4 bf4(u32x2 v) { return (f32x4){lo_bf(v.x), hi_bf(v.x), lo_bf(v.y), hi_bf(v.y)}; }
; __device__ __forceinline__ void ph_prep_tok(CArgs& a, int l, LAS unsigned char* lds, int gw, int ngw) {
;     ...
;         for (int g = 0; g < 3; ++g) { const int col = g * 256 + 4 * lane;
;             f32x4 x[6];
; #pragma unroll
;             for (int r = 0; r < 6; ++r) { const int t = tpos + r - 1; x[r] = (t >= lo && t < hi) ? bf4(xr[g][r]) : (f32x4){0.f, 0.f, 0.f, 0.f}; }
;             const f32x4 w0 = *(const LAS f32x4*)(cw + col), w1 = *(const LAS f32x4*)(cw + 768 + col), w2 = *(const LAS f32x4*)(cw + 1536 + col);
; #pragma unroll
;             for (int r = 0; r < 4; ++r) { f32x4 y = w0 * x[r] + w1 * x[r + 1] + w2 * x[r + 2];
;                 y[0] = siluf_(y[0]); y[1] = siluf_(y[1]); y[2] = siluf_(y[2]); y[3] = siluf_(y[3]);
;                 if (g == 0) { qv[r] = y; sq[r] = (y[0] * y[0] + y[1] * y[1]) + (y[2] * y[2] + y[3] * y[3]); }
;                 else if (g == 1) { kv[r] = y; sk[r] = (y[0] * y[0] + y[1] * y[1]) + (y[2] * y[2] + y[3] * y[3]); }
	v_fma_f32 v86, -v86, v89, v88
	v_div_fmas_f32 v86, v86, v87, v89
	v_div_fixup_f32 v37, v86, v39, v37
	v_div_scale_f32 v39, s[8:9], v38, v38, v36
	v_rcp_f32_e32 v86, v39
	v_pk_add_f32 v[32:33], v[32:33], 1.0 op_sel_hi:[1,0]
	v_pk_fma_f32 v[42:43], v[42:43], v[76:77], v[70:71]
	v_div_scale_f32 v68, s[8:9], v33, v33, v31
	v_fma_f32 v87, -v39, v86, 1.0
	v_fmac_f32_e32 v86, v87, v86
	v_div_scale_f32 v87, vcc, v36, v38, v36
	v_mul_f32_e32 v88, v87, v86
	v_fma_f32 v89, -v39, v88, v87
	v_fmac_f32_e32 v88, v89, v86
	v_fma_f32 v39, -v39, v88, v87
	v_div_fmas_f32 v39, v39, v86, v88
	v_div_fixup_f32 v36, v39, v38, v36
	v_mul_f32_e32 v38, 0xbfb8aa3b, v48
	v_mul_f32_e32 v39, 0xbfb8aa3b, v49
	v_exp_f32_e32 v38, v38
	v_exp_f32_e32 v39, v39
	v_rcp_f32_e32 v69, v68
	v_pk_fma_f32 v[42:43], v[72:73], v[84:85], v[42:43]
	v_and_b32_e32 v74, 0xffff0000, v63
	v_pk_add_f32 v[38:39], v[38:39], 1.0 op_sel_hi:[1,0]
	v_fma_f32 v70, -v68, v69, 1.0
	v_div_scale_f32 v86, s[8:9], v39, v39, v49
	v_rcp_f32_e32 v87, v86
	v_fmac_f32_e32 v69, v70, v69
	v_fma_f32 v88, -v86, v87, 1.0
	v_fmac_f32_e32 v87, v88, v87
	v_div_scale_f32 v88, vcc, v49, v39, v49
	v_mul_f32_e32 v89, v88, v87
	v_fma_f32 v90, -v86, v89, v88
	v_fmac_f32_e32 v89, v90, v87
	v_fma_f32 v86, -v86, v89, v88
	v_div_fmas_f32 v86, v86, v87, v89
	v_div_fixup_f32 v39, v86, v39, v49
	v_div_scale_f32 v49, s[8:9], v38, v38, v48
	v_rcp_f32_e32 v86, v49
	s_nop 0
	v_fma_f32 v87, -v49, v86, 1.0
	v_fmac_f32_e32 v86, v87, v86
	v_div_scale_f32 v87, vcc, v48, v38, v48
	v_mul_f32_e32 v88, v87, v86
	v_fma_f32 v89, -v49, v88, v87
	v_fmac_f32_e32 v88, v89, v86
	v_fma_f32 v49, -v49, v88, v87
	v_div_fmas_f32 v49, v49, v86, v88
	v_div_scale_f32 v70, vcc, v31, v33, v31
	v_mul_f32_e32 v71, v70, v69
	v_fma_f32 v72, -v68, v71, v70
	v_fmac_f32_e32 v71, v72, v69
	v_fma_f32 v68, -v68, v71, v70
	v_div_fmas_f32 v68, v68, v69, v71
	v_div_fixup_f32 v31, v68, v33, v31
	v_div_scale_f32 v33, s[8:9], v32, v32, v30
	v_rcp_f32_e32 v68, v33
	v_div_fixup_f32 v38, v49, v38, v48
	v_mov_b32_e32 v86, v37
	v_mov_b32_e32 v87, v39
	v_fma_f32 v69, -v33, v68, 1.0
	v_fmac_f32_e32 v68, v69, v68
	v_div_scale_f32 v69, vcc, v30, v32, v30
	v_mul_f32_e32 v70, v69, v68
	v_fma_f32 v71, -v33, v70, v69
	v_fmac_f32_e32 v70, v71, v68
	v_fma_f32 v33, -v33, v70, v69
	v_div_fmas_f32 v33, v33, v68, v70
	v_div_fixup_f32 v30, v33, v32, v30
	v_mul_f32_e32 v32, 0xbfb8aa3b, v42
	v_mul_f32_e32 v33, 0xbfb8aa3b, v43
	v_exp_f32_e32 v32, v32
	v_exp_f32_e32 v33, v33
	v_mov_b32_e32 v48, v36
	v_mov_b32_e32 v49, v38
	v_pk_mul_f32 v[86:87], v[86:87], v[86:87]
	v_pk_add_f32 v[32:33], v[32:33], 1.0 op_sel_hi:[1,0]
	v_pk_fma_f32 v[48:49], v[48:49], v[48:49], v[86:87]
	v_div_scale_f32 v68, s[8:9], v33, v33, v43
	v_rcp_f32_e32 v69, v68
	v_cndmask_b32_e64 v89, v74, 0, s[4:5]
	v_fma_f32 v70, -v68, v69, 1.0
	v_fmac_f32_e32 v69, v70, v69
	v_div_scale_f32 v70, vcc, v43, v33, v43
	v_mul_f32_e32 v71, v70, v69
	v_fma_f32 v72, -v68, v71, v70
	v_fmac_f32_e32 v71, v72, v69
	v_fma_f32 v68, -v68, v71, v70
	v_div_fmas_f32 v68, v68, v69, v71
	v_div_fixup_f32 v33, v68, v33, v43
	v_div_scale_f32 v43, s[8:9], v32, v32, v42
	v_rcp_f32_e32 v68, v43
	v_and_b32_e32 v72, 0xffff0000, v65
	v_cndmask_b32_e64 v73, v72, 0, s[4:5]
	v_fma_f32 v69, -v43, v68, 1.0
	v_fmac_f32_e32 v68, v69, v68
	v_div_scale_f32 v69, vcc, v42, v32, v42
	v_mul_f32_e32 v70, v69, v68
	v_fma_f32 v71, -v43, v70, v69
	v_fmac_f32_e32 v70, v71, v68
	v_fma_f32 v43, -v43, v70, v69
	v_div_fmas_f32 v43, v43, v68, v70
	v_lshlrev_b32_e32 v70, 16, v64
	v_and_b32_e32 v64, 0xffff0000, v64
	v_lshlrev_b32_e32 v71, 16, v65
	v_cndmask_b32_e64 v65, v64, 0, s[4:5]
	v_cndmask_b32_e64 v64, v70, 0, s[4:5]
	v_cndmask_b32_e64 v72, v71, 0, s[4:5]
	v_lshlrev_b32_e32 v70, 16, v62
	v_and_b32_e32 v62, 0xffff0000, v62
	v_lshlrev_b32_e32 v71, 16, v63
	v_cndmask_b32_e64 v63, v62, 0, s[4:5]
	v_cndmask_b32_e64 v62, v70, 0, s[4:5]
	v_cndmask_b32_e64 v88, v71, 0, s[4:5]
	v_lshlrev_b32_e32 v70, 16, v60
	v_and_b32_e32 v60, 0xffff0000, v60
	v_lshlrev_b32_e32 v71, 16, v61
	v_and_b32_e32 v61, 0xffff0000, v61
	v_cndmask_b32_e64 v91, v60, 0, s[14:15]
	v_cndmask_b32_e64 v93, v61, 0, s[14:15]
	v_lshlrev_b32_e32 v60, 16, v58
	v_and_b32_e32 v58, 0xffff0000, v58
	v_lshlrev_b32_e32 v61, 16, v59
	v_and_b32_e32 v59, 0xffff0000, v59
	v_cndmask_b32_e64 v95, v58, 0, s[4:5]
	v_cndmask_b32_e64 v97, v59, 0, s[4:5]
	v_lshlrev_b32_e32 v58, 16, v56
	v_and_b32_e32 v56, 0xffff0000, v56
	v_lshlrev_b32_e32 v59, 16, v57
	v_and_b32_e32 v57, 0xffff0000, v57
	v_cndmask_b32_e64 v99, v56, 0, s[26:27]
	v_cndmask_b32_e64 v98, v58, 0, s[26:27]
	v_cndmask_b32_e64 v101, v57, 0, s[26:27]
	v_cndmask_b32_e64 v100, v59, 0, s[26:27]
	ds_read_b128 v[56:59], v117 offset:59392
	ds_read_b128 v[80:83], v117 offset:62464
	v_cndmask_b32_e64 v94, v60, 0, s[4:5]
	v_lshl_add_u32 v60, v111, 2, v116
	v_div_fixup_f32 v32, v43, v32, v42
	v_mov_b32_e32 v68, v31
	v_mov_b32_e32 v69, v33
	ds_read_b128 v[84:87], v60
	v_mov_b32_e32 v42, v30
	v_mov_b32_e32 v43, v32
	v_pk_mul_f32 v[68:69], v[68:69], v[68:69]
	v_cndmask_b32_e64 v90, v70, 0, s[14:15]
	v_pk_fma_f32 v[42:43], v[42:43], v[42:43], v[68:69]
	v_lshlrev_b32_e32 v68, 16, v66
	v_and_b32_e32 v69, 0xffff0000, v66
	v_lshlrev_b32_e32 v66, 16, v67
	v_and_b32_e32 v67, 0xffff0000, v67
	v_cndmask_b32_e64 v69, v69, 0, s[6:7]
	v_cndmask_b32_e64 v68, v68, 0, s[6:7]
	v_cndmask_b32_e64 v92, v71, 0, s[14:15]
	s_waitcnt lgkmcnt(1)
	v_pk_mul_f32 v[70:71], v[64:65], v[80:81]
	v_cndmask_b32_e64 v67, v67, 0, s[6:7]
	v_cndmask_b32_e64 v66, v66, 0, s[6:7]
	v_cndmask_b32_e64 v96, v61, 0, s[4:5]
	v_pk_mul_f32 v[60:61], v[72:73], v[82:83]
	v_pk_fma_f32 v[68:69], v[68:69], v[56:57], v[70:71]
	v_pk_fma_f32 v[60:61], v[66:67], v[58:59], v[60:61]
	s_waitcnt lgkmcnt(0)
; #define LAS __attribute__((address_space(3)))
; __device__ __forceinline__ float siluf_(float x) { return x / (1.f + __expf(-x)); }
; __device__ __forceinline__ f32x4 bf4(u32x2 v) { return (f32x4){lo_bf(v.x), hi_bf(v.x), lo_bf(v.y), hi_bf(v.y)}; }
; __device__ __forceinline__ void ph_prep_tok(CArgs& a, int l, LAS unsigned char* lds, int gw, int ngw) {
;     ...
;         for (int g = 0; g < 3; ++g) { const int col = g * 256 + 4 * lane;
;             f32x4 x[6];
; #pragma unroll
;             for (int r = 0; r < 6; ++r) { const int t = tpos + r - 1; x[r] = (t >= lo && t < hi) ? bf4(xr[g][r]) : (f32x4){0.f, 0.f, 0.f, 0.f}; }
;             const f32x4 w0 = *(const LAS f32x4*)(cw + col), w1 = *(const LAS f32x4*)(cw + 768 + col), w2 = *(const LAS f32x4*)(cw + 1536 + col);
; #pragma unroll
;             for (int r = 0; r < 4; ++r) { f32x4 y = w0 * x[r] + w1 * x[r + 1] + w2 * x[r + 2];
;                 y[0] = siluf_(y[0]); y[1] = siluf_(y[1]); y[2] = siluf_(y[2]); y[3] = siluf_(y[3]);
;                 if (g == 0) { qv[r] = y; sq[r] = (y[0] * y[0] + y[1] * y[1]) + (y[2] * y[2] + y[3] * y[3]); }
;                 else if (g == 1) { kv[r] = y; sk[r] = (y[0] * y[0] + y[1] * y[1]) + (y[2] * y[2] + y[3] * y[3]); }
	v_pk_fma_f32 v[66:67], v[62:63], v[84:85], v[68:69]
	v_pk_fma_f32 v[60:61], v[88:89], v[86:87], v[60:61]
	v_mul_f32_e32 v68, 0xbfb8aa3b, v66
	v_mul_f32_e32 v69, 0xbfb8aa3b, v67
	v_exp_f32_e32 v68, v68
	v_exp_f32_e32 v69, v69
	s_nop 0
	v_pk_add_f32 v[68:69], v[68:69], 1.0 op_sel_hi:[1,0]
	s_nop 0
	v_div_scale_f32 v70, s[8:9], v69, v69, v67
	v_rcp_f32_e32 v71, v70
	s_nop 0
	v_fma_f32 v74, -v70, v71, 1.0
	v_fmac_f32_e32 v71, v74, v71
	v_div_scale_f32 v74, vcc, v67, v69, v67
	v_mul_f32_e32 v75, v74, v71
	v_fma_f32 v76, -v70, v75, v74
	v_fmac_f32_e32 v75, v76, v71
	v_fma_f32 v70, -v70, v75, v74
	v_div_fmas_f32 v70, v70, v71, v75
	v_div_fixup_f32 v71, v70, v69, v67
	v_div_scale_f32 v67, s[8:9], v68, v68, v66
	v_rcp_f32_e32 v69, v67
	s_nop 0
	v_fma_f32 v70, -v67, v69, 1.0
	v_fmac_f32_e32 v69, v70, v69
	v_div_scale_f32 v70, vcc, v66, v68, v66
	v_mul_f32_e32 v74, v70, v69
	v_fma_f32 v75, -v67, v74, v70
	v_fmac_f32_e32 v74, v75, v69
	v_fma_f32 v67, -v67, v74, v70
	v_div_fmas_f32 v67, v67, v69, v74
	v_div_fixup_f32 v70, v67, v68, v66
	v_mul_f32_e32 v66, 0xbfb8aa3b, v60
	v_mul_f32_e32 v67, 0xbfb8aa3b, v61
	v_exp_f32_e32 v66, v66
	v_exp_f32_e32 v67, v67
	s_nop 0
	v_pk_add_f32 v[66:67], v[66:67], 1.0 op_sel_hi:[1,0]
	s_nop 0
	v_div_scale_f32 v68, s[8:9], v67, v67, v61
	v_rcp_f32_e32 v69, v68
	s_nop 0
	v_fma_f32 v74, -v68, v69, 1.0
	v_fmac_f32_e32 v69, v74, v69
	v_div_scale_f32 v74, vcc, v61, v67, v61
	v_mul_f32_e32 v75, v74, v69
	v_fma_f32 v76, -v68, v75, v74
	v_fmac_f32_e32 v75, v76, v69
	v_fma_f32 v68, -v68, v75, v74
	v_div_fmas_f32 v68, v68, v69, v75
	v_div_fixup_f32 v75, v68, v67, v61
	v_div_scale_f32 v61, s[8:9], v66, v66, v60
	v_rcp_f32_e32 v67, v61
	s_nop 0
	v_fma_f32 v68, -v61, v67, 1.0
	v_fmac_f32_e32 v67, v68, v67
	v_div_scale_f32 v68, vcc, v60, v66, v60
	v_mul_f32_e32 v69, v68, v67
	v_fma_f32 v74, -v61, v69, v68
	v_fmac_f32_e32 v69, v74, v67
	v_fma_f32 v61, -v61, v69, v68
	v_div_fmas_f32 v61, v61, v67, v69
	v_div_fixup_f32 v74, v61, v66, v60
	v_mov_b32_e32 v66, v71
	v_mov_b32_e32 v67, v75
	v_mov_b32_e32 v60, v70
	v_mov_b32_e32 v61, v74
	v_pk_mul_f32 v[66:67], v[66:67], v[66:67]
	s_nop 0
	v_pk_fma_f32 v[78:79], v[60:61], v[60:61], v[66:67]
	v_pk_mul_f32 v[66:67], v[62:63], v[80:81]
	v_pk_mul_f32 v[60:61], v[88:89], v[82:83]
	v_pk_fma_f32 v[64:65], v[64:65], v[56:57], v[66:67]
	v_pk_fma_f32 v[60:61], v[72:73], v[58:59], v[60:61]
	v_pk_fma_f32 v[64:65], v[90:91], v[84:85], v[64:65]
	v_pk_fma_f32 v[60:61], v[92:93], v[86:87], v[60:61]
	v_mul_f32_e32 v66, 0xbfb8aa3b, v64
	v_mul_f32_e32 v67, 0xbfb8aa3b, v65
	v_exp_f32_e32 v66, v66
	v_exp_f32_e32 v67, v67
	s_nop 0
	v_pk_add_f32 v[66:67], v[66:67], 1.0 op_sel_hi:[1,0]
	s_nop 0
	v_div_scale_f32 v68, s[8:9], v67, v67, v65
	v_rcp_f32_e32 v69, v68
	s_nop 0
	v_fma_f32 v72, -v68, v69, 1.0
	v_fmac_f32_e32 v69, v72, v69
	v_div_scale_f32 v72, vcc, v65, v67, v65
	v_mul_f32_e32 v73, v72, v69
	v_fma_f32 v76, -v68, v73, v72
	v_fmac_f32_e32 v73, v76, v69
	v_fma_f32 v68, -v68, v73, v72
	v_div_fmas_f32 v68, v68, v69, v73
	v_div_fixup_f32 v65, v68, v67, v65
	v_div_scale_f32 v67, s[8:9], v66, v66, v64
	v_rcp_f32_e32 v68, v67
	s_nop 0
	v_fma_f32 v69, -v67, v68, 1.0
	v_fmac_f32_e32 v68, v69, v68
	v_div_scale_f32 v69, vcc, v64, v66, v64
	v_mul_f32_e32 v72, v69, v68
	v_fma_f32 v73, -v67, v72, v69
	v_fmac_f32_e32 v72, v73, v68
	v_fma_f32 v67, -v67, v72, v69
	v_div_fmas_f32 v67, v67, v68, v72
	v_div_fixup_f32 v64, v67, v66, v64
	v_mul_f32_e32 v66, 0xbfb8aa3b, v60
	v_mul_f32_e32 v67, 0xbfb8aa3b, v61
	v_exp_f32_e32 v66, v66
	v_exp_f32_e32 v67, v67
	s_nop 0
	v_pk_add_f32 v[66:67], v[66:67], 1.0 op_sel_hi:[1,0]
	s_nop 0
	v_div_scale_f32 v68, s[8:9], v67, v67, v61
	v_rcp_f32_e32 v69, v68
	s_nop 0
	v_fma_f32 v72, -v68, v69, 1.0
	v_fmac_f32_e32 v69, v72, v69
	v_div_scale_f32 v72, vcc, v61, v67, v61
	v_mul_f32_e32 v73, v72, v69
	v_fma_f32 v76, -v68, v73, v72
	v_fmac_f32_e32 v73, v76, v69
	v_fma_f32 v68, -v68, v73, v72
	v_div_fmas_f32 v68, v68, v69, v73
	v_div_fixup_f32 v67, v68, v67, v61
	v_div_scale_f32 v61, s[8:9], v66, v66, v60
	v_rcp_f32_e32 v68, v61
	s_nop 0
	v_fma_f32 v69, -v61, v68, 1.0
	v_fmac_f32_e32 v68, v69, v68
	v_div_scale_f32 v69, vcc, v60, v66, v60
	v_mul_f32_e32 v72, v69, v68
	v_fma_f32 v73, -v61, v72, v69
	v_fmac_f32_e32 v72, v73, v68
	v_fma_f32 v61, -v61, v72, v69
	v_div_fmas_f32 v61, v61, v68, v72
	v_div_fixup_f32 v66, v61, v66, v60
	v_mov_b32_e32 v68, v65
	v_mov_b32_e32 v69, v67
	v_mov_b32_e32 v60, v64
	v_mov_b32_e32 v61, v66
	v_pk_mul_f32 v[68:69], v[68:69], v[68:69]
	s_nop 0
	v_pk_fma_f32 v[76:77], v[60:61], v[60:61], v[68:69]
	v_pk_mul_f32 v[60:61], v[92:93], v[82:83]
	v_pk_mul_f32 v[68:69], v[90:91], v[80:81]
	v_pk_fma_f32 v[60:61], v[88:89], v[58:59], v[60:61]
	v_pk_fma_f32 v[62:63], v[62:63], v[56:57], v[68:69]
	v_pk_fma_f32 v[68:69], v[96:97], v[86:87], v[60:61]
	v_pk_fma_f32 v[60:61], v[94:95], v[84:85], v[62:63]
	v_pk_mul_f32 v[80:81], v[94:95], v[80:81]
	v_mul_f32_e32 v62, 0xbfb8aa3b, v60
	v_mul_f32_e32 v63, 0xbfb8aa3b, v61
	v_exp_f32_e32 v62, v62
	v_exp_f32_e32 v63, v63
	v_pk_fma_f32 v[56:57], v[90:91], v[56:57], v[80:81]
	v_pk_add_f32 v[62:63], v[62:63], 1.0 op_sel_hi:[1,0]
	s_nop 0
	v_div_scale_f32 v72, s[8:9], v63, v63, v61
	v_rcp_f32_e32 v73, v72
	v_pk_fma_f32 v[56:57], v[98:99], v[84:85], v[56:57]
	v_fma_f32 v88, -v72, v73, 1.0
	v_fmac_f32_e32 v73, v88, v73
	v_div_scale_f32 v88, vcc, v61, v63, v61
	v_mul_f32_e32 v89, v88, v73
	v_fma_f32 v102, -v72, v89, v88
	v_fmac_f32_e32 v89, v102, v73
	v_fma_f32 v72, -v72, v89, v88
	v_div_fmas_f32 v72, v72, v73, v89
	v_div_fixup_f32 v61, v72, v63, v61
	v_div_scale_f32 v63, s[8:9], v62, v62, v60
	v_rcp_f32_e32 v72, v63
	s_nop 0
	v_fma_f32 v73, -v63, v72, 1.0
; #define LAS __attribute__((address_space(3)))
; __device__ __forceinline__ unsigned pk2(float lo, float hi) { return f2bf(lo) | (f2bf(hi) << 16); }
; __device__ __forceinline__ float siluf_(float x) { return x / (1.f + __expf(-x)); }
; __device__ __forceinline__ f32x4 bf4(u32x2 v) { return (f32x4){lo_bf(v.x), hi_bf(v.x), lo_bf(v.y), hi_bf(v.y)}; }
; __device__ __forceinline__ void ph_prep_tok(CArgs& a, int l, LAS unsigned char* lds, int gw, int ngw) {
;     ...
;         for (int g = 0; g < 3; ++g) { const int col = g * 256 + 4 * lane;
;             f32x4 x[6];
; #pragma unroll
;             for (int r = 0; r < 6; ++r) { const int t = tpos + r - 1; x[r] = (t >= lo && t < hi) ? bf4(xr[g][r]) : (f32x4){0.f, 0.f, 0.f, 0.f}; }
;             const f32x4 w0 = *(const LAS f32x4*)(cw + col), w1 = *(const LAS f32x4*)(cw + 768 + col), w2 = *(const LAS f32x4*)(cw + 1536 + col);
; #pragma unroll
;             for (int r = 0; r < 4; ++r) { f32x4 y = w0 * x[r] + w1 * x[r + 1] + w2 * x[r + 2];
;                 y[0] = siluf_(y[0]); y[1] = siluf_(y[1]); y[2] = siluf_(y[2]); y[3] = siluf_(y[3]);
;                 if (g == 0) { qv[r] = y; sq[r] = (y[0] * y[0] + y[1] * y[1]) + (y[2] * y[2] + y[3] * y[3]); }
;                 else if (g == 1) { kv[r] = y; sk[r] = (y[0] * y[0] + y[1] * y[1]) + (y[2] * y[2] + y[3] * y[3]); }
;                 else *(u32x2*)((bf16*)DV + (size_t)(row0 + r) * 256 + 4 * lane) = (u32x2){pk2(y[0], y[1]), pk2(y[2], y[3])}; } }
	v_fmac_f32_e32 v72, v73, v72
	v_div_scale_f32 v73, vcc, v60, v62, v60
	v_mul_f32_e32 v88, v73, v72
	v_fma_f32 v89, -v63, v88, v73
	v_fmac_f32_e32 v88, v89, v72
	v_fma_f32 v63, -v63, v88, v73
	v_div_fmas_f32 v63, v63, v72, v88
	v_div_fixup_f32 v60, v63, v62, v60
	v_mul_f32_e32 v62, 0xbfb8aa3b, v68
	v_mul_f32_e32 v63, 0xbfb8aa3b, v69
	v_exp_f32_e32 v62, v62
	v_exp_f32_e32 v63, v63
	s_nop 0
	v_pk_add_f32 v[62:63], v[62:63], 1.0 op_sel_hi:[1,0]
	s_nop 0
	v_div_scale_f32 v72, s[8:9], v63, v63, v69
	v_rcp_f32_e32 v73, v72
	s_nop 0
	v_fma_f32 v88, -v72, v73, 1.0
	v_fmac_f32_e32 v73, v88, v73
	v_div_scale_f32 v88, vcc, v69, v63, v69
	v_mul_f32_e32 v89, v88, v73
	v_fma_f32 v102, -v72, v89, v88
	v_fmac_f32_e32 v89, v102, v73
	v_fma_f32 v72, -v72, v89, v88
	v_div_fmas_f32 v72, v72, v73, v89
	v_div_fixup_f32 v63, v72, v63, v69
	v_div_scale_f32 v69, s[8:9], v62, v62, v68
	v_rcp_f32_e32 v72, v69
	s_nop 0
	v_fma_f32 v73, -v69, v72, 1.0
	v_fmac_f32_e32 v72, v73, v72
	v_div_scale_f32 v73, vcc, v68, v62, v68
	v_mul_f32_e32 v88, v73, v72
	v_fma_f32 v89, -v69, v88, v73
	v_fmac_f32_e32 v88, v89, v72
	v_fma_f32 v69, -v69, v88, v73
	v_div_fmas_f32 v69, v69, v72, v88
	v_div_fixup_f32 v62, v69, v62, v68
	v_mov_b32_e32 v72, v61
	v_mov_b32_e32 v73, v63
	v_mov_b32_e32 v68, v60
	v_mov_b32_e32 v69, v62
	v_pk_mul_f32 v[72:73], v[72:73], v[72:73]
	s_nop 0
	v_pk_fma_f32 v[72:73], v[68:69], v[68:69], v[72:73]
	v_pk_mul_f32 v[68:69], v[96:97], v[82:83]
	s_nop 0
	v_pk_fma_f32 v[58:59], v[92:93], v[58:59], v[68:69]
	v_mul_f32_e32 v68, 0xbfb8aa3b, v56
	v_mul_f32_e32 v69, 0xbfb8aa3b, v57
	v_exp_f32_e32 v68, v68
	v_exp_f32_e32 v69, v69
	v_pk_fma_f32 v[58:59], v[100:101], v[86:87], v[58:59]
	v_pk_add_f32 v[68:69], v[68:69], 1.0 op_sel_hi:[1,0]
	s_nop 0
	v_div_scale_f32 v80, s[8:9], v69, v69, v57
	v_rcp_f32_e32 v81, v80
	s_nop 0
	v_fma_f32 v82, -v80, v81, 1.0
	v_fmac_f32_e32 v81, v82, v81
	v_div_scale_f32 v82, vcc, v57, v69, v57
	v_mul_f32_e32 v83, v82, v81
	v_fma_f32 v84, -v80, v83, v82
	v_fmac_f32_e32 v83, v84, v81
	v_fma_f32 v80, -v80, v83, v82
	v_div_fmas_f32 v80, v80, v81, v83
	v_div_fixup_f32 v57, v80, v69, v57
	v_div_scale_f32 v69, s[8:9], v68, v68, v56
	v_rcp_f32_e32 v80, v69
	s_nop 0
	v_fma_f32 v81, -v69, v80, 1.0
	v_fmac_f32_e32 v80, v81, v80
	v_div_scale_f32 v81, vcc, v56, v68, v56
	v_mul_f32_e32 v82, v81, v80
	v_fma_f32 v83, -v69, v82, v81
	v_fmac_f32_e32 v82, v83, v80
	v_fma_f32 v69, -v69, v82, v81
	v_div_fmas_f32 v69, v69, v80, v82
	v_div_fixup_f32 v56, v69, v68, v56
	v_mul_f32_e32 v68, 0xbfb8aa3b, v58
	v_mul_f32_e32 v69, 0xbfb8aa3b, v59
	v_exp_f32_e32 v68, v68
	v_exp_f32_e32 v69, v69
	s_nop 0
	v_pk_add_f32 v[68:69], v[68:69], 1.0 op_sel_hi:[1,0]
	s_nop 0
	v_div_scale_f32 v80, s[8:9], v69, v69, v59
	v_rcp_f32_e32 v81, v80
	s_nop 0
	v_fma_f32 v82, -v80, v81, 1.0
	v_fmac_f32_e32 v81, v82, v81
	v_div_scale_f32 v82, vcc, v59, v69, v59
	v_mul_f32_e32 v83, v82, v81
	v_fma_f32 v84, -v80, v83, v82
	v_fmac_f32_e32 v83, v84, v81
	v_fma_f32 v80, -v80, v83, v82
	v_div_fmas_f32 v80, v80, v81, v83
	v_div_fixup_f32 v59, v80, v69, v59
	v_div_scale_f32 v69, s[8:9], v68, v68, v58
	v_rcp_f32_e32 v80, v69
	s_nop 0
	v_fma_f32 v81, -v69, v80, 1.0
	v_fmac_f32_e32 v80, v81, v80
	v_div_scale_f32 v81, vcc, v58, v68, v58
	v_mul_f32_e32 v82, v81, v80
	v_fma_f32 v83, -v69, v82, v81
	v_fmac_f32_e32 v82, v83, v80
	v_fma_f32 v69, -v69, v82, v81
	v_div_fmas_f32 v69, v69, v80, v82
	v_div_fixup_f32 v58, v69, v68, v58
	v_mov_b32_e32 v80, v57
	v_mov_b32_e32 v81, v59
	v_mov_b32_e32 v68, v56
	v_mov_b32_e32 v69, v58
	v_pk_mul_f32 v[80:81], v[80:81], v[80:81]
	s_nop 0
	v_pk_fma_f32 v[68:69], v[68:69], v[68:69], v[80:81]
	v_lshlrev_b32_e32 v80, 16, v12
	v_and_b32_e32 v12, 0xffff0000, v12
	v_lshlrev_b32_e32 v81, 16, v13
	v_and_b32_e32 v13, 0xffff0000, v13
	v_cndmask_b32_e64 v101, v12, 0, s[6:7]
	v_cndmask_b32_e64 v103, v13, 0, s[6:7]
	v_lshlrev_b32_e32 v12, 16, v10
	v_and_b32_e32 v10, 0xffff0000, v10
	v_lshlrev_b32_e32 v13, 16, v11
	v_and_b32_e32 v11, 0xffff0000, v11
	v_cndmask_b32_e64 v97, v11, 0, s[4:5]
	v_cndmask_b32_e64 v99, v10, 0, s[4:5]
	v_lshlrev_b32_e32 v10, 16, v8
	v_and_b32_e32 v8, 0xffff0000, v8
	v_lshlrev_b32_e32 v11, 16, v9
	v_and_b32_e32 v9, 0xffff0000, v9
	v_cndmask_b32_e64 v93, v9, 0, s[4:5]
	v_cndmask_b32_e64 v95, v8, 0, s[4:5]
	v_lshlrev_b32_e32 v8, 16, v6
	v_and_b32_e32 v6, 0xffff0000, v6
	v_lshlrev_b32_e32 v9, 16, v7
	v_and_b32_e32 v7, 0xffff0000, v7
	v_cndmask_b32_e64 v102, v81, 0, s[6:7]
	v_cndmask_b32_e64 v81, v7, 0, s[14:15]
	v_cndmask_b32_e64 v83, v6, 0, s[14:15]
	v_lshlrev_b32_e32 v6, 16, v4
	v_and_b32_e32 v4, 0xffff0000, v4
	v_lshlrev_b32_e32 v7, 16, v5
	v_and_b32_e32 v5, 0xffff0000, v5
	v_cndmask_b32_e64 v87, v5, 0, s[4:5]
	v_cndmask_b32_e64 v89, v4, 0, s[4:5]
	v_lshlrev_b32_e32 v4, 16, v2
	v_and_b32_e32 v2, 0xffff0000, v2
	v_lshlrev_b32_e32 v5, 16, v3
	v_and_b32_e32 v3, 0xffff0000, v3
	v_cndmask_b32_e64 v100, v80, 0, s[6:7]
	v_cndmask_b32_e64 v80, v9, 0, s[14:15]
	v_cndmask_b32_e64 v82, v8, 0, s[14:15]
	v_cndmask_b32_e64 v86, v7, 0, s[4:5]
	v_cndmask_b32_e64 v88, v6, 0, s[4:5]
	v_cndmask_b32_e64 v85, v3, 0, s[26:27]
	v_cndmask_b32_e64 v84, v5, 0, s[26:27]
	v_cndmask_b32_e64 v91, v2, 0, s[26:27]
	v_cndmask_b32_e64 v90, v4, 0, s[26:27]
	ds_read_b128 v[2:5], v117 offset:60416
	ds_read_b128 v[6:9], v117 offset:63488
	v_cndmask_b32_e64 v94, v10, 0, s[4:5]
	v_lshl_add_u32 v10, v112, 2, v116
	v_cndmask_b32_e64 v96, v13, 0, s[4:5]
	v_cndmask_b32_e64 v98, v12, 0, s[4:5]
	v_cndmask_b32_e64 v92, v11, 0, s[4:5]
	ds_read_b128 v[10:13], v10
	s_waitcnt lgkmcnt(1)
	v_pk_mul_f32 v[118:119], v[96:97], v[8:9]
	v_pk_mul_f32 v[116:117], v[98:99], v[6:7]
	v_pk_fma_f32 v[102:103], v[102:103], v[4:5], v[118:119]
	v_pk_fma_f32 v[100:101], v[100:101], v[2:3], v[116:117]
	s_waitcnt lgkmcnt(0)
; #define LAS __attribute__((address_space(3)))
; __device__ __forceinline__ unsigned pk2(float lo, float hi) { return f2bf(lo) | (f2bf(hi) << 16); }
; __device__ __forceinline__ float siluf_(float x) { return x / (1.f + __expf(-x)); }
; __device__ __forceinline__ f32x4 bf4(u32x2 v) { return (f32x4){lo_bf(v.x), hi_bf(v.x), lo_bf(v.y), hi_bf(v.y)}; }
; __device__ __forceinline__ void ph_prep_tok(CArgs& a, int l, LAS unsigned char* lds, int gw, int ngw) {
;     ...
; #pragma unroll
;         for (int g = 0; g < 3; ++g) { const int col = g * 256 + 4 * lane;
;             f32x4 x[6];
; #pragma unroll
;             for (int r = 0; r < 6; ++r) { const int t = tpos + r - 1; x[r] = (t >= lo && t < hi) ? bf4(xr[g][r]) : (f32x4){0.f, 0.f, 0.f, 0.f}; }
;             const f32x4 w0 = *(const LAS f32x4*)(cw + col), w1 = *(const LAS f32x4*)(cw + 768 + col), w2 = *(const LAS f32x4*)(cw + 1536 + col);
; #pragma unroll
;             for (int r = 0; r < 4; ++r) { f32x4 y = w0 * x[r] + w1 * x[r + 1] + w2 * x[r + 2];
;                 y[0] = siluf_(y[0]); y[1] = siluf_(y[1]); y[2] = siluf_(y[2]); y[3] = siluf_(y[3]);
;                 if (g == 0) { qv[r] = y; sq[r] = (y[0] * y[0] + y[1] * y[1]) + (y[2] * y[2] + y[3] * y[3]); }
;                 else if (g == 1) { kv[r] = y; sk[r] = (y[0] * y[0] + y[1] * y[1]) + (y[2] * y[2] + y[3] * y[3]); }
;                 else *(u32x2*)((bf16*)DV + (size_t)(row0 + r) * 256 + 4 * lane) = (u32x2){pk2(y[0], y[1]), pk2(y[2], y[3])}; } }
	v_pk_fma_f32 v[102:103], v[92:93], v[12:13], v[102:103]
	v_pk_fma_f32 v[100:101], v[94:95], v[10:11], v[100:101]
	v_mul_f32_e32 v116, 0xbfb8aa3b, v103
	v_exp_f32_e32 v117, v116
	v_mul_f32_e32 v116, 0xbfb8aa3b, v102
	v_exp_f32_e32 v119, v116
	v_mul_f32_e32 v116, 0xbfb8aa3b, v101
	v_exp_f32_e32 v116, v116
	v_mul_f32_e32 v118, 0xbfb8aa3b, v100
	v_exp_f32_e32 v118, v118
	s_mov_b32 s6, 0x358637bd
	v_pk_add_f32 v[116:117], v[116:117], 1.0 op_sel_hi:[1,0]
	s_nop 0
	v_div_scale_f32 v120, s[4:5], v116, v116, v101
	v_rcp_f32_e32 v121, v120
	s_nop 0
	v_fma_f32 v122, -v120, v121, 1.0
	v_fmac_f32_e32 v121, v122, v121
	v_div_scale_f32 v122, vcc, v101, v116, v101
	v_mul_f32_e32 v123, v122, v121
	v_fma_f32 v124, -v120, v123, v122
	v_fmac_f32_e32 v123, v124, v121
	v_fma_f32 v120, -v120, v123, v122
	v_div_fmas_f32 v120, v120, v121, v123
	v_div_fixup_f32 v101, v120, v116, v101
	v_div_scale_f32 v116, s[4:5], v117, v117, v103
	v_rcp_f32_e32 v120, v116
	s_nop 0
	v_fma_f32 v121, -v116, v120, 1.0
	v_fmac_f32_e32 v120, v121, v120
	v_div_scale_f32 v121, vcc, v103, v117, v103
	v_mul_f32_e32 v122, v121, v120
	v_fma_f32 v123, -v116, v122, v121
	v_fmac_f32_e32 v122, v123, v120
	v_fma_f32 v116, -v116, v122, v121
	v_div_fmas_f32 v116, v116, v120, v122
	v_div_fixup_f32 v103, v116, v117, v103
	v_pk_add_f32 v[116:117], v[118:119], 1.0 op_sel_hi:[1,0]
	s_nop 0
	v_div_scale_f32 v118, s[4:5], v116, v116, v100
	v_rcp_f32_e32 v119, v118
	s_nop 0
	v_fma_f32 v120, -v118, v119, 1.0
	v_fmac_f32_e32 v119, v120, v119
	v_div_scale_f32 v120, vcc, v100, v116, v100
	v_mul_f32_e32 v121, v120, v119
	v_fma_f32 v122, -v118, v121, v120
	v_fmac_f32_e32 v121, v122, v119
	v_fma_f32 v118, -v118, v121, v120
	v_div_fmas_f32 v118, v118, v119, v121
	v_div_fixup_f32 v100, v118, v116, v100
	v_div_scale_f32 v116, s[4:5], v117, v117, v102
	v_rcp_f32_e32 v118, v116
	s_nop 0
	v_fma_f32 v119, -v116, v118, 1.0
	v_fmac_f32_e32 v118, v119, v118
	v_div_scale_f32 v119, vcc, v102, v117, v102
	v_mul_f32_e32 v120, v119, v118
	v_fma_f32 v121, -v116, v120, v119
	v_fmac_f32_e32 v120, v121, v118
	v_fma_f32 v116, -v116, v120, v119
	v_div_fmas_f32 v116, v116, v118, v120
	v_div_fixup_f32 v102, v116, v117, v102
	v_and_b32_sdwa v116, v102, v169 dst_sel:DWORD dst_unused:UNUSED_PAD src0_sel:WORD_1 src1_sel:DWORD
	v_and_b32_sdwa v117, v100, v169 dst_sel:DWORD dst_unused:UNUSED_PAD src0_sel:WORD_1 src1_sel:DWORD
	v_add3_u32 v100, v100, v117, s81
	v_add3_u32 v102, v102, v116, s81
	v_and_b32_sdwa v116, v103, v169 dst_sel:DWORD dst_unused:UNUSED_PAD src0_sel:WORD_1 src1_sel:DWORD
	v_and_b32_sdwa v117, v101, v169 dst_sel:DWORD dst_unused:UNUSED_PAD src0_sel:WORD_1 src1_sel:DWORD
	v_add3_u32 v103, v103, v116, s81
	v_add3_u32 v101, v101, v117, s81
	v_and_b32_e32 v103, 0xffff0000, v103
	v_and_b32_e32 v101, 0xffff0000, v101
	v_or_b32_sdwa v103, v103, v102 dst_sel:DWORD dst_unused:UNUSED_PAD src0_sel:DWORD src1_sel:WORD_1
	v_or_b32_sdwa v102, v101, v100 dst_sel:DWORD dst_unused:UNUSED_PAD src0_sel:DWORD src1_sel:WORD_1
	v_lshl_add_u64 v[100:101], s[2:3], 0, v[20:21]
	v_add_co_u32_e32 v116, vcc, s1, v100
	s_nop 1
	v_addc_co_u32_e32 v117, vcc, 0, v101, vcc
	global_store_dwordx2 v[116:117], v[102:103], off
	v_pk_mul_f32 v[116:117], v[92:93], v[8:9]
	v_pk_mul_f32 v[102:103], v[94:95], v[6:7]
	v_pk_fma_f32 v[96:97], v[96:97], v[4:5], v[116:117]
	v_pk_fma_f32 v[98:99], v[98:99], v[2:3], v[102:103]
	v_pk_fma_f32 v[96:97], v[80:81], v[12:13], v[96:97]
	v_pk_fma_f32 v[98:99], v[82:83], v[10:11], v[98:99]
	v_mul_f32_e32 v102, 0xbfb8aa3b, v97
	v_exp_f32_e32 v103, v102
	v_mul_f32_e32 v102, 0xbfb8aa3b, v96
	v_exp_f32_e32 v117, v102
	v_mul_f32_e32 v102, 0xbfb8aa3b, v99
	v_exp_f32_e32 v102, v102
	v_mul_f32_e32 v116, 0xbfb8aa3b, v98
	v_exp_f32_e32 v116, v116
	v_pk_add_f32 v[102:103], v[102:103], 1.0 op_sel_hi:[1,0]
	s_nop 0
	v_div_scale_f32 v118, s[4:5], v102, v102, v99
	v_rcp_f32_e32 v119, v118
	s_nop 0
	v_fma_f32 v120, -v118, v119, 1.0
	v_fmac_f32_e32 v119, v120, v119
	v_div_scale_f32 v120, vcc, v99, v102, v99
	v_mul_f32_e32 v121, v120, v119
	v_fma_f32 v122, -v118, v121, v120
	v_fmac_f32_e32 v121, v122, v119
	v_fma_f32 v118, -v118, v121, v120
	v_div_fmas_f32 v118, v118, v119, v121
	v_div_fixup_f32 v99, v118, v102, v99
	v_div_scale_f32 v102, s[4:5], v103, v103, v97
	v_rcp_f32_e32 v118, v102
	s_nop 0
	v_fma_f32 v119, -v102, v118, 1.0
	v_fmac_f32_e32 v118, v119, v118
	v_div_scale_f32 v119, vcc, v97, v103, v97
	v_mul_f32_e32 v120, v119, v118
	v_fma_f32 v121, -v102, v120, v119
	v_fmac_f32_e32 v120, v121, v118
	v_fma_f32 v102, -v102, v120, v119
	v_div_fmas_f32 v102, v102, v118, v120
	v_div_fixup_f32 v97, v102, v103, v97
	v_pk_add_f32 v[102:103], v[116:117], 1.0 op_sel_hi:[1,0]
	s_nop 0
	v_div_scale_f32 v116, s[4:5], v102, v102, v98
	v_rcp_f32_e32 v117, v116
	s_nop 0
	v_fma_f32 v118, -v116, v117, 1.0
	v_fmac_f32_e32 v117, v118, v117
	v_div_scale_f32 v118, vcc, v98, v102, v98
	v_mul_f32_e32 v119, v118, v117
	v_fma_f32 v120, -v116, v119, v118
	v_fmac_f32_e32 v119, v120, v117
	v_fma_f32 v116, -v116, v119, v118
	v_div_fmas_f32 v116, v116, v117, v119
	v_div_fixup_f32 v98, v116, v102, v98
	v_div_scale_f32 v102, s[4:5], v103, v103, v96
	v_rcp_f32_e32 v116, v102
	s_nop 0
	v_fma_f32 v117, -v102, v116, 1.0
	v_fmac_f32_e32 v116, v117, v116
	v_div_scale_f32 v117, vcc, v96, v103, v96
	v_mul_f32_e32 v118, v117, v116
	v_fma_f32 v119, -v102, v118, v117
	v_fmac_f32_e32 v118, v119, v116
	v_fma_f32 v102, -v102, v118, v117
	v_div_fmas_f32 v102, v102, v116, v118
	v_div_fixup_f32 v96, v102, v103, v96
	v_and_b32_sdwa v102, v96, v169 dst_sel:DWORD dst_unused:UNUSED_PAD src0_sel:WORD_1 src1_sel:DWORD
	v_and_b32_sdwa v103, v98, v169 dst_sel:DWORD dst_unused:UNUSED_PAD src0_sel:WORD_1 src1_sel:DWORD
; #define LAS __attribute__((address_space(3)))
; __device__ __forceinline__ unsigned pk2(float lo, float hi) { return f2bf(lo) | (f2bf(hi) << 16); }
; __device__ __forceinline__ float siluf_(float x) { return x / (1.f + __expf(-x)); }
; __device__ __forceinline__ f32x4 bf4(u32x2 v) { return (f32x4){lo_bf(v.x), hi_bf(v.x), lo_bf(v.y), hi_bf(v.y)}; }
; __device__ __forceinline__ void ph_prep_tok(CArgs& a, int l, LAS unsigned char* lds, int gw, int ngw) {
;     ...
; #pragma unroll
;         for (int g = 0; g < 3; ++g) { const int col = g * 256 + 4 * lane;
;             f32x4 x[6];
; #pragma unroll
;             for (int r = 0; r < 6; ++r) { const int t = tpos + r - 1; x[r] = (t >= lo && t < hi) ? bf4(xr[g][r]) : (f32x4){0.f, 0.f, 0.f, 0.f}; }
;             const f32x4 w0 = *(const LAS f32x4*)(cw + col), w1 = *(const LAS f32x4*)(cw + 768 + col), w2 = *(const LAS f32x4*)(cw + 1536 + col);
; #pragma unroll
;             for (int r = 0; r < 4; ++r) { f32x4 y = w0 * x[r] + w1 * x[r + 1] + w2 * x[r + 2];
;                 y[0] = siluf_(y[0]); y[1] = siluf_(y[1]); y[2] = siluf_(y[2]); y[3] = siluf_(y[3]);
;                 if (g == 0) { qv[r] = y; sq[r] = (y[0] * y[0] + y[1] * y[1]) + (y[2] * y[2] + y[3] * y[3]); }
;                 else if (g == 1) { kv[r] = y; sk[r] = (y[0] * y[0] + y[1] * y[1]) + (y[2] * y[2] + y[3] * y[3]); }
;                 else *(u32x2*)((bf16*)DV + (size_t)(row0 + r) * 256 + 4 * lane) = (u32x2){pk2(y[0], y[1]), pk2(y[2], y[3])}; } }
	v_add3_u32 v96, v96, v102, s81
	v_and_b32_sdwa v102, v97, v169 dst_sel:DWORD dst_unused:UNUSED_PAD src0_sel:WORD_1 src1_sel:DWORD
	v_add3_u32 v98, v98, v103, s81
	v_and_b32_sdwa v103, v99, v169 dst_sel:DWORD dst_unused:UNUSED_PAD src0_sel:WORD_1 src1_sel:DWORD
	v_add3_u32 v97, v97, v102, s81
	v_add3_u32 v99, v99, v103, s81
	v_and_b32_e32 v97, 0xffff0000, v97
	v_and_b32_e32 v99, 0xffff0000, v99
	v_or_b32_sdwa v103, v97, v96 dst_sel:DWORD dst_unused:UNUSED_PAD src0_sel:DWORD src1_sel:WORD_1
	v_lshl_add_u64 v[96:97], s[2:3], 0, v[16:17]
	v_or_b32_sdwa v102, v99, v98 dst_sel:DWORD dst_unused:UNUSED_PAD src0_sel:DWORD src1_sel:WORD_1
	v_add_co_u32_e32 v98, vcc, s1, v96
	v_pk_mul_f32 v[116:117], v[80:81], v[8:9]
	s_nop 0
	v_addc_co_u32_e32 v99, vcc, 0, v97, vcc
	v_pk_fma_f32 v[92:93], v[92:93], v[4:5], v[116:117]
	global_store_dwordx2 v[98:99], v[102:103], off offset:512
	v_pk_mul_f32 v[102:103], v[82:83], v[6:7]
	v_pk_fma_f32 v[92:93], v[86:87], v[12:13], v[92:93]
	v_pk_fma_f32 v[94:95], v[94:95], v[2:3], v[102:103]
	v_mul_f32_e32 v102, 0xbfb8aa3b, v93
	v_pk_fma_f32 v[94:95], v[88:89], v[10:11], v[94:95]
	v_exp_f32_e32 v103, v102
	v_mul_f32_e32 v102, 0xbfb8aa3b, v92
	v_exp_f32_e32 v117, v102
	v_mul_f32_e32 v102, 0xbfb8aa3b, v95
	v_exp_f32_e32 v102, v102
	v_mul_f32_e32 v116, 0xbfb8aa3b, v94
	v_exp_f32_e32 v116, v116
	v_pk_mul_f32 v[8:9], v[86:87], v[8:9]
	v_pk_add_f32 v[102:103], v[102:103], 1.0 op_sel_hi:[1,0]
	v_pk_fma_f32 v[4:5], v[80:81], v[4:5], v[8:9]
	v_div_scale_f32 v118, s[4:5], v102, v102, v95
	v_rcp_f32_e32 v119, v118
	v_pk_mul_f32 v[6:7], v[88:89], v[6:7]
	v_pk_fma_f32 v[4:5], v[84:85], v[12:13], v[4:5]
	v_pk_fma_f32 v[2:3], v[82:83], v[2:3], v[6:7]
	v_fma_f32 v120, -v118, v119, 1.0
	v_fmac_f32_e32 v119, v120, v119
	v_div_scale_f32 v120, vcc, v95, v102, v95
	v_mul_f32_e32 v121, v120, v119
	v_fma_f32 v122, -v118, v121, v120
	v_fmac_f32_e32 v121, v122, v119
	v_fma_f32 v118, -v118, v121, v120
	v_div_fmas_f32 v118, v118, v119, v121
	v_div_fixup_f32 v95, v118, v102, v95
	v_div_scale_f32 v102, s[4:5], v103, v103, v93
	v_rcp_f32_e32 v118, v102
	v_mul_f32_e32 v6, 0xbfb8aa3b, v5
	v_pk_fma_f32 v[2:3], v[90:91], v[10:11], v[2:3]
	v_exp_f32_e32 v7, v6
	v_fma_f32 v119, -v102, v118, 1.0
	v_fmac_f32_e32 v118, v119, v118
	v_div_scale_f32 v119, vcc, v93, v103, v93
	v_mul_f32_e32 v120, v119, v118
	v_fma_f32 v121, -v102, v120, v119
	v_fmac_f32_e32 v120, v121, v118
	v_fma_f32 v102, -v102, v120, v119
	v_div_fmas_f32 v102, v102, v118, v120
	v_div_fixup_f32 v93, v102, v103, v93
	v_pk_add_f32 v[102:103], v[116:117], 1.0 op_sel_hi:[1,0]
	v_mul_f32_e32 v6, 0xbfb8aa3b, v4
	v_div_scale_f32 v116, s[4:5], v102, v102, v94
	v_rcp_f32_e32 v117, v116
	v_exp_f32_e32 v9, v6
	v_mul_f32_e32 v6, 0xbfb8aa3b, v3
	v_exp_f32_e32 v6, v6
	v_fma_f32 v118, -v116, v117, 1.0
	v_fmac_f32_e32 v117, v118, v117
	v_div_scale_f32 v118, vcc, v94, v102, v94
	v_mul_f32_e32 v119, v118, v117
	v_fma_f32 v120, -v116, v119, v118
	v_fmac_f32_e32 v119, v120, v117
	v_fma_f32 v116, -v116, v119, v118
	v_div_fmas_f32 v116, v116, v117, v119
	v_div_fixup_f32 v94, v116, v102, v94
	v_div_scale_f32 v102, s[4:5], v103, v103, v92
	v_rcp_f32_e32 v116, v102
	v_pk_add_f32 v[6:7], v[6:7], 1.0 op_sel_hi:[1,0]
	v_mul_f32_e32 v8, 0xbfb8aa3b, v2
	v_div_scale_f32 v10, s[4:5], v6, v6, v3
	v_fma_f32 v117, -v102, v116, 1.0
	v_fmac_f32_e32 v116, v117, v116
	v_div_scale_f32 v117, vcc, v92, v103, v92
	v_rcp_f32_e32 v11, v10
	v_mul_f32_e32 v118, v117, v116
	v_fma_f32 v119, -v102, v118, v117
	v_fmac_f32_e32 v118, v119, v116
	v_fma_f32 v102, -v102, v118, v117
	v_fma_f32 v12, -v10, v11, 1.0
	v_div_fmas_f32 v102, v102, v116, v118
	v_fmac_f32_e32 v11, v12, v11
	v_div_scale_f32 v12, vcc, v3, v6, v3
	v_mul_f32_e32 v13, v12, v11
	v_fma_f32 v80, -v10, v13, v12
	v_fmac_f32_e32 v13, v80, v11
	v_fma_f32 v10, -v10, v13, v12
	v_div_fmas_f32 v10, v10, v11, v13
	v_div_fixup_f32 v3, v10, v6, v3
	v_div_scale_f32 v6, s[4:5], v7, v7, v5
	v_rcp_f32_e32 v10, v6
	v_exp_f32_e32 v8, v8
	v_div_fixup_f32 v92, v102, v103, v92
	v_and_b32_sdwa v102, v92, v169 dst_sel:DWORD dst_unused:UNUSED_PAD src0_sel:WORD_1 src1_sel:DWORD
	v_fma_f32 v11, -v6, v10, 1.0
	v_fmac_f32_e32 v10, v11, v10
	v_div_scale_f32 v11, vcc, v5, v7, v5
	v_mul_f32_e32 v12, v11, v10
	v_fma_f32 v13, -v6, v12, v11
	v_fmac_f32_e32 v12, v13, v10
	v_fma_f32 v6, -v6, v12, v11
	v_div_fmas_f32 v6, v6, v10, v12
	v_div_fixup_f32 v5, v6, v7, v5
	v_pk_add_f32 v[6:7], v[8:9], 1.0 op_sel_hi:[1,0]
	v_and_b32_sdwa v103, v94, v169 dst_sel:DWORD dst_unused:UNUSED_PAD src0_sel:WORD_1 src1_sel:DWORD
	v_div_scale_f32 v8, s[4:5], v6, v6, v2
	v_rcp_f32_e32 v9, v8
	v_add3_u32 v94, v94, v103, s81
	v_add3_u32 v92, v92, v102, s81
	v_and_b32_sdwa v102, v93, v169 dst_sel:DWORD dst_unused:UNUSED_PAD src0_sel:WORD_1 src1_sel:DWORD
	v_fma_f32 v10, -v8, v9, 1.0
	v_fmac_f32_e32 v9, v10, v9
	v_div_scale_f32 v10, vcc, v2, v6, v2
	v_mul_f32_e32 v11, v10, v9
	v_fma_f32 v12, -v8, v11, v10
	v_fmac_f32_e32 v11, v12, v9
	v_fma_f32 v8, -v8, v11, v10
	v_div_fmas_f32 v8, v8, v9, v11
	v_div_fixup_f32 v2, v8, v6, v2
	v_div_scale_f32 v6, s[4:5], v7, v7, v4
	v_rcp_f32_e32 v8, v6
	v_and_b32_sdwa v103, v95, v169 dst_sel:DWORD dst_unused:UNUSED_PAD src0_sel:WORD_1 src1_sel:DWORD
	v_add3_u32 v93, v93, v102, s81
	v_add3_u32 v95, v95, v103, s81
	v_fma_f32 v9, -v6, v8, 1.0
	v_fmac_f32_e32 v8, v9, v8
	v_div_scale_f32 v9, vcc, v4, v7, v4
	v_mul_f32_e32 v10, v9, v8
	v_fma_f32 v11, -v6, v10, v9
	v_fmac_f32_e32 v10, v11, v8
	v_fma_f32 v6, -v6, v10, v9
	v_div_fmas_f32 v6, v6, v8, v10
	v_div_fixup_f32 v4, v6, v7, v4
	v_and_b32_sdwa v6, v4, v169 dst_sel:DWORD dst_unused:UNUSED_PAD src0_sel:WORD_1 src1_sel:DWORD
; __device__ __forceinline__ unsigned pk2(float lo, float hi) { return f2bf(lo) | (f2bf(hi) << 16); }
; __device__ __forceinline__ float siluf_(float x) { return x / (1.f + __expf(-x)); }
; __device__ __forceinline__ float row16_sum(float v) { v += dpp_f<0xB1>(v); v += dpp_f<0x4E>(v); v += dpp_f<0x141>(v); v += dpp_f<0x140>(v); return v; }
; __device__ __forceinline__ void ph_prep_tok(CArgs& a, int l, LAS unsigned char* lds, int gw, int ngw) {
;     ...
;             for (int r = 0; r < 4; ++r) { f32x4 y = w0 * x[r] + w1 * x[r + 1] + w2 * x[r + 2];
;                 y[0] = siluf_(y[0]); y[1] = siluf_(y[1]); y[2] = siluf_(y[2]); y[3] = siluf_(y[3]);
;                 if (g == 0) { qv[r] = y; sq[r] = (y[0] * y[0] + y[1] * y[1]) + (y[2] * y[2] + y[3] * y[3]); }
;                 else if (g == 1) { kv[r] = y; sk[r] = (y[0] * y[0] + y[1] * y[1]) + (y[2] * y[2] + y[3] * y[3]); }
;                 else *(u32x2*)((bf16*)DV + (size_t)(row0 + r) * 256 + 4 * lane) = (u32x2){pk2(y[0], y[1]), pk2(y[2], y[3])}; } }
; #pragma unroll
;         for (int r = 0; r < 4; ++r) { const float rq = rsqrtf(row16_sum(sq[r]) + 1e-6f) * 0.125f, rk = rsqrtf(row16_sum(sk[r]) + 1e-6f);
;             const f32x4 qn = qv[r] * rq, kn = kv[r] * rk;
;             *(u32x2*)((bf16*)(a.ws + WS_CKD + CD_QB) + (size_t)(row0 + r) * 256 + 4 * lane) = (u32x2){pk2(qn[0], qn[1]), pk2(qn[2], qn[3])};
;             *(u32x2*)((bf16*)(a.ws + WS_CKD + CD_KB) + (size_t)(row0 + r) * 256 + 4 * lane) = (u32x2){pk2(kn[0], kn[1]), pk2(kn[2], kn[3])}; }
	v_and_b32_sdwa v7, v2, v169 dst_sel:DWORD dst_unused:UNUSED_PAD src0_sel:WORD_1 src1_sel:DWORD
	v_add3_u32 v2, v2, v7, s81
	v_add3_u32 v4, v4, v6, s81
	v_and_b32_sdwa v6, v5, v169 dst_sel:DWORD dst_unused:UNUSED_PAD src0_sel:WORD_1 src1_sel:DWORD
	v_and_b32_sdwa v7, v3, v169 dst_sel:DWORD dst_unused:UNUSED_PAD src0_sel:WORD_1 src1_sel:DWORD
	v_add3_u32 v5, v5, v6, s81
	v_add3_u32 v3, v3, v7, s81
	v_and_b32_e32 v5, 0xffff0000, v5
	v_and_b32_e32 v6, 0xffff0000, v3
	v_or_b32_sdwa v3, v5, v4 dst_sel:DWORD dst_unused:UNUSED_PAD src0_sel:DWORD src1_sel:WORD_1
	v_or_b32_sdwa v2, v6, v2 dst_sel:DWORD dst_unused:UNUSED_PAD src0_sel:DWORD src1_sel:WORD_1
	global_store_dwordx2 v[98:99], v[2:3], off offset:1536
	v_mov_b32_e32 v2, v78
	v_mov_b32_e32 v3, v54
	v_mov_b32_e32 v54, v79
	v_pk_add_f32 v[2:3], v[2:3], v[54:55]
	s_mov_b32 s1, 0x73e00000
	v_and_b32_e32 v93, 0xffff0000, v93
	v_mov_b32_dpp v5, v3 quad_perm:[1,0,3,2] row_mask:0xf bank_mask:0xf bound_ctrl:1
	v_mov_b32_dpp v4, v2 quad_perm:[1,0,3,2] row_mask:0xf bank_mask:0xf bound_ctrl:1
	v_pk_add_f32 v[2:3], v[2:3], v[4:5]
	v_and_b32_e32 v95, 0xffff0000, v95
	v_or_b32_sdwa v93, v93, v92 dst_sel:DWORD dst_unused:UNUSED_PAD src0_sel:DWORD src1_sel:WORD_1
	v_mov_b32_dpp v5, v3 quad_perm:[2,3,0,1] row_mask:0xf bank_mask:0xf bound_ctrl:1
	v_mov_b32_dpp v4, v2 quad_perm:[2,3,0,1] row_mask:0xf bank_mask:0xf bound_ctrl:1
	v_pk_add_f32 v[2:3], v[2:3], v[4:5]
	v_or_b32_sdwa v92, v95, v94 dst_sel:DWORD dst_unused:UNUSED_PAD src0_sel:DWORD src1_sel:WORD_1
	global_store_dwordx2 v[98:99], v[92:93], off offset:1024
	v_mov_b32_dpp v5, v3 row_half_mirror row_mask:0xf bank_mask:0xf bound_ctrl:1
	v_mov_b32_dpp v4, v2 row_half_mirror row_mask:0xf bank_mask:0xf bound_ctrl:1
	v_pk_add_f32 v[2:3], v[2:3], v[4:5]
	s_mov_b32 s4, 0x72c00000
	s_nop 0
	v_mov_b32_dpp v5, v3 row_mirror row_mask:0xf bank_mask:0xf bound_ctrl:1
	v_mov_b32_dpp v4, v2 row_mirror row_mask:0xf bank_mask:0xf bound_ctrl:1
	v_pk_add_f32 v[2:3], v[2:3], v[4:5]
	s_nop 0
	v_pk_add_f32 v[2:3], v[2:3], s[6:7] op_sel_hi:[1,0]
	s_nop 0
	v_mul_f32_e32 v4, 0x4b800000, v3
	v_cmp_gt_f32_e64 s[40:41], s21, v3
	v_cmp_gt_f32_e32 vcc, s21, v2
	s_nop 0
	v_cndmask_b32_e64 v3, v3, v4, s[40:41]
	v_rsq_f32_e32 v3, v3
	s_nop 0
	v_mul_f32_e32 v4, 0x45800000, v3
	v_cndmask_b32_e64 v3, v3, v4, s[40:41]
	v_mul_f32_e32 v4, 0x3e000000, v3
	v_mul_f32_e32 v3, 0x4b800000, v2
	v_pk_mul_f32 v[6:7], v[50:51], v[4:5] op_sel_hi:[1,0]
	v_pk_mul_f32 v[4:5], v[46:47], v[4:5] op_sel_hi:[1,0]
	v_cndmask_b32_e32 v2, v2, v3, vcc
	v_rsq_f32_e32 v2, v2
	v_cvt_pk_bf16_f32 v4, v4, v5
	v_mul_f32_e32 v3, 0x45800000, v2
	v_cndmask_b32_e32 v2, v2, v3, vcc
	v_cvt_pk_bf16_f32 v5, v6, v7
	v_add_co_u32_e32 v6, vcc, s1, v100
	v_pk_mul_f32 v[8:9], v[74:75], v[2:3] op_sel_hi:[1,0]
	v_pk_mul_f32 v[2:3], v[70:71], v[2:3] op_sel_hi:[1,0]
	v_addc_co_u32_e32 v7, vcc, 0, v101, vcc
	global_store_dwordx2 v[6:7], v[4:5], off
	v_cvt_pk_bf16_f32 v2, v2, v3
	v_cvt_pk_bf16_f32 v3, v8, v9
	v_add_co_u32_e32 v4, vcc, s4, v100
	s_nop 1
	v_addc_co_u32_e32 v5, vcc, 0, v101, vcc
	global_store_dwordx2 v[4:5], v[2:3], off
	v_mov_b32_e32 v2, v76
	v_mov_b32_e32 v3, v52
	v_mov_b32_e32 v52, v77
	v_pk_add_f32 v[2:3], v[2:3], v[52:53]
	s_nop 1
	v_mov_b32_dpp v5, v3 quad_perm:[1,0,3,2] row_mask:0xf bank_mask:0xf bound_ctrl:1
	v_mov_b32_dpp v4, v2 quad_perm:[1,0,3,2] row_mask:0xf bank_mask:0xf bound_ctrl:1
	v_pk_add_f32 v[2:3], v[2:3], v[4:5]
	s_nop 1
	v_mov_b32_dpp v5, v3 quad_perm:[2,3,0,1] row_mask:0xf bank_mask:0xf bound_ctrl:1
	v_mov_b32_dpp v4, v2 quad_perm:[2,3,0,1] row_mask:0xf bank_mask:0xf bound_ctrl:1
	v_pk_add_f32 v[2:3], v[2:3], v[4:5]
	s_nop 1
	v_mov_b32_dpp v5, v3 row_half_mirror row_mask:0xf bank_mask:0xf bound_ctrl:1
	v_mov_b32_dpp v4, v2 row_half_mirror row_mask:0xf bank_mask:0xf bound_ctrl:1
	v_pk_add_f32 v[2:3], v[2:3], v[4:5]
	s_nop 1
	v_mov_b32_dpp v5, v3 row_mirror row_mask:0xf bank_mask:0xf bound_ctrl:1
	v_mov_b32_dpp v4, v2 row_mirror row_mask:0xf bank_mask:0xf bound_ctrl:1
	v_pk_add_f32 v[2:3], v[2:3], v[4:5]
	s_nop 0
	v_pk_add_f32 v[2:3], v[2:3], s[6:7] op_sel_hi:[1,0]
	s_nop 0
	v_mul_f32_e32 v4, 0x4b800000, v3
	v_cmp_gt_f32_e64 s[40:41], s21, v3
	v_cmp_gt_f32_e32 vcc, s21, v2
	s_nop 0
	v_cndmask_b32_e64 v3, v3, v4, s[40:41]
	v_rsq_f32_e32 v3, v3
	s_nop 0
	v_mul_f32_e32 v4, 0x45800000, v3
	v_cndmask_b32_e64 v3, v3, v4, s[40:41]
	v_mul_f32_e32 v4, 0x3e000000, v3
	v_mul_f32_e32 v3, 0x4b800000, v2
	v_pk_mul_f32 v[6:7], v[44:45], v[4:5] op_sel_hi:[1,0]
	v_pk_mul_f32 v[4:5], v[40:41], v[4:5] op_sel_hi:[1,0]
	v_cndmask_b32_e32 v2, v2, v3, vcc
	v_rsq_f32_e32 v2, v2
	v_cvt_pk_bf16_f32 v4, v4, v5
	v_mul_f32_e32 v3, 0x45800000, v2
	v_cndmask_b32_e32 v2, v2, v3, vcc
	v_cvt_pk_bf16_f32 v5, v6, v7
	v_add_co_u32_e32 v6, vcc, s1, v96
	v_pk_mul_f32 v[8:9], v[66:67], v[2:3] op_sel_hi:[1,0]
	v_pk_mul_f32 v[2:3], v[64:65], v[2:3] op_sel_hi:[1,0]
	v_addc_co_u32_e32 v7, vcc, 0, v97, vcc
	global_store_dwordx2 v[6:7], v[4:5], off offset:512
	v_cvt_pk_bf16_f32 v2, v2, v3
	v_cvt_pk_bf16_f32 v3, v8, v9
	v_add_co_u32_e32 v4, vcc, s4, v96
	s_nop 1
	v_addc_co_u32_e32 v5, vcc, 0, v97, vcc
	global_store_dwordx2 v[4:5], v[2:3], off offset:512
	v_mov_b32_e32 v2, v72
	v_mov_b32_e32 v3, v48
	v_mov_b32_e32 v48, v73
	v_pk_add_f32 v[2:3], v[2:3], v[48:49]
	s_nop 1
	v_mov_b32_dpp v9, v3 quad_perm:[1,0,3,2] row_mask:0xf bank_mask:0xf bound_ctrl:1
	v_mov_b32_dpp v8, v2 quad_perm:[1,0,3,2] row_mask:0xf bank_mask:0xf bound_ctrl:1
	v_pk_add_f32 v[2:3], v[2:3], v[8:9]
	s_nop 1
	v_mov_b32_dpp v9, v3 quad_perm:[2,3,0,1] row_mask:0xf bank_mask:0xf bound_ctrl:1
	v_mov_b32_dpp v8, v2 quad_perm:[2,3,0,1] row_mask:0xf bank_mask:0xf bound_ctrl:1
; __device__ __forceinline__ float bf2f(unsigned v) { return __uint_as_float(v << 16); }
; __device__ __forceinline__ unsigned pk2(float lo, float hi) { return f2bf(lo) | (f2bf(hi) << 16); }
; __device__ __forceinline__ float sigmoidf_(float x) { return 1.f / (1.f + __expf(-x)); }
; __device__ __forceinline__ float siluf_(float x) { return x / (1.f + __expf(-x)); }
; __device__ __forceinline__ float softplusf_(float x) { return fmaxf(x, 0.f) + __logf(1.f + __expf(-fabsf(x))); }
; __device__ __forceinline__ float row16_sum(float v) { v += dpp_f<0xB1>(v); v += dpp_f<0x4E>(v); v += dpp_f<0x141>(v); v += dpp_f<0x140>(v); return v; }
; __device__ __forceinline__ void ph_prep_tok(CArgs& a, int l, LAS unsigned char* lds, int gw, int ngw) {
;     ...
;             for (int r = 0; r < 4; ++r) { f32x4 y = w0 * x[r] + w1 * x[r + 1] + w2 * x[r + 2];
;                 y[0] = siluf_(y[0]); y[1] = siluf_(y[1]); y[2] = siluf_(y[2]); y[3] = siluf_(y[3]);
;                 if (g == 0) { qv[r] = y; sq[r] = (y[0] * y[0] + y[1] * y[1]) + (y[2] * y[2] + y[3] * y[3]); }
;                 else if (g == 1) { kv[r] = y; sk[r] = (y[0] * y[0] + y[1] * y[1]) + (y[2] * y[2] + y[3] * y[3]); }
;                 else *(u32x2*)((bf16*)DV + (size_t)(row0 + r) * 256 + 4 * lane) = (u32x2){pk2(y[0], y[1]), pk2(y[2], y[3])}; } }
; #pragma unroll
;         for (int r = 0; r < 4; ++r) { const float rq = rsqrtf(row16_sum(sq[r]) + 1e-6f) * 0.125f, rk = rsqrtf(row16_sum(sk[r]) + 1e-6f);
;             const f32x4 qn = qv[r] * rq, kn = kv[r] * rk;
;             *(u32x2*)((bf16*)(a.ws + WS_CKD + CD_QB) + (size_t)(row0 + r) * 256 + 4 * lane) = (u32x2){pk2(qn[0], qn[1]), pk2(qn[2], qn[3])};
;             *(u32x2*)((bf16*)(a.ws + WS_CKD + CD_KB) + (size_t)(row0 + r) * 256 + 4 * lane) = (u32x2){pk2(kn[0], kn[1]), pk2(kn[2], kn[3])}; }
;         if (lane < 16) { const float af = bf2f(gb4[0]), ab = bf2f(gb4[1]), bfv = bf2f(gb4[2]), bbv = bf2f(gb4[3]);
;             const float gf = eaf * softplusf_(af + dtf), gb = eab * softplusf_(ab + dtb);
;             *(f32x4*)(DG + (size_t)(row0 + gr) * 16 + 4 * gh) = (f32x4){sigmoidf_(bfv), gf, sigmoidf_(bbv), gb}; }
	v_pk_add_f32 v[2:3], v[2:3], v[8:9]
	s_nop 1
	v_mov_b32_dpp v9, v3 row_half_mirror row_mask:0xf bank_mask:0xf bound_ctrl:1
	v_mov_b32_dpp v8, v2 row_half_mirror row_mask:0xf bank_mask:0xf bound_ctrl:1
	v_pk_add_f32 v[2:3], v[2:3], v[8:9]
	s_nop 1
	v_mov_b32_dpp v9, v3 row_mirror row_mask:0xf bank_mask:0xf bound_ctrl:1
	v_mov_b32_dpp v8, v2 row_mirror row_mask:0xf bank_mask:0xf bound_ctrl:1
	v_pk_add_f32 v[2:3], v[2:3], v[8:9]
	s_nop 0
	v_pk_add_f32 v[2:3], v[2:3], s[6:7] op_sel_hi:[1,0]
	s_nop 0
	v_mul_f32_e32 v8, 0x4b800000, v3
	v_cmp_gt_f32_e64 s[40:41], s21, v3
	v_cmp_gt_f32_e32 vcc, s21, v2
	s_nop 0
	v_cndmask_b32_e64 v3, v3, v8, s[40:41]
	v_rsq_f32_e32 v3, v3
	s_nop 0
	v_mul_f32_e32 v8, 0x45800000, v3
	v_cndmask_b32_e64 v3, v3, v8, s[40:41]
	v_mul_f32_e32 v8, 0x3e000000, v3
	v_mul_f32_e32 v3, 0x4b800000, v2
	v_cndmask_b32_e32 v2, v2, v3, vcc
	v_pk_mul_f32 v[10:11], v[38:39], v[8:9] op_sel_hi:[1,0]
	v_pk_mul_f32 v[8:9], v[36:37], v[8:9] op_sel_hi:[1,0]
	v_rsq_f32_e32 v2, v2
	v_bfe_u32 v36, v8, 16, 1
	v_add3_u32 v8, v8, v36, s81
	v_bfe_u32 v36, v9, 16, 1
	v_lshrrev_b32_e32 v8, 16, v8
	v_add3_u32 v9, v9, v36, s81
	v_and_or_b32 v8, v9, s80, v8
	v_mul_f32_e32 v3, 0x45800000, v2
	v_cndmask_b32_e32 v2, v2, v3, vcc
	v_pk_mul_f32 v[12:13], v[62:63], v[2:3] op_sel_hi:[1,0]
	v_pk_mul_f32 v[2:3], v[60:61], v[2:3] op_sel_hi:[1,0]
	v_cvt_pk_bf16_f32 v9, v10, v11
	global_store_dwordx2 v[6:7], v[8:9], off offset:1024
	v_cvt_pk_bf16_f32 v2, v2, v3
	v_bfe_u32 v3, v12, 16, 1
	v_add3_u32 v3, v12, v3, s81
	v_bfe_u32 v8, v13, 16, 1
	v_lshrrev_b32_e32 v3, 16, v3
	v_add3_u32 v8, v13, v8, s81
	v_and_or_b32 v3, v8, s80, v3
	global_store_dwordx2 v[4:5], v[2:3], off offset:1024
	v_mov_b32_e32 v2, v68
	v_mov_b32_e32 v3, v42
	v_mov_b32_e32 v42, v69
	v_pk_add_f32 v[2:3], v[2:3], v[42:43]
	s_nop 1
	v_mov_b32_dpp v9, v3 quad_perm:[1,0,3,2] row_mask:0xf bank_mask:0xf bound_ctrl:1
	v_mov_b32_dpp v8, v2 quad_perm:[1,0,3,2] row_mask:0xf bank_mask:0xf bound_ctrl:1
	v_pk_add_f32 v[2:3], v[2:3], v[8:9]
	s_nop 1
	v_mov_b32_dpp v9, v3 quad_perm:[2,3,0,1] row_mask:0xf bank_mask:0xf bound_ctrl:1
	v_mov_b32_dpp v8, v2 quad_perm:[2,3,0,1] row_mask:0xf bank_mask:0xf bound_ctrl:1
	v_pk_add_f32 v[2:3], v[2:3], v[8:9]
	s_nop 1
	v_mov_b32_dpp v9, v3 row_half_mirror row_mask:0xf bank_mask:0xf bound_ctrl:1
	v_mov_b32_dpp v8, v2 row_half_mirror row_mask:0xf bank_mask:0xf bound_ctrl:1
	v_pk_add_f32 v[2:3], v[2:3], v[8:9]
	s_nop 1
	v_mov_b32_dpp v9, v3 row_mirror row_mask:0xf bank_mask:0xf bound_ctrl:1
	v_mov_b32_dpp v8, v2 row_mirror row_mask:0xf bank_mask:0xf bound_ctrl:1
	v_pk_add_f32 v[2:3], v[2:3], v[8:9]
	s_nop 0
	v_pk_add_f32 v[2:3], v[2:3], s[6:7] op_sel_hi:[1,0]
	s_nop 0
	v_mul_f32_e32 v8, 0x4b800000, v3
	v_cmp_gt_f32_e64 s[40:41], s21, v3
	v_cmp_gt_f32_e32 vcc, s21, v2
	s_nop 0
	v_cndmask_b32_e64 v3, v3, v8, s[40:41]
	v_rsq_f32_e32 v3, v3
	s_nop 0
	v_mul_f32_e32 v8, 0x45800000, v3
	v_cndmask_b32_e64 v3, v3, v8, s[40:41]
	v_mul_f32_e32 v8, 0x3e000000, v3
	v_mul_f32_e32 v3, 0x4b800000, v2
	v_cndmask_b32_e32 v2, v2, v3, vcc
	v_pk_mul_f32 v[10:11], v[32:33], v[8:9] op_sel_hi:[1,0]
	v_pk_mul_f32 v[8:9], v[30:31], v[8:9] op_sel_hi:[1,0]
	v_rsq_f32_e32 v2, v2
	v_bfe_u32 v30, v8, 16, 1
	v_add3_u32 v8, v8, v30, s81
	v_bfe_u32 v30, v9, 16, 1
	v_lshrrev_b32_e32 v8, 16, v8
	v_add3_u32 v9, v9, v30, s81
	v_and_or_b32 v8, v9, s80, v8
	v_bfe_u32 v9, v10, 16, 1
	v_mul_f32_e32 v3, 0x45800000, v2
	v_add3_u32 v9, v10, v9, s81
	v_bfe_u32 v10, v11, 16, 1
	v_cndmask_b32_e32 v2, v2, v3, vcc
	v_lshrrev_b32_e32 v9, 16, v9
	v_add3_u32 v10, v11, v10, s81
	v_pk_mul_f32 v[12:13], v[58:59], v[2:3] op_sel_hi:[1,0]
	v_pk_mul_f32 v[2:3], v[56:57], v[2:3] op_sel_hi:[1,0]
	v_and_or_b32 v9, v10, s80, v9
	global_store_dwordx2 v[6:7], v[8:9], off offset:1536
	v_cvt_pk_bf16_f32 v2, v2, v3
	v_bfe_u32 v3, v12, 16, 1
	v_add3_u32 v3, v12, v3, s81
	v_bfe_u32 v6, v13, 16, 1
	v_lshrrev_b32_e32 v3, 16, v3
	v_add3_u32 v6, v13, v6, s81
	v_and_or_b32 v3, v6, s80, v3
	global_store_dwordx2 v[4:5], v[2:3], off offset:1536
	s_and_saveexec_b64 s[4:5], s[38:39]
	s_cbranch_execz .LBB0_301
	v_lshlrev_b32_e32 v2, 16, v34
	v_add_f32_e32 v2, v1, v2
	s_mov_b32 s1, 0xbfb8aa3b
	v_max_f32_e32 v3, 0, v2
	v_mul_f32_e64 v2, |v2|, s1
	v_exp_f32_e32 v2, v2
	s_mov_b32 s6, 0x3f317217
	s_mov_b32 s7, 0x7f800000
	v_lshlrev_b32_e32 v4, 16, v113
	v_add_f32_e32 v2, 1.0, v2
	v_cmp_gt_f32_e32 vcc, s21, v2
	v_lshlrev_b32_e32 v6, 16, v114
	v_lshlrev_b32_e32 v7, 16, v115
	v_cndmask_b32_e64 v5, 0, 32, vcc
	v_ldexp_f32 v2, v2, v5
	v_log_f32_e32 v2, v2
	s_nop 0
	v_mul_f32_e32 v5, 0x3f317217, v2
	v_fma_f32 v5, v2, s6, -v5
	v_fmac_f32_e32 v5, 0x3377d1cf, v2
	v_fmac_f32_e32 v5, 0x3f317217, v2
	v_cmp_lt_f32_e64 s[40:41], |v2|, s7
	s_nop 1
	v_cndmask_b32_e64 v2, v2, v5, s[40:41]
	v_cndmask_b32_e32 v5, 0, v193, vcc
	v_sub_f32_e32 v2, v2, v5
	v_add_f32_e32 v2, v3, v2
	v_mul_f32_e64 v3, v2, -v105
	v_add_f32_e32 v2, v104, v4
	v_max_f32_e32 v4, 0, v2
	v_mul_f32_e64 v2, |v2|, s1
	v_exp_f32_e32 v2, v2
	s_nop 0
	v_add_f32_e32 v2, 1.0, v2
	v_cmp_gt_f32_e32 vcc, s21, v2
	s_nop 1
	v_cndmask_b32_e64 v5, 0, 32, vcc
	v_ldexp_f32 v2, v2, v5
	v_log_f32_e32 v2, v2
	s_nop 0
	v_mul_f32_e32 v5, 0x3f317217, v2
	v_fma_f32 v5, v2, s6, -v5
	v_fmac_f32_e32 v5, 0x3377d1cf, v2
	v_fmac_f32_e32 v5, 0x3f317217, v2
	v_cmp_lt_f32_e64 s[40:41], |v2|, s7
	s_nop 1
	v_cndmask_b32_e64 v2, v2, v5, s[40:41]
	v_cndmask_b32_e32 v5, 0, v193, vcc
	v_sub_f32_e32 v2, v2, v5
	v_add_f32_e32 v2, v4, v2
	v_mul_f32_e64 v5, v2, -v106
	v_mul_f32_e32 v2, 0xbfb8aa3b, v6
	v_exp_f32_e32 v2, v2
	s_nop 0
	v_add_f32_e32 v2, 1.0, v2
	v_div_scale_f32 v4, s[6:7], v2, v2, 1.0
	v_rcp_f32_e32 v6, v4
	s_nop 0
	v_fma_f32 v8, -v4, v6, 1.0
	v_fmac_f32_e32 v6, v8, v6
	v_div_scale_f32 v8, vcc, 1.0, v2, 1.0
	v_mul_f32_e32 v9, v8, v6
	v_fma_f32 v10, -v4, v9, v8
	v_fmac_f32_e32 v9, v10, v6
	v_fma_f32 v4, -v4, v9, v8
	v_div_fmas_f32 v4, v4, v6, v9
	v_div_fixup_f32 v2, v4, v2, 1.0
	v_mul_f32_e32 v4, 0xbfb8aa3b, v7
	v_exp_f32_e32 v4, v4
	s_nop 0
	v_add_f32_e32 v4, 1.0, v4
	v_div_scale_f32 v6, s[6:7], v4, v4, 1.0
	v_rcp_f32_e32 v7, v6
	s_nop 0
	v_fma_f32 v8, -v6, v7, 1.0
	v_fmac_f32_e32 v7, v8, v7
	v_div_scale_f32 v8, vcc, 1.0, v4, 1.0
	v_mul_f32_e32 v9, v8, v7
	v_fma_f32 v10, -v6, v9, v8
	v_fmac_f32_e32 v9, v10, v7
	v_fma_f32 v6, -v6, v9, v8
	v_div_fmas_f32 v6, v6, v7, v9
	v_div_fixup_f32 v4, v6, v4, 1.0
	v_add_u32_e32 v6, s0, v107
	v_ashrrev_i32_e32 v7, 31, v6
	v_lshlrev_b64 v[6:7], 6, v[6:7]
	v_lshl_add_u64 v[6:7], v[14:15], 0, v[6:7]
	global_store_dwordx4 v[6:7], v[2:5], off
	s_branch .LBB0_301

; #define LAS __attribute__((address_space(3)))
; __device__ __forceinline__ unsigned f2bf(float f) { unsigned u = __float_as_uint(f); return (u + 0x7fffu + ((u >> 16) & 1u)) >> 16; }
; __device__ __forceinline__ u32x2 cvt4(f32x4 v) { return (u32x2){pk2(v[0], v[1]), pk2(v[2], v[3])}; }
; __device__ __forceinline__ void gla_s2(CArgs& a, int u, LAS unsigned char* ub, int w, int lane) {
;     ...
;     const int It = w & 3, vh = w >> 2;
;     const bf16x8 qf = *(const LAS bf16x8*)(QE + (16 * It + fr) * 40 + 8 * kg);
;     f32x4 st[4];
; #pragma unroll
;     for (int Jt = 0; Jt < 4; ++Jt) { const bf16x8 kf = *(const LAS bf16x8*)(KE + (16 * Jt + fr) * 40 + 8 * kg);
;         st[Jt] = __builtin_amdgcn_mfma_f32_16x16x32_bf16(kf, qf, (f32x4){0.f, 0.f, 0.f, 0.f}, 0, 0, 0);
; #pragma unroll
;         for (int e = 0; e < 4; ++e) st[Jt][e] = (16 * Jt + 4 * kg + e <= 16 * It + fr) ? st[Jt][e] : 0.f; }
;     const bf16x8 Sb01 = frag2(cvt4(st[0]), cvt4(st[1])), Sb23 = frag2(cvt4(st[2]), cvt4(st[3]));
;     bf16* ftp = FT + (4 * kg) * 64 + 16 * It + fr;
; #pragma unroll
;     for (int vv = 0; vv < 2; ++vv) { const int Vt = 2 * vh + vv; const LAS bf16* vr = VT + (16 * Vt + fr) * 72 + 4 * kg;
;         f32x4 f = (f32x4){0.f, 0.f, 0.f, 0.f};
;         f = __builtin_amdgcn_mfma_f32_16x16x32_bf16(frag2(*(const LAS u32x2*)vr, *(const LAS u32x2*)(vr + 16)), Sb01, f, 0, 0, 0);
;         f = __builtin_amdgcn_mfma_f32_16x16x32_bf16(frag2(*(const LAS u32x2*)(vr + 32), *(const LAS u32x2*)(vr + 48)), Sb23, f, 0, 0, 0);
; #pragma unroll
;         for (int e = 0; e < 4; ++e) ftp[(16 * Vt + e) * 64] = (bf16)f2bf(f[e]); }
;     const int kt = w & 1, Vu = w >> 1;
;     f32x4 uu = (f32x4){0.f, 0.f, 0.f, 0.f};
; #pragma unroll
;     for (int s = 0; s < 2; ++s) uu = __builtin_amdgcn_mfma_f32_16x16x32_bf16(*(const LAS bf16x8*)(KTT + (16 * kt + fr) * 72 + 32 * s + 8 * kg), *(const LAS bf16x8*)(VT + (16 * Vu + fr) * 72 + 32 * s + 8 * kg), uu, 0, 0, 0);
;     *(u32x2*)(UT + (16 * Vu + fr) * 32 + 16 * kt + 4 * kg) = cvt4(uu);
.LBB0_369:
	v_and_b32_e32 v7, 15, v1
	v_and_b32_e32 v2, -16, v1
	v_or_b32_e32 v4, s68, v7
	v_add_u32_e32 v2, 0, v2
	v_mad_u32_u24 v5, v4, s33, v2
	ds_read_b128 v[8:11], v5 offset:24064
	v_mad_u32_u24 v5, v7, s33, v2
	ds_read_b128 v[12:15], v5 offset:29184
	v_ashrrev_i32_e32 v3, 4, v1
	v_lshlrev_b32_e32 v6, 2, v3
	v_cmp_le_i32_e32 vcc, v6, v4
	v_add_u32_e32 v20, 16, v6
	s_waitcnt vmcnt(13)
	v_add_u32_e32 v24, 32, v6
	s_waitcnt lgkmcnt(0)
	v_mfma_f32_16x16x32_bf16 v[12:15], v[12:15], v[8:11], 0
	s_add_i32 s54, s54, 2
	s_lshl_b64 s[2:3], s[78:79], 13
	s_add_u32 s2, s31, s2
	s_waitcnt vmcnt(9)
	s_nop 3
	v_cndmask_b32_e32 v16, 0, v12, vcc
	v_cmp_lt_i32_e32 vcc, v6, v4
	v_or_b32_e32 v12, 2, v6
	s_addc_u32 s3, s44, s3
	v_cndmask_b32_e32 v17, 0, v13, vcc
	v_cmp_le_i32_e32 vcc, v12, v4
	v_or_b32_e32 v12, 3, v6
	s_mov_b32 s27, s79
	v_cndmask_b32_e32 v18, 0, v14, vcc
	v_cmp_le_i32_e32 vcc, v12, v4
	v_lshlrev_b32_e32 v34, 1, v7
	s_mov_b32 s29, s79
	v_cndmask_b32_e32 v19, 0, v15, vcc
	ds_read_b128 v[12:15], v5 offset:30464
	s_waitcnt lgkmcnt(0)
	v_mfma_f32_16x16x32_bf16 v[12:15], v[12:15], v[8:11], 0
	v_cmp_le_i32_e32 vcc, v20, v4
	s_nop 6
	v_cndmask_b32_e32 v20, 0, v12, vcc
	v_add_u32_e32 v12, 17, v6
	v_cmp_le_i32_e32 vcc, v12, v4
	v_add_u32_e32 v12, 18, v6
	s_nop 0
	v_cndmask_b32_e32 v21, 0, v13, vcc
	v_cmp_le_i32_e32 vcc, v12, v4
	v_add_u32_e32 v12, 19, v6
	s_nop 0
	v_cndmask_b32_e32 v22, 0, v14, vcc
	v_cmp_le_i32_e32 vcc, v12, v4
	s_nop 1
	v_cndmask_b32_e32 v23, 0, v15, vcc
	ds_read_b128 v[12:15], v5 offset:31744
	s_waitcnt lgkmcnt(0)
	v_mfma_f32_16x16x32_bf16 v[12:15], v[12:15], v[8:11], 0
	v_cmp_le_i32_e32 vcc, v24, v4
	s_nop 6
	v_cndmask_b32_e32 v24, 0, v12, vcc
	v_add_u32_e32 v12, 33, v6
	v_cmp_le_i32_e32 vcc, v12, v4
	v_add_u32_e32 v12, 34, v6
	s_nop 0
	v_cndmask_b32_e32 v25, 0, v13, vcc
	v_cmp_le_i32_e32 vcc, v12, v4
	v_add_u32_e32 v12, 35, v6
	s_nop 0
	v_cndmask_b32_e32 v26, 0, v14, vcc
	v_cmp_le_i32_e32 vcc, v12, v4
	s_nop 1
	v_cndmask_b32_e32 v27, 0, v15, vcc
	ds_read_b128 v[12:15], v5 offset:33024
	s_waitcnt lgkmcnt(0)
	v_mfma_f32_16x16x32_bf16 v[8:11], v[12:15], v[8:11], 0
	v_add_u32_e32 v5, 48, v6
	v_cmp_le_i32_e32 vcc, v5, v4
	s_nop 3
	s_nop 1
	v_cndmask_b32_e32 v5, 0, v8, vcc
	v_add_u32_e32 v8, 49, v6
	v_cmp_le_i32_e32 vcc, v8, v4
	v_add_u32_e32 v8, 50, v6
	s_nop 0
	v_cndmask_b32_e32 v14, 0, v9, vcc
	v_cmp_le_i32_e32 vcc, v8, v4
	v_add_u32_e32 v8, 51, v6
	s_nop 0
	v_cndmask_b32_e32 v15, 0, v10, vcc
	v_cmp_le_i32_e32 vcc, v8, v4
	v_cvt_pk_bf16_f32 v8, v16, v17
	v_cvt_pk_bf16_f32 v9, v18, v19
	v_cndmask_b32_e32 v4, 0, v11, vcc
	v_cvt_pk_bf16_f32 v10, v20, v21
	v_cvt_pk_bf16_f32 v11, v22, v23
	v_cvt_pk_bf16_f32 v12, v24, v25
	v_cvt_pk_bf16_f32 v13, v26, v27
	v_cvt_pk_bf16_f32 v14, v5, v14
	v_cvt_pk_bf16_f32 v15, v15, v4
	v_lshlrev_b32_e32 v4, 8, v3
	v_ashrrev_i32_e32 v5, 31, v4
	v_lshl_add_u32 v24, v3, 3, 0
	v_or_b32_e32 v3, s45, v7
	v_lshl_add_u64 v[4:5], v[4:5], 1, s[2:3]
	v_mad_u64_u32 v[16:17], s[2:3], v3, s75, v[24:25]
	v_add_u32_e32 v3, 0x9800, v16
	ds_read2_b64 v[16:19], v3 offset1:4
	ds_read2_b64 v[20:23], v3 offset0:8 offset1:12
	s_waitcnt lgkmcnt(1)
	v_mfma_f32_16x16x32_bf16 v[16:19], v[16:19], v[8:11], 0
	v_lshl_add_u64 v[4:5], v[4:5], 0, s[26:27]
	v_lshl_add_u64 v[4:5], v[4:5], 0, v[34:35]
	s_waitcnt lgkmcnt(0)
	v_mfma_f32_16x16x32_bf16 v[16:19], v[20:23], v[12:15], v[16:19]
	v_lshl_add_u64 v[20:21], s[92:93], 1, v[4:5]
	s_nop 6
	v_cvt_pk_bf16_f32 v3, v16, v16
	global_store_short v[20:21], v3, off
	v_cvt_pk_bf16_f32 v3, v17, v17
	global_store_short v[20:21], v3, off offset:128
	v_cvt_pk_bf16_f32 v3, v18, v18
	global_store_short v[20:21], v3, off offset:256
	v_cvt_pk_bf16_f32 v3, v19, v19
	global_store_short v[20:21], v3, off offset:384
	v_or_b32_e32 v3, s47, v7
	v_mad_u64_u32 v[16:17], s[2:3], v3, s75, v[24:25]
	v_add_u32_e32 v3, 0x9800, v16
	ds_read2_b64 v[16:19], v3 offset1:4
	s_waitcnt lgkmcnt(0)
	v_mfma_f32_16x16x32_bf16 v[8:11], v[16:19], v[8:11], 0
	ds_read2_b64 v[16:19], v3 offset0:8 offset1:12
	s_waitcnt lgkmcnt(0)
	v_mfma_f32_16x16x32_bf16 v[8:11], v[16:19], v[12:15], v[8:11]
	v_lshl_add_u64 v[12:13], s[94:95], 1, v[4:5]
	s_nop 6
	v_cvt_pk_bf16_f32 v3, v8, v8
	global_store_short v[12:13], v3, off
	v_cvt_pk_bf16_f32 v3, v9, v9
	v_lshl_add_u64 v[8:9], s[96:97], 1, v[4:5]
	global_store_short v[8:9], v3, off
	v_cvt_pk_bf16_f32 v3, v10, v10
	v_lshl_add_u64 v[8:9], s[58:59], 1, v[4:5]
	global_store_short v[8:9], v3, off
	v_cvt_pk_bf16_f32 v3, v11, v11
	v_lshl_add_u64 v[4:5], s[4:5], 1, v[4:5]
	global_store_short v[4:5], v3, off
	v_or_b32_e32 v3, s67, v7
	v_mad_u32_u24 v14, v3, s75, v2
	v_or_b32_e32 v3, s46, v7
	v_mad_u64_u32 v[8:9], s[2:3], v3, s75, v[2:3]
	ds_read_b128 v[2:5], v14 offset:34304
	ds_read_b128 v[10:13], v8 offset:38912
	s_waitcnt lgkmcnt(0)
	v_mfma_f32_16x16x32_bf16 v[2:5], v[2:5], v[10:13], 0
	ds_read_b128 v[10:13], v14 offset:34368
	ds_read_b128 v[14:17], v8 offset:38976
	s_add_u32 s2, s74, s76
	s_addc_u32 s3, s22, s77
	s_waitcnt lgkmcnt(0)
	v_mfma_f32_16x16x32_bf16 v[2:5], v[10:13], v[14:17], v[2:5]
	s_add_i32 s9, s9, 2
	s_addk_i32 s20, 0x80
	s_addk_i32 s0, 0xff80
	s_nop 4
	v_bfe_u32 v8, v2, 16, 1
	v_add3_u32 v2, v2, v8, s81
	v_bfe_u32 v8, v3, 16, 1
	v_lshrrev_b32_e32 v2, 16, v2
	v_add3_u32 v3, v3, v8, s81
	v_and_or_b32 v2, v3, s80, v2
	v_cvt_pk_bf16_f32 v3, v4, v5
	v_lshl_or_b32 v4, v7, 5, s23
	v_ashrrev_i32_e32 v5, 31, v4
	v_lshl_add_u64 v[4:5], v[4:5], 1, s[2:3]
	v_lshl_add_u64 v[4:5], v[4:5], 0, s[28:29]
	v_ashrrev_i32_e32 v7, 31, v6
	v_lshl_add_u64 v[4:5], v[6:7], 1, v[4:5]
	s_addk_i32 s55, 0xff80
	s_andn2_b64 vcc, exec, s[48:49]
	global_store_dwordx2 v[4:5], v[2:3], off
	s_cbranch_vccz .LBB0_1679

; #define LAS __attribute__((address_space(3)))
; __device__ __forceinline__ void gla_s1(CArgs& a, int u, GlaIn& in, LAS unsigned char* ub, int w, int lane) {
;     ...
;         const int vv = 16 * (w - 4) + (lane & 15), tq = lane >> 4;
; #pragma unroll
;         for (int i = 0; i < 16; ++i) VT[vv * 72 + 16 * tq + i] = in.px[i];
; __device__ __forceinline__ void gla_s2(CArgs& a, int u, LAS unsigned char* ub, int w, int lane) {
;     const int fr = lane & 15, kg = lane >> 4;
;     bf16* FT = (bf16*)(a.ws + WS_CKA + CA_FT) + (size_t)u * 4096; bf16* UT = (bf16*)(a.ws + WS_CKA + CA_UT) + (size_t)u * 2048;
;     LAS bf16* QE = (LAS bf16*)ub; LAS bf16* KE = QE + 2560; LAS bf16* KTT = KE + 2560; LAS bf16* VT = KTT + 2304;
;     const int It = w & 3, vh = w >> 2;
;     const bf16x8 qf = *(const LAS bf16x8*)(QE + (16 * It + fr) * 40 + 8 * kg);
;     f32x4 st[4];
; #pragma unroll
;     for (int Jt = 0; Jt < 4; ++Jt) { const bf16x8 kf = *(const LAS bf16x8*)(KE + (16 * Jt + fr) * 40 + 8 * kg);
;         st[Jt] = __builtin_amdgcn_mfma_f32_16x16x32_bf16(kf, qf, (f32x4){0.f, 0.f, 0.f, 0.f}, 0, 0, 0);
; #pragma unroll
;         for (int e = 0; e < 4; ++e) st[Jt][e] = (16 * Jt + 4 * kg + e <= 16 * It + fr) ? st[Jt][e] : 0.f; }
;     const bf16x8 Sb01 = frag2(cvt4(st[0]), cvt4(st[1])), Sb23 = frag2(cvt4(st[2]), cvt4(st[3]));
;     bf16* ftp = FT + (4 * kg) * 64 + 16 * It + fr;
; #pragma unroll
;     for (int vv = 0; vv < 2; ++vv) { const int Vt = 2 * vh + vv; const LAS bf16* vr = VT + (16 * Vt + fr) * 72 + 4 * kg;
;         f32x4 f = (f32x4){0.f, 0.f, 0.f, 0.f};
;         f = __builtin_amdgcn_mfma_f32_16x16x32_bf16(frag2(*(const LAS u32x2*)vr, *(const LAS u32x2*)(vr + 16)), Sb01, f, 0, 0, 0);
;         f = __builtin_amdgcn_mfma_f32_16x16x32_bf16(frag2(*(const LAS u32x2*)(vr + 32), *(const LAS u32x2*)(vr + 48)), Sb23, f, 0, 0, 0);
; #pragma unroll
;         for (int e = 0; e < 4; ++e) ftp[(16 * Vt + e) * 64] = (bf16)f2bf(f[e]); }
;     const int kt = w & 1, Vu = w >> 1;
;     f32x4 uu = (f32x4){0.f, 0.f, 0.f, 0.f};
; #pragma unroll
;     for (int s = 0; s < 2; ++s) uu = __builtin_amdgcn_mfma_f32_16x16x32_bf16(*(const LAS bf16x8*)(KTT + (16 * kt + fr) * 72 + 32 * s + 8 * kg), *(const LAS bf16x8*)(VT + (16 * Vu + fr) * 72 + 32 * s + 8 * kg), uu, 0, 0, 0);
;     *(u32x2*)(UT + (16 * Vu + fr) * 32 + 16 * kt + 4 * kg) = cvt4(uu);
; }
.LBB0_1022:
	global_load_ushort v159, v[2:3], off
	global_load_ushort v158, v[4:5], off
	global_load_ushort v60, v[6:7], off
	global_load_ushort v59, v[8:9], off
	global_load_ushort v58, v[10:11], off
	global_load_ushort v57, v[12:13], off
	global_load_ushort v56, v[14:15], off
	global_load_ushort v55, v[16:17], off
	global_load_ushort v54, v[18:19], off
	global_load_ushort v53, v[22:23], off
	global_load_ushort v43, v[24:25], off
	s_nop 0
	global_load_ushort v24, v[26:27], off
	global_load_ushort v23, v[28:29], off
	global_load_ushort v22, v[30:31], off
	global_load_ushort v18, v[32:33], off
	global_load_ushort v16, v[20:21], off
	v_or_b32_e32 v9, s68, v34
	v_add_u32_e32 v8, 0, v161
	v_mad_u32_u24 v2, v9, s33, v8
	v_mad_u32_u24 v14, v34, s33, v8
	ds_read_b128 v[2:5], v2
	ds_read_b128 v[10:13], v14 offset:5120
	v_ashrrev_i32_e32 v7, 4, v1
	v_lshlrev_b32_e32 v6, 2, v7
	v_cmp_le_i32_e32 vcc, v6, v9
	v_add_u32_e32 v21, 16, v6
	s_waitcnt lgkmcnt(0)
	v_mfma_f32_16x16x32_bf16 v[10:13], v[10:13], v[2:5], 0
	v_add_u32_e32 v28, 32, v6
	s_lshl_b64 s[2:3], s[78:79], 13
	s_add_u32 s2, s31, s2
	s_nop 4
	v_cndmask_b32_e32 v15, 0, v10, vcc
	v_cmp_lt_i32_e32 vcc, v6, v9
	v_or_b32_e32 v10, 2, v6
	s_addc_u32 s3, s44, s3
	v_cndmask_b32_e32 v17, 0, v11, vcc
	v_cmp_le_i32_e32 vcc, v10, v9
	v_or_b32_e32 v10, 3, v6
	s_lshl_b32 s26, s68, 1
	v_cndmask_b32_e32 v19, 0, v12, vcc
	v_cmp_le_i32_e32 vcc, v10, v9
	s_mov_b32 s27, s79
	s_nop 0
	v_cndmask_b32_e32 v20, 0, v13, vcc
	ds_read_b128 v[10:13], v14 offset:6400
	s_waitcnt lgkmcnt(0)
	v_mfma_f32_16x16x32_bf16 v[10:13], v[10:13], v[2:5], 0
	v_cmp_le_i32_e32 vcc, v21, v9
	s_nop 6
	v_cndmask_b32_e32 v21, 0, v10, vcc
	v_add_u32_e32 v10, 17, v6
	v_cmp_le_i32_e32 vcc, v10, v9
	v_add_u32_e32 v10, 18, v6
	s_nop 0
	v_cndmask_b32_e32 v25, 0, v11, vcc
	v_cmp_le_i32_e32 vcc, v10, v9
	v_add_u32_e32 v10, 19, v6
	s_nop 0
	v_cndmask_b32_e32 v26, 0, v12, vcc
	v_cmp_le_i32_e32 vcc, v10, v9
	s_nop 1
	v_cndmask_b32_e32 v27, 0, v13, vcc
	ds_read_b128 v[10:13], v14 offset:7680
	s_waitcnt lgkmcnt(0)
	v_mfma_f32_16x16x32_bf16 v[10:13], v[10:13], v[2:5], 0
	v_cmp_le_i32_e32 vcc, v28, v9
	s_nop 6
	v_cndmask_b32_e32 v28, 0, v10, vcc
	v_add_u32_e32 v10, 33, v6
	v_cmp_le_i32_e32 vcc, v10, v9
	v_add_u32_e32 v10, 34, v6
	s_nop 0
	v_cndmask_b32_e32 v29, 0, v11, vcc
	v_cmp_le_i32_e32 vcc, v10, v9
	v_add_u32_e32 v10, 35, v6
	s_nop 0
	v_cndmask_b32_e32 v30, 0, v12, vcc
	v_cmp_le_i32_e32 vcc, v10, v9
	s_nop 1
	v_cndmask_b32_e32 v31, 0, v13, vcc
	ds_read_b128 v[10:13], v14 offset:8960
	s_waitcnt lgkmcnt(0)
	v_mfma_f32_16x16x32_bf16 v[2:5], v[10:13], v[2:5], 0
	v_add_u32_e32 v10, 48, v6
	v_cmp_le_i32_e32 vcc, v10, v9
	s_nop 3
	s_nop 1
	v_cndmask_b32_e32 v12, 0, v2, vcc
	v_add_u32_e32 v2, 49, v6
	v_cmp_le_i32_e32 vcc, v2, v9
	v_add_u32_e32 v2, 50, v6
	s_nop 0
	v_cndmask_b32_e32 v13, 0, v3, vcc
	v_cmp_le_i32_e32 vcc, v2, v9
	v_add_u32_e32 v2, 51, v6
	s_nop 0
	v_cndmask_b32_e32 v14, 0, v4, vcc
	v_cmp_le_i32_e32 vcc, v2, v9
	v_cvt_pk_bf16_f32 v2, v15, v17
	v_cvt_pk_bf16_f32 v3, v19, v20
	v_cndmask_b32_e32 v9, 0, v5, vcc
	v_cvt_pk_bf16_f32 v4, v21, v25
	v_cvt_pk_bf16_f32 v5, v26, v27
	v_cvt_pk_bf16_f32 v10, v28, v29
	v_cvt_pk_bf16_f32 v11, v30, v31
	v_cvt_pk_bf16_f32 v12, v12, v13
	v_bfe_u32 v13, v14, 16, 1
	v_add3_u32 v13, v14, v13, s81
	v_bfe_u32 v14, v9, 16, 1
	v_add3_u32 v9, v9, v14, s81
	v_lshlrev_b32_e32 v14, 8, v7
	v_ashrrev_i32_e32 v15, 31, v14
	v_lshl_add_u32 v20, v7, 3, 0
	v_or_b32_e32 v7, s45, v34
	v_lshl_add_u64 v[14:15], v[14:15], 1, s[2:3]
	v_mad_u64_u32 v[26:27], s[2:3], v7, s75, v[20:21]
	v_add_u32_e32 v7, 0x3800, v26
	ds_read2_b64 v[26:29], v7 offset0:64 offset1:68
	ds_read2_b64 v[30:33], v7 offset0:72 offset1:76
	s_waitcnt lgkmcnt(1)
	v_mfma_f32_16x16x32_bf16 v[26:29], v[26:29], v[2:5], 0
	v_lshrrev_b32_e32 v13, 16, v13
	v_and_or_b32 v13, v9, s80, v13
	v_lshl_add_u64 v[14:15], v[14:15], 0, s[26:27]
	v_lshl_add_u64 v[14:15], v[34:35], 1, v[14:15]
	s_waitcnt lgkmcnt(0)
	v_mfma_f32_16x16x32_bf16 v[26:29], v[30:33], v[10:13], v[26:29]
	v_lshl_add_u64 v[30:31], s[92:93], 1, v[14:15]
	s_nop 6
	v_cvt_pk_bf16_f32 v7, v26, v26
	global_store_short v[30:31], v7, off
	v_cvt_pk_bf16_f32 v7, v27, v27
	global_store_short v[30:31], v7, off offset:128
	v_cvt_pk_bf16_f32 v7, v28, v28
	global_store_short v[30:31], v7, off offset:256
	v_cvt_pk_bf16_f32 v7, v29, v29
	global_store_short v[30:31], v7, off offset:384
	v_or_b32_e32 v7, s47, v34
	v_mad_u64_u32 v[20:21], s[2:3], v7, s75, v[20:21]
	v_add_u32_e32 v7, 0x3800, v20
	ds_read2_b64 v[26:29], v7 offset0:64 offset1:68
	s_waitcnt lgkmcnt(0)
	v_mfma_f32_16x16x32_bf16 v[2:5], v[26:29], v[2:5], 0
	ds_read2_b64 v[26:29], v7 offset0:72 offset1:76
	s_waitcnt lgkmcnt(0)
	v_mfma_f32_16x16x32_bf16 v[2:5], v[26:29], v[10:13], v[2:5]
	v_lshl_add_u64 v[10:11], s[94:95], 1, v[14:15]
	s_nop 6
	v_cvt_pk_bf16_f32 v2, v2, v2
	global_store_short v[10:11], v2, off
	v_cvt_pk_bf16_f32 v7, v3, v3
	v_lshl_add_u64 v[2:3], s[96:97], 1, v[14:15]
	global_store_short v[2:3], v7, off
	v_cvt_pk_bf16_f32 v4, v4, v4
	v_lshl_add_u64 v[2:3], s[58:59], 1, v[14:15]
	global_store_short v[2:3], v4, off
	v_cvt_pk_bf16_f32 v4, v5, v5
	v_lshl_add_u64 v[2:3], s[4:5], 1, v[14:15]
	global_store_short v[2:3], v4, off
	v_or_b32_e32 v2, s67, v34
	v_mad_u32_u24 v7, v2, s75, v8
	v_or_b32_e32 v2, s46, v34
	v_mad_u64_u32 v[8:9], s[2:3], v2, s75, v[8:9]
	ds_read_b128 v[2:5], v7 offset:10240
	ds_read_b128 v[10:13], v8 offset:14848
	s_waitcnt lgkmcnt(0)
	v_mfma_f32_16x16x32_bf16 v[2:5], v[2:5], v[10:13], 0
	ds_read_b128 v[10:13], v7 offset:10304
	ds_read_b128 v[26:29], v8 offset:14912
	s_add_u32 s2, s74, s28
	s_addc_u32 s3, s22, s29
	s_waitcnt lgkmcnt(0)
	v_mfma_f32_16x16x32_bf16 v[2:5], v[10:13], v[26:29], v[2:5]
	s_lshl_b32 s28, s67, 1
	s_mov_b32 s29, s79
	s_and_b64 vcc, s[38:39], exec
	s_nop 4
	v_cvt_pk_bf16_f32 v2, v2, v3
	v_cvt_pk_bf16_f32 v3, v4, v5
	v_lshl_or_b32 v4, v34, 5, s23
	v_ashrrev_i32_e32 v5, 31, v4
	v_lshl_add_u64 v[4:5], v[4:5], 1, s[2:3]
	v_lshl_add_u64 v[4:5], v[4:5], 0, s[28:29]
	v_ashrrev_i32_e32 v7, 31, v6
	v_lshl_add_u64 v[4:5], v[6:7], 1, v[4:5]
	s_mov_b64 s[2:3], -1
	global_store_dwordx2 v[4:5], v[2:3], off
	s_cbranch_vccz .LBB0_1024
	v_and_or_b32 v2, v1, 15, s34
	v_and_b32_e32 v3, 0x7ffffff0, v1
	v_mul_lo_u32 v2, v2, s75
	v_lshlrev_b32_e32 v3, 1, v3
	s_mov_b32 s2, 0x5040100
	v_add3_u32 v6, 0, v2, v3
	s_waitcnt vmcnt(17)
	v_perm_b32 v5, v55, v56, s2
	v_perm_b32 v4, v57, v58, s2
	v_perm_b32 v3, v59, v60, s2
	v_perm_b32 v2, v158, v159, s2
	ds_write_b128 v6, v[2:5] offset:38912
	s_waitcnt vmcnt(9)
	v_perm_b32 v5, v16, v18, s2
	v_perm_b32 v4, v22, v23, s2
	v_perm_b32 v3, v24, v43, s2
	v_perm_b32 v2, v53, v54, s2
	ds_write_b128 v6, v[2:5] offset:38928
	s_mov_b64 s[2:3], 0

; #define LAS __attribute__((address_space(3)))
; __device__ __forceinline__ unsigned f2bf(float f) { unsigned u = __float_as_uint(f); return (u + 0x7fffu + ((u >> 16) & 1u)) >> 16; }
; __device__ __forceinline__ float rdlane_f(float v, int l) { return __builtin_bit_cast(float, __builtin_amdgcn_readlane(__builtin_bit_cast(int, v), l)); }
; __device__ __forceinline__ float gdn_s1(const GdnIn& in, LAS unsigned char* ub, LAS unsigned char* dwb, int w, int lane) {
;     ...
;     float beta = in.g2.x, cum = in.g2.y;
; #pragma unroll
;     for (int o = 1; o < 64; o <<= 1) { const float t = __shfl_up(cum, o); if (lane >= o) cum += t; }
;     const float cl = rdlane_f(cum, 63);
;     GT[lane] = beta; GT[64 + lane] = cum; GT[128 + lane] = __expf(cum);
;     asm volatile("s_waitcnt lgkmcnt(0)" ::: "memory");
;     { const f32x4 ci = *(const LAS f32x4*)(GT + 64 + 16 * I1 + 4 * kg), bi = *(const LAS f32x4*)(GT + 16 * I1 + 4 * kg);
; #pragma unroll
;       for (int jj = 0; jj < 2; ++jj) { const int J = 2 * (w & 1) + jj;
;           f32x4 ck = (f32x4){0.f, 0.f, 0.f, 0.f}, cq = (f32x4){0.f, 0.f, 0.f, 0.f};
; #pragma unroll
;           for (int s = 0; s < 2; ++s) { ck = __builtin_amdgcn_mfma_f32_16x16x32_bf16(in.ak[s], in.bk[jj][s], ck, 0, 0, 0); cq = __builtin_amdgcn_mfma_f32_16x16x32_bf16(in.aq[s], in.bk[jj][s], cq, 0, 0, 0); }
;           const int j = 16 * J + fr; const float cj = GT[64 + j];
; #pragma unroll
;           for (int e = 0; e < 4; ++e) { const int i = 16 * I1 + 4 * kg + e; const float gm = __expf(fminf(ci[e] - cj, 0.f));
;               AB[i * 72 + j] = (bf16)f2bf(j < i ? bi[e] * ck[e] * gm : 0.f); ATT[i * 72 + j] = (bf16)f2bf(j <= i ? cq[e] * gm : 0.f); } } }
.LBB0_1719:
	v_and_b32_e32 v32, 64, v195
	v_add_u32_e32 v33, -1, v195
	v_cmp_lt_i32_e32 vcc, v33, v32
	v_add_u32_e32 v46, -2, v195
	v_add_u32_e32 v67, s42, v54
	v_cndmask_b32_e32 v33, v33, v195, vcc
	v_lshlrev_b32_e32 v125, 2, v33
	ds_bpermute_b32 v33, v125, v113
	v_cmp_gt_i32_e32 vcc, 1, v110
	v_mfma_f32_16x16x32_bf16 v[58:61], v[6:9], v[10:13], 0
	s_movk_i32 s2, 0x48
	v_or_b32_e32 v69, 1, v67
	s_waitcnt lgkmcnt(0)
	v_add_f32_e32 v33, v113, v33
	v_cndmask_b32_e32 v33, v33, v113, vcc
	v_cmp_lt_i32_e32 vcc, v46, v32
	v_or_b32_e32 v70, 2, v67
	s_add_i32 s28, s26, 1
	v_cndmask_b32_e32 v46, v46, v195, vcc
	v_lshlrev_b32_e32 v126, 2, v46
	ds_bpermute_b32 v46, v126, v33
	v_cmp_gt_i32_e32 vcc, 2, v110
	s_mov_b64 s[48:49], -1
	s_waitcnt lgkmcnt(0)
	v_add_f32_e32 v46, v33, v46
	v_cndmask_b32_e32 v33, v46, v33, vcc
	v_add_u32_e32 v46, -4, v195
	v_cmp_lt_i32_e32 vcc, v46, v32
	s_nop 1
	v_cndmask_b32_e32 v46, v46, v195, vcc
	v_lshlrev_b32_e32 v127, 2, v46
	ds_bpermute_b32 v46, v127, v33
	v_cmp_gt_i32_e32 vcc, 4, v110
	s_waitcnt lgkmcnt(0)
	v_add_f32_e32 v46, v33, v46
	v_cndmask_b32_e32 v33, v46, v33, vcc
	v_add_u32_e32 v46, -8, v195
	v_cmp_lt_i32_e32 vcc, v46, v32
	s_nop 1
	v_cndmask_b32_e32 v46, v46, v195, vcc
	v_lshlrev_b32_e32 v128, 2, v46
	ds_bpermute_b32 v46, v128, v33
	v_cmp_gt_i32_e32 vcc, 8, v110
	s_waitcnt lgkmcnt(0)
	v_add_f32_e32 v46, v33, v46
	v_cndmask_b32_e32 v33, v46, v33, vcc
	v_add_u32_e32 v46, -16, v195
	v_cmp_lt_i32_e32 vcc, v46, v32
	s_nop 1
	v_cndmask_b32_e32 v46, v46, v195, vcc
	v_lshlrev_b32_e32 v129, 2, v46
	ds_bpermute_b32 v46, v129, v33
	v_cmp_gt_i32_e32 vcc, 16, v110
	s_waitcnt lgkmcnt(0)
	v_add_f32_e32 v46, v33, v46
	v_cndmask_b32_e32 v33, v46, v33, vcc
	v_subrev_u32_e32 v46, 32, v195
	v_cmp_lt_i32_e32 vcc, v46, v32
	s_nop 1
	v_cndmask_b32_e32 v32, v46, v195, vcc
	v_lshlrev_b32_e32 v130, 2, v32
	ds_bpermute_b32 v32, v130, v33
	v_cmp_gt_i32_e32 vcc, 32, v110
	s_waitcnt lgkmcnt(0)
	v_add_f32_e32 v32, v33, v32
	v_cndmask_b32_e32 v66, v32, v33, vcc
	v_mul_f32_e32 v33, 0x3fb8aa3b, v66
	v_exp_f32_e32 v33, v33
	v_lshl_add_u32 v32, v110, 2, s8
	ds_write2st64_b32 v32, v112, v66 offset0:224 offset1:225
	v_readlane_b32 s36, v66, 63
	ds_write_b32 v32, v33 offset:57856
	s_waitcnt lgkmcnt(0)
	v_lshl_add_u32 v32, v54, 2, s30
	v_mfma_f32_16x16x32_bf16 v[54:57], v[2:5], v[10:13], 0
	ds_read_b128 v[50:53], v32 offset:57600
	ds_read_b128 v[46:49], v32 offset:57344
	v_or_b32_e32 v32, s43, v119
	v_lshl_add_u32 v33, v32, 2, s8
	v_add_u32_e32 v33, 0xe000, v33
	v_mfma_f32_16x16x32_bf16 v[62:65], v[18:21], v[26:29], v[54:57]
	v_cmp_lt_i32_e32 vcc, v32, v67
	s_nop 1
	ds_read2_b32 v[54:55], v33 offset0:64 offset1:80
	v_mfma_f32_16x16x32_bf16 v[56:59], v[22:25], v[26:29], v[58:61]
	s_waitcnt lgkmcnt(0)
	v_sub_f32_e32 v33, v50, v54
	v_min_f32_e32 v33, 0, v33
	v_mul_f32_e32 v33, 0x3fb8aa3b, v33
	v_exp_f32_e32 v33, v33
	v_mul_f32_e32 v60, v46, v62
	v_sub_f32_e32 v50, v50, v55
	v_min_f32_e32 v50, 0, v50
	v_mul_f32_e32 v60, v60, v33
	v_cndmask_b32_e32 v60, 0, v60, vcc
	v_bfe_u32 v61, v60, 16, 1
	v_add3_u32 v62, v60, v61, s81
	v_mad_u64_u32 v[60:61], s[2:3], v67, s2, v[32:33]
	v_cmp_gt_i32_e32 vcc, v32, v67
	v_mul_f32_e32 v33, v56, v33
	v_lshl_add_u32 v68, v60, 1, 0
	v_cndmask_b32_e64 v33, v33, 0, vcc
	v_cvt_pk_bf16_f32 v33, v33, v33
	ds_write_b16 v68, v33 offset:9216
	v_sub_f32_e32 v33, v51, v54
	v_min_f32_e32 v33, 0, v33
	v_mul_f32_e32 v33, 0x3fb8aa3b, v33
	v_exp_f32_e32 v33, v33
	v_mul_f32_e32 v56, v47, v63
	v_mul_f32_e32 v50, 0x3fb8aa3b, v50
	ds_write_b16_d16_hi v68, v62
	v_mul_f32_e32 v56, v56, v33
	v_cndmask_b32_e64 v56, v56, 0, vcc
	v_bfe_u32 v60, v56, 16, 1
	v_mul_f32_e32 v33, v57, v33
	v_cmp_le_i32_e32 vcc, v32, v69
	v_add3_u32 v56, v56, v60, s81
	ds_write_b16_d16_hi v68, v56 offset:144
	v_cndmask_b32_e32 v33, 0, v33, vcc
	v_cvt_pk_bf16_f32 v33, v33, v33
	ds_write_b16 v68, v33 offset:9360
	v_sub_f32_e32 v33, v52, v54
	v_min_f32_e32 v33, 0, v33
	v_mul_f32_e32 v33, 0x3fb8aa3b, v33
	v_exp_f32_e32 v33, v33
	v_mul_f32_e32 v56, v48, v64
	v_cmp_lt_i32_e32 vcc, v32, v70
	v_or_b32_e32 v64, 3, v67
	v_mul_f32_e32 v56, v56, v33
	v_cndmask_b32_e32 v56, 0, v56, vcc
	v_bfe_u32 v57, v56, 16, 1
	v_mul_f32_e32 v33, v58, v33
	v_cmp_le_i32_e32 vcc, v32, v70
	v_add3_u32 v56, v56, v57, s81
	ds_write_b16_d16_hi v68, v56 offset:288
	v_cndmask_b32_e32 v33, 0, v33, vcc
	v_cvt_pk_bf16_f32 v33, v33, v33
	ds_write_b16 v68, v33 offset:9504
	v_sub_f32_e32 v33, v53, v54
	v_min_f32_e32 v33, 0, v33
	v_mul_f32_e32 v33, 0x3fb8aa3b, v33
	v_exp_f32_e32 v33, v33
	v_mul_f32_e32 v54, v49, v65
	v_cmp_lt_i32_e32 vcc, v32, v64
	v_mfma_f32_16x16x32_bf16 v[60:63], v[6:9], v[14:17], 0
	v_mul_f32_e32 v54, v54, v33
	v_cndmask_b32_e32 v54, 0, v54, vcc
	v_bfe_u32 v56, v54, 16, 1
	v_add3_u32 v54, v54, v56, s81
	v_mul_f32_e32 v33, v59, v33
	v_mfma_f32_16x16x32_bf16 v[56:59], v[2:5], v[14:17], 0
	v_cmp_le_i32_e32 vcc, v32, v64
	v_exp_f32_e32 v50, v50
	ds_write_b16_d16_hi v68, v54 offset:432
	v_mfma_f32_16x16x32_bf16 v[56:59], v[18:21], v[36:39], v[56:59]
	v_cndmask_b32_e32 v33, 0, v33, vcc
	v_cvt_pk_bf16_f32 v33, v33, v33
; #define LAS __attribute__((address_space(3)))
; __device__ __forceinline__ unsigned f2bf(float f) { unsigned u = __float_as_uint(f); return (u + 0x7fffu + ((u >> 16) & 1u)) >> 16; }
; __device__ __forceinline__ float gdn_s1(const GdnIn& in, LAS unsigned char* ub, LAS unsigned char* dwb, int w, int lane) {
;     ...
;           const int j = 16 * J + fr; const float cj = GT[64 + j];
; #pragma unroll
;           for (int e = 0; e < 4; ++e) { const int i = 16 * I1 + 4 * kg + e; const float gm = __expf(fminf(ci[e] - cj, 0.f));
;               AB[i * 72 + j] = (bf16)f2bf(j < i ? bi[e] * ck[e] * gm : 0.f); ATT[i * 72 + j] = (bf16)f2bf(j <= i ? cq[e] * gm : 0.f); } } }
;     { const f32x4 c8a = *(const LAS f32x4*)(GT + 64 + 8 * w), c8b = *(const LAS f32x4*)(GT + 64 + 8 * w + 4);
; #pragma unroll
;       for (int tt = 0; tt < 8; ++tt) KTT[lane * 72 + 8 * w + tt] = (bf16)f2bf(__uint_as_float(in.kt8[tt] << 16) * __expf(cl - (tt < 4 ? c8a[tt & 3] : c8b[tt & 3]))); }
;     asm volatile("s_waitcnt lgkmcnt(0)" ::: "memory");
	ds_write_b16 v68, v33 offset:9648
	v_or_b32_e32 v33, 16, v32
	s_nop 2
	s_nop 0
	v_mul_f32_e32 v46, v46, v56
	v_mfma_f32_16x16x32_bf16 v[60:63], v[22:25], v[36:39], v[60:63]
	v_cmp_lt_i32_e32 vcc, v33, v67
	v_mul_f32_e32 v46, v46, v50
	v_mul_f32_e32 v47, v47, v57
	v_cndmask_b32_e32 v46, 0, v46, vcc
	v_cvt_pk_bf16_f32 v46, v46, v46
	ds_write_b16 v68, v46 offset:32
	v_cmp_gt_i32_e32 vcc, v33, v67
	s_nop 0
	v_mul_f32_e32 v46, v60, v50
	v_mul_lo_u32 v54, v110, s75
	v_cndmask_b32_e64 v46, v46, 0, vcc
	v_cvt_pk_bf16_f32 v46, v46, v46
	ds_write_b16 v68, v46 offset:9248
	v_sub_f32_e32 v46, v51, v55
	v_min_f32_e32 v46, 0, v46
	v_mul_f32_e32 v46, 0x3fb8aa3b, v46
	v_exp_f32_e32 v46, v46
	v_lshlrev_b32_e32 v57, 16, v1
	v_lshlrev_b32_e32 v56, 16, v30
	s_mov_b32 s2, 0x7060302
	v_mul_f32_e32 v47, v47, v46
	v_cndmask_b32_e64 v47, v47, 0, vcc
	v_mul_f32_e32 v46, v61, v46
	v_cmp_le_i32_e32 vcc, v33, v69
	v_cvt_pk_bf16_f32 v47, v47, v47
	ds_write_b16 v68, v47 offset:176
	v_cndmask_b32_e32 v46, 0, v46, vcc
	v_cvt_pk_bf16_f32 v46, v46, v46
	ds_write_b16 v68, v46 offset:9392
	v_sub_f32_e32 v46, v52, v55
	v_min_f32_e32 v46, 0, v46
	v_mul_f32_e32 v46, 0x3fb8aa3b, v46
	v_exp_f32_e32 v46, v46
	v_mul_f32_e32 v47, v48, v58
	v_cmp_lt_i32_e32 vcc, v33, v70
	v_mov_b32_e32 v50, s84
	v_mul_f32_e32 v47, v47, v46
	v_cndmask_b32_e32 v47, 0, v47, vcc
	v_mul_f32_e32 v46, v62, v46
	v_cmp_le_i32_e32 vcc, v33, v70
	v_cvt_pk_bf16_f32 v47, v47, v47
	ds_write_b16 v68, v47 offset:320
	v_cndmask_b32_e32 v46, 0, v46, vcc
	v_cvt_pk_bf16_f32 v46, v46, v46
	ds_write_b16 v68, v46 offset:9536
	v_sub_f32_e32 v46, v53, v55
	v_min_f32_e32 v46, 0, v46
	v_mul_f32_e32 v46, 0x3fb8aa3b, v46
	v_exp_f32_e32 v46, v46
	v_mul_f32_e32 v47, v49, v59
	v_cmp_lt_i32_e32 vcc, v33, v64
	v_add_u32_e32 v58, s11, v54
	v_mul_f32_e32 v47, v47, v46
	v_cndmask_b32_e32 v47, 0, v47, vcc
	v_mul_f32_e32 v46, v63, v46
	v_cmp_le_i32_e32 vcc, v33, v64
	v_cvt_pk_bf16_f32 v47, v47, v47
	ds_write_b16 v68, v47 offset:464
	v_cndmask_b32_e32 v46, 0, v46, vcc
	v_cvt_pk_bf16_f32 v46, v46, v46
	ds_write_b16 v68, v46 offset:9680
	ds_read_b128 v[46:49], v50 offset:57600
	ds_read_b128 v[50:53], v50 offset:57616
	v_lshlrev_b32_e32 v55, 16, v31
	v_lshlrev_b32_e32 v54, 16, v40
	s_waitcnt lgkmcnt(1)
	v_sub_f32_e32 v46, s36, v46
	v_sub_f32_e32 v47, s36, v47
	v_sub_f32_e32 v48, s36, v48
	v_sub_f32_e32 v49, s36, v49
	v_mul_f32_e32 v46, 0x3fb8aa3b, v46
	v_mul_f32_e32 v47, 0x3fb8aa3b, v47
	v_mul_f32_e32 v48, 0x3fb8aa3b, v48
	v_mul_f32_e32 v49, 0x3fb8aa3b, v49
	v_exp_f32_e32 v46, v46
	v_exp_f32_e32 v47, v47
	v_exp_f32_e32 v48, v48
	v_exp_f32_e32 v49, v49
	s_waitcnt lgkmcnt(0)
	v_sub_f32_e32 v50, s36, v50
	v_sub_f32_e32 v51, s36, v51
	v_sub_f32_e32 v52, s36, v52
	v_sub_f32_e32 v53, s36, v53
	v_mul_f32_e32 v50, 0x3fb8aa3b, v50
	v_mul_f32_e32 v51, 0x3fb8aa3b, v51
	v_mul_f32_e32 v52, 0x3fb8aa3b, v52
	v_mul_f32_e32 v53, 0x3fb8aa3b, v53
	v_exp_f32_e32 v50, v50
	v_exp_f32_e32 v51, v51
	v_exp_f32_e32 v52, v52
	v_exp_f32_e32 v53, v53
	v_pk_mul_f32 v[46:47], v[46:47], v[56:57]
	v_pk_mul_f32 v[48:49], v[48:49], v[54:55]
	v_bfe_u32 v56, v47, 16, 1
	v_bfe_u32 v54, v49, 16, 1
	v_bfe_u32 v55, v48, 16, 1
	v_bfe_u32 v57, v46, 16, 1
	v_add3_u32 v57, v46, v57, s81
	v_add3_u32 v56, v47, v56, s81
	v_add3_u32 v55, v48, v55, s81
	v_add3_u32 v54, v49, v54, s81
	v_lshlrev_b32_e32 v47, 16, v43
	v_lshlrev_b32_e32 v46, 16, v44
	v_lshlrev_b32_e32 v49, 16, v41
	v_lshlrev_b32_e32 v48, 16, v42
	v_pk_mul_f32 v[48:49], v[50:51], v[48:49]
	v_pk_mul_f32 v[46:47], v[52:53], v[46:47]
	v_bfe_u32 v52, v49, 16, 1
	v_bfe_u32 v50, v47, 16, 1
	v_bfe_u32 v51, v46, 16, 1
	v_bfe_u32 v53, v48, 16, 1
	v_add3_u32 v48, v48, v53, s81
	v_add3_u32 v52, v49, v52, s81
	v_add3_u32 v46, v46, v51, s81
	v_add3_u32 v47, v47, v50, s81
	v_perm_b32 v49, v47, v46, s2
	v_perm_b32 v48, v52, v48, s2
	v_perm_b32 v47, v54, v55, s2
	v_perm_b32 v46, v56, v57, s2
	s_mul_hi_i32 s2, s28, 0x38e38e39
	s_lshr_b32 s3, s2, 31
	s_ashr_i32 s9, s2, 3
	s_add_i32 s9, s9, s3
	s_mul_i32 s2, s9, 36
	s_sub_i32 s2, s28, s2
	ds_write_b128 v58, v[46:49] offset:18432
	s_ashr_i32 s29, s9, 3
	s_and_b32 s27, s9, 1
	s_lshl_b32 s20, s2, 6
	s_waitcnt lgkmcnt(0)
	s_cmp_gt_i32 s2, 3
	s_cselect_b64 s[56:57], -1, 0
	s_and_b64 vcc, exec, s[56:57]
	s_waitcnt lgkmcnt(0)
	s_barrier
	s_waitcnt vmcnt(0)
	v_lshlrev_b32_e32 v151, 16, v151
	v_lshlrev_b32_e32 v150, 16, v150
	v_lshlrev_b32_e32 v153, 16, v153
	v_lshlrev_b32_e32 v152, 16, v152
	v_lshlrev_b32_e32 v147, 16, v147
	v_lshlrev_b32_e32 v146, 16, v146
	v_lshlrev_b32_e32 v149, 16, v149
	v_lshlrev_b32_e32 v148, 16, v148
	v_lshlrev_b32_e32 v144, 16, v144
	v_lshlrev_b32_e32 v142, 16, v142
	v_lshlrev_b32_e32 v145, 16, v145
	v_lshlrev_b32_e32 v143, 16, v143
	v_lshlrev_b32_e32 v140, 16, v140
	v_lshlrev_b32_e32 v138, 16, v138
	v_lshlrev_b32_e32 v141, 16, v141
	v_lshlrev_b32_e32 v139, 16, v139
	s_cbranch_vccz .LBB0_1721
	s_add_i32 s2, s20, 0xffffff00
	s_lshl_b32 s3, s29, 11
	s_sub_i32 s48, 0x8ff, s20
	s_cmp_eq_u32 s27, 0
	s_cselect_b32 s2, s2, s48
	s_add_i32 s2, s3, s2
	s_addk_i32 s2, 0x1000
	s_mov_b64 s[48:49], 0

; #define LAS __attribute__((address_space(3)))
; __device__ __forceinline__ unsigned f2bf(float f) { unsigned u = __float_as_uint(f); return (u + 0x7fffu + ((u >> 16) & 1u)) >> 16; }
; __device__ __forceinline__ float lo_bf(unsigned w) { return __uint_as_float(w << 16); }
; __device__ __forceinline__ float hi_bf(unsigned w) { return __uint_as_float(w & 0xffff0000u); }
; __device__ __forceinline__ void gdn_fetch(CArgs& a, int u, int w, int lane, GdnIn& in) {
;     ...
;     in.g2 = *(const f32x2*)(DG + (size_t)(r0 + step * lane) * 16 + h * 4 + dir * 2);
; #pragma unroll
;     for (int s = 0; s < 2; ++s) { in.ak[s] = *(const bf16x8*)(KB + (ptrdiff_t)(16 * I1 + fr) * ldt + 32 * s + 8 * kg); in.aq[s] = *(const bf16x8*)(QB + (ptrdiff_t)(16 * I1 + fr) * ldt + 32 * s + 8 * kg);
; #pragma unroll
;         for (int jj = 0; jj < 2; ++jj) in.bk[jj][s] = *(const bf16x8*)(KB + (ptrdiff_t)(16 * (2 * (w & 1) + jj) + fr) * ldt + 32 * s + 8 * kg); }
; #pragma unroll
;     for (int tt = 0; tt < 8; ++tt) in.kt8[tt] = KB[(ptrdiff_t)(8 * w + tt) * ldt + lane];
; __device__ __forceinline__ void gdn_s23(CArgs& a, int u, const GdnIn2& in, LAS unsigned char* ub, LAS unsigned char* dwb, int w, int lane, float cl) {
;     ...
;     { const int blk = lane >> 4, c = lane & 15; float T[16];
; #pragma unroll
;       for (int hb = 0; hb < 4; ++hb) {
;           u32x4 arow[4][2];
; #pragma unroll
;           for (int rr = 0; rr < 4; ++rr) { const int r = 4 * hb + rr; arow[rr][0] = *(const LAS u32x4*)(AB + (16 * blk + r) * 72 + 16 * blk); if (hb >= 2) arow[rr][1] = *(const LAS u32x4*)(AB + (16 * blk + r) * 72 + 16 * blk + 8); }
;           asm volatile("s_waitcnt lgkmcnt(0)" ::: "memory");
; #pragma unroll
;           for (int rr = 0; rr < 4; ++rr) { const int r = 4 * hb + rr; float t = (r == c) ? 1.f : 0.f;
;               float t2 = 0.f;
; #pragma unroll
;               for (int j = 0; j < r; ++j) { const unsigned wv = arow[rr][j >> 3][(j >> 1) & 3]; const float av = (j & 1) ? hi_bf(wv) : lo_bf(wv); if (j & 1) t2 -= av * T[j]; else t -= av * T[j]; }
;               t += t2;
;               T[r] = t; DW[(blk * 16 + r) * 16 + c] = (bf16)f2bf(t); } } }
.LBB0_1723:
	s_bfe_u32 s76, s9, 0x20001
	s_cmp_eq_u32 s27, 0
	s_cselect_b64 s[52:53], -1, 0
	s_and_b64 s[48:49], s[52:53], exec
	s_cselect_b32 s77, 1, -1
	s_ashr_i32 s3, s2, 31
	s_lshl_b64 s[48:49], s[2:3], 9
	v_readlane_b32 s3, v251, 14
	s_add_u32 s3, s3, s48
	v_readlane_b32 s54, v249, 10
	s_addc_u32 s55, s54, s49
	s_lshl_b32 s62, s76, 7
	s_add_u32 s54, s3, s62
	s_addc_u32 s55, s55, 0
	s_add_u32 s3, s37, s48
	s_addc_u32 s49, s72, s49
	v_mul_lo_u32 v46, v110, s77
	s_add_u32 s48, s3, s62
	v_add_u32_e32 v46, s2, v46
	s_addc_u32 s49, s49, 0
	v_ashrrev_i32_e32 v47, 31, v46
	s_and_b64 s[62:63], s[52:53], exec
	s_movk_i32 s3, 0xff00
	v_lshlrev_b64 v[46:47], 6, v[46:47]
	s_cselect_b32 s62, 0x100, s3
	v_lshl_add_u64 v[46:47], s[6:7], 0, v[46:47]
	s_lshl_b32 s78, s76, 4
	v_lshl_add_u64 v[46:47], v[46:47], 0, s[78:79]
	s_lshl_b32 s78, s27, 3
	v_lshl_add_u64 v[46:47], v[46:47], 0, s[78:79]
	global_load_dwordx2 v[114:115], v[46:47], off
	v_or_b32_e32 v46, s42, v119
	v_ashrrev_i32_e32 v50, 1, v110
	v_mad_i64_i32 v[46:47], s[2:3], s62, v46, 0
	v_and_b32_e32 v50, -8, v50
	v_lshlrev_b64 v[46:47], 1, v[46:47]
	v_ashrrev_i32_e32 v51, 31, v50
	v_lshl_add_u64 v[48:49], s[54:55], 0, v[46:47]
	v_lshlrev_b64 v[50:51], 1, v[50:51]
	v_lshl_add_u64 v[46:47], s[48:49], 0, v[46:47]
	v_lshl_add_u64 v[52:53], v[48:49], 0, v[50:51]
	v_lshl_add_u64 v[54:55], v[46:47], 0, v[50:51]
	v_lshl_add_u64 v[50:51], s[54:55], 0, v[50:51]
	v_mul_hi_i32_i24_e32 v57, s62, v32
	v_mul_i32_i24_e32 v56, s62, v32
	v_lshl_add_u64 v[66:67], v[56:57], 1, v[50:51]
	v_mul_hi_i32_i24_e32 v57, s62, v33
	v_mul_i32_i24_e32 v56, s62, v33
	v_lshl_add_u64 v[32:33], v[56:57], 1, v[50:51]
	v_ashrrev_i32_e32 v111, 31, v110
	global_load_dwordx4 v[58:61], v[52:53], off
	global_load_dwordx4 v[46:49], v[54:55], off
	global_load_dwordx4 v[70:73], v[66:67], off
	global_load_dwordx4 v[62:65], v[32:33], off
	s_nop 0
	global_load_dwordx4 v[50:53], v[52:53], off offset:64
	s_nop 0
	global_load_dwordx4 v[54:57], v[54:55], off offset:64
	s_nop 0
	global_load_dwordx4 v[74:77], v[66:67], off offset:64
	s_nop 0
	global_load_dwordx4 v[66:69], v[32:33], off offset:64
	v_lshl_add_u64 v[32:33], v[110:111], 1, s[54:55]
	s_mul_hi_i32 s3, s62, s73
	s_mul_i32 s2, s62, s73
	v_lshl_add_u64 v[86:87], s[2:3], 1, v[32:33]
	s_mul_hi_i32 s3, s62, s16
	s_mul_i32 s2, s62, s16
	global_load_ushort v131, v[86:87], off
	v_lshl_add_u64 v[86:87], s[2:3], 1, v[32:33]
	s_mul_hi_i32 s3, s62, s17
	s_mul_i32 s2, s62, s17
	global_load_ushort v133, v[86:87], off
	v_lshl_add_u64 v[86:87], s[2:3], 1, v[32:33]
	s_mul_hi_i32 s3, s62, s35
	s_mul_i32 s2, s62, s35
	global_load_ushort v135, v[86:87], off
	v_lshl_add_u64 v[86:87], s[2:3], 1, v[32:33]
	s_mul_hi_i32 s3, s62, s14
	s_mul_i32 s2, s62, s14
	global_load_ushort v137, v[86:87], off
	v_lshl_add_u64 v[86:87], s[2:3], 1, v[32:33]
	s_mul_hi_i32 s3, s62, s82
	s_mul_i32 s2, s62, s82
	global_load_ushort v111, v[86:87], off
	v_lshl_add_u64 v[86:87], s[2:3], 1, v[32:33]
	s_mul_hi_i32 s3, s62, s83
	s_mul_i32 s2, s62, s83
	global_load_ushort v132, v[86:87], off
	v_lshl_add_u64 v[86:87], s[2:3], 1, v[32:33]
	s_mul_hi_i32 s3, s62, s10
	s_mul_i32 s2, s62, s10
	v_lshl_add_u64 v[32:33], s[2:3], 1, v[32:33]
	v_and_b32_e32 v85, -16, v110
	global_load_ushort v134, v[86:87], off
	global_load_ushort v136, v[32:33], off
	v_lshl_add_u32 v32, v85, 1, 0
	v_mad_u64_u32 v[154:155], s[2:3], v85, s75, v[32:33]
	ds_read_b128 v[86:89], v154 offset:432
	s_waitcnt lgkmcnt(0)
	ds_read2_b32 v[88:89], v154 offset0:36 offset1:72
	v_cmp_eq_u32_e32 vcc, 0, v119
	v_lshlrev_b32_e32 v33, 5, v110
	v_lshlrev_b32_e32 v118, 1, v119
	v_cndmask_b32_e64 v116, 0, 1.0, vcc
	v_and_b32_e32 v33, 0xfffffe00, v33
	v_cmp_eq_u32_e32 vcc, 1, v119
	v_add3_u32 v158, s8, v118, v33
	s_waitcnt lgkmcnt(0)
	v_lshlrev_b32_e32 v88, 16, v88
	v_cndmask_b32_e64 v33, 0, 1.0, vcc
	v_fma_f32 v159, -v116, v88, v33
	v_cvt_pk_bf16_f32 v33, v159, v159
	v_cmp_eq_u32_e32 vcc, 2, v119
	s_waitcnt lgkmcnt(0)
	ds_write_b16 v158, v33 offset:55328
	v_lshlrev_b32_e32 v88, 16, v89
	v_cndmask_b32_e64 v33, 0, 1.0, vcc
	v_fma_f32 v33, -v116, v88, v33
	v_and_b32_e32 v88, 0xffff0000, v89
	v_fma_f32 v88, -v159, v88, 0
	v_add_f32_e32 v161, v33, v88
	v_cvt_pk_bf16_f32 v33, v161, v161
	v_cmp_eq_u32_e32 vcc, 3, v119
	ds_write_b16 v158, v33 offset:55360
	v_lshlrev_b32_e32 v88, 16, v86
	v_cndmask_b32_e64 v33, 0, 1.0, vcc
	v_fma_f32 v33, -v116, v88, v33
	v_and_b32_e32 v86, 0xffff0000, v86
	v_lshlrev_b32_e32 v87, 16, v87
	v_fma_f32 v86, -v159, v86, 0
	v_fma_f32 v33, -v161, v87, v33
	v_add_f32_e32 v162, v86, v33
	v_cvt_pk_bf16_f32 v33, v162, v162
	ds_write_b16_d16_hi v158, v116 offset:55296
	ds_write_b16 v158, v33 offset:55392
	ds_read_b128 v[86:89], v154 offset:576
	ds_read_b128 v[94:97], v154 offset:720
	ds_read_b128 v[98:101], v154 offset:864
	ds_read_b128 v[102:105], v154 offset:1008
	v_cmp_eq_u32_e32 vcc, 4, v119
	s_waitcnt lgkmcnt(3)
	v_lshlrev_b32_e32 v88, 16, v86
	v_and_b32_e32 v86, 0xffff0000, v86
	v_cndmask_b32_e64 v33, 0, 1.0, vcc
	v_fma_f32 v33, -v116, v88, v33
	v_fma_f32 v86, -v159, v86, 0
	v_lshlrev_b32_e32 v88, 16, v87
	v_and_b32_e32 v87, 0xffff0000, v87
	v_fma_f32 v33, -v161, v88, v33
	v_fma_f32 v86, -v162, v87, v86
	v_add_f32_e32 v163, v86, v33
	v_cvt_pk_bf16_f32 v33, v163, v163
	v_cmp_eq_u32_e32 vcc, 5, v119
	s_waitcnt lgkmcnt(0)
	ds_write_b16 v158, v33 offset:55424
	s_waitcnt lgkmcnt(3)
	v_lshlrev_b32_e32 v86, 16, v94
	v_cndmask_b32_e64 v33, 0, 1.0, vcc
	v_fma_f32 v33, -v116, v86, v33
	v_and_b32_e32 v86, 0xffff0000, v94
	v_lshlrev_b32_e32 v87, 16, v95
	v_fma_f32 v86, -v159, v86, 0
	v_fma_f32 v33, -v161, v87, v33
	v_and_b32_e32 v87, 0xffff0000, v95
	v_fma_f32 v86, -v162, v87, v86
	v_lshlrev_b32_e32 v87, 16, v96
	v_fma_f32 v33, -v163, v87, v33
	v_add_f32_e32 v178, v86, v33
	v_cvt_pk_bf16_f32 v33, v178, v178
	v_cmp_eq_u32_e32 vcc, 6, v119
	ds_write_b16 v158, v33 offset:55456
	s_waitcnt lgkmcnt(3)
; #define LAS __attribute__((address_space(3)))
; __device__ __forceinline__ unsigned f2bf(float f) { unsigned u = __float_as_uint(f); return (u + 0x7fffu + ((u >> 16) & 1u)) >> 16; }
; __device__ __forceinline__ float lo_bf(unsigned w) { return __uint_as_float(w << 16); }
; __device__ __forceinline__ float hi_bf(unsigned w) { return __uint_as_float(w & 0xffff0000u); }
; __device__ __forceinline__ void gdn_s23(CArgs& a, int u, const GdnIn2& in, LAS unsigned char* ub, LAS unsigned char* dwb, int w, int lane, float cl) {
;     ...
;     { const int blk = lane >> 4, c = lane & 15; float T[16];
; #pragma unroll
;       for (int hb = 0; hb < 4; ++hb) {
;           u32x4 arow[4][2];
; #pragma unroll
;           for (int rr = 0; rr < 4; ++rr) { const int r = 4 * hb + rr; arow[rr][0] = *(const LAS u32x4*)(AB + (16 * blk + r) * 72 + 16 * blk); if (hb >= 2) arow[rr][1] = *(const LAS u32x4*)(AB + (16 * blk + r) * 72 + 16 * blk + 8); }
;           asm volatile("s_waitcnt lgkmcnt(0)" ::: "memory");
; #pragma unroll
;           for (int rr = 0; rr < 4; ++rr) { const int r = 4 * hb + rr; float t = (r == c) ? 1.f : 0.f;
;               float t2 = 0.f;
; #pragma unroll
;               for (int j = 0; j < r; ++j) { const unsigned wv = arow[rr][j >> 3][(j >> 1) & 3]; const float av = (j & 1) ? hi_bf(wv) : lo_bf(wv); if (j & 1) t2 -= av * T[j]; else t -= av * T[j]; }
;               t += t2;
;               T[r] = t; DW[(blk * 16 + r) * 16 + c] = (bf16)f2bf(t); } } }
	v_lshlrev_b32_e32 v86, 16, v98
	v_cndmask_b32_e64 v33, 0, 1.0, vcc
	v_fma_f32 v33, -v116, v86, v33
	v_and_b32_e32 v86, 0xffff0000, v98
	v_lshlrev_b32_e32 v87, 16, v99
	v_fma_f32 v86, -v159, v86, 0
	v_fma_f32 v33, -v161, v87, v33
	v_and_b32_e32 v87, 0xffff0000, v99
	v_fma_f32 v86, -v162, v87, v86
	v_lshlrev_b32_e32 v87, 16, v100
	v_fma_f32 v33, -v163, v87, v33
	v_and_b32_e32 v87, 0xffff0000, v100
	v_fma_f32 v86, -v178, v87, v86
	v_add_f32_e32 v179, v33, v86
	v_cvt_pk_bf16_f32 v33, v179, v179
	v_cmp_eq_u32_e32 vcc, 7, v119
	ds_write_b16 v158, v33 offset:55488
	s_waitcnt lgkmcnt(3)
	v_lshlrev_b32_e32 v86, 16, v102
	v_cndmask_b32_e64 v33, 0, 1.0, vcc
	v_fma_f32 v33, -v116, v86, v33
	v_and_b32_e32 v86, 0xffff0000, v102
	v_lshlrev_b32_e32 v87, 16, v103
	v_fma_f32 v86, -v159, v86, 0
	v_fma_f32 v33, -v161, v87, v33
	v_and_b32_e32 v87, 0xffff0000, v103
	v_fma_f32 v86, -v162, v87, v86
	v_lshlrev_b32_e32 v87, 16, v104
	v_fma_f32 v33, -v163, v87, v33
	v_and_b32_e32 v87, 0xffff0000, v104
	v_fma_f32 v86, -v178, v87, v86
	v_lshlrev_b32_e32 v87, 16, v105
	v_fma_f32 v33, -v179, v87, v33
	v_add_f32_e32 v180, v86, v33
	v_cvt_pk_bf16_f32 v33, v180, v180
	ds_write_b16 v158, v33 offset:55520
	ds_read_b128 v[86:89], v154 offset:1152
	ds_read_b128 v[94:97], v154 offset:1296
	ds_read_b128 v[98:101], v154 offset:1440
	ds_read_b128 v[102:105], v154 offset:1584
	ds_read_b128 v[106:109], v154 offset:1600
	v_add_u32_e32 v33, 0x400, v154
	v_cmp_eq_u32_e32 vcc, 8, v119
	s_waitcnt lgkmcnt(0)
	ds_read2_b32 v[108:109], v33 offset0:72 offset1:108
	v_lshlrev_b32_e32 v155, 16, v86
	v_cndmask_b32_e64 v33, 0, 1.0, vcc
	v_and_b32_e32 v86, 0xffff0000, v86
	v_fma_f32 v33, -v116, v155, v33
	v_fma_f32 v86, -v159, v86, 0
	v_lshlrev_b32_e32 v155, 16, v87
	v_and_b32_e32 v87, 0xffff0000, v87
	v_fma_f32 v33, -v161, v155, v33
	v_fma_f32 v86, -v162, v87, v86
	v_lshlrev_b32_e32 v87, 16, v88
	v_fma_f32 v33, -v163, v87, v33
	v_and_b32_e32 v87, 0xffff0000, v88
	v_fma_f32 v86, -v178, v87, v86
	v_lshlrev_b32_e32 v87, 16, v89
	v_fma_f32 v33, -v179, v87, v33
	v_and_b32_e32 v87, 0xffff0000, v89
	v_fma_f32 v86, -v180, v87, v86
	v_add_f32_e32 v181, v33, v86
	v_cvt_pk_bf16_f32 v33, v181, v181
	v_cmp_eq_u32_e32 vcc, 9, v119
	s_waitcnt lgkmcnt(0)
	ds_write_b16 v158, v33 offset:55552
	v_lshlrev_b32_e32 v86, 16, v94
	v_cndmask_b32_e64 v33, 0, 1.0, vcc
	v_fma_f32 v33, -v116, v86, v33
	v_and_b32_e32 v86, 0xffff0000, v94
	v_lshlrev_b32_e32 v87, 16, v95
	v_fma_f32 v86, -v159, v86, 0
	v_fma_f32 v33, -v161, v87, v33
	v_and_b32_e32 v87, 0xffff0000, v95
	v_fma_f32 v86, -v162, v87, v86
	v_lshlrev_b32_e32 v87, 16, v96
	v_fma_f32 v33, -v163, v87, v33
	v_and_b32_e32 v87, 0xffff0000, v96
	v_fma_f32 v86, -v178, v87, v86
	v_lshlrev_b32_e32 v87, 16, v97
	v_fma_f32 v33, -v179, v87, v33
	v_and_b32_e32 v87, 0xffff0000, v97
	v_fma_f32 v86, -v180, v87, v86
	s_waitcnt lgkmcnt(1)
	v_lshlrev_b32_e32 v87, 16, v108
	v_fma_f32 v33, -v181, v87, v33
	v_add_f32_e32 v108, v86, v33
	v_cvt_pk_bf16_f32 v33, v108, v108
	v_cmp_eq_u32_e32 vcc, 10, v119
	ds_write_b16 v158, v33 offset:55584
	v_lshlrev_b32_e32 v86, 16, v98
	v_cndmask_b32_e64 v33, 0, 1.0, vcc
	v_fma_f32 v33, -v116, v86, v33
	v_and_b32_e32 v86, 0xffff0000, v98
	v_lshlrev_b32_e32 v87, 16, v99
	v_fma_f32 v86, -v159, v86, 0
	v_fma_f32 v33, -v161, v87, v33
	v_and_b32_e32 v87, 0xffff0000, v99
	v_fma_f32 v86, -v162, v87, v86
	v_lshlrev_b32_e32 v87, 16, v100
	v_fma_f32 v33, -v163, v87, v33
	v_and_b32_e32 v87, 0xffff0000, v100
	v_fma_f32 v86, -v178, v87, v86
	v_lshlrev_b32_e32 v87, 16, v101
	v_fma_f32 v33, -v179, v87, v33
	v_and_b32_e32 v87, 0xffff0000, v101
	v_fma_f32 v86, -v180, v87, v86
	v_lshlrev_b32_e32 v87, 16, v109
	v_fma_f32 v33, -v181, v87, v33
	v_and_b32_e32 v87, 0xffff0000, v109
	v_fma_f32 v86, -v108, v87, v86
	v_add_f32_e32 v109, v33, v86
	v_cvt_pk_bf16_f32 v33, v109, v109
	v_cmp_eq_u32_e32 vcc, 11, v119
	ds_write_b16 v158, v33 offset:55616
	v_lshlrev_b32_e32 v86, 16, v102
	v_cndmask_b32_e64 v33, 0, 1.0, vcc
	v_fma_f32 v33, -v116, v86, v33
	v_and_b32_e32 v86, 0xffff0000, v102
	v_lshlrev_b32_e32 v87, 16, v103
	v_fma_f32 v86, -v159, v86, 0
	v_fma_f32 v33, -v161, v87, v33
	v_and_b32_e32 v87, 0xffff0000, v103
	v_fma_f32 v86, -v162, v87, v86
	v_lshlrev_b32_e32 v87, 16, v104
	v_fma_f32 v33, -v163, v87, v33
	v_and_b32_e32 v87, 0xffff0000, v104
	v_fma_f32 v86, -v178, v87, v86
	v_lshlrev_b32_e32 v87, 16, v105
	v_fma_f32 v33, -v179, v87, v33
	v_and_b32_e32 v87, 0xffff0000, v105
	v_fma_f32 v86, -v180, v87, v86
	v_lshlrev_b32_e32 v87, 16, v106
	v_fma_f32 v33, -v181, v87, v33
	v_and_b32_e32 v87, 0xffff0000, v106
	v_fma_f32 v86, -v108, v87, v86
	v_lshlrev_b32_e32 v87, 16, v107
	v_fma_f32 v33, -v109, v87, v33
	v_add_f32_e32 v182, v86, v33
	v_cvt_pk_bf16_f32 v33, v182, v182
	ds_write_b16 v158, v33 offset:55648
	ds_read_b128 v[86:89], v154 offset:1728
	ds_read_b128 v[94:97], v154 offset:1744
	v_or_b32_e32 v33, 15, v110
	v_mad_u64_u32 v[32:33], s[2:3], v33, s75, v[32:33]
	v_cmp_eq_u32_e32 vcc, 12, v119
	s_waitcnt lgkmcnt(0)
	ds_read_b128 v[96:99], v154 offset:1872
	ds_read_b128 v[100:103], v154 offset:1888
	ds_read_b128 v[104:107], v154 offset:2016
	ds_read_b128 v[154:157], v154 offset:2032
	ds_read_b128 v[170:173], v32
	ds_read_b128 v[174:177], v32 offset:16
	v_cndmask_b32_e64 v32, 0, 1.0, vcc
	v_lshlrev_b32_e32 v33, 16, v86
	v_fma_f32 v32, -v116, v33, v32
	v_and_b32_e32 v33, 0xffff0000, v86
	v_lshlrev_b32_e32 v86, 16, v87
	v_fma_f32 v33, -v159, v33, 0
	v_fma_f32 v32, -v161, v86, v32
	v_and_b32_e32 v86, 0xffff0000, v87
	v_fma_f32 v33, -v162, v86, v33
	v_lshlrev_b32_e32 v86, 16, v88
	v_fma_f32 v32, -v163, v86, v32
	v_and_b32_e32 v86, 0xffff0000, v88
	v_fma_f32 v33, -v178, v86, v33
	v_lshlrev_b32_e32 v86, 16, v89
	v_fma_f32 v32, -v179, v86, v32
	v_and_b32_e32 v86, 0xffff0000, v89
	v_fma_f32 v33, -v180, v86, v33
	v_lshlrev_b32_e32 v86, 16, v94
	v_fma_f32 v32, -v181, v86, v32
	v_and_b32_e32 v86, 0xffff0000, v94
	v_fma_f32 v33, -v108, v86, v33
	v_lshlrev_b32_e32 v86, 16, v95
	v_fma_f32 v32, -v109, v86, v32
	v_and_b32_e32 v86, 0xffff0000, v95
	v_fma_f32 v33, -v182, v86, v33
	v_add_f32_e32 v32, v33, v32
	v_cvt_pk_bf16_f32 v33, v32, v32
	v_cmp_eq_u32_e32 vcc, 13, v119
	s_waitcnt lgkmcnt(0)
; #define LAS __attribute__((address_space(3)))
; __device__ __forceinline__ unsigned f2bf(float f) { unsigned u = __float_as_uint(f); return (u + 0x7fffu + ((u >> 16) & 1u)) >> 16; }
; __device__ __forceinline__ float lo_bf(unsigned w) { return __uint_as_float(w << 16); }
; __device__ __forceinline__ float hi_bf(unsigned w) { return __uint_as_float(w & 0xffff0000u); }
; __device__ __forceinline__ u32x2 cvt4(f32x4 v) { return (u32x2){pk2(v[0], v[1]), pk2(v[2], v[3])}; }
; __device__ __forceinline__ void gdn_s23(CArgs& a, int u, const GdnIn2& in, LAS unsigned char* ub, LAS unsigned char* dwb, int w, int lane, float cl) {
;     ...
;           for (int rr = 0; rr < 4; ++rr) { const int r = 4 * hb + rr; float t = (r == c) ? 1.f : 0.f;
;               float t2 = 0.f;
; #pragma unroll
;               for (int j = 0; j < r; ++j) { const unsigned wv = arow[rr][j >> 3][(j >> 1) & 3]; const float av = (j & 1) ? hi_bf(wv) : lo_bf(wv); if (j & 1) t2 -= av * T[j]; else t -= av * T[j]; }
;               t += t2;
;               T[r] = t; DW[(blk * 16 + r) * 16 + c] = (bf16)f2bf(t); } } }
;     asm volatile("s_waitcnt lgkmcnt(0)" ::: "memory");
;     f32x4 X[4];
; #pragma unroll
;     for (int I = 0; I < 4; ++I) {
;         const f32x4 br = *(const LAS f32x4*)(GT + 16 * I + 4 * kg), er = *(const LAS f32x4*)(GT + 128 + 16 * I + 4 * kg);
;         const f32x4 Rf = (f32x4){__uint_as_float(in.R[I].x << 16), __uint_as_float(in.R[I].y << 16), __uint_as_float(in.R[I].z << 16), __uint_as_float(in.R[I].w << 16)};
;         f32x4 acc = isW ? br * er * Rf : br * Rf;
; #pragma unroll
;         for (int P = 0; 2 * P < I; ++P) {
;             const u32x2 alo = *(const LAS u32x2*)(AB + (16 * I + fr) * 72 + 32 * P + 4 * kg);
;             const u32x2 ahi = (2 * P + 1 < I) ? *(const LAS u32x2*)(AB + (16 * I + fr) * 72 + 32 * P + 16 + 4 * kg) : (u32x2){0u, 0u};
;             const u32x2 xlo = cvt4(-X[2 * P]); const u32x2 xhi = (2 * P + 1 < I) ? cvt4(-X[2 * P + 1]) : (u32x2){0u, 0u};
;             acc = __builtin_amdgcn_mfma_f32_16x16x32_bf16(frag2(alo, ahi), frag2(xlo, xhi), acc, 0, 0, 0); }
;         const u32x2 dlo = *(const LAS u32x2*)(DW + (I * 16 + fr) * 16 + 4 * kg);
;         X[I] = __builtin_amdgcn_mfma_f32_16x16x32_bf16(frag2(dlo, (u32x2){0u, 0u}), frag2(cvt4(acc), (u32x2){0u, 0u}), (f32x4){0.f, 0.f, 0.f, 0.f}, 0, 0, 0);
	ds_write_b16 v158, v33 offset:55680
	s_waitcnt lgkmcnt(6)
	v_lshlrev_b32_e32 v86, 16, v96
	v_cndmask_b32_e64 v33, 0, 1.0, vcc
	v_fma_f32 v33, -v116, v86, v33
	v_and_b32_e32 v86, 0xffff0000, v96
	v_lshlrev_b32_e32 v87, 16, v97
	v_fma_f32 v86, -v159, v86, 0
	v_fma_f32 v33, -v161, v87, v33
	v_and_b32_e32 v87, 0xffff0000, v97
	v_fma_f32 v86, -v162, v87, v86
	v_lshlrev_b32_e32 v87, 16, v98
	v_fma_f32 v33, -v163, v87, v33
	v_and_b32_e32 v87, 0xffff0000, v98
	v_fma_f32 v86, -v178, v87, v86
	v_lshlrev_b32_e32 v87, 16, v99
	v_fma_f32 v33, -v179, v87, v33
	v_and_b32_e32 v87, 0xffff0000, v99
	v_fma_f32 v86, -v180, v87, v86
	s_waitcnt lgkmcnt(5)
	v_lshlrev_b32_e32 v87, 16, v100
	v_fma_f32 v33, -v181, v87, v33
	v_and_b32_e32 v87, 0xffff0000, v100
	v_fma_f32 v86, -v108, v87, v86
	v_lshlrev_b32_e32 v87, 16, v101
	v_fma_f32 v33, -v109, v87, v33
	v_and_b32_e32 v87, 0xffff0000, v101
	v_fma_f32 v86, -v182, v87, v86
	v_lshlrev_b32_e32 v87, 16, v102
	v_fma_f32 v33, -v32, v87, v33
	v_add_f32_e32 v33, v86, v33
	v_cvt_pk_bf16_f32 v86, v33, v33
	v_cmp_eq_u32_e32 vcc, 14, v119
	ds_write_b16 v158, v86 offset:55712
	s_waitcnt lgkmcnt(5)
	v_lshlrev_b32_e32 v87, 16, v104
	v_cndmask_b32_e64 v86, 0, 1.0, vcc
	v_fma_f32 v86, -v116, v87, v86
	v_and_b32_e32 v87, 0xffff0000, v104
	v_lshlrev_b32_e32 v88, 16, v105
	v_fma_f32 v87, -v159, v87, 0
	v_fma_f32 v86, -v161, v88, v86
	v_and_b32_e32 v88, 0xffff0000, v105
	v_fma_f32 v87, -v162, v88, v87
	v_lshlrev_b32_e32 v88, 16, v106
	v_fma_f32 v86, -v163, v88, v86
	v_and_b32_e32 v88, 0xffff0000, v106
	v_fma_f32 v87, -v178, v88, v87
	v_lshlrev_b32_e32 v88, 16, v107
	v_fma_f32 v86, -v179, v88, v86
	v_and_b32_e32 v88, 0xffff0000, v107
	v_fma_f32 v87, -v180, v88, v87
	s_waitcnt lgkmcnt(4)
	v_lshlrev_b32_e32 v88, 16, v154
	v_fma_f32 v86, -v181, v88, v86
	v_and_b32_e32 v88, 0xffff0000, v154
	v_fma_f32 v87, -v108, v88, v87
	v_lshlrev_b32_e32 v88, 16, v155
	v_fma_f32 v86, -v109, v88, v86
	v_and_b32_e32 v88, 0xffff0000, v155
	v_fma_f32 v87, -v182, v88, v87
	v_lshlrev_b32_e32 v88, 16, v156
	v_fma_f32 v86, -v32, v88, v86
	v_and_b32_e32 v88, 0xffff0000, v156
	v_fma_f32 v87, -v33, v88, v87
	v_add_f32_e32 v86, v86, v87
	v_cvt_pk_bf16_f32 v87, v86, v86
	v_cmp_eq_u32_e32 vcc, 15, v119
	ds_write_b16 v158, v87 offset:55744
	s_waitcnt lgkmcnt(4)
	v_lshlrev_b32_e32 v88, 16, v170
	v_cndmask_b32_e64 v87, 0, 1.0, vcc
	v_fma_f32 v87, -v116, v88, v87
	v_and_b32_e32 v88, 0xffff0000, v170
	v_lshlrev_b32_e32 v89, 16, v171
	v_fma_f32 v88, -v159, v88, 0
	v_fma_f32 v87, -v161, v89, v87
	v_and_b32_e32 v89, 0xffff0000, v171
	v_fma_f32 v88, -v162, v89, v88
	v_lshlrev_b32_e32 v89, 16, v172
	v_fma_f32 v87, -v163, v89, v87
	v_and_b32_e32 v89, 0xffff0000, v172
	v_fma_f32 v88, -v178, v89, v88
	v_lshlrev_b32_e32 v89, 16, v173
	v_fma_f32 v87, -v179, v89, v87
	v_and_b32_e32 v89, 0xffff0000, v173
	v_fma_f32 v88, -v180, v89, v88
	s_waitcnt lgkmcnt(3)
	v_lshlrev_b32_e32 v89, 16, v174
	v_fma_f32 v87, -v181, v89, v87
	v_and_b32_e32 v89, 0xffff0000, v174
	v_fma_f32 v88, -v108, v89, v88
	v_lshlrev_b32_e32 v89, 16, v175
	v_fma_f32 v87, -v109, v89, v87
	v_and_b32_e32 v89, 0xffff0000, v175
	v_fma_f32 v88, -v182, v89, v88
	v_lshlrev_b32_e32 v89, 16, v176
	v_fma_f32 v32, -v32, v89, v87
	v_and_b32_e32 v87, 0xffff0000, v176
	v_fma_f32 v33, -v33, v87, v88
	v_lshlrev_b32_e32 v87, 16, v177
	v_fma_f32 v32, -v86, v87, v32
	v_add_f32_e32 v32, v33, v32
	v_cvt_pk_bf16_f32 v32, v32, v32
	ds_write_b16 v158, v32 offset:55776
	s_waitcnt lgkmcnt(0)
	v_add_u32_e32 v157, s8, v85
	ds_read_b128 v[94:97], v157 offset:57344
	ds_read_b128 v[86:89], v157 offset:57856
	v_ashrrev_i32_e32 v123, 4, v110
	v_lshlrev_b32_e32 v104, 3, v123
	v_lshlrev_b32_e32 v33, 16, v82
	v_lshlrev_b32_e32 v82, 16, v83
	v_lshlrev_b32_e32 v83, 16, v84
	s_waitcnt lgkmcnt(0)
	v_pk_mul_f32 v[84:85], v[96:97], v[88:89]
	v_pk_mul_f32 v[98:99], v[94:95], v[86:87]
	v_sub_u32_e32 v158, v157, v104
	v_lshlrev_b32_e32 v32, 16, v34
	v_cndmask_b32_e64 v85, v97, v85, s[38:39]
	v_cndmask_b32_e64 v84, v96, v84, s[38:39]
	v_cndmask_b32_e64 v95, v95, v99, s[38:39]
	v_cndmask_b32_e64 v94, v94, v98, s[38:39]
	v_pk_mul_f32 v[84:85], v[84:85], v[82:83]
	v_pk_mul_f32 v[82:83], v[94:95], v[32:33]
	v_lshl_add_u32 v32, v119, 5, v158
	ds_read_b64 v[32:33], v32 offset:55296
	v_bfe_u32 v94, v82, 16, 1
	v_add3_u32 v82, v82, v94, s81
	v_bfe_u32 v94, v83, 16, 1
	v_mov_b32_e32 v34, v35
	v_lshrrev_b32_e32 v82, 16, v82
	v_add3_u32 v83, v83, v94, s81
	v_and_or_b32 v82, v83, s80, v82
	v_cvt_pk_bf16_f32 v83, v84, v85
	v_mov_b32_e32 v84, v35
	v_mov_b32_e32 v85, v35
	v_or_b32_e32 v156, 16, v119
	v_add_u32_e32 v154, 0, v104
	s_waitcnt lgkmcnt(0)
	v_mfma_f32_16x16x32_bf16 v[94:97], v[32:35], v[82:85], 0
	ds_read_b128 v[98:101], v157 offset:57408
	ds_read_b128 v[82:85], v157 offset:57920
	v_lshlrev_b32_e32 v32, 16, v78
	s_waitcnt vmcnt(27)
	v_lshlrev_b32_e32 v33, 16, v79
	s_waitcnt vmcnt(26)
	v_lshlrev_b32_e32 v78, 16, v80
	s_waitcnt vmcnt(25)
	v_lshlrev_b32_e32 v79, 16, v81
	s_waitcnt lgkmcnt(0)
	v_pk_mul_f32 v[80:81], v[100:101], v[84:85]
	v_pk_mul_f32 v[102:103], v[98:99], v[82:83]
	v_cndmask_b32_e64 v81, v101, v81, s[38:39]
	v_cndmask_b32_e64 v80, v100, v80, s[38:39]
	v_cndmask_b32_e64 v99, v99, v103, s[38:39]
	v_cndmask_b32_e64 v98, v98, v102, s[38:39]
	v_xor_b32_e32 v100, 0x80000000, v95
	v_pk_mul_f32 v[80:81], v[80:81], v[78:79]
	v_pk_mul_f32 v[78:79], v[98:99], v[32:33]
	v_xor_b32_e32 v99, 0x80000000, v94
	v_bfe_u32 v101, v100, 16, 1
	v_add3_u32 v100, v100, v101, s81
	v_bfe_u32 v101, v99, 16, 1
	v_add3_u32 v99, v99, v101, s81
	v_mad_u32_u24 v159, v156, s75, v154
	v_xor_b32_e32 v98, 0x80000000, v97
	v_lshrrev_b32_e32 v99, 16, v99
	ds_read_b64 v[32:33], v159
	v_xor_b32_e32 v34, 0x80000000, v96
	v_and_or_b32 v106, v100, s80, v99
	v_bfe_u32 v99, v98, 16, 1
	v_add3_u32 v98, v98, v99, s81
	v_bfe_u32 v99, v34, 16, 1
	v_add3_u32 v34, v34, v99, s81
	v_lshrrev_b32_e32 v34, 16, v34
	v_and_or_b32 v107, v98, s80, v34
	v_mov_b32_e32 v34, v35
	v_mov_b32_e32 v108, v35
	v_mov_b32_e32 v109, v35
	v_or_b32_e32 v155, 32, v119
	s_ashr_i32 s27, s26, 31
	s_waitcnt lgkmcnt(0)
; #define LAS __attribute__((address_space(3)))
; __device__ __forceinline__ void gdn_s23(CArgs& a, int u, const GdnIn2& in, LAS unsigned char* ub, LAS unsigned char* dwb, int w, int lane, float cl) {
;     ...
; #pragma unroll
;     for (int I = 0; I < 4; ++I) {
;         const f32x4 br = *(const LAS f32x4*)(GT + 16 * I + 4 * kg), er = *(const LAS f32x4*)(GT + 128 + 16 * I + 4 * kg);
;         const f32x4 Rf = (f32x4){__uint_as_float(in.R[I].x << 16), __uint_as_float(in.R[I].y << 16), __uint_as_float(in.R[I].z << 16), __uint_as_float(in.R[I].w << 16)};
;         f32x4 acc = isW ? br * er * Rf : br * Rf;
; #pragma unroll
;         for (int P = 0; 2 * P < I; ++P) {
;             const u32x2 alo = *(const LAS u32x2*)(AB + (16 * I + fr) * 72 + 32 * P + 4 * kg);
;             const u32x2 ahi = (2 * P + 1 < I) ? *(const LAS u32x2*)(AB + (16 * I + fr) * 72 + 32 * P + 16 + 4 * kg) : (u32x2){0u, 0u};
;             const u32x2 xlo = cvt4(-X[2 * P]); const u32x2 xhi = (2 * P + 1 < I) ? cvt4(-X[2 * P + 1]) : (u32x2){0u, 0u};
;             acc = __builtin_amdgcn_mfma_f32_16x16x32_bf16(frag2(alo, ahi), frag2(xlo, xhi), acc, 0, 0, 0); }
;         const u32x2 dlo = *(const LAS u32x2*)(DW + (I * 16 + fr) * 16 + 4 * kg);
;         X[I] = __builtin_amdgcn_mfma_f32_16x16x32_bf16(frag2(dlo, (u32x2){0u, 0u}), frag2(cvt4(acc), (u32x2){0u, 0u}), (f32x4){0.f, 0.f, 0.f, 0.f}, 0, 0, 0);
;     }
;     const bf16x8 Xb01 = frag2(cvt4(X[0]), cvt4(X[1])), Xb23 = frag2(cvt4(X[2]), cvt4(X[3]));
;     const float ecl = __expf(cl);
;     bf16* ftp = FTo + (c0 + fr) * 64 + 4 * kg; bf16* btp = BTo + (c0 + fr) * 64 + 4 * kg; bf16* ep = Eo + (4 * kg) * 64 + c0 + fr; bf16* mp = Mo + (4 * kg) * 64 + c0 + fr;
; #pragma unroll
;     for (int t4 = 0; t4 < 4; ++t4) {
;         const LAS bf16* ar = ATT + (16 * t4 + fr) * 72 + 4 * kg; const LAS bf16* kr = KTT + (16 * t4 + fr) * 72 + 4 * kg;
;         f32x4 pa = (f32x4){0.f, 0.f, 0.f, 0.f}, pk = (f32x4){0.f, 0.f, 0.f, 0.f};
;         pa = __builtin_amdgcn_mfma_f32_16x16x32_bf16(frag2(*(const LAS u32x2*)ar, *(const LAS u32x2*)(ar + 16)), Xb01, pa, 0, 0, 0);
;         pa = __builtin_amdgcn_mfma_f32_16x16x32_bf16(frag2(*(const LAS u32x2*)(ar + 32), *(const LAS u32x2*)(ar + 48)), Xb23, pa, 0, 0, 0);
;         pk = __builtin_amdgcn_mfma_f32_16x16x32_bf16(frag2(*(const LAS u32x2*)kr, *(const LAS u32x2*)(kr + 16)), Xb01, pk, 0, 0, 0);
	v_mfma_f32_16x16x32_bf16 v[78:81], v[32:35], v[106:109], v[78:81]
	v_lshl_add_u32 v32, v156, 5, v158
	ds_read_b64 v[32:33], v32 offset:55296
	s_lshl_b64 s[76:77], s[26:27], 13
	s_add_u32 s62, s85, s76
	s_addc_u32 s63, s64, s77
	s_nop 2
	v_bfe_u32 v98, v78, 16, 1
	v_add3_u32 v78, v78, v98, s81
	v_bfe_u32 v98, v79, 16, 1
	v_lshrrev_b32_e32 v78, 16, v78
	v_add3_u32 v79, v79, v98, s81
	v_and_or_b32 v78, v79, s80, v78
	v_cvt_pk_bf16_f32 v79, v80, v81
	v_mov_b32_e32 v80, v35
	v_mov_b32_e32 v81, v35
	s_add_u32 s48, s71, s76
	s_addc_u32 s49, s18, s77
	s_waitcnt lgkmcnt(0)
	v_mfma_f32_16x16x32_bf16 v[98:101], v[32:35], v[78:81], 0
	ds_read_b128 v[102:105], v157 offset:57472
	ds_read_b128 v[78:81], v157 offset:57984
	s_waitcnt vmcnt(24)
	v_lshlrev_b32_e32 v32, 16, v90
	s_waitcnt vmcnt(23)
	v_lshlrev_b32_e32 v33, 16, v91
	s_waitcnt vmcnt(22)
	v_lshlrev_b32_e32 v90, 16, v92
	s_waitcnt vmcnt(21)
	v_lshlrev_b32_e32 v91, 16, v93
	s_waitcnt lgkmcnt(0)
	v_pk_mul_f32 v[92:93], v[104:105], v[80:81]
	v_pk_mul_f32 v[108:109], v[102:103], v[78:79]
	v_cndmask_b32_e64 v93, v105, v93, s[38:39]
	v_cndmask_b32_e64 v92, v104, v92, s[38:39]
	v_cndmask_b32_e64 v103, v103, v109, s[38:39]
	v_cndmask_b32_e64 v102, v102, v108, s[38:39]
	v_pk_mul_f32 v[92:93], v[92:93], v[90:91]
	v_pk_mul_f32 v[90:91], v[102:103], v[32:33]
	v_add_u32_e32 v32, 0x800, v159
	v_xor_b32_e32 v108, 0x80000000, v99
	ds_read2_b64 v[102:105], v32 offset0:32 offset1:36
	v_xor_b32_e32 v34, 0x80000000, v98
	v_xor_b32_e32 v33, 0x80000000, v101
	v_xor_b32_e32 v32, 0x80000000, v100
	v_cvt_pk_bf16_f32 v108, v34, v108
	v_cvt_pk_bf16_f32 v109, v32, v33
	v_lshl_add_u32 v32, v155, 5, v158
	ds_read_b64 v[32:33], v32 offset:55296
	s_waitcnt lgkmcnt(1)
	v_mfma_f32_16x16x32_bf16 v[90:93], v[102:105], v[106:109], v[90:93]
	v_mov_b32_e32 v34, v35
	s_add_u32 s2, s19, s76
	v_lshlrev_b32_e32 v116, 2, v123
	s_addc_u32 s3, s66, s77
	s_add_u32 s54, s21, s76
	s_nop 2
	v_bfe_u32 v102, v90, 16, 1
	v_add3_u32 v90, v90, v102, s81
	v_bfe_u32 v102, v91, 16, 1
	v_lshrrev_b32_e32 v90, 16, v90
	v_add3_u32 v91, v91, v102, s81
	v_and_or_b32 v90, v91, s80, v90
	v_cvt_pk_bf16_f32 v91, v92, v93
	v_mov_b32_e32 v92, v35
	v_mov_b32_e32 v93, v35
	s_addc_u32 s55, s70, s77
	s_mov_b64 s[76:77], -1
	s_waitcnt lgkmcnt(0)
	v_mfma_f32_16x16x32_bf16 v[102:105], v[32:35], v[90:93], 0
	ds_read_b128 v[170:173], v157 offset:57536
	ds_read_b128 v[90:93], v157 offset:58048
	s_waitcnt vmcnt(20)
	v_lshlrev_b32_e32 v32, 16, v117
	s_waitcnt vmcnt(19)
	v_lshlrev_b32_e32 v33, 16, v120
	s_waitcnt vmcnt(18)
	v_lshlrev_b32_e32 v120, 16, v121
	s_waitcnt vmcnt(17)
	v_lshlrev_b32_e32 v121, 16, v122
	s_waitcnt lgkmcnt(0)
	v_pk_mul_f32 v[174:175], v[170:171], v[90:91]
	v_pk_mul_f32 v[162:163], v[172:173], v[92:93]
	v_cndmask_b32_e64 v171, v171, v175, s[38:39]
	v_cndmask_b32_e64 v170, v170, v174, s[38:39]
	v_pk_mul_f32 v[170:171], v[170:171], v[32:33]
	v_add_u32_e32 v32, 0x1000, v159
	ds_read2_b64 v[174:177], v32 offset0:64 offset1:68
	v_cndmask_b32_e64 v163, v173, v163, s[38:39]
	v_cndmask_b32_e64 v162, v172, v162, s[38:39]
	v_pk_mul_f32 v[172:173], v[162:163], v[120:121]
	v_xor_b32_e32 v121, 0x80000000, v103
	v_xor_b32_e32 v120, 0x80000000, v102
	v_bfe_u32 v122, v121, 16, 1
	v_add3_u32 v121, v121, v122, s81
	v_bfe_u32 v122, v120, 16, 1
	v_add3_u32 v120, v120, v122, s81
	v_xor_b32_e32 v117, 0x80000000, v105
	v_lshrrev_b32_e32 v120, 16, v120
	s_waitcnt lgkmcnt(0)
	v_mfma_f32_16x16x32_bf16 v[106:109], v[174:177], v[106:109], v[170:173]
	ds_read_b64 v[32:33], v159 offset:4672
	v_xor_b32_e32 v34, 0x80000000, v104
	v_or_b32_e32 v157, 48, v119
	v_and_or_b32 v170, v121, s80, v120
	v_cvt_pk_bf16_f32 v171, v34, v117
	v_mov_b32_e32 v34, v35
	v_mov_b32_e32 v172, v35
	v_mov_b32_e32 v173, v35
	s_andn2_b64 vcc, exec, s[60:61]
	s_waitcnt lgkmcnt(0)
	v_mfma_f32_16x16x32_bf16 v[106:109], v[32:35], v[170:173], v[106:109]
	v_lshl_add_u32 v32, v157, 5, v158
	ds_read_b64 v[32:33], v32 offset:55296
	s_nop 5
	v_cvt_pk_bf16_f32 v106, v106, v107
	v_cvt_pk_bf16_f32 v107, v108, v109
	v_mov_b32_e32 v108, v35
	v_mov_b32_e32 v109, v35
	v_ashrrev_i32_e32 v117, 31, v116
	s_waitcnt lgkmcnt(0)
	v_mfma_f32_16x16x32_bf16 v[106:109], v[32:35], v[106:109], 0
	v_cvt_pk_bf16_f32 v94, v94, v95
	v_cvt_pk_bf16_f32 v95, v96, v97
	v_cvt_pk_bf16_f32 v96, v98, v99
	v_cvt_pk_bf16_f32 v97, v100, v101
	v_cvt_pk_bf16_f32 v98, v102, v103
	v_cvt_pk_bf16_f32 v99, v104, v105
	s_nop 1
	v_cvt_pk_bf16_f32 v100, v106, v107
	v_lshlrev_b32_e32 v34, 7, v45
	v_cvt_pk_bf16_f32 v101, v108, v109
	v_lshl_add_u64 v[32:33], s[48:49], 0, v[34:35]
	v_lshlrev_b64 v[102:103], 1, v[116:117]
	v_lshl_add_u64 v[120:121], v[32:33], 0, v[102:103]
	v_lshl_add_u64 v[32:33], s[54:55], 0, v[34:35]
	v_mul_u32_u24_e32 v34, 0x48, v119
	v_lshl_add_u32 v34, v34, 1, v154
	v_add_u32_e32 v106, 0x2000, v34
	v_lshl_add_u64 v[32:33], v[32:33], 0, v[102:103]
	ds_read2_b64 v[102:105], v106 offset0:128 offset1:132
	ds_read2_b64 v[106:109], v106 offset0:136 offset1:140
	s_waitcnt lgkmcnt(1)
	v_mfma_f32_16x16x32_bf16 v[102:105], v[102:105], v[94:97], 0
	v_add_u32_e32 v34, 0x4800, v34
	ds_read2_b64 v[170:173], v34 offset0:8 offset1:12
	s_waitcnt lgkmcnt(1)
	v_mfma_f32_16x16x32_bf16 v[102:105], v[106:109], v[98:101], v[102:105]
	ds_read2_b64 v[106:109], v34 offset1:4
	v_cndmask_b32_e64 v34, 0, 1, s[60:61]
	v_cmp_ne_u32_e64 s[48:49], 1, v34
	s_waitcnt lgkmcnt(0)
	v_mfma_f32_16x16x32_bf16 v[106:109], v[106:109], v[94:97], 0
	v_mfma_f32_16x16x32_bf16 v[106:109], v[170:173], v[98:101], v[106:109]
	s_cbranch_vccnz .LBB0_1725
	s_nop 0
	v_cvt_pk_bf16_f32 v158, v102, v103
	v_cvt_pk_bf16_f32 v159, v104, v105
	global_store_dwordx2 v[120:121], v[158:159], off
	s_nop 2
	v_cvt_pk_bf16_f32 v158, v106, v107
	v_bfe_u32 v34, v108, 16, 1
	v_add3_u32 v34, v108, v34, s81
	v_bfe_u32 v117, v109, 16, 1
	v_lshrrev_b32_e32 v34, 16, v34
	v_add3_u32 v117, v109, v117, s81
	v_and_or_b32 v159, v117, s80, v34
	s_mov_b64 s[76:77], 0
	global_store_dwordx2 v[32:33], v[158:159], off
; #define LAS __attribute__((address_space(3)))
; __device__ __forceinline__ unsigned f2bf(float f) { unsigned u = __float_as_uint(f); return (u + 0x7fffu + ((u >> 16) & 1u)) >> 16; }
; __device__ __forceinline__ u32x2 cvt4(f32x4 v) { return (u32x2){pk2(v[0], v[1]), pk2(v[2], v[3])}; }
; __device__ __forceinline__ void gdn_s23(CArgs& a, int u, const GdnIn2& in, LAS unsigned char* ub, LAS unsigned char* dwb, int w, int lane, float cl) {
;     ...
;     const float ecl = __expf(cl);
;     bf16* ftp = FTo + (c0 + fr) * 64 + 4 * kg; bf16* btp = BTo + (c0 + fr) * 64 + 4 * kg; bf16* ep = Eo + (4 * kg) * 64 + c0 + fr; bf16* mp = Mo + (4 * kg) * 64 + c0 + fr;
; #pragma unroll
;     for (int t4 = 0; t4 < 4; ++t4) {
;         const LAS bf16* ar = ATT + (16 * t4 + fr) * 72 + 4 * kg; const LAS bf16* kr = KTT + (16 * t4 + fr) * 72 + 4 * kg;
;         f32x4 pa = (f32x4){0.f, 0.f, 0.f, 0.f}, pk = (f32x4){0.f, 0.f, 0.f, 0.f};
;         pa = __builtin_amdgcn_mfma_f32_16x16x32_bf16(frag2(*(const LAS u32x2*)ar, *(const LAS u32x2*)(ar + 16)), Xb01, pa, 0, 0, 0);
;         pa = __builtin_amdgcn_mfma_f32_16x16x32_bf16(frag2(*(const LAS u32x2*)(ar + 32), *(const LAS u32x2*)(ar + 48)), Xb23, pa, 0, 0, 0);
;         pk = __builtin_amdgcn_mfma_f32_16x16x32_bf16(frag2(*(const LAS u32x2*)kr, *(const LAS u32x2*)(kr + 16)), Xb01, pk, 0, 0, 0);
;         pk = __builtin_amdgcn_mfma_f32_16x16x32_bf16(frag2(*(const LAS u32x2*)(kr + 32), *(const LAS u32x2*)(kr + 48)), Xb23, pk, 0, 0, 0);
;         if (!isW) {
;             *(u32x2*)(ftp + 16 * t4) = cvt4(pa);
;             *(u32x2*)(btp + 16 * t4) = cvt4(pk);
;         } else {
;             const f32x4 ec = *(const LAS f32x4*)(GT + 128 + 16 * t4 + 4 * kg);
; #pragma unroll
;             for (int e = 0; e < 4; ++e) { const int row = 16 * t4 + 4 * kg + e, col = c0 + fr;
;                 ep[(16 * t4 + e) * 64] = (bf16)f2bf(ec[e] * __uint_as_float(in.Qv[t4][e] << 16) - pa[e]);
;                 mp[(16 * t4 + e) * 64] = (bf16)f2bf((row == col ? ecl : 0.f) - pk[e]); }
.LBB0_1725:
	v_lshlrev_b32_e32 v122, 8, v123
	v_mul_f32_e32 v34, s36, v196
	v_ashrrev_i32_e32 v123, 31, v122
	v_exp_f32_e32 v34, v34
	v_lshlrev_b64 v[158:159], 1, v[122:123]
	v_lshl_add_u64 v[122:123], s[62:63], 0, v[158:159]
	s_lshl_b32 s78, s68, 1
	v_lshl_add_u64 v[158:159], s[2:3], 0, v[158:159]
	v_lshl_add_u64 v[122:123], v[122:123], 0, s[78:79]
	v_mov_b32_e32 v119, v35
	v_lshl_add_u64 v[158:159], v[158:159], 0, s[78:79]
	v_lshl_add_u64 v[122:123], v[122:123], 0, v[118:119]
	s_andn2_b64 vcc, exec, s[76:77]
	v_lshl_add_u64 v[118:119], v[158:159], 0, v[118:119]
	s_cbranch_vccnz .LBB0_1727
	v_fma_f32 v86, v151, v86, -v102
	v_cvt_pk_bf16_f32 v86, v86, v86
	v_cmp_eq_u32_e32 vcc, v116, v45
	global_store_short v[122:123], v86, off
	v_fma_f32 v87, v150, v87, -v103
	v_cndmask_b32_e32 v86, 0, v34, vcc
	v_sub_f32_e32 v86, v86, v106
	v_cvt_pk_bf16_f32 v86, v86, v86
	global_store_short v[118:119], v86, off
	v_or_b32_e32 v86, 1, v116
	v_cmp_eq_u32_e32 vcc, v86, v45
	v_cvt_pk_bf16_f32 v87, v87, v87
	s_nop 0
	v_cndmask_b32_e32 v86, 0, v34, vcc
	v_sub_f32_e32 v86, v86, v107
	global_store_short v[122:123], v87, off offset:128
	v_cvt_pk_bf16_f32 v86, v86, v86
	global_store_short v[118:119], v86, off offset:128
	v_or_b32_e32 v86, 2, v116
	v_fma_f32 v87, v153, v88, -v104
	v_cmp_eq_u32_e32 vcc, v86, v45
	v_cvt_pk_bf16_f32 v87, v87, v87
	s_nop 0
	v_cndmask_b32_e32 v86, 0, v34, vcc
	v_sub_f32_e32 v86, v86, v108
	global_store_short v[122:123], v87, off offset:256
	v_cvt_pk_bf16_f32 v86, v86, v86
	global_store_short v[118:119], v86, off offset:256
	v_or_b32_e32 v86, 3, v116
	v_fma_f32 v87, v152, v89, -v105
	v_cmp_eq_u32_e32 vcc, v86, v45
	v_cvt_pk_bf16_f32 v87, v87, v87
	s_nop 0
	v_cndmask_b32_e32 v86, 0, v34, vcc
	v_sub_f32_e32 v86, v86, v109
	global_store_short v[122:123], v87, off offset:384
	v_cvt_pk_bf16_f32 v86, v86, v86
	global_store_short v[118:119], v86, off offset:384
.LBB0_1727:
	v_mul_u32_u24_e32 v86, 0x48, v156
	v_lshl_add_u32 v106, v86, 1, v154
	v_add_u32_e32 v102, 0x2000, v106
	ds_read2_b64 v[86:89], v102 offset0:128 offset1:132
	ds_read2_b64 v[102:105], v102 offset0:136 offset1:140
	v_add_u32_e32 v106, 0x4800, v106
	s_mov_b64 s[2:3], -1
	s_and_b64 vcc, exec, s[48:49]
	s_waitcnt lgkmcnt(1)
	v_mfma_f32_16x16x32_bf16 v[86:89], v[86:89], v[94:97], 0
	s_waitcnt lgkmcnt(0)
	v_mfma_f32_16x16x32_bf16 v[86:89], v[102:105], v[98:101], v[86:89]
	ds_read2_b64 v[102:105], v106 offset1:4
	ds_read2_b64 v[106:109], v106 offset0:8 offset1:12
	s_waitcnt lgkmcnt(1)
	v_mfma_f32_16x16x32_bf16 v[102:105], v[102:105], v[94:97], 0
	s_waitcnt lgkmcnt(0)
	v_mfma_f32_16x16x32_bf16 v[102:105], v[106:109], v[98:101], v[102:105]
	s_cbranch_vccnz .LBB0_1729
	s_nop 0
	v_cvt_pk_bf16_f32 v106, v86, v87
	v_cvt_pk_bf16_f32 v107, v88, v89
	global_store_dwordx2 v[120:121], v[106:107], off offset:32
	s_nop 2
	v_cvt_pk_bf16_f32 v106, v102, v103
	v_bfe_u32 v107, v104, 16, 1
	v_add3_u32 v107, v104, v107, s81
	v_bfe_u32 v108, v105, 16, 1
	v_lshrrev_b32_e32 v107, 16, v107
	v_add3_u32 v108, v105, v108, s81
	v_and_or_b32 v107, v108, s80, v107
	s_mov_b64 s[2:3], 0
	global_store_dwordx2 v[32:33], v[106:107], off offset:32
.LBB0_1729:
	s_andn2_b64 vcc, exec, s[2:3]
	s_cbranch_vccnz .LBB0_1731
	v_fma_f32 v82, v147, v82, -v86
	v_add_u32_e32 v106, 16, v116
	v_cvt_pk_bf16_f32 v82, v82, v82
	v_cmp_eq_u32_e32 vcc, v106, v45
	global_store_short v[122:123], v82, off offset:2048
	v_fma_f32 v83, v146, v83, -v87
	v_cndmask_b32_e32 v82, 0, v34, vcc
	v_sub_f32_e32 v82, v82, v102
	v_cvt_pk_bf16_f32 v82, v82, v82
	global_store_short v[118:119], v82, off offset:2048
	v_add_u32_e32 v82, 17, v116
	v_cmp_eq_u32_e32 vcc, v82, v45
	v_cvt_pk_bf16_f32 v83, v83, v83
	s_nop 0
	v_cndmask_b32_e32 v82, 0, v34, vcc
	v_sub_f32_e32 v82, v82, v103
	global_store_short v[122:123], v83, off offset:2176
	v_cvt_pk_bf16_f32 v82, v82, v82
	global_store_short v[118:119], v82, off offset:2176
	v_add_u32_e32 v82, 18, v116
	v_fma_f32 v83, v149, v84, -v88
	v_cmp_eq_u32_e32 vcc, v82, v45
	v_cvt_pk_bf16_f32 v83, v83, v83
	s_nop 0
	v_cndmask_b32_e32 v82, 0, v34, vcc
	v_sub_f32_e32 v82, v82, v104
	global_store_short v[122:123], v83, off offset:2304
	v_cvt_pk_bf16_f32 v82, v82, v82
	global_store_short v[118:119], v82, off offset:2304
	v_add_u32_e32 v82, 19, v116
	v_fma_f32 v83, v148, v85, -v89
	v_cmp_eq_u32_e32 vcc, v82, v45
	v_cvt_pk_bf16_f32 v83, v83, v83
	s_nop 0
	v_cndmask_b32_e32 v82, 0, v34, vcc
	v_sub_f32_e32 v82, v82, v105
	global_store_short v[122:123], v83, off offset:2432
	v_cvt_pk_bf16_f32 v82, v82, v82
	global_store_short v[118:119], v82, off offset:2432
; #define LAS __attribute__((address_space(3)))
; __device__ __forceinline__ unsigned f2bf(float f) { unsigned u = __float_as_uint(f); return (u + 0x7fffu + ((u >> 16) & 1u)) >> 16; }
; __device__ __forceinline__ u32x2 cvt4(f32x4 v) { return (u32x2){pk2(v[0], v[1]), pk2(v[2], v[3])}; }
; __device__ __forceinline__ void gdn_s23(CArgs& a, int u, const GdnIn2& in, LAS unsigned char* ub, LAS unsigned char* dwb, int w, int lane, float cl) {
;     ...
;     for (int t4 = 0; t4 < 4; ++t4) {
;         const LAS bf16* ar = ATT + (16 * t4 + fr) * 72 + 4 * kg; const LAS bf16* kr = KTT + (16 * t4 + fr) * 72 + 4 * kg;
;         f32x4 pa = (f32x4){0.f, 0.f, 0.f, 0.f}, pk = (f32x4){0.f, 0.f, 0.f, 0.f};
;         pa = __builtin_amdgcn_mfma_f32_16x16x32_bf16(frag2(*(const LAS u32x2*)ar, *(const LAS u32x2*)(ar + 16)), Xb01, pa, 0, 0, 0);
;         pa = __builtin_amdgcn_mfma_f32_16x16x32_bf16(frag2(*(const LAS u32x2*)(ar + 32), *(const LAS u32x2*)(ar + 48)), Xb23, pa, 0, 0, 0);
;         pk = __builtin_amdgcn_mfma_f32_16x16x32_bf16(frag2(*(const LAS u32x2*)kr, *(const LAS u32x2*)(kr + 16)), Xb01, pk, 0, 0, 0);
;         pk = __builtin_amdgcn_mfma_f32_16x16x32_bf16(frag2(*(const LAS u32x2*)(kr + 32), *(const LAS u32x2*)(kr + 48)), Xb23, pk, 0, 0, 0);
;         if (!isW) {
;             *(u32x2*)(ftp + 16 * t4) = cvt4(pa);
;             *(u32x2*)(btp + 16 * t4) = cvt4(pk);
;         } else {
;             const f32x4 ec = *(const LAS f32x4*)(GT + 128 + 16 * t4 + 4 * kg);
; #pragma unroll
;             for (int e = 0; e < 4; ++e) { const int row = 16 * t4 + 4 * kg + e, col = c0 + fr;
;                 ep[(16 * t4 + e) * 64] = (bf16)f2bf(ec[e] * __uint_as_float(in.Qv[t4][e] << 16) - pa[e]);
;                 mp[(16 * t4 + e) * 64] = (bf16)f2bf((row == col ? ecl : 0.f) - pk[e]); }
.LBB0_1731:
	v_mul_u32_u24_e32 v82, 0x48, v155
	s_nop 3
	v_lshl_add_u32 v102, v82, 1, v154
	v_add_u32_e32 v86, 0x2000, v102
	ds_read2_b64 v[82:85], v86 offset0:128 offset1:132
	ds_read2_b64 v[86:89], v86 offset0:136 offset1:140
	v_add_u32_e32 v102, 0x4800, v102
	s_mov_b64 s[2:3], -1
	s_and_b64 vcc, exec, s[48:49]
	s_waitcnt lgkmcnt(1)
	v_mfma_f32_16x16x32_bf16 v[82:85], v[82:85], v[94:97], 0
	s_waitcnt lgkmcnt(0)
	v_mfma_f32_16x16x32_bf16 v[82:85], v[86:89], v[98:101], v[82:85]
	ds_read2_b64 v[86:89], v102 offset1:4
	ds_read2_b64 v[102:105], v102 offset0:8 offset1:12
	s_waitcnt lgkmcnt(1)
	v_mfma_f32_16x16x32_bf16 v[86:89], v[86:89], v[94:97], 0
	s_waitcnt lgkmcnt(0)
	v_mfma_f32_16x16x32_bf16 v[86:89], v[102:105], v[98:101], v[86:89]
	s_cbranch_vccnz .LBB0_1733
	s_nop 0
	v_cvt_pk_bf16_f32 v102, v82, v83
	v_cvt_pk_bf16_f32 v103, v84, v85
	global_store_dwordx2 v[120:121], v[102:103], off offset:64
	s_nop 2
	v_cvt_pk_bf16_f32 v102, v86, v87
	v_bfe_u32 v103, v88, 16, 1
	v_add3_u32 v103, v88, v103, s81
	v_bfe_u32 v104, v89, 16, 1
	v_lshrrev_b32_e32 v103, 16, v103
	v_add3_u32 v104, v89, v104, s81
	v_and_or_b32 v103, v104, s80, v103
	s_mov_b64 s[2:3], 0
	global_store_dwordx2 v[32:33], v[102:103], off offset:64
.LBB0_1733:
	s_andn2_b64 vcc, exec, s[2:3]
	s_cbranch_vccnz .LBB0_1735
	v_fma_f32 v78, v144, v78, -v82
	v_add_co_u32_e32 v102, vcc, 0x1000, v122
	v_add_u32_e32 v104, 32, v116
	s_nop 0
	v_addc_co_u32_e32 v103, vcc, 0, v123, vcc
	v_cvt_pk_bf16_f32 v78, v78, v78
	v_cmp_eq_u32_e32 vcc, v104, v45
	global_store_short v[102:103], v78, off
	v_fma_f32 v79, v142, v79, -v83
	v_cndmask_b32_e32 v78, 0, v34, vcc
	v_sub_f32_e32 v78, v78, v86
	v_add_co_u32_e32 v104, vcc, 0x1000, v118
	v_cvt_pk_bf16_f32 v78, v78, v78
	s_nop 0
	v_addc_co_u32_e32 v105, vcc, 0, v119, vcc
	global_store_short v[104:105], v78, off
	v_add_u32_e32 v78, 33, v116
	v_cmp_eq_u32_e32 vcc, v78, v45
	v_cvt_pk_bf16_f32 v79, v79, v79
	s_nop 0
	v_cndmask_b32_e32 v78, 0, v34, vcc
	v_sub_f32_e32 v78, v78, v87
	global_store_short v[102:103], v79, off offset:128
	v_cvt_pk_bf16_f32 v78, v78, v78
	global_store_short v[104:105], v78, off offset:128
	v_add_u32_e32 v78, 34, v116
	v_fma_f32 v79, v145, v80, -v84
	v_cmp_eq_u32_e32 vcc, v78, v45
	v_cvt_pk_bf16_f32 v79, v79, v79
	s_nop 0
	v_cndmask_b32_e32 v78, 0, v34, vcc
	v_sub_f32_e32 v78, v78, v88
	global_store_short v[102:103], v79, off offset:256
	v_cvt_pk_bf16_f32 v78, v78, v78
	global_store_short v[104:105], v78, off offset:256
	v_add_u32_e32 v78, 35, v116
	v_fma_f32 v79, v143, v81, -v85
	v_cmp_eq_u32_e32 vcc, v78, v45
	v_cvt_pk_bf16_f32 v79, v79, v79
	s_nop 0
	v_cndmask_b32_e32 v78, 0, v34, vcc
	v_sub_f32_e32 v78, v78, v89
	global_store_short v[102:103], v79, off offset:384
	v_cvt_pk_bf16_f32 v78, v78, v78
	global_store_short v[104:105], v78, off offset:384
.LBB0_1735:
	v_mul_u32_u24_e32 v78, 0x48, v157
	s_nop 3
	v_lshl_add_u32 v86, v78, 1, v154
	v_add_u32_e32 v82, 0x2000, v86
	ds_read2_b64 v[78:81], v82 offset0:128 offset1:132
	ds_read2_b64 v[82:85], v82 offset0:136 offset1:140
	v_add_u32_e32 v86, 0x4800, v86
	s_mov_b64 s[2:3], -1
	s_and_b64 vcc, exec, s[48:49]
	s_waitcnt lgkmcnt(1)
	v_mfma_f32_16x16x32_bf16 v[78:81], v[78:81], v[94:97], 0
	s_waitcnt lgkmcnt(0)
	v_mfma_f32_16x16x32_bf16 v[78:81], v[82:85], v[98:101], v[78:81]
	ds_read2_b64 v[82:85], v86 offset1:4
	ds_read2_b64 v[86:89], v86 offset0:8 offset1:12
	s_waitcnt lgkmcnt(1)
	v_mfma_f32_16x16x32_bf16 v[82:85], v[82:85], v[94:97], 0
	s_waitcnt lgkmcnt(0)
	v_mfma_f32_16x16x32_bf16 v[82:85], v[86:89], v[98:101], v[82:85]
	s_cbranch_vccnz .LBB0_1737
	s_nop 0
	v_cvt_pk_bf16_f32 v86, v78, v79
	v_cvt_pk_bf16_f32 v87, v80, v81
	global_store_dwordx2 v[120:121], v[86:87], off offset:96
	s_nop 2
	v_cvt_pk_bf16_f32 v86, v82, v83
	v_bfe_u32 v87, v84, 16, 1
	v_add3_u32 v87, v84, v87, s81
	v_bfe_u32 v88, v85, 16, 1
	v_lshrrev_b32_e32 v87, 16, v87
	v_add3_u32 v88, v85, v88, s81
	v_and_or_b32 v87, v88, s80, v87
	s_mov_b64 s[2:3], 0
	global_store_dwordx2 v[32:33], v[86:87], off offset:96
.LBB0_1737:
	s_andn2_b64 vcc, exec, s[2:3]
	s_cbranch_vccnz .LBB0_1739
	v_fma_f32 v32, v140, v90, -v78
	v_cvt_pk_bf16_f32 v78, v32, v32
	v_add_co_u32_e32 v32, vcc, 0x1000, v122
	v_add_u32_e32 v86, 48, v116
	s_nop 0
	v_addc_co_u32_e32 v33, vcc, 0, v123, vcc
	v_cmp_eq_u32_e32 vcc, v86, v45
	global_store_short v[32:33], v78, off offset:2048
	v_fma_f32 v79, v138, v91, -v79
	v_cndmask_b32_e32 v78, 0, v34, vcc
	v_sub_f32_e32 v78, v78, v82
	v_add_co_u32_e32 v86, vcc, 0x1000, v118
	v_cvt_pk_bf16_f32 v78, v78, v78
	s_nop 0
	v_addc_co_u32_e32 v87, vcc, 0, v119, vcc
	global_store_short v[86:87], v78, off offset:2048
	v_add_u32_e32 v78, 49, v116
	v_cmp_eq_u32_e32 vcc, v78, v45
	v_bfe_u32 v82, v79, 16, 1
	v_add3_u32 v79, v79, v82, s81
	v_cndmask_b32_e32 v78, 0, v34, vcc
	v_sub_f32_e32 v78, v78, v83
	global_store_short_d16_hi v[32:33], v79, off offset:2176
	v_cvt_pk_bf16_f32 v78, v78, v78
	global_store_short v[86:87], v78, off offset:2176
	v_add_u32_e32 v78, 50, v116
	v_fma_f32 v79, v141, v92, -v80
	v_cmp_eq_u32_e32 vcc, v78, v45
	v_cvt_pk_bf16_f32 v79, v79, v79
	s_nop 0
	v_cndmask_b32_e32 v78, 0, v34, vcc
	v_sub_f32_e32 v78, v78, v84
	global_store_short v[32:33], v79, off offset:2304
	v_cvt_pk_bf16_f32 v78, v78, v78
	v_fma_f32 v79, v139, v93, -v81
	global_store_short v[86:87], v78, off offset:2304
	v_add_u32_e32 v78, 51, v116
	v_bfe_u32 v80, v79, 16, 1
	v_add3_u32 v79, v79, v80, s81
	v_cmp_eq_u32_e32 vcc, v78, v45
	global_store_short_d16_hi v[32:33], v79, off offset:2432
	s_nop 0
	v_cndmask_b32_e32 v32, 0, v34, vcc
	v_sub_f32_e32 v32, v32, v85
	v_bfe_u32 v33, v32, 16, 1
	v_add3_u32 v32, v32, v33, s81
	global_store_short_d16_hi v[86:87], v32, off offset:2432

; #define LAS __attribute__((address_space(3)))
; __device__ __forceinline__ unsigned f2bf(float f) { unsigned u = __float_as_uint(f); return (u + 0x7fffu + ((u >> 16) & 1u)) >> 16; }
; __device__ __forceinline__ float rdlane_f(float v, int l) { return __builtin_bit_cast(float, __builtin_amdgcn_readlane(__builtin_bit_cast(int, v), l)); }
; __device__ __forceinline__ float gdn_s1(const GdnIn& in, LAS unsigned char* ub, LAS unsigned char* dwb, int w, int lane) {
;     ...
;     float beta = in.g2.x, cum = in.g2.y;
; #pragma unroll
;     for (int o = 1; o < 64; o <<= 1) { const float t = __shfl_up(cum, o); if (lane >= o) cum += t; }
;     const float cl = rdlane_f(cum, 63);
;     GT[lane] = beta; GT[64 + lane] = cum; GT[128 + lane] = __expf(cum);
;     asm volatile("s_waitcnt lgkmcnt(0)" ::: "memory");
;     { const f32x4 ci = *(const LAS f32x4*)(GT + 64 + 16 * I1 + 4 * kg), bi = *(const LAS f32x4*)(GT + 16 * I1 + 4 * kg);
; #pragma unroll
;       for (int jj = 0; jj < 2; ++jj) { const int J = 2 * (w & 1) + jj;
;           f32x4 ck = (f32x4){0.f, 0.f, 0.f, 0.f}, cq = (f32x4){0.f, 0.f, 0.f, 0.f};
; #pragma unroll
;           for (int s = 0; s < 2; ++s) { ck = __builtin_amdgcn_mfma_f32_16x16x32_bf16(in.ak[s], in.bk[jj][s], ck, 0, 0, 0); cq = __builtin_amdgcn_mfma_f32_16x16x32_bf16(in.aq[s], in.bk[jj][s], cq, 0, 0, 0); }
;           const int j = 16 * J + fr; const float cj = GT[64 + j];
; #pragma unroll
;           for (int e = 0; e < 4; ++e) { const int i = 16 * I1 + 4 * kg + e; const float gm = __expf(fminf(ci[e] - cj, 0.f));
;               AB[i * 72 + j] = (bf16)f2bf(j < i ? bi[e] * ck[e] * gm : 0.f); ATT[i * 72 + j] = (bf16)f2bf(j <= i ? cq[e] * gm : 0.f); } } }
.LBB0_1775:
	s_waitcnt vmcnt(32)
	ds_bpermute_b32 v32, v125, v115
	v_cmp_gt_i32_e32 vcc, 1, v110
	s_waitcnt vmcnt(29)
	v_mfma_f32_16x16x32_bf16 v[86:89], v[58:61], v[70:73], 0
	s_movk_i32 s2, 0x48
	s_cmp_gt_u32 s0, 33
	s_waitcnt lgkmcnt(0)
	v_add_f32_e32 v32, v115, v32
	v_cndmask_b32_e32 v32, v32, v115, vcc
	ds_bpermute_b32 v33, v126, v32
	v_cmp_gt_i32_e32 vcc, 2, v110
	v_mfma_f32_16x16x32_bf16 v[70:73], v[46:49], v[70:73], 0
	s_cselect_b64 s[50:51], -1, 0
	s_mov_b64 s[62:63], 0x40000
	s_waitcnt lgkmcnt(0)
	v_add_f32_e32 v33, v32, v33
	v_cndmask_b32_e32 v32, v33, v32, vcc
	ds_bpermute_b32 v33, v127, v32
	v_cmp_gt_i32_e32 vcc, 4, v110
	s_waitcnt vmcnt(25)
	v_mfma_f32_16x16x32_bf16 v[86:89], v[50:53], v[74:77], v[86:89]
	s_waitcnt lgkmcnt(0)
	v_add_f32_e32 v33, v32, v33
	v_cndmask_b32_e32 v32, v33, v32, vcc
	ds_bpermute_b32 v33, v128, v32
	v_cmp_gt_i32_e32 vcc, 8, v110
	v_mfma_f32_16x16x32_bf16 v[70:73], v[54:57], v[74:77], v[70:73]
	s_waitcnt lgkmcnt(0)
	v_add_f32_e32 v33, v32, v33
	v_cndmask_b32_e32 v32, v33, v32, vcc
	ds_bpermute_b32 v33, v129, v32
	v_cmp_gt_i32_e32 vcc, 16, v110
	v_mfma_f32_16x16x32_bf16 v[46:49], v[46:49], v[62:65], 0
	s_waitcnt lgkmcnt(0)
	v_add_f32_e32 v33, v32, v33
	v_cndmask_b32_e32 v32, v33, v32, vcc
	ds_bpermute_b32 v33, v130, v32
	v_cmp_gt_i32_e32 vcc, 32, v110
	v_mfma_f32_16x16x32_bf16 v[58:61], v[58:61], v[62:65], 0
	s_waitcnt lgkmcnt(0)
	v_add_f32_e32 v33, v32, v33
	v_cndmask_b32_e32 v33, v33, v32, vcc
	v_mul_f32_e32 v78, 0x3fb8aa3b, v33
	v_exp_f32_e32 v78, v78
	v_lshl_add_u32 v32, v110, 2, s8
	ds_write2st64_b32 v32, v114, v33 offset0:224 offset1:225
	v_add_u32_e32 v114, s42, v34
	ds_write_b32 v32, v78 offset:57856
	s_waitcnt lgkmcnt(0)
	v_lshl_add_u32 v32, v34, 2, s30
	ds_read_b128 v[82:85], v32 offset:57600
	ds_read_b128 v[78:81], v32 offset:57344
	v_or_b32_e32 v32, s43, v106
	v_lshl_add_u32 v34, v32, 2, s8
	v_add_u32_e32 v34, 0xe000, v34
	ds_read2_b32 v[74:75], v34 offset0:64 offset1:80
	s_waitcnt lgkmcnt(1)
	v_mul_f32_e32 v76, v78, v86
	v_cmp_lt_i32_e32 vcc, v32, v114
	s_waitcnt vmcnt(24)
	v_mfma_f32_16x16x32_bf16 v[46:49], v[54:57], v[66:69], v[46:49]
	v_readlane_b32 s9, v33, 63
	s_waitcnt lgkmcnt(0)
	v_sub_f32_e32 v34, v82, v74
	v_min_f32_e32 v34, 0, v34
	v_mul_f32_e32 v34, 0x3fb8aa3b, v34
	v_exp_f32_e32 v34, v34
	v_sub_f32_e32 v54, v82, v75
	v_min_f32_e32 v54, 0, v54
	v_mfma_f32_16x16x32_bf16 v[50:53], v[50:53], v[66:69], v[58:61]
	v_mul_f32_e32 v76, v76, v34
	v_cndmask_b32_e32 v76, 0, v76, vcc
	v_cmp_gt_i32_e32 vcc, v32, v114
	v_mul_f32_e32 v34, v70, v34
	s_nop 0
	v_cndmask_b32_e64 v34, v34, 0, vcc
	v_cvt_pk_bf16_f32 v86, v76, v76
	v_mad_u64_u32 v[76:77], s[2:3], v114, s2, v[32:33]
	v_lshl_add_u32 v76, v76, 1, 0
	v_cvt_pk_bf16_f32 v34, v34, v34
	ds_write_b16 v76, v34 offset:36864
	v_sub_f32_e32 v34, v83, v74
	v_min_f32_e32 v34, 0, v34
	v_mul_f32_e32 v34, 0x3fb8aa3b, v34
	v_exp_f32_e32 v34, v34
	v_mul_f32_e32 v77, v79, v87
	v_or_b32_e32 v70, 1, v114
	ds_write_b16 v76, v86 offset:27648
	v_mul_f32_e32 v77, v77, v34
	v_cndmask_b32_e64 v77, v77, 0, vcc
	v_mul_f32_e32 v34, v71, v34
	v_cmp_le_i32_e32 vcc, v32, v70
	v_cvt_pk_bf16_f32 v77, v77, v77
	s_nop 0
	v_cndmask_b32_e32 v34, 0, v34, vcc
	v_cvt_pk_bf16_f32 v34, v34, v34
	ds_write_b16 v76, v34 offset:37008
	v_sub_f32_e32 v34, v84, v74
	v_min_f32_e32 v34, 0, v34
	v_mul_f32_e32 v34, 0x3fb8aa3b, v34
	v_exp_f32_e32 v34, v34
	ds_write_b16 v76, v77 offset:27792
	v_or_b32_e32 v71, 2, v114
	v_mul_f32_e32 v77, v80, v88
	v_cmp_lt_i32_e32 vcc, v32, v71
	v_mul_f32_e32 v77, v77, v34
	v_mul_f32_e32 v34, v72, v34
	v_cndmask_b32_e32 v77, 0, v77, vcc
	v_cmp_le_i32_e32 vcc, v32, v71
	v_mul_f32_e32 v54, 0x3fb8aa3b, v54
	v_exp_f32_e32 v54, v54
	v_cndmask_b32_e32 v34, 0, v34, vcc
	v_cvt_pk_bf16_f32 v34, v34, v34
	ds_write_b16 v76, v34 offset:37152
	v_sub_f32_e32 v34, v85, v74
	v_min_f32_e32 v34, 0, v34
	v_mul_f32_e32 v34, 0x3fb8aa3b, v34
	v_exp_f32_e32 v34, v34
	v_or_b32_e32 v72, 3, v114
	v_mul_f32_e32 v74, v81, v89
	v_cmp_lt_i32_e32 vcc, v32, v72
	v_mul_f32_e32 v74, v74, v34
	v_mul_f32_e32 v34, v73, v34
	v_cndmask_b32_e32 v74, 0, v74, vcc
	v_cmp_le_i32_e32 vcc, v32, v72
	v_mul_f32_e32 v50, v78, v50
	v_mul_f32_e32 v50, v50, v54
	v_cndmask_b32_e32 v34, 0, v34, vcc
	v_bfe_u32 v73, v34, 16, 1
	v_add3_u32 v34, v34, v73, s81
	ds_write_b16_d16_hi v76, v34 offset:37296
	v_or_b32_e32 v34, 16, v32
	v_cmp_lt_i32_e32 vcc, v34, v114
	v_mul_f32_e32 v46, v46, v54
	v_bfe_u32 v86, v77, 16, 1
	v_cndmask_b32_e32 v50, 0, v50, vcc
	v_cmp_gt_i32_e32 vcc, v34, v114
	v_cvt_pk_bf16_f32 v50, v50, v50
	ds_write_b16 v76, v50 offset:27680
	v_cndmask_b32_e64 v46, v46, 0, vcc
	v_cvt_pk_bf16_f32 v46, v46, v46
	ds_write_b16 v76, v46 offset:36896
	v_sub_f32_e32 v46, v83, v75
	v_min_f32_e32 v46, 0, v46
	v_mul_f32_e32 v46, 0x3fb8aa3b, v46
	v_exp_f32_e32 v46, v46
	v_mul_f32_e32 v50, v79, v51
	v_add3_u32 v77, v77, v86, s81
	ds_write_b16_d16_hi v76, v77 offset:27936
	v_mul_f32_e32 v50, v50, v46
	v_cndmask_b32_e64 v50, v50, 0, vcc
	v_mul_f32_e32 v46, v47, v46
	v_cmp_le_i32_e32 vcc, v34, v70
	v_cvt_pk_bf16_f32 v50, v50, v50
	s_nop 0
	v_cndmask_b32_e32 v46, 0, v46, vcc
	v_cvt_pk_bf16_f32 v46, v46, v46
	ds_write_b16 v76, v46 offset:37040
	v_sub_f32_e32 v46, v84, v75
	v_min_f32_e32 v46, 0, v46
	v_mul_f32_e32 v46, 0x3fb8aa3b, v46
	v_exp_f32_e32 v46, v46
	v_mul_f32_e32 v47, v80, v52
	v_cmp_lt_i32_e32 vcc, v34, v71
	ds_write_b16 v76, v50 offset:27824
	v_mul_f32_e32 v47, v47, v46
	v_cndmask_b32_e32 v47, 0, v47, vcc
	v_mul_f32_e32 v46, v48, v46
	v_cmp_le_i32_e32 vcc, v34, v71
	v_cvt_pk_bf16_f32 v47, v47, v47
	ds_write_b16 v76, v47 offset:27968
	v_cndmask_b32_e32 v46, 0, v46, vcc
	v_cvt_pk_bf16_f32 v46, v46, v46
	ds_write_b16 v76, v46 offset:37184
	v_sub_f32_e32 v46, v85, v75
	v_min_f32_e32 v46, 0, v46
	v_mul_f32_e32 v46, 0x3fb8aa3b, v46
	v_exp_f32_e32 v46, v46
	v_mul_f32_e32 v47, v81, v53
	v_cmp_lt_i32_e32 vcc, v34, v72
	v_bfe_u32 v77, v74, 16, 1
	v_mul_f32_e32 v47, v47, v46
	v_cndmask_b32_e32 v47, 0, v47, vcc
	v_mul_f32_e32 v46, v49, v46
	v_cmp_le_i32_e32 vcc, v34, v72
	v_cvt_pk_bf16_f32 v47, v47, v47
	ds_write_b16 v76, v47 offset:28112
	v_cndmask_b32_e32 v46, 0, v46, vcc
	v_add3_u32 v74, v74, v77, s81
	v_cvt_pk_bf16_f32 v46, v46, v46
	ds_write_b16_d16_hi v76, v74 offset:28080
	ds_write_b16 v76, v46 offset:37328
	v_mov_b32_e32 v33, s84
	ds_read_b128 v[46:49], v33 offset:57600
	ds_read_b128 v[50:53], v33 offset:57616
	s_waitcnt vmcnt(20)
; #define LAS __attribute__((address_space(3)))
; __device__ __forceinline__ unsigned f2bf(float f) { unsigned u = __float_as_uint(f); return (u + 0x7fffu + ((u >> 16) & 1u)) >> 16; }
; __device__ __forceinline__ float gdn_s1(const GdnIn& in, LAS unsigned char* ub, LAS unsigned char* dwb, int w, int lane) {
;     ...
;     { const f32x4 c8a = *(const LAS f32x4*)(GT + 64 + 8 * w), c8b = *(const LAS f32x4*)(GT + 64 + 8 * w + 4);
; #pragma unroll
;       for (int tt = 0; tt < 8; ++tt) KTT[lane * 72 + 8 * w + tt] = (bf16)f2bf(__uint_as_float(in.kt8[tt] << 16) * __expf(cl - (tt < 4 ? c8a[tt & 3] : c8b[tt & 3]))); }
;     asm volatile("s_waitcnt lgkmcnt(0)" ::: "memory");
	v_lshlrev_b32_e32 v55, 16, v137
	v_lshlrev_b32_e32 v54, 16, v135
	v_lshlrev_b32_e32 v57, 16, v133
	s_waitcnt lgkmcnt(1)
	v_sub_f32_e32 v46, s9, v46
	v_sub_f32_e32 v47, s9, v47
	v_sub_f32_e32 v48, s9, v48
	v_sub_f32_e32 v49, s9, v49
	v_mul_f32_e32 v46, 0x3fb8aa3b, v46
	v_mul_f32_e32 v47, 0x3fb8aa3b, v47
	v_mul_f32_e32 v48, 0x3fb8aa3b, v48
	v_mul_f32_e32 v49, 0x3fb8aa3b, v49
	v_exp_f32_e32 v46, v46
	v_exp_f32_e32 v47, v47
	v_exp_f32_e32 v48, v48
	v_exp_f32_e32 v49, v49
	s_waitcnt lgkmcnt(0)
	v_sub_f32_e32 v50, s9, v50
	v_sub_f32_e32 v51, s9, v51
	v_sub_f32_e32 v52, s9, v52
	v_sub_f32_e32 v53, s9, v53
	v_mul_f32_e32 v50, 0x3fb8aa3b, v50
	v_mul_f32_e32 v51, 0x3fb8aa3b, v51
	v_mul_f32_e32 v52, 0x3fb8aa3b, v52
	v_mul_f32_e32 v53, 0x3fb8aa3b, v53
	v_lshlrev_b32_e32 v56, 16, v131
	v_exp_f32_e32 v50, v50
	v_exp_f32_e32 v51, v51
	v_exp_f32_e32 v52, v52
	v_exp_f32_e32 v53, v53
	v_pk_mul_f32 v[46:47], v[46:47], v[56:57]
	v_pk_mul_f32 v[48:49], v[48:49], v[54:55]
	v_bfe_u32 v56, v47, 16, 1
	v_bfe_u32 v54, v49, 16, 1
	v_bfe_u32 v55, v48, 16, 1
	v_bfe_u32 v57, v46, 16, 1
	v_add3_u32 v57, v46, v57, s81
	v_add3_u32 v56, v47, v56, s81
	v_add3_u32 v55, v48, v55, s81
	v_add3_u32 v54, v49, v54, s81
	s_waitcnt vmcnt(16)
	v_lshlrev_b32_e32 v47, 16, v136
	v_lshlrev_b32_e32 v46, 16, v134
	v_lshlrev_b32_e32 v49, 16, v132
	v_lshlrev_b32_e32 v48, 16, v111
	v_pk_mul_f32 v[48:49], v[50:51], v[48:49]
	v_pk_mul_f32 v[46:47], v[52:53], v[46:47]
	v_bfe_u32 v52, v49, 16, 1
	v_bfe_u32 v50, v47, 16, 1
	v_bfe_u32 v51, v46, 16, 1
	v_bfe_u32 v53, v48, 16, 1
	v_mul_lo_u32 v33, v110, s75
	v_add3_u32 v48, v48, v53, s81
	v_add3_u32 v52, v49, v52, s81
	v_add3_u32 v46, v46, v51, s81
	v_add3_u32 v47, v47, v50, s81
	s_mov_b32 s2, 0x7060302
	v_add_u32_e32 v33, s11, v33
	v_perm_b32 v49, v47, v46, s2
	v_perm_b32 v48, v52, v48, s2
	v_perm_b32 v47, v54, v55, s2
	v_perm_b32 v46, v56, v57, s2
	ds_write_b128 v33, v[46:49] offset:46080
	s_waitcnt lgkmcnt(0)
	s_and_b64 vcc, exec, s[50:51]
	s_waitcnt lgkmcnt(0)
	s_barrier
	s_waitcnt vmcnt(0)
	v_lshlrev_b32_e32 v103, 16, v103
	v_lshlrev_b32_e32 v102, 16, v102
	v_lshlrev_b32_e32 v105, 16, v105
	v_lshlrev_b32_e32 v104, 16, v104
	v_lshlrev_b32_e32 v99, 16, v99
	v_lshlrev_b32_e32 v98, 16, v98
	v_lshlrev_b32_e32 v101, 16, v101
	v_lshlrev_b32_e32 v100, 16, v100
	v_lshlrev_b32_e32 v96, 16, v96
	v_lshlrev_b32_e32 v94, 16, v94
	v_lshlrev_b32_e32 v97, 16, v97
	v_lshlrev_b32_e32 v95, 16, v95
	v_lshlrev_b32_e32 v92, 16, v92
	v_lshlrev_b32_e32 v90, 16, v90
	v_lshlrev_b32_e32 v93, 16, v93
	v_lshlrev_b32_e32 v91, 16, v91
	s_cbranch_vccnz .LBB0_1781
	s_add_i32 s2, s26, 2
	s_mul_hi_i32 s3, s2, 0x38e38e39
	s_lshr_b32 s20, s3, 31
	s_ashr_i32 s3, s3, 3
	s_add_i32 s3, s3, s20
	s_mul_i32 s20, s3, 36
	s_sub_i32 s2, s2, s20
	s_ashr_i32 s36, s3, 3
	s_and_b32 s20, s3, 1
	s_lshl_b32 s29, s2, 6
	s_cmp_gt_i32 s2, 3
	s_mov_b64 s[26:27], -1
	s_cbranch_scc0 .LBB0_1778
	s_add_i32 s2, s29, 0xffffff00
	s_lshl_b32 s26, s36, 11
	s_sub_i32 s27, 0x8ff, s29
	s_cmp_eq_u32 s20, 0
	s_cselect_b32 s2, s2, s27
	s_add_i32 s2, s26, s2
	s_addk_i32 s2, 0x1000
	s_mov_b64 s[26:27], 0

; #define LAS __attribute__((address_space(3)))
; __device__ __forceinline__ unsigned f2bf(float f) { unsigned u = __float_as_uint(f); return (u + 0x7fffu + ((u >> 16) & 1u)) >> 16; }
; __device__ __forceinline__ float lo_bf(unsigned w) { return __uint_as_float(w << 16); }
; __device__ __forceinline__ float hi_bf(unsigned w) { return __uint_as_float(w & 0xffff0000u); }
; __device__ __forceinline__ void gdn_s23(CArgs& a, int u, const GdnIn2& in, LAS unsigned char* ub, LAS unsigned char* dwb, int w, int lane, float cl) {
;     ...
;     { const int blk = lane >> 4, c = lane & 15; float T[16];
; #pragma unroll
;       for (int hb = 0; hb < 4; ++hb) {
;           u32x4 arow[4][2];
; #pragma unroll
;           for (int rr = 0; rr < 4; ++rr) { const int r = 4 * hb + rr; arow[rr][0] = *(const LAS u32x4*)(AB + (16 * blk + r) * 72 + 16 * blk); if (hb >= 2) arow[rr][1] = *(const LAS u32x4*)(AB + (16 * blk + r) * 72 + 16 * blk + 8); }
;           asm volatile("s_waitcnt lgkmcnt(0)" ::: "memory");
; #pragma unroll
;           for (int rr = 0; rr < 4; ++rr) { const int r = 4 * hb + rr; float t = (r == c) ? 1.f : 0.f;
;               float t2 = 0.f;
; #pragma unroll
;               for (int j = 0; j < r; ++j) { const unsigned wv = arow[rr][j >> 3][(j >> 1) & 3]; const float av = (j & 1) ? hi_bf(wv) : lo_bf(wv); if (j & 1) t2 -= av * T[j]; else t -= av * T[j]; }
;               t += t2;
;               T[r] = t; DW[(blk * 16 + r) * 16 + c] = (bf16)f2bf(t); } } }
.LBB0_1781:
	v_and_b32_e32 v76, -16, v110
	v_lshl_add_u32 v32, v76, 1, 0
	v_mad_u64_u32 v[66:67], s[2:3], v76, s75, v[32:33]
	ds_read_b128 v[46:49], v66 offset:28080
	v_add_u32_e32 v33, 0x6c00, v66
	s_waitcnt lgkmcnt(0)
	ds_read2_b32 v[48:49], v33 offset0:36 offset1:72
	v_cmp_eq_u32_e32 vcc, 0, v106
	v_lshlrev_b32_e32 v33, 5, v110
	v_lshlrev_b32_e32 v34, 1, v106
	v_cndmask_b32_e64 v77, 0, 1.0, vcc
	v_and_b32_e32 v33, 0xfffffe00, v33
	v_cmp_eq_u32_e32 vcc, 1, v106
	v_add3_u32 v78, s8, v34, v33
	s_waitcnt lgkmcnt(0)
	v_lshlrev_b32_e32 v48, 16, v48
	v_cndmask_b32_e64 v33, 0, 1.0, vcc
	v_fma_f32 v79, -v77, v48, v33
	v_cvt_pk_bf16_f32 v33, v79, v79
	v_cmp_eq_u32_e32 vcc, 2, v106
	s_waitcnt lgkmcnt(0)
	ds_write_b16 v78, v33 offset:55328
	v_lshlrev_b32_e32 v48, 16, v49
	v_cndmask_b32_e64 v33, 0, 1.0, vcc
	v_fma_f32 v33, -v77, v48, v33
	v_and_b32_e32 v48, 0xffff0000, v49
	v_fma_f32 v48, -v79, v48, 0
	v_add_f32_e32 v80, v33, v48
	v_cvt_pk_bf16_f32 v33, v80, v80
	v_cmp_eq_u32_e32 vcc, 3, v106
	ds_write_b16 v78, v33 offset:55360
	v_lshlrev_b32_e32 v48, 16, v46
	v_cndmask_b32_e64 v33, 0, 1.0, vcc
	v_fma_f32 v33, -v77, v48, v33
	v_and_b32_e32 v46, 0xffff0000, v46
	v_lshlrev_b32_e32 v47, 16, v47
	v_fma_f32 v46, -v79, v46, 0
	v_fma_f32 v33, -v80, v47, v33
	v_add_f32_e32 v81, v46, v33
	v_cvt_pk_bf16_f32 v33, v81, v81
	ds_write_b16_d16_hi v78, v77 offset:55296
	ds_write_b16 v78, v33 offset:55392
	ds_read_b128 v[46:49], v66 offset:28224
	s_waitcnt lgkmcnt(0)
	ds_read_b128 v[48:51], v66 offset:28368
	ds_read_b128 v[52:55], v66 offset:28512
	ds_read_b128 v[56:59], v66 offset:28656
	v_cmp_eq_u32_e32 vcc, 4, v106
	s_waitcnt lgkmcnt(0)
	v_ashrrev_i32_e32 v82, 4, v110
	s_waitcnt lgkmcnt(2)
	v_lshlrev_b32_e32 v51, 16, v46
	v_cndmask_b32_e64 v33, 0, 1.0, vcc
	v_and_b32_e32 v46, 0xffff0000, v46
	v_fma_f32 v33, -v77, v51, v33
	v_fma_f32 v46, -v79, v46, 0
	v_lshlrev_b32_e32 v51, 16, v47
	v_and_b32_e32 v47, 0xffff0000, v47
	v_fma_f32 v33, -v80, v51, v33
	v_fma_f32 v46, -v81, v47, v46
	v_add_f32_e32 v83, v46, v33
	v_cvt_pk_bf16_f32 v33, v83, v83
	v_cmp_eq_u32_e32 vcc, 5, v106
	ds_write_b16 v78, v33 offset:55424
	v_lshlrev_b32_e32 v46, 16, v48
	v_cndmask_b32_e64 v33, 0, 1.0, vcc
	v_fma_f32 v33, -v77, v46, v33
	v_and_b32_e32 v46, 0xffff0000, v48
	v_lshlrev_b32_e32 v47, 16, v49
	v_fma_f32 v46, -v79, v46, 0
	v_fma_f32 v33, -v80, v47, v33
	v_and_b32_e32 v47, 0xffff0000, v49
	v_fma_f32 v46, -v81, v47, v46
	v_lshlrev_b32_e32 v47, 16, v50
	v_fma_f32 v33, -v83, v47, v33
	v_add_f32_e32 v84, v46, v33
	v_cvt_pk_bf16_f32 v33, v84, v84
	v_cmp_eq_u32_e32 vcc, 6, v106
	ds_write_b16 v78, v33 offset:55456
	s_waitcnt lgkmcnt(3)
	v_lshlrev_b32_e32 v46, 16, v52
	v_cndmask_b32_e64 v33, 0, 1.0, vcc
	v_fma_f32 v33, -v77, v46, v33
	v_and_b32_e32 v46, 0xffff0000, v52
	v_lshlrev_b32_e32 v47, 16, v53
	v_fma_f32 v46, -v79, v46, 0
	v_fma_f32 v33, -v80, v47, v33
	v_and_b32_e32 v47, 0xffff0000, v53
	v_fma_f32 v46, -v81, v47, v46
	v_lshlrev_b32_e32 v47, 16, v54
	v_fma_f32 v33, -v83, v47, v33
	v_and_b32_e32 v47, 0xffff0000, v54
	v_fma_f32 v46, -v84, v47, v46
	v_add_f32_e32 v85, v33, v46
	v_cvt_pk_bf16_f32 v33, v85, v85
	v_cmp_eq_u32_e32 vcc, 7, v106
	ds_write_b16 v78, v33 offset:55488
	s_waitcnt lgkmcnt(3)
	v_lshlrev_b32_e32 v46, 16, v56
	v_cndmask_b32_e64 v33, 0, 1.0, vcc
	v_fma_f32 v33, -v77, v46, v33
	v_and_b32_e32 v46, 0xffff0000, v56
	v_lshlrev_b32_e32 v47, 16, v57
	v_fma_f32 v46, -v79, v46, 0
	v_fma_f32 v33, -v80, v47, v33
	v_and_b32_e32 v47, 0xffff0000, v57
	v_fma_f32 v46, -v81, v47, v46
	v_lshlrev_b32_e32 v47, 16, v58
	v_fma_f32 v33, -v83, v47, v33
	v_and_b32_e32 v47, 0xffff0000, v58
	v_fma_f32 v46, -v84, v47, v46
	v_lshlrev_b32_e32 v47, 16, v59
	v_fma_f32 v33, -v85, v47, v33
	v_add_f32_e32 v86, v46, v33
	v_cvt_pk_bf16_f32 v33, v86, v86
	ds_write_b16 v78, v33 offset:55520
	ds_read_b128 v[46:49], v66 offset:28800
	ds_read_b128 v[50:53], v66 offset:28944
	ds_read_b128 v[54:57], v66 offset:29088
	ds_read_b128 v[58:61], v66 offset:29232
	ds_read_b128 v[62:65], v66 offset:29248
	v_add_u32_e32 v33, 0x7000, v66
	v_cmp_eq_u32_e32 vcc, 8, v106
	s_waitcnt lgkmcnt(0)
	ds_read2_b32 v[64:65], v33 offset0:72 offset1:108
	v_lshlrev_b32_e32 v67, 16, v46
	v_cndmask_b32_e64 v33, 0, 1.0, vcc
	v_and_b32_e32 v46, 0xffff0000, v46
	v_fma_f32 v33, -v77, v67, v33
	v_fma_f32 v46, -v79, v46, 0
	v_lshlrev_b32_e32 v67, 16, v47
	v_and_b32_e32 v47, 0xffff0000, v47
	v_fma_f32 v33, -v80, v67, v33
	v_fma_f32 v46, -v81, v47, v46
	v_lshlrev_b32_e32 v47, 16, v48
	v_fma_f32 v33, -v83, v47, v33
	v_and_b32_e32 v47, 0xffff0000, v48
	v_fma_f32 v46, -v84, v47, v46
	v_lshlrev_b32_e32 v47, 16, v49
	v_fma_f32 v33, -v85, v47, v33
	v_and_b32_e32 v47, 0xffff0000, v49
	v_fma_f32 v46, -v86, v47, v46
	v_add_f32_e32 v87, v33, v46
	v_cvt_pk_bf16_f32 v33, v87, v87
	v_cmp_eq_u32_e32 vcc, 9, v106
	s_waitcnt lgkmcnt(0)
	ds_write_b16 v78, v33 offset:55552
	v_lshlrev_b32_e32 v46, 16, v50
	v_cndmask_b32_e64 v33, 0, 1.0, vcc
	v_fma_f32 v33, -v77, v46, v33
	v_and_b32_e32 v46, 0xffff0000, v50
	v_lshlrev_b32_e32 v47, 16, v51
	v_fma_f32 v46, -v79, v46, 0
	v_fma_f32 v33, -v80, v47, v33
	v_and_b32_e32 v47, 0xffff0000, v51
	v_fma_f32 v46, -v81, v47, v46
	v_lshlrev_b32_e32 v47, 16, v52
	v_fma_f32 v33, -v83, v47, v33
	v_and_b32_e32 v47, 0xffff0000, v52
	v_fma_f32 v46, -v84, v47, v46
	v_lshlrev_b32_e32 v47, 16, v53
	v_fma_f32 v33, -v85, v47, v33
	v_and_b32_e32 v47, 0xffff0000, v53
	v_fma_f32 v46, -v86, v47, v46
	s_waitcnt lgkmcnt(1)
; #define LAS __attribute__((address_space(3)))
; __device__ __forceinline__ unsigned f2bf(float f) { unsigned u = __float_as_uint(f); return (u + 0x7fffu + ((u >> 16) & 1u)) >> 16; }
; __device__ __forceinline__ float lo_bf(unsigned w) { return __uint_as_float(w << 16); }
; __device__ __forceinline__ float hi_bf(unsigned w) { return __uint_as_float(w & 0xffff0000u); }
; __device__ __forceinline__ void gdn_s23(CArgs& a, int u, const GdnIn2& in, LAS unsigned char* ub, LAS unsigned char* dwb, int w, int lane, float cl) {
;     ...
;     { const int blk = lane >> 4, c = lane & 15; float T[16];
; #pragma unroll
;       for (int hb = 0; hb < 4; ++hb) {
;           u32x4 arow[4][2];
; #pragma unroll
;           for (int rr = 0; rr < 4; ++rr) { const int r = 4 * hb + rr; arow[rr][0] = *(const LAS u32x4*)(AB + (16 * blk + r) * 72 + 16 * blk); if (hb >= 2) arow[rr][1] = *(const LAS u32x4*)(AB + (16 * blk + r) * 72 + 16 * blk + 8); }
;           asm volatile("s_waitcnt lgkmcnt(0)" ::: "memory");
; #pragma unroll
;           for (int rr = 0; rr < 4; ++rr) { const int r = 4 * hb + rr; float t = (r == c) ? 1.f : 0.f;
;               float t2 = 0.f;
; #pragma unroll
;               for (int j = 0; j < r; ++j) { const unsigned wv = arow[rr][j >> 3][(j >> 1) & 3]; const float av = (j & 1) ? hi_bf(wv) : lo_bf(wv); if (j & 1) t2 -= av * T[j]; else t -= av * T[j]; }
;               t += t2;
;               T[r] = t; DW[(blk * 16 + r) * 16 + c] = (bf16)f2bf(t); } } }
	v_lshlrev_b32_e32 v47, 16, v64
	v_fma_f32 v33, -v87, v47, v33
	v_add_f32_e32 v88, v46, v33
	v_cvt_pk_bf16_f32 v33, v88, v88
	v_cmp_eq_u32_e32 vcc, 10, v106
	ds_write_b16 v78, v33 offset:55584
	v_lshlrev_b32_e32 v46, 16, v54
	v_cndmask_b32_e64 v33, 0, 1.0, vcc
	v_fma_f32 v33, -v77, v46, v33
	v_and_b32_e32 v46, 0xffff0000, v54
	v_lshlrev_b32_e32 v47, 16, v55
	v_fma_f32 v46, -v79, v46, 0
	v_fma_f32 v33, -v80, v47, v33
	v_and_b32_e32 v47, 0xffff0000, v55
	v_fma_f32 v46, -v81, v47, v46
	v_lshlrev_b32_e32 v47, 16, v56
	v_fma_f32 v33, -v83, v47, v33
	v_and_b32_e32 v47, 0xffff0000, v56
	v_fma_f32 v46, -v84, v47, v46
	v_lshlrev_b32_e32 v47, 16, v57
	v_fma_f32 v33, -v85, v47, v33
	v_and_b32_e32 v47, 0xffff0000, v57
	v_fma_f32 v46, -v86, v47, v46
	v_lshlrev_b32_e32 v47, 16, v65
	v_fma_f32 v33, -v87, v47, v33
	v_and_b32_e32 v47, 0xffff0000, v65
	v_fma_f32 v46, -v88, v47, v46
	v_add_f32_e32 v89, v33, v46
	v_cvt_pk_bf16_f32 v33, v89, v89
	v_cmp_eq_u32_e32 vcc, 11, v106
	ds_write_b16 v78, v33 offset:55616
	v_lshlrev_b32_e32 v46, 16, v58
	v_cndmask_b32_e64 v33, 0, 1.0, vcc
	v_fma_f32 v33, -v77, v46, v33
	v_and_b32_e32 v46, 0xffff0000, v58
	v_lshlrev_b32_e32 v47, 16, v59
	v_fma_f32 v46, -v79, v46, 0
	v_fma_f32 v33, -v80, v47, v33
	v_and_b32_e32 v47, 0xffff0000, v59
	v_fma_f32 v46, -v81, v47, v46
	v_lshlrev_b32_e32 v47, 16, v60
	v_fma_f32 v33, -v83, v47, v33
	v_and_b32_e32 v47, 0xffff0000, v60
	v_fma_f32 v46, -v84, v47, v46
	v_lshlrev_b32_e32 v47, 16, v61
	v_fma_f32 v33, -v85, v47, v33
	v_and_b32_e32 v47, 0xffff0000, v61
	v_fma_f32 v46, -v86, v47, v46
	v_lshlrev_b32_e32 v47, 16, v62
	v_fma_f32 v33, -v87, v47, v33
	v_and_b32_e32 v47, 0xffff0000, v62
	v_fma_f32 v46, -v88, v47, v46
	v_lshlrev_b32_e32 v47, 16, v63
	v_fma_f32 v33, -v89, v47, v33
	v_add_f32_e32 v111, v46, v33
	v_cvt_pk_bf16_f32 v33, v111, v111
	ds_write_b16 v78, v33 offset:55648
	ds_read_b128 v[46:49], v66 offset:29376
	ds_read_b128 v[50:53], v66 offset:29392
	v_or_b32_e32 v33, 15, v110
	v_mad_u64_u32 v[32:33], s[2:3], v33, s75, v[32:33]
	v_cmp_eq_u32_e32 vcc, 12, v106
	s_waitcnt lgkmcnt(0)
	ds_read_b128 v[52:55], v66 offset:29520
	ds_read_b128 v[56:59], v66 offset:29536
	ds_read_b128 v[60:63], v66 offset:29664
	ds_read_b128 v[64:67], v66 offset:29680
	ds_read_b128 v[68:71], v32 offset:27648
	ds_read_b128 v[72:75], v32 offset:27664
	v_cndmask_b32_e64 v32, 0, 1.0, vcc
	v_lshlrev_b32_e32 v33, 16, v46
	v_fma_f32 v32, -v77, v33, v32
	v_and_b32_e32 v33, 0xffff0000, v46
	v_lshlrev_b32_e32 v46, 16, v47
	v_fma_f32 v33, -v79, v33, 0
	v_fma_f32 v32, -v80, v46, v32
	v_and_b32_e32 v46, 0xffff0000, v47
	v_fma_f32 v33, -v81, v46, v33
	v_lshlrev_b32_e32 v46, 16, v48
	v_fma_f32 v32, -v83, v46, v32
	v_and_b32_e32 v46, 0xffff0000, v48
	v_fma_f32 v33, -v84, v46, v33
	v_lshlrev_b32_e32 v46, 16, v49
	v_fma_f32 v32, -v85, v46, v32
	v_and_b32_e32 v46, 0xffff0000, v49
	v_fma_f32 v33, -v86, v46, v33
	v_lshlrev_b32_e32 v46, 16, v50
	v_fma_f32 v32, -v87, v46, v32
	v_and_b32_e32 v46, 0xffff0000, v50
	v_fma_f32 v33, -v88, v46, v33
	v_lshlrev_b32_e32 v46, 16, v51
	v_fma_f32 v32, -v89, v46, v32
	v_and_b32_e32 v46, 0xffff0000, v51
	v_fma_f32 v33, -v111, v46, v33
	v_add_f32_e32 v32, v33, v32
	v_cvt_pk_bf16_f32 v33, v32, v32
	v_cmp_eq_u32_e32 vcc, 13, v106
	s_waitcnt lgkmcnt(0)
	ds_write_b16 v78, v33 offset:55680
	s_waitcnt lgkmcnt(6)
	v_lshlrev_b32_e32 v46, 16, v52
	v_cndmask_b32_e64 v33, 0, 1.0, vcc
	v_fma_f32 v33, -v77, v46, v33
	v_and_b32_e32 v46, 0xffff0000, v52
	v_lshlrev_b32_e32 v47, 16, v53
	v_fma_f32 v46, -v79, v46, 0
	v_fma_f32 v33, -v80, v47, v33
	v_and_b32_e32 v47, 0xffff0000, v53
	v_fma_f32 v46, -v81, v47, v46
	v_lshlrev_b32_e32 v47, 16, v54
	v_fma_f32 v33, -v83, v47, v33
	v_and_b32_e32 v47, 0xffff0000, v54
	v_fma_f32 v46, -v84, v47, v46
	v_lshlrev_b32_e32 v47, 16, v55
	v_fma_f32 v33, -v85, v47, v33
	v_and_b32_e32 v47, 0xffff0000, v55
	v_fma_f32 v46, -v86, v47, v46
	s_waitcnt lgkmcnt(5)
	v_lshlrev_b32_e32 v47, 16, v56
	v_fma_f32 v33, -v87, v47, v33
	v_and_b32_e32 v47, 0xffff0000, v56
	v_fma_f32 v46, -v88, v47, v46
	v_lshlrev_b32_e32 v47, 16, v57
	v_fma_f32 v33, -v89, v47, v33
	v_and_b32_e32 v47, 0xffff0000, v57
	v_fma_f32 v46, -v111, v47, v46
	v_lshlrev_b32_e32 v47, 16, v58
	v_fma_f32 v33, -v32, v47, v33
	v_add_f32_e32 v33, v46, v33
	v_cvt_pk_bf16_f32 v46, v33, v33
	v_cmp_eq_u32_e32 vcc, 14, v106
	ds_write_b16 v78, v46 offset:55712
	s_waitcnt lgkmcnt(5)
	v_lshlrev_b32_e32 v47, 16, v60
	v_cndmask_b32_e64 v46, 0, 1.0, vcc
	v_fma_f32 v46, -v77, v47, v46
	v_and_b32_e32 v47, 0xffff0000, v60
	v_lshlrev_b32_e32 v48, 16, v61
	v_fma_f32 v47, -v79, v47, 0
	v_fma_f32 v46, -v80, v48, v46
	v_and_b32_e32 v48, 0xffff0000, v61
	v_fma_f32 v47, -v81, v48, v47
	v_lshlrev_b32_e32 v48, 16, v62
	v_fma_f32 v46, -v83, v48, v46
	v_and_b32_e32 v48, 0xffff0000, v62
	v_fma_f32 v47, -v84, v48, v47
	v_lshlrev_b32_e32 v48, 16, v63
	v_fma_f32 v46, -v85, v48, v46
	v_and_b32_e32 v48, 0xffff0000, v63
	v_fma_f32 v47, -v86, v48, v47
	s_waitcnt lgkmcnt(4)
	v_lshlrev_b32_e32 v48, 16, v64
	v_fma_f32 v46, -v87, v48, v46
	v_and_b32_e32 v48, 0xffff0000, v64
	v_fma_f32 v47, -v88, v48, v47
	v_lshlrev_b32_e32 v48, 16, v65
	v_fma_f32 v46, -v89, v48, v46
	v_and_b32_e32 v48, 0xffff0000, v65
	v_fma_f32 v47, -v111, v48, v47
	v_lshlrev_b32_e32 v48, 16, v66
	v_fma_f32 v46, -v32, v48, v46
	v_and_b32_e32 v48, 0xffff0000, v66
	v_fma_f32 v47, -v33, v48, v47
	v_add_f32_e32 v46, v46, v47
	v_cvt_pk_bf16_f32 v47, v46, v46
	v_cmp_eq_u32_e32 vcc, 15, v106
	ds_write_b16 v78, v47 offset:55744
	s_waitcnt lgkmcnt(4)
; #define LAS __attribute__((address_space(3)))
; __device__ __forceinline__ void gdn_s23(CArgs& a, int u, const GdnIn2& in, LAS unsigned char* ub, LAS unsigned char* dwb, int w, int lane, float cl) {
;     ...
;     { const int blk = lane >> 4, c = lane & 15; float T[16];
; #pragma unroll
;       for (int hb = 0; hb < 4; ++hb) {
;           u32x4 arow[4][2];
; #pragma unroll
;           for (int rr = 0; rr < 4; ++rr) { const int r = 4 * hb + rr; arow[rr][0] = *(const LAS u32x4*)(AB + (16 * blk + r) * 72 + 16 * blk); if (hb >= 2) arow[rr][1] = *(const LAS u32x4*)(AB + (16 * blk + r) * 72 + 16 * blk + 8); }
;           asm volatile("s_waitcnt lgkmcnt(0)" ::: "memory");
; #pragma unroll
;           for (int rr = 0; rr < 4; ++rr) { const int r = 4 * hb + rr; float t = (r == c) ? 1.f : 0.f;
;               float t2 = 0.f;
; #pragma unroll
;               for (int j = 0; j < r; ++j) { const unsigned wv = arow[rr][j >> 3][(j >> 1) & 3]; const float av = (j & 1) ? hi_bf(wv) : lo_bf(wv); if (j & 1) t2 -= av * T[j]; else t -= av * T[j]; }
;               t += t2;
;               T[r] = t; DW[(blk * 16 + r) * 16 + c] = (bf16)f2bf(t); } } }
;     asm volatile("s_waitcnt lgkmcnt(0)" ::: "memory");
;     f32x4 X[4];
; #pragma unroll
;     for (int I = 0; I < 4; ++I) {
;         const f32x4 br = *(const LAS f32x4*)(GT + 16 * I + 4 * kg), er = *(const LAS f32x4*)(GT + 128 + 16 * I + 4 * kg);
;         const f32x4 Rf = (f32x4){__uint_as_float(in.R[I].x << 16), __uint_as_float(in.R[I].y << 16), __uint_as_float(in.R[I].z << 16), __uint_as_float(in.R[I].w << 16)};
;         f32x4 acc = isW ? br * er * Rf : br * Rf;
; #pragma unroll
;         for (int P = 0; 2 * P < I; ++P) {
;             const u32x2 alo = *(const LAS u32x2*)(AB + (16 * I + fr) * 72 + 32 * P + 4 * kg);
;             const u32x2 ahi = (2 * P + 1 < I) ? *(const LAS u32x2*)(AB + (16 * I + fr) * 72 + 32 * P + 16 + 4 * kg) : (u32x2){0u, 0u};
;             const u32x2 xlo = cvt4(-X[2 * P]); const u32x2 xhi = (2 * P + 1 < I) ? cvt4(-X[2 * P + 1]) : (u32x2){0u, 0u};
;             acc = __builtin_amdgcn_mfma_f32_16x16x32_bf16(frag2(alo, ahi), frag2(xlo, xhi), acc, 0, 0, 0); }
;         const u32x2 dlo = *(const LAS u32x2*)(DW + (I * 16 + fr) * 16 + 4 * kg);
;         X[I] = __builtin_amdgcn_mfma_f32_16x16x32_bf16(frag2(dlo, (u32x2){0u, 0u}), frag2(cvt4(acc), (u32x2){0u, 0u}), (f32x4){0.f, 0.f, 0.f, 0.f}, 0, 0, 0);
;     }
	v_lshlrev_b32_e32 v48, 16, v68
	v_cndmask_b32_e64 v47, 0, 1.0, vcc
	v_fma_f32 v47, -v77, v48, v47
	v_and_b32_e32 v48, 0xffff0000, v68
	v_lshlrev_b32_e32 v49, 16, v69
	v_fma_f32 v48, -v79, v48, 0
	v_fma_f32 v47, -v80, v49, v47
	v_and_b32_e32 v49, 0xffff0000, v69
	v_fma_f32 v48, -v81, v49, v48
	v_lshlrev_b32_e32 v49, 16, v70
	v_fma_f32 v47, -v83, v49, v47
	v_and_b32_e32 v49, 0xffff0000, v70
	v_fma_f32 v48, -v84, v49, v48
	v_lshlrev_b32_e32 v49, 16, v71
	v_fma_f32 v47, -v85, v49, v47
	v_and_b32_e32 v49, 0xffff0000, v71
	v_fma_f32 v48, -v86, v49, v48
	s_waitcnt lgkmcnt(3)
	v_lshlrev_b32_e32 v49, 16, v72
	v_fma_f32 v47, -v87, v49, v47
	v_and_b32_e32 v49, 0xffff0000, v72
	v_fma_f32 v48, -v88, v49, v48
	v_lshlrev_b32_e32 v49, 16, v73
	v_fma_f32 v47, -v89, v49, v47
	v_and_b32_e32 v49, 0xffff0000, v73
	v_fma_f32 v48, -v111, v49, v48
	v_lshlrev_b32_e32 v49, 16, v74
	v_fma_f32 v32, -v32, v49, v47
	v_and_b32_e32 v47, 0xffff0000, v74
	v_fma_f32 v33, -v33, v47, v48
	v_lshlrev_b32_e32 v47, 16, v75
	v_fma_f32 v32, -v46, v47, v32
	v_add_f32_e32 v32, v33, v32
	v_cvt_pk_bf16_f32 v32, v32, v32
	ds_write_b16 v78, v32 offset:55776
	s_waitcnt lgkmcnt(0)
	v_add_u32_e32 v79, s8, v76
	ds_read_b128 v[46:49], v79 offset:57344
	ds_read_b128 v[54:57], v79 offset:57856
	v_lshlrev_b32_e32 v70, 3, v82
	v_sub_u32_e32 v33, v79, v70
	s_waitcnt vmcnt(15)
	v_lshlrev_b32_e32 v50, 16, v123
	s_waitcnt vmcnt(14)
	v_lshlrev_b32_e32 v51, 16, v139
	s_waitcnt lgkmcnt(0)
	v_pk_mul_f32 v[60:61], v[46:47], v[54:55]
	v_pk_mul_f32 v[58:59], v[48:49], v[56:57]
	v_cndmask_b32_e64 v47, v47, v61, s[38:39]
	v_cndmask_b32_e64 v46, v46, v60, s[38:39]
	v_pk_mul_f32 v[50:51], v[46:47], v[50:51]
	v_lshl_add_u32 v46, v106, 5, v33
	ds_read_b64 v[46:47], v46 offset:55296
	v_cndmask_b32_e64 v48, v48, v58, s[38:39]
	s_waitcnt vmcnt(13)
	v_lshlrev_b32_e32 v52, 16, v141
	s_waitcnt vmcnt(12)
	v_lshlrev_b32_e32 v53, 16, v142
	v_cndmask_b32_e64 v49, v49, v59, s[38:39]
	v_pk_mul_f32 v[52:53], v[48:49], v[52:53]
	v_mov_b32_e32 v48, v35
	v_mov_b32_e32 v49, v35
	v_cvt_pk_bf16_f32 v50, v50, v51
	v_cvt_pk_bf16_f32 v51, v52, v53
	v_mov_b32_e32 v52, v35
	v_mov_b32_e32 v53, v35
	s_waitcnt vmcnt(9)
	v_lshlrev_b32_e32 v60, 16, v138
	s_waitcnt vmcnt(8)
	v_lshlrev_b32_e32 v61, 16, v140
	s_waitcnt lgkmcnt(0)
	v_mfma_f32_16x16x32_bf16 v[62:65], v[46:49], v[50:53], 0
	ds_read_b128 v[46:49], v79 offset:57408
	ds_read_b128 v[50:53], v79 offset:57920
	v_or_b32_e32 v89, 16, v106
	v_add_u32_e32 v86, 0, v70
	v_lshlrev_b32_e32 v58, 16, v121
	v_lshlrev_b32_e32 v59, 16, v122
	s_waitcnt lgkmcnt(0)
	v_pk_mul_f32 v[66:67], v[48:49], v[52:53]
	v_pk_mul_f32 v[68:69], v[46:47], v[50:51]
	v_cndmask_b32_e64 v49, v49, v67, s[38:39]
	v_xor_b32_e32 v67, 0x80000000, v63
	v_cndmask_b32_e64 v48, v48, v66, s[38:39]
	v_cndmask_b32_e64 v46, v46, v68, s[38:39]
	v_xor_b32_e32 v66, 0x80000000, v62
	v_bfe_u32 v68, v67, 16, 1
	v_add3_u32 v67, v67, v68, s81
	v_bfe_u32 v68, v66, 16, 1
	v_add3_u32 v66, v66, v68, s81
	v_cndmask_b32_e64 v47, v47, v69, s[38:39]
	v_pk_mul_f32 v[48:49], v[48:49], v[60:61]
	v_mad_u32_u24 v78, v89, s75, v86
	v_xor_b32_e32 v61, 0x80000000, v65
	v_lshrrev_b32_e32 v66, 16, v66
	v_pk_mul_f32 v[46:47], v[46:47], v[58:59]
	ds_read_b64 v[58:59], v78 offset:27648
	v_xor_b32_e32 v60, 0x80000000, v64
	v_and_or_b32 v74, v67, s80, v66
	v_cvt_pk_bf16_f32 v75, v60, v61
	v_mov_b32_e32 v60, v35
	v_mov_b32_e32 v61, v35
	v_mov_b32_e32 v76, v35
	v_mov_b32_e32 v77, v35
	s_waitcnt vmcnt(7)
	v_lshlrev_b32_e32 v70, 16, v107
	s_waitcnt vmcnt(6)
	v_lshlrev_b32_e32 v71, 16, v108
	s_waitcnt lgkmcnt(0)
	v_mfma_f32_16x16x32_bf16 v[46:49], v[58:61], v[74:77], v[46:49]
	v_lshl_add_u32 v58, v89, 5, v33
	ds_read_b64 v[58:59], v58 offset:55296
	s_waitcnt vmcnt(5)
	v_lshlrev_b32_e32 v72, 16, v109
	s_waitcnt vmcnt(4)
	v_lshlrev_b32_e32 v73, 16, v117
	v_or_b32_e32 v88, 32, v106
	s_nop 0
	v_bfe_u32 v66, v46, 16, 1
	v_add3_u32 v46, v46, v66, s81
	v_bfe_u32 v66, v47, 16, 1
	v_lshrrev_b32_e32 v46, 16, v46
	v_add3_u32 v47, v47, v66, s81
	v_and_or_b32 v46, v47, s80, v46
	v_cvt_pk_bf16_f32 v47, v48, v49
	v_mov_b32_e32 v48, v35
	v_mov_b32_e32 v49, v35
	s_waitcnt vmcnt(1)
	v_lshlrev_b32_e32 v84, 16, v119
	s_waitcnt vmcnt(0)
	v_lshlrev_b32_e32 v85, 16, v120
	s_waitcnt lgkmcnt(0)
	v_mfma_f32_16x16x32_bf16 v[66:69], v[58:61], v[46:49], 0
	ds_read_b128 v[46:49], v79 offset:57472
	ds_read_b128 v[58:61], v79 offset:57984
	v_or_b32_e32 v87, 48, v106
	s_ashr_i32 s29, s28, 31
	s_lshl_b64 s[52:53], s[28:29], 13
	s_add_u32 s26, s85, s52
	s_waitcnt lgkmcnt(0)
	v_pk_mul_f32 v[80:81], v[46:47], v[58:59]
	v_pk_mul_f32 v[76:77], v[48:49], v[60:61]
	v_cndmask_b32_e64 v47, v47, v81, s[38:39]
	v_cndmask_b32_e64 v46, v46, v80, s[38:39]
	v_cndmask_b32_e64 v49, v49, v77, s[38:39]
	v_cndmask_b32_e64 v48, v48, v76, s[38:39]
	v_pk_mul_f32 v[46:47], v[46:47], v[70:71]
	v_add_u32_e32 v70, 0x7000, v78
	v_xor_b32_e32 v81, 0x80000000, v67
	v_pk_mul_f32 v[48:49], v[48:49], v[72:73]
	ds_read2_b64 v[70:73], v70 offset0:160 offset1:164
	v_xor_b32_e32 v76, 0x80000000, v66
	v_xor_b32_e32 v80, 0x80000000, v69
	v_xor_b32_e32 v77, 0x80000000, v68
	v_cvt_pk_bf16_f32 v76, v76, v81
	v_cvt_pk_bf16_f32 v77, v77, v80
	v_lshlrev_b32_e32 v81, 16, v118
	s_addc_u32 s27, s64, s53
	s_waitcnt lgkmcnt(0)
	v_mfma_f32_16x16x32_bf16 v[46:49], v[70:73], v[74:77], v[46:49]
	v_lshl_add_u32 v70, v88, 5, v33
	ds_read_b64 v[70:71], v70 offset:55296
	v_mov_b32_e32 v72, v35
	v_mov_b32_e32 v73, v35
	v_lshl_add_u32 v33, v87, 5, v33
	s_nop 2
	v_cvt_pk_bf16_f32 v46, v46, v47
	v_cvt_pk_bf16_f32 v47, v48, v49
	v_mov_b32_e32 v48, v35
	v_mov_b32_e32 v49, v35
	v_lshlrev_b32_e32 v80, 16, v116
	s_add_u32 s28, s71, s52
	s_waitcnt lgkmcnt(0)
; #define LAS __attribute__((address_space(3)))
; __device__ __forceinline__ unsigned f2bf(float f) { unsigned u = __float_as_uint(f); return (u + 0x7fffu + ((u >> 16) & 1u)) >> 16; }
; __device__ __forceinline__ void gdn_s23(CArgs& a, int u, const GdnIn2& in, LAS unsigned char* ub, LAS unsigned char* dwb, int w, int lane, float cl) {
;     ...
;             acc = __builtin_amdgcn_mfma_f32_16x16x32_bf16(frag2(alo, ahi), frag2(xlo, xhi), acc, 0, 0, 0); }
;         const u32x2 dlo = *(const LAS u32x2*)(DW + (I * 16 + fr) * 16 + 4 * kg);
;         X[I] = __builtin_amdgcn_mfma_f32_16x16x32_bf16(frag2(dlo, (u32x2){0u, 0u}), frag2(cvt4(acc), (u32x2){0u, 0u}), (f32x4){0.f, 0.f, 0.f, 0.f}, 0, 0, 0);
;     }
;     const bf16x8 Xb01 = frag2(cvt4(X[0]), cvt4(X[1])), Xb23 = frag2(cvt4(X[2]), cvt4(X[3]));
;     const float ecl = __expf(cl);
;     bf16* ftp = FTo + (c0 + fr) * 64 + 4 * kg; bf16* btp = BTo + (c0 + fr) * 64 + 4 * kg; bf16* ep = Eo + (4 * kg) * 64 + c0 + fr; bf16* mp = Mo + (4 * kg) * 64 + c0 + fr;
; #pragma unroll
;     for (int t4 = 0; t4 < 4; ++t4) {
;         const LAS bf16* ar = ATT + (16 * t4 + fr) * 72 + 4 * kg; const LAS bf16* kr = KTT + (16 * t4 + fr) * 72 + 4 * kg;
;         f32x4 pa = (f32x4){0.f, 0.f, 0.f, 0.f}, pk = (f32x4){0.f, 0.f, 0.f, 0.f};
;         pa = __builtin_amdgcn_mfma_f32_16x16x32_bf16(frag2(*(const LAS u32x2*)ar, *(const LAS u32x2*)(ar + 16)), Xb01, pa, 0, 0, 0);
;         pa = __builtin_amdgcn_mfma_f32_16x16x32_bf16(frag2(*(const LAS u32x2*)(ar + 32), *(const LAS u32x2*)(ar + 48)), Xb23, pa, 0, 0, 0);
;         pk = __builtin_amdgcn_mfma_f32_16x16x32_bf16(frag2(*(const LAS u32x2*)kr, *(const LAS u32x2*)(kr + 16)), Xb01, pk, 0, 0, 0);
;         pk = __builtin_amdgcn_mfma_f32_16x16x32_bf16(frag2(*(const LAS u32x2*)(kr + 32), *(const LAS u32x2*)(kr + 48)), Xb23, pk, 0, 0, 0);
;         if (!isW) {
;             *(u32x2*)(ftp + 16 * t4) = cvt4(pa);
;             *(u32x2*)(btp + 16 * t4) = cvt4(pk);
;         } else {
;             const f32x4 ec = *(const LAS f32x4*)(GT + 128 + 16 * t4 + 4 * kg);
; #pragma unroll
;             for (int e = 0; e < 4; ++e) { const int row = 16 * t4 + 4 * kg + e, col = c0 + fr;
;                 ep[(16 * t4 + e) * 64] = (bf16)f2bf(ec[e] * __uint_as_float(in.Qv[t4][e] << 16) - pa[e]);
;                 mp[(16 * t4 + e) * 64] = (bf16)f2bf((row == col ? ecl : 0.f) - pk[e]); }
;         }
;     }
	v_mfma_f32_16x16x32_bf16 v[70:73], v[70:73], v[46:49], 0
	ds_read_b128 v[126:129], v79 offset:57536
	ds_read_b128 v[46:49], v79 offset:58048
	v_add_u32_e32 v79, 0x7800, v78
	ds_read2_b64 v[118:121], v79 offset0:192 offset1:196
	ds_read_b64 v[78:79], v78 offset:32320
	s_nop 2
	v_xor_b32_e32 v83, 0x80000000, v70
	s_waitcnt lgkmcnt(2)
	v_pk_mul_f32 v[108:109], v[128:129], v[48:49]
	v_pk_mul_f32 v[114:115], v[126:127], v[46:47]
	v_cndmask_b32_e64 v109, v129, v109, s[38:39]
	v_cndmask_b32_e64 v108, v128, v108, s[38:39]
	v_pk_mul_f32 v[116:117], v[108:109], v[84:85]
	v_xor_b32_e32 v84, 0x80000000, v71
	v_bfe_u32 v85, v84, 16, 1
	v_add3_u32 v84, v84, v85, s81
	v_bfe_u32 v85, v83, 16, 1
	v_cndmask_b32_e64 v115, v127, v115, s[38:39]
	v_cndmask_b32_e64 v114, v126, v114, s[38:39]
	v_add3_u32 v83, v83, v85, s81
	v_pk_mul_f32 v[114:115], v[114:115], v[80:81]
	v_xor_b32_e32 v81, 0x80000000, v73
	v_lshrrev_b32_e32 v83, 16, v83
	s_waitcnt lgkmcnt(1)
	v_mfma_f32_16x16x32_bf16 v[74:77], v[118:121], v[74:77], v[114:117]
	v_xor_b32_e32 v80, 0x80000000, v72
	s_addc_u32 s29, s18, s53
	s_add_u32 s2, s19, s52
	v_and_or_b32 v114, v84, s80, v83
	v_bfe_u32 v83, v81, 16, 1
	v_add3_u32 v81, v81, v83, s81
	v_bfe_u32 v83, v80, 16, 1
	v_add3_u32 v80, v80, v83, s81
	v_lshrrev_b32_e32 v80, 16, v80
	v_and_or_b32 v115, v81, s80, v80
	v_mov_b32_e32 v80, v35
	v_mov_b32_e32 v81, v35
	v_mov_b32_e32 v116, v35
	v_mov_b32_e32 v117, v35
	v_lshlrev_b32_e32 v32, 2, v82
	s_addc_u32 s3, s66, s53
	s_waitcnt lgkmcnt(0)
	v_mfma_f32_16x16x32_bf16 v[74:77], v[78:81], v[114:117], v[74:77]
	ds_read_b64 v[78:79], v33 offset:55296
	s_add_u32 s52, s21, s52
	s_addc_u32 s53, s70, s53
	s_and_b64 vcc, exec, s[48:49]
	s_nop 3
	v_cvt_pk_bf16_f32 v74, v74, v75
	v_cvt_pk_bf16_f32 v75, v76, v77
	v_cvt_pk_bf16_f32 v62, v62, v63
	v_cvt_pk_bf16_f32 v63, v64, v65
	v_cvt_pk_bf16_f32 v64, v66, v67
	v_cvt_pk_bf16_f32 v65, v68, v69
	v_mov_b32_e32 v76, v35
	v_mov_b32_e32 v77, v35
	s_waitcnt lgkmcnt(0)
	s_nop 0
	v_mfma_f32_16x16x32_bf16 v[74:77], v[78:81], v[74:77], 0
	v_cvt_pk_bf16_f32 v66, v70, v71
	v_cvt_pk_bf16_f32 v67, v72, v73
	s_nop 5
	v_cvt_pk_bf16_f32 v68, v74, v75
	v_cvt_pk_bf16_f32 v69, v76, v77
	v_ashrrev_i32_e32 v33, 31, v32
	v_lshlrev_b32_e32 v70, 7, v45
	v_mov_b32_e32 v71, v35
	v_lshlrev_b64 v[74:75], 1, v[32:33]
	v_mul_u32_u24_e32 v33, 0x48, v106
	v_lshl_add_u64 v[72:73], s[28:29], 0, v[70:71]
	v_lshl_add_u64 v[70:71], s[52:53], 0, v[70:71]
	v_lshl_add_u32 v33, v33, 1, v86
	v_lshl_add_u64 v[80:81], v[72:73], 0, v[74:75]
	v_lshl_add_u64 v[78:79], v[70:71], 0, v[74:75]
	v_add_u32_e32 v74, 0x9000, v33
	ds_read2_b64 v[70:73], v74 offset1:4
	ds_read2_b64 v[74:77], v74 offset0:8 offset1:12
	s_waitcnt lgkmcnt(1)
	v_mfma_f32_16x16x32_bf16 v[70:73], v[70:73], v[62:65], 0
	v_add_u32_e32 v33, 0xb000, v33
	ds_read2_b64 v[106:109], v33 offset0:136 offset1:140
	s_mov_b64 s[28:29], -1
	s_waitcnt lgkmcnt(1)
	v_mfma_f32_16x16x32_bf16 v[70:73], v[74:77], v[66:69], v[70:73]
	ds_read2_b64 v[74:77], v33 offset0:128 offset1:132
	s_waitcnt lgkmcnt(0)
	v_mfma_f32_16x16x32_bf16 v[74:77], v[74:77], v[62:65], 0
	v_mfma_f32_16x16x32_bf16 v[74:77], v[106:109], v[66:69], v[74:77]
	s_cbranch_vccnz .LBB0_1783
	s_nop 2
	v_cvt_pk_bf16_f32 v84, v70, v71
	v_cvt_pk_bf16_f32 v85, v72, v73
	global_store_dwordx2 v[80:81], v[84:85], off
	s_nop 0
	v_cvt_pk_bf16_f32 v84, v74, v75
	v_cvt_pk_bf16_f32 v85, v76, v77
	s_mov_b64 s[28:29], 0
	global_store_dwordx2 v[78:79], v[84:85], off
.LBB0_1783:
	v_lshlrev_b32_e32 v82, 8, v82
	v_mul_f32_e32 v33, s9, v196
	v_ashrrev_i32_e32 v83, 31, v82
	v_exp_f32_e32 v33, v33
	v_lshlrev_b64 v[82:83], 1, v[82:83]
	v_lshl_add_u64 v[84:85], s[26:27], 0, v[82:83]
	v_lshl_add_u64 v[82:83], s[2:3], 0, v[82:83]
	v_lshl_add_u64 v[84:85], v[84:85], 0, s[78:79]
	v_lshl_add_u64 v[82:83], v[82:83], 0, s[78:79]
	v_lshl_add_u64 v[84:85], v[84:85], 0, v[34:35]
	s_andn2_b64 vcc, exec, s[28:29]
	v_lshl_add_u64 v[82:83], v[82:83], 0, v[34:35]
	s_cbranch_vccnz .LBB0_1785
	v_fma_f32 v34, v103, v54, -v70
	v_cvt_pk_bf16_f32 v34, v34, v34
	v_cmp_eq_u32_e32 vcc, v32, v45
	global_store_short v[84:85], v34, off
	s_nop 0
	v_cndmask_b32_e32 v34, 0, v33, vcc
	v_sub_f32_e32 v34, v34, v74
	v_cvt_pk_bf16_f32 v34, v34, v34
	global_store_short v[82:83], v34, off
	v_or_b32_e32 v34, 1, v32
	v_fma_f32 v54, v102, v55, -v71
	v_cmp_eq_u32_e32 vcc, v34, v45
	v_cvt_pk_bf16_f32 v54, v54, v54
	s_nop 0
	v_cndmask_b32_e32 v34, 0, v33, vcc
	v_sub_f32_e32 v34, v34, v75
	global_store_short v[84:85], v54, off offset:128
	v_cvt_pk_bf16_f32 v34, v34, v34
	global_store_short v[82:83], v34, off offset:128
	v_or_b32_e32 v34, 2, v32
	v_fma_f32 v54, v105, v56, -v72
	v_cmp_eq_u32_e32 vcc, v34, v45
	v_cvt_pk_bf16_f32 v54, v54, v54
	s_nop 0
	v_cndmask_b32_e32 v34, 0, v33, vcc
	v_sub_f32_e32 v34, v34, v76
	global_store_short v[84:85], v54, off offset:256
	v_cvt_pk_bf16_f32 v34, v34, v34
	global_store_short v[82:83], v34, off offset:256
	v_or_b32_e32 v34, 3, v32
	v_fma_f32 v54, v104, v57, -v73
	v_cmp_eq_u32_e32 vcc, v34, v45
	v_cvt_pk_bf16_f32 v54, v54, v54
	s_nop 0
	v_cndmask_b32_e32 v34, 0, v33, vcc
	v_sub_f32_e32 v34, v34, v77
	global_store_short v[84:85], v54, off offset:384
	v_cvt_pk_bf16_f32 v34, v34, v34
	global_store_short v[82:83], v34, off offset:384
; #define LAS __attribute__((address_space(3)))
; __device__ __forceinline__ unsigned f2bf(float f) { unsigned u = __float_as_uint(f); return (u + 0x7fffu + ((u >> 16) & 1u)) >> 16; }
; __device__ __forceinline__ u32x2 cvt4(f32x4 v) { return (u32x2){pk2(v[0], v[1]), pk2(v[2], v[3])}; }
; __device__ __forceinline__ void gdn_s23(CArgs& a, int u, const GdnIn2& in, LAS unsigned char* ub, LAS unsigned char* dwb, int w, int lane, float cl) {
;     ...
;     for (int t4 = 0; t4 < 4; ++t4) {
;         const LAS bf16* ar = ATT + (16 * t4 + fr) * 72 + 4 * kg; const LAS bf16* kr = KTT + (16 * t4 + fr) * 72 + 4 * kg;
;         f32x4 pa = (f32x4){0.f, 0.f, 0.f, 0.f}, pk = (f32x4){0.f, 0.f, 0.f, 0.f};
;         pa = __builtin_amdgcn_mfma_f32_16x16x32_bf16(frag2(*(const LAS u32x2*)ar, *(const LAS u32x2*)(ar + 16)), Xb01, pa, 0, 0, 0);
;         pa = __builtin_amdgcn_mfma_f32_16x16x32_bf16(frag2(*(const LAS u32x2*)(ar + 32), *(const LAS u32x2*)(ar + 48)), Xb23, pa, 0, 0, 0);
;         pk = __builtin_amdgcn_mfma_f32_16x16x32_bf16(frag2(*(const LAS u32x2*)kr, *(const LAS u32x2*)(kr + 16)), Xb01, pk, 0, 0, 0);
;         pk = __builtin_amdgcn_mfma_f32_16x16x32_bf16(frag2(*(const LAS u32x2*)(kr + 32), *(const LAS u32x2*)(kr + 48)), Xb23, pk, 0, 0, 0);
;         if (!isW) {
;             *(u32x2*)(ftp + 16 * t4) = cvt4(pa);
;             *(u32x2*)(btp + 16 * t4) = cvt4(pk);
;         } else {
;             const f32x4 ec = *(const LAS f32x4*)(GT + 128 + 16 * t4 + 4 * kg);
; #pragma unroll
;             for (int e = 0; e < 4; ++e) { const int row = 16 * t4 + 4 * kg + e, col = c0 + fr;
;                 ep[(16 * t4 + e) * 64] = (bf16)f2bf(ec[e] * __uint_as_float(in.Qv[t4][e] << 16) - pa[e]);
;                 mp[(16 * t4 + e) * 64] = (bf16)f2bf((row == col ? ecl : 0.f) - pk[e]); }
;         }
;     }
.LBB0_1785:
	v_mul_u32_u24_e32 v34, 0x48, v89
	v_lshl_add_u32 v34, v34, 1, v86
	v_add_u32_e32 v70, 0x9000, v34
	ds_read2_b64 v[54:57], v70 offset1:4
	ds_read2_b64 v[70:73], v70 offset0:8 offset1:12
	v_add_u32_e32 v34, 0xb000, v34
	ds_read2_b64 v[74:77], v34 offset0:136 offset1:140
	s_mov_b64 s[2:3], -1
	s_and_b64 vcc, exec, s[48:49]
	s_waitcnt lgkmcnt(2)
	v_mfma_f32_16x16x32_bf16 v[54:57], v[54:57], v[62:65], 0
	s_waitcnt lgkmcnt(1)
	v_mfma_f32_16x16x32_bf16 v[54:57], v[70:73], v[66:69], v[54:57]
	ds_read2_b64 v[70:73], v34 offset0:128 offset1:132
	s_waitcnt lgkmcnt(0)
	v_mfma_f32_16x16x32_bf16 v[70:73], v[70:73], v[62:65], 0
	v_mfma_f32_16x16x32_bf16 v[70:73], v[74:77], v[66:69], v[70:73]
	s_cbranch_vccnz .LBB0_1787
	s_nop 2
	v_cvt_pk_bf16_f32 v74, v54, v55
	v_cvt_pk_bf16_f32 v75, v56, v57
	global_store_dwordx2 v[80:81], v[74:75], off offset:32
	s_nop 0
	v_cvt_pk_bf16_f32 v74, v70, v71
	v_bfe_u32 v34, v72, 16, 1
	v_add3_u32 v34, v72, v34, s81
	v_bfe_u32 v75, v73, 16, 1
	v_lshrrev_b32_e32 v34, 16, v34
	v_add3_u32 v75, v73, v75, s81
	v_and_or_b32 v75, v75, s80, v34
	s_mov_b64 s[2:3], 0
	global_store_dwordx2 v[78:79], v[74:75], off offset:32
.LBB0_1787:
	s_andn2_b64 vcc, exec, s[2:3]
	s_cbranch_vccnz .LBB0_1789
	v_add_u32_e32 v34, 16, v32
	v_fma_f32 v50, v99, v50, -v54
	v_cmp_eq_u32_e32 vcc, v34, v45
	v_cvt_pk_bf16_f32 v50, v50, v50
	s_nop 0
	v_cndmask_b32_e32 v34, 0, v33, vcc
	v_sub_f32_e32 v34, v34, v70
	global_store_short v[84:85], v50, off offset:2048
	v_cvt_pk_bf16_f32 v34, v34, v34
	global_store_short v[82:83], v34, off offset:2048
	v_add_u32_e32 v34, 17, v32
	v_fma_f32 v50, v98, v51, -v55
	v_cmp_eq_u32_e32 vcc, v34, v45
	v_cvt_pk_bf16_f32 v50, v50, v50
	s_nop 0
	v_cndmask_b32_e32 v34, 0, v33, vcc
	v_sub_f32_e32 v34, v34, v71
	global_store_short v[84:85], v50, off offset:2176
	v_cvt_pk_bf16_f32 v34, v34, v34
	global_store_short v[82:83], v34, off offset:2176
	v_add_u32_e32 v34, 18, v32
	v_fma_f32 v50, v101, v52, -v56
	v_cmp_eq_u32_e32 vcc, v34, v45
	v_cvt_pk_bf16_f32 v50, v50, v50
	s_nop 0
	v_cndmask_b32_e32 v34, 0, v33, vcc
	v_sub_f32_e32 v34, v34, v72
	global_store_short v[84:85], v50, off offset:2304
	v_cvt_pk_bf16_f32 v34, v34, v34
	global_store_short v[82:83], v34, off offset:2304
	v_add_u32_e32 v34, 19, v32
	v_fma_f32 v50, v100, v53, -v57
	v_cmp_eq_u32_e32 vcc, v34, v45
	v_cvt_pk_bf16_f32 v50, v50, v50
	s_nop 0
	v_cndmask_b32_e32 v34, 0, v33, vcc
	v_sub_f32_e32 v34, v34, v73
	global_store_short v[84:85], v50, off offset:2432
	v_cvt_pk_bf16_f32 v34, v34, v34
	global_store_short v[82:83], v34, off offset:2432
.LBB0_1789:
	v_mul_u32_u24_e32 v34, 0x48, v88
	v_lshl_add_u32 v34, v34, 1, v86
	v_add_u32_e32 v54, 0x9000, v34
	ds_read2_b64 v[50:53], v54 offset1:4
	ds_read2_b64 v[54:57], v54 offset0:8 offset1:12
	v_add_u32_e32 v34, 0xb000, v34
	ds_read2_b64 v[70:73], v34 offset0:136 offset1:140
	s_mov_b64 s[2:3], -1
	s_and_b64 vcc, exec, s[48:49]
	s_waitcnt lgkmcnt(2)
	v_mfma_f32_16x16x32_bf16 v[50:53], v[50:53], v[62:65], 0
	s_waitcnt lgkmcnt(1)
	v_mfma_f32_16x16x32_bf16 v[50:53], v[54:57], v[66:69], v[50:53]
	ds_read2_b64 v[54:57], v34 offset0:128 offset1:132
	s_waitcnt lgkmcnt(0)
	v_mfma_f32_16x16x32_bf16 v[54:57], v[54:57], v[62:65], 0
	v_mfma_f32_16x16x32_bf16 v[54:57], v[70:73], v[66:69], v[54:57]
	s_cbranch_vccnz .LBB0_1791
	s_nop 2
	v_cvt_pk_bf16_f32 v70, v50, v51
	v_cvt_pk_bf16_f32 v71, v52, v53
	global_store_dwordx2 v[80:81], v[70:71], off offset:64
	s_nop 0
	v_cvt_pk_bf16_f32 v70, v54, v55
	v_bfe_u32 v34, v56, 16, 1
	v_add3_u32 v34, v56, v34, s81
	v_bfe_u32 v71, v57, 16, 1
	v_lshrrev_b32_e32 v34, 16, v34
	v_add3_u32 v71, v57, v71, s81
	v_and_or_b32 v71, v71, s80, v34
	s_mov_b64 s[2:3], 0
	global_store_dwordx2 v[78:79], v[70:71], off offset:64
.LBB0_1791:
	s_andn2_b64 vcc, exec, s[2:3]
	s_cbranch_vccnz .LBB0_1793
	v_add_co_u32_e32 v70, vcc, 0x1000, v84
	v_add_u32_e32 v34, 32, v32
	s_nop 0
	v_addc_co_u32_e32 v71, vcc, 0, v85, vcc
	v_fma_f32 v50, v96, v58, -v50
	v_cmp_eq_u32_e32 vcc, v34, v45
	v_cvt_pk_bf16_f32 v50, v50, v50
	s_nop 0
	v_cndmask_b32_e32 v34, 0, v33, vcc
	v_sub_f32_e32 v34, v34, v54
	global_store_short v[70:71], v50, off
	v_add_co_u32_e32 v72, vcc, 0x1000, v82
	v_cvt_pk_bf16_f32 v34, v34, v34
	s_nop 0
	v_addc_co_u32_e32 v73, vcc, 0, v83, vcc
	global_store_short v[72:73], v34, off
	v_add_u32_e32 v34, 33, v32
	v_fma_f32 v50, v94, v59, -v51
	v_cmp_eq_u32_e32 vcc, v34, v45
	v_cvt_pk_bf16_f32 v50, v50, v50
	s_nop 0
	v_cndmask_b32_e32 v34, 0, v33, vcc
	v_sub_f32_e32 v34, v34, v55
	global_store_short v[70:71], v50, off offset:128
	v_cvt_pk_bf16_f32 v34, v34, v34
	global_store_short v[72:73], v34, off offset:128
	v_add_u32_e32 v34, 34, v32
	v_fma_f32 v50, v97, v60, -v52
	v_cmp_eq_u32_e32 vcc, v34, v45
	v_cvt_pk_bf16_f32 v50, v50, v50
	s_nop 0
	v_cndmask_b32_e32 v34, 0, v33, vcc
	v_sub_f32_e32 v34, v34, v56
	global_store_short v[70:71], v50, off offset:256
	v_cvt_pk_bf16_f32 v34, v34, v34
	global_store_short v[72:73], v34, off offset:256
	v_add_u32_e32 v34, 35, v32
	v_fma_f32 v50, v95, v61, -v53
	v_cmp_eq_u32_e32 vcc, v34, v45
	v_cvt_pk_bf16_f32 v50, v50, v50
	s_nop 0
	v_cndmask_b32_e32 v34, 0, v33, vcc
	v_sub_f32_e32 v34, v34, v57
	global_store_short v[70:71], v50, off offset:384
	v_cvt_pk_bf16_f32 v34, v34, v34
	global_store_short v[72:73], v34, off offset:384
.LBB0_1793:
	v_mul_u32_u24_e32 v34, 0x48, v87
	v_lshl_add_u32 v34, v34, 1, v86
	v_add_u32_e32 v58, 0x9000, v34
	ds_read2_b64 v[50:53], v58 offset1:4
	ds_read2_b64 v[58:61], v58 offset0:8 offset1:12
	v_add_u32_e32 v34, 0xb000, v34
	ds_read2_b64 v[54:57], v34 offset0:128 offset1:132
	s_and_b64 vcc, exec, s[48:49]
	s_mov_b64 s[2:3], -1
	s_waitcnt lgkmcnt(2)
	v_mfma_f32_16x16x32_bf16 v[50:53], v[50:53], v[62:65], 0
	s_waitcnt lgkmcnt(1)
	v_mfma_f32_16x16x32_bf16 v[50:53], v[58:61], v[66:69], v[50:53]
	ds_read2_b64 v[58:61], v34 offset0:136 offset1:140
	s_waitcnt lgkmcnt(1)
	v_mfma_f32_16x16x32_bf16 v[54:57], v[54:57], v[62:65], 0
	s_waitcnt lgkmcnt(0)
	v_mfma_f32_16x16x32_bf16 v[54:57], v[58:61], v[66:69], v[54:57]
	s_cbranch_vccnz .LBB0_1795
	s_nop 1
	v_cvt_pk_bf16_f32 v58, v50, v51
	v_cvt_pk_bf16_f32 v59, v52, v53
	global_store_dwordx2 v[80:81], v[58:59], off offset:96
	s_nop 1
	v_cvt_pk_bf16_f32 v58, v54, v55
	v_bfe_u32 v34, v56, 16, 1
	v_add3_u32 v34, v56, v34, s81
	v_bfe_u32 v59, v57, 16, 1
	v_lshrrev_b32_e32 v34, 16, v34
	v_add3_u32 v59, v57, v59, s81
	v_and_or_b32 v59, v59, s80, v34
	global_store_dwordx2 v[78:79], v[58:59], off offset:96
	s_cbranch_execnz .LBB0_1682
	s_branch .LBB0_1796

; #define LAS __attribute__((address_space(3)))
; __device__ __forceinline__ unsigned f2bf(float f) { unsigned u = __float_as_uint(f); return (u + 0x7fffu + ((u >> 16) & 1u)) >> 16; }
; __device__ __forceinline__ void gdn_s23(CArgs& a, int u, const GdnIn2& in, LAS unsigned char* ub, LAS unsigned char* dwb, int w, int lane, float cl) {
;     ...
;         } else {
;             const f32x4 ec = *(const LAS f32x4*)(GT + 128 + 16 * t4 + 4 * kg);
; #pragma unroll
;             for (int e = 0; e < 4; ++e) { const int row = 16 * t4 + 4 * kg + e, col = c0 + fr;
;                 ep[(16 * t4 + e) * 64] = (bf16)f2bf(ec[e] * __uint_as_float(in.Qv[t4][e] << 16) - pa[e]);
;                 mp[(16 * t4 + e) * 64] = (bf16)f2bf((row == col ? ecl : 0.f) - pk[e]); }
;         }
.LBB0_1796:
	v_add_co_u32_e32 v58, vcc, 0x1000, v84
	v_add_u32_e32 v34, 48, v32
	s_nop 0
	v_addc_co_u32_e32 v59, vcc, 0, v85, vcc
	v_fma_f32 v46, v92, v46, -v50
	v_cmp_eq_u32_e32 vcc, v34, v45
	v_bfe_u32 v50, v46, 16, 1
	v_add3_u32 v46, v46, v50, s81
	v_cndmask_b32_e32 v34, 0, v33, vcc
	v_sub_f32_e32 v34, v34, v54
	global_store_short_d16_hi v[58:59], v46, off offset:2048
	v_add_co_u32_e32 v60, vcc, 0x1000, v82
	v_cvt_pk_bf16_f32 v34, v34, v34
	s_nop 0
	v_addc_co_u32_e32 v61, vcc, 0, v83, vcc
	global_store_short v[60:61], v34, off offset:2048
	v_add_u32_e32 v34, 49, v32
	v_fma_f32 v46, v90, v47, -v51
	v_cmp_eq_u32_e32 vcc, v34, v45
	v_cvt_pk_bf16_f32 v46, v46, v46
	s_nop 0
	v_cndmask_b32_e32 v34, 0, v33, vcc
	v_sub_f32_e32 v34, v34, v55
	global_store_short v[58:59], v46, off offset:2176
	v_cvt_pk_bf16_f32 v34, v34, v34
	global_store_short v[60:61], v34, off offset:2176
	v_add_u32_e32 v34, 50, v32
	v_fma_f32 v46, v93, v48, -v52
	v_cmp_eq_u32_e32 vcc, v34, v45
	v_bfe_u32 v47, v46, 16, 1
	v_add3_u32 v46, v46, v47, s81
	v_cndmask_b32_e32 v34, 0, v33, vcc
	v_sub_f32_e32 v34, v34, v56
	v_add_u32_e32 v32, 51, v32
	global_store_short_d16_hi v[58:59], v46, off offset:2304
	v_cmp_eq_u32_e32 vcc, v32, v45
	v_cvt_pk_bf16_f32 v34, v34, v34
	global_store_short v[60:61], v34, off offset:2304
	v_cndmask_b32_e32 v32, 0, v33, vcc
	v_fma_f32 v34, v91, v49, -v53
	v_sub_f32_e32 v32, v32, v57
	v_bfe_u32 v46, v34, 16, 1
	v_bfe_u32 v33, v32, 16, 1
	v_add3_u32 v34, v34, v46, s81
	v_add3_u32 v32, v32, v33, s81
	global_store_short_d16_hi v[58:59], v34, off offset:2432
	global_store_short_d16_hi v[60:61], v32, off offset:2432
	s_branch .LBB0_1682

; #define LAS __attribute__((address_space(3)))
; __device__ __forceinline__ unsigned f2bf(float f) { unsigned u = __float_as_uint(f); return (u + 0x7fffu + ((u >> 16) & 1u)) >> 16; }
; __device__ __forceinline__ float lo_bf(unsigned w) { return __uint_as_float(w << 16); }
; __device__ __forceinline__ float hi_bf(unsigned w) { return __uint_as_float(w & 0xffff0000u); }
; __device__ __forceinline__ u32x2 cvt4(f32x4 v) { return (u32x2){pk2(v[0], v[1]), pk2(v[2], v[3])}; }
; __device__ __forceinline__ void gla_seq_block(CArgs& a, int chain, LAS unsigned char* lds, int w, int lane) {
;     ...
;         for (int n = 0; n < 36; ++n) {
;             const LAS unsigned char* sl = lds + (n % 3) * SLOT; const int r0 = scan_row(b, dir, n * 64);
;             const bf16x8 Sb = frag2(cvt4(S[0]), cvt4(S[1]));
;             f32x4 o[4];
; #pragma unroll
;             for (int t = 0; t < 4; ++t) { const u32x2 ff = *(const LAS u32x2*)(sl + 5120 + v * 144 + (16 * t + 4 * kg) * 2);
;                 o[t] = (f32x4){lo_bf(ff.x), hi_bf(ff.x), lo_bf(ff.y), hi_bf(ff.y)};
;                 const LAS unsigned char* qr = sl + (16 * t + fr) * 80 + 4 * kg * 2;
;                 o[t] = __builtin_amdgcn_mfma_f32_16x16x32_bf16(frag2(*(const LAS u32x2*)qr, *(const LAS u32x2*)(qr + 32)), Sb, o[t], 0, 0, 0); }
; #pragma unroll
;             for (int kt = 0; kt < 2; ++kt) { const f32x4 d4 = *(const LAS f32x4*)(sl + 19456 + (16 * kt + 4 * kg) * 4); const u32x2 u2 = *(const LAS u32x2*)(sl + 14336 + v * 80 + (16 * kt + 4 * kg) * 2);
;                 S[kt] = d4 * S[kt] + (f32x4){lo_bf(u2.x), hi_bf(u2.x), lo_bf(u2.y), hi_bf(u2.y)}; }
;             { bf16* gp = GO + (ptrdiff_t)(r0 + step * 4 * kg) * 256 + h * 64 + v; const ptrdiff_t sd = (ptrdiff_t)step * 256;
; #pragma unroll
;               for (int t = 0; t < 4; ++t)
; #pragma unroll
;                   for (int e = 0; e < 4; ++e) gp[(16 * t + e) * sd] = (bf16)f2bf(o[t][e]); }
;             __syncthreads();
.LBB0_1801:
	s_mul_i32 s2, s51, 0xab
	s_bfe_u32 s2, s2, 0x70009
	v_cvt_pk_bf16_f32 v28, v16, v17
	s_mul_i32 s2, s2, 3
	s_sub_i32 s2, s51, s2
	s_and_b32 s2, s2, 0xff
	v_cvt_pk_bf16_f32 v29, v18, v19
	s_mulk_i32 s2, 0x4c80
	s_add_i32 s2, s2, 0
	v_cvt_pk_bf16_f32 v30, v12, v13
	v_add_u32_e32 v8, s2, v21
	v_add_u32_e32 v33, v8, v24
	ds_read2_b64 v[36:39], v33 offset1:4
	v_cvt_pk_bf16_f32 v31, v14, v15
	v_add_u32_e32 v2, v8, v20
	v_add_u32_e32 v32, 0x1000, v2
	ds_read2_b64 v[4:7], v32 offset0:128 offset1:132
	v_add_u32_e32 v34, s2, v22
	s_add_i32 s51, s51, 1
	s_sub_i32 s50, s50, 64
	s_add_i32 s9, s9, 64
	s_waitcnt lgkmcnt(0)
	v_lshlrev_b32_e32 v2, 16, v4
	v_and_b32_e32 v3, 0xffff0000, v4
	v_lshlrev_b32_e32 v4, 16, v5
	v_and_b32_e32 v5, 0xffff0000, v5
	s_cmp_lg_u32 s50, -1
	s_nop 0
	v_mfma_f32_16x16x32_bf16 v[2:5], v[36:39], v[28:31], v[2:5]
	v_lshlrev_b32_e32 v36, 16, v6
	v_and_b32_e32 v37, 0xffff0000, v6
	v_lshlrev_b32_e32 v38, 16, v7
	v_and_b32_e32 v39, 0xffff0000, v7
	ds_read2_b64 v[6:9], v33 offset0:160 offset1:164
	s_waitcnt lgkmcnt(0)
	v_mfma_f32_16x16x32_bf16 v[6:9], v[6:9], v[28:31], v[36:39]
	s_nop 2
	ds_read2_b64 v[36:39], v32 offset0:136 offset1:140
	v_add_u32_e32 v32, 0x800, v33
	ds_read2_b64 v[44:47], v32 offset0:64 offset1:68
	s_waitcnt lgkmcnt(1)
	v_lshlrev_b32_e32 v40, 16, v36
	v_and_b32_e32 v41, 0xffff0000, v36
	v_lshlrev_b32_e32 v42, 16, v37
	v_and_b32_e32 v43, 0xffff0000, v37
	v_lshlrev_b32_e32 v36, 16, v38
	v_and_b32_e32 v37, 0xffff0000, v38
	s_waitcnt lgkmcnt(0)
	v_mfma_f32_16x16x32_bf16 v[40:43], v[44:47], v[28:31], v[40:43]
	ds_read2_b64 v[44:47], v32 offset0:224 offset1:228
	v_lshlrev_b32_e32 v38, 16, v39
	v_and_b32_e32 v39, 0xffff0000, v39
	v_add_u32_e32 v32, s2, v25
	s_waitcnt lgkmcnt(0)
	v_mfma_f32_16x16x32_bf16 v[28:31], v[44:47], v[28:31], v[36:39]
	s_nop 2
	ds_read_b128 v[36:39], v32 offset:19456
	v_add_u32_e32 v32, v34, v21
	ds_read_b64 v[32:33], v32 offset:14336
	s_waitcnt lgkmcnt(0)
	v_lshlrev_b32_e32 v44, 16, v32
	v_and_b32_e32 v45, 0xffff0000, v32
	v_lshlrev_b32_e32 v32, 16, v33
	v_and_b32_e32 v33, 0xffff0000, v33
	v_pk_fma_f32 v[18:19], v[38:39], v[18:19], v[32:33]
	v_add_u32_e32 v32, s2, v26
	v_pk_fma_f32 v[16:17], v[36:37], v[16:17], v[44:45]
	ds_read_b128 v[36:39], v32 offset:19456
	v_add_u32_e32 v32, v34, v27
	ds_read_b64 v[32:33], v32 offset:14336
	v_cvt_pk_bf16_f32 v2, v2, v2
	s_waitcnt lgkmcnt(0)
	v_lshlrev_b32_e32 v44, 16, v32
	v_and_b32_e32 v45, 0xffff0000, v32
	v_lshlrev_b32_e32 v32, 16, v33
	v_and_b32_e32 v33, 0xffff0000, v33
	v_pk_fma_f32 v[14:15], v[38:39], v[14:15], v[32:33]
	v_add_u32_e32 v32, s52, v23
	v_ashrrev_i32_e32 v33, 31, v32
	v_lshlrev_b64 v[32:33], 9, v[32:33]
	v_lshl_add_u64 v[32:33], v[10:11], 0, v[32:33]
	global_store_short v[32:33], v2, off
	v_bfe_u32 v2, v3, 16, 1
	v_add3_u32 v34, v3, v2, s81
	v_lshl_add_u64 v[2:3], v[32:33], 0, s[28:29]
	v_bfe_u32 v32, v4, 16, 1
	global_store_short_d16_hi v[2:3], v34, off
	v_add3_u32 v4, v4, v32, s81
	v_lshl_add_u64 v[2:3], v[2:3], 0, s[28:29]
	global_store_short_d16_hi v[2:3], v4, off
	v_cvt_pk_bf16_f32 v4, v5, v5
	v_lshl_add_u64 v[2:3], v[2:3], 0, s[28:29]
	global_store_short v[2:3], v4, off
	v_cvt_pk_bf16_f32 v4, v6, v6
	v_lshl_add_u64 v[2:3], v[2:3], 0, s[48:49]
	global_store_short v[2:3], v4, off
	v_cvt_pk_bf16_f32 v4, v7, v7
	v_lshl_add_u64 v[2:3], v[2:3], 0, s[28:29]
	global_store_short v[2:3], v4, off
	v_cvt_pk_bf16_f32 v4, v8, v8
	v_lshl_add_u64 v[2:3], v[2:3], 0, s[28:29]
	global_store_short v[2:3], v4, off
	v_cvt_pk_bf16_f32 v4, v9, v9
	v_lshl_add_u64 v[2:3], v[2:3], 0, s[28:29]
	global_store_short v[2:3], v4, off
	v_cvt_pk_bf16_f32 v4, v40, v40
	v_lshl_add_u64 v[2:3], v[2:3], 0, s[48:49]
	global_store_short v[2:3], v4, off
	v_cvt_pk_bf16_f32 v4, v41, v41
	v_lshl_add_u64 v[2:3], v[2:3], 0, s[28:29]
	global_store_short v[2:3], v4, off
	v_cvt_pk_bf16_f32 v4, v42, v42
	v_lshl_add_u64 v[2:3], v[2:3], 0, s[28:29]
	global_store_short v[2:3], v4, off
	v_cvt_pk_bf16_f32 v4, v43, v43
	v_lshl_add_u64 v[2:3], v[2:3], 0, s[28:29]
	global_store_short v[2:3], v4, off
	v_cvt_pk_bf16_f32 v4, v28, v28
	v_lshl_add_u64 v[2:3], v[2:3], 0, s[48:49]
	global_store_short v[2:3], v4, off
	v_cvt_pk_bf16_f32 v4, v29, v29
	v_lshl_add_u64 v[2:3], v[2:3], 0, s[28:29]
	global_store_short v[2:3], v4, off
	v_cvt_pk_bf16_f32 v4, v30, v30
	v_lshl_add_u64 v[2:3], v[2:3], 0, s[28:29]
	global_store_short v[2:3], v4, off
	v_bfe_u32 v4, v31, 16, 1
	v_pk_fma_f32 v[12:13], v[36:37], v[12:13], v[44:45]
	v_add3_u32 v4, v31, v4, s81
	v_lshl_add_u64 v[2:3], v[2:3], 0, s[28:29]
	global_store_short_d16_hi v[2:3], v4, off
	s_barrier
	s_cbranch_scc0 .LBB0_1806

; #define LAS __attribute__((address_space(3)))
; __device__ __forceinline__ unsigned f2bf(float f) { unsigned u = __float_as_uint(f); return (u + 0x7fffu + ((u >> 16) & 1u)) >> 16; }
; __device__ __forceinline__ float lo_bf(unsigned w) { return __uint_as_float(w << 16); }
; __device__ __forceinline__ float hi_bf(unsigned w) { return __uint_as_float(w & 0xffff0000u); }
; __device__ __forceinline__ u32x2 cvt4(f32x4 v) { return (u32x2){pk2(v[0], v[1]), pk2(v[2], v[3])}; }
; __device__ __forceinline__ void gdn_seq_block(CArgs& a, int chain, LAS unsigned char* lds, int w, int lane) {
;     ...
;         for (int n = 0; n < 36; ++n) {
;             const LAS unsigned char* sl = lds + (n % 3) * SLOT; const int r0 = scan_row(b, dir, n * 64);
;             bf16x8 Sb[2];
; #pragma unroll
;             for (int s = 0; s < 2; ++s) Sb[s] = frag2(cvt4(S[2 * s]), cvt4(S[2 * s + 1]));
;             f32x4 o[4];
; #pragma unroll
;             for (int t = 0; t < 4; ++t) {
;                 const u32x2 ff = *(const LAS u32x2*)(sl + 27648 + v * 144 + (16 * t + 4 * kg) * 2);
;                 o[t] = (f32x4){lo_bf(ff.x), hi_bf(ff.x), lo_bf(ff.y), hi_bf(ff.y)};
;                 const u32x2 bb2 = *(const LAS u32x2*)(sl + 18432 + v * 144 + (16 * t + 4 * kg) * 2);
;                 f32x4 sn = (f32x4){lo_bf(bb2.x), hi_bf(bb2.x), lo_bf(bb2.y), hi_bf(bb2.y)};
; #pragma unroll
;                 for (int s = 0; s < 2; ++s) { const LAS unsigned char* er = sl + 9216 + (16 * t + fr) * 144 + (32 * s + 4 * kg) * 2; const LAS unsigned char* mr = sl + (16 * t + fr) * 144 + (32 * s + 4 * kg) * 2;
;                     o[t] = __builtin_amdgcn_mfma_f32_16x16x32_bf16(frag2(*(const LAS u32x2*)er, *(const LAS u32x2*)(er + 32)), Sb[s], o[t], 0, 0, 0);
;                     sn = __builtin_amdgcn_mfma_f32_16x16x32_bf16(frag2(*(const LAS u32x2*)mr, *(const LAS u32x2*)(mr + 32)), Sb[s], sn, 0, 0, 0); }
;                 S[t] = sn; }
;             { bf16* dp = DO + (ptrdiff_t)(r0 + step * 4 * kg) * 256 + h * 64 + v; const ptrdiff_t sd = (ptrdiff_t)step * 256;
; #pragma unroll
;               for (int t = 0; t < 4; ++t)
; #pragma unroll
;                   for (int e = 0; e < 4; ++e) dp[(16 * t + e) * sd] = (bf16)f2bf(o[t][e]); }
;             __syncthreads();
.LBB0_1885:
	v_cvt_pk_bf16_f32 v2, v10, v11
	v_cvt_pk_bf16_f32 v3, v12, v13
	s_mul_i32 s2, s50, 0xab
	s_bfe_u32 s2, s2, 0x70009
	v_cvt_pk_bf16_f32 v4, v14, v15
	s_mul_i32 s2, s2, 3
	s_sub_i32 s2, s50, s2
	s_and_b32 s2, s2, 0xff
	v_cvt_pk_bf16_f32 v5, v16, v17
	s_mul_i32 s2, s2, 0x9000
	s_add_i32 s2, s2, 0
	v_cvt_pk_bf16_f32 v6, v22, v23
	v_add3_u32 v16, s2, v34, v38
	v_add_u32_e32 v41, 0x4800, v16
	ds_read2_b64 v[20:23], v41 offset1:4
	v_cvt_pk_bf16_f32 v7, v24, v25
	v_cvt_pk_bf16_f32 v8, v30, v31
	v_bfe_u32 v9, v32, 16, 1
	v_add3_u32 v54, s2, v40, v38
	v_add3_u32 v9, v32, v9, s81
	v_add_u32_e32 v32, 0x6800, v16
	s_waitcnt lgkmcnt(0)
	v_lshlrev_b32_e32 v16, 16, v20
	v_and_b32_e32 v17, 0xffff0000, v20
	v_add_u32_e32 v20, 0x2000, v54
	ds_read2_b64 v[24:27], v20 offset0:128 offset1:132
	ds_read2_b64 v[12:15], v32 offset0:128 offset1:132
	v_bfe_u32 v10, v33, 16, 1
	v_lshrrev_b32_e32 v9, 16, v9
	v_add3_u32 v10, v33, v10, s81
	v_and_or_b32 v9, v10, s80, v9
	s_waitcnt lgkmcnt(0)
	v_lshlrev_b32_e32 v10, 16, v12
	v_and_b32_e32 v11, 0xffff0000, v12
	v_lshlrev_b32_e32 v12, 16, v13
	v_and_b32_e32 v13, 0xffff0000, v13
	v_lshlrev_b32_e32 v18, 16, v21
	v_and_b32_e32 v19, 0xffff0000, v21
	v_mfma_f32_16x16x32_bf16 v[10:13], v[24:27], v[2:5], v[10:13]
	ds_read2_b64 v[24:27], v54 offset1:4
	v_add_u32_e32 v33, 0x2800, v54
	ds_read2_b64 v[28:31], v33 offset0:160 offset1:164
	s_waitcnt lgkmcnt(1)
	v_mfma_f32_16x16x32_bf16 v[24:27], v[24:27], v[2:5], v[16:19]
	s_nop 2
	ds_read2_b64 v[16:19], v20 offset0:136 offset1:140
	ds_read2_b64 v[42:45], v41 offset0:8 offset1:12
	v_add_u32_e32 v41, 0x3800, v54
	s_waitcnt lgkmcnt(1)
	v_mfma_f32_16x16x32_bf16 v[18:21], v[16:19], v[6:9], v[10:13]
	s_nop 2
	ds_read2_b64 v[10:13], v54 offset0:8 offset1:12
	v_lshlrev_b32_e32 v16, 16, v23
	v_and_b32_e32 v17, 0xffff0000, v23
	s_waitcnt lgkmcnt(0)
	v_mfma_f32_16x16x32_bf16 v[10:13], v[10:13], v[6:9], v[24:27]
	s_nop 2
	v_lshlrev_b32_e32 v24, 16, v14
	v_and_b32_e32 v25, 0xffff0000, v14
	v_lshlrev_b32_e32 v26, 16, v15
	v_and_b32_e32 v27, 0xffff0000, v15
	v_lshlrev_b32_e32 v14, 16, v22
	v_and_b32_e32 v15, 0xffff0000, v22
	v_mfma_f32_16x16x32_bf16 v[22:25], v[28:31], v[2:5], v[24:27]
	v_add_u32_e32 v30, 0x800, v54
	v_lshlrev_b32_e32 v46, 16, v42
	v_and_b32_e32 v47, 0xffff0000, v42
	ds_read2_b64 v[26:29], v30 offset0:32 offset1:36
	s_waitcnt lgkmcnt(0)
	v_mfma_f32_16x16x32_bf16 v[14:17], v[26:29], v[2:5], v[14:17]
	ds_read2_b64 v[26:29], v33 offset0:168 offset1:172
	v_lshlrev_b32_e32 v48, 16, v43
	v_and_b32_e32 v49, 0xffff0000, v43
	s_waitcnt lgkmcnt(0)
	v_mfma_f32_16x16x32_bf16 v[26:29], v[26:29], v[6:9], v[22:25]
	s_nop 2
	ds_read2_b64 v[22:25], v30 offset0:40 offset1:44
	ds_read2_b64 v[30:33], v32 offset0:136 offset1:140
	v_lshlrev_b32_e32 v42, 16, v44
	s_waitcnt lgkmcnt(1)
	v_mfma_f32_16x16x32_bf16 v[14:17], v[22:25], v[6:9], v[14:17]
	s_waitcnt lgkmcnt(0)
	v_lshlrev_b32_e32 v22, 16, v30
	v_and_b32_e32 v23, 0xffff0000, v30
	v_add_u32_e32 v30, 0x3000, v54
	ds_read2_b64 v[50:53], v30 offset0:192 offset1:196
	v_lshlrev_b32_e32 v24, 16, v31
	v_and_b32_e32 v25, 0xffff0000, v31
	v_add_u32_e32 v31, 0x1000, v54
	v_add_u32_e32 v54, 0x1800, v54
	s_waitcnt lgkmcnt(0)
	v_mfma_f32_16x16x32_bf16 v[22:25], v[50:53], v[2:5], v[22:25]
	ds_read2_b64 v[50:53], v31 offset0:64 offset1:68
	v_and_b32_e32 v43, 0xffff0000, v44
	v_lshlrev_b32_e32 v44, 16, v45
	s_waitcnt lgkmcnt(0)
	v_mfma_f32_16x16x32_bf16 v[46:49], v[50:53], v[2:5], v[46:49]
	ds_read2_b64 v[50:53], v30 offset0:200 offset1:204
	v_lshlrev_b32_e32 v30, 16, v32
	v_and_b32_e32 v45, 0xffff0000, v45
	s_waitcnt lgkmcnt(0)
	v_mfma_f32_16x16x32_bf16 v[50:53], v[50:53], v[6:9], v[22:25]
	s_nop 2
	ds_read2_b64 v[22:25], v31 offset0:72 offset1:76
	v_and_b32_e32 v31, 0xffff0000, v32
	v_lshlrev_b32_e32 v32, 16, v33
	s_waitcnt lgkmcnt(0)
	v_mfma_f32_16x16x32_bf16 v[22:25], v[22:25], v[6:9], v[46:49]
	s_nop 2
	ds_read2_b64 v[46:49], v41 offset0:224 offset1:228
	v_and_b32_e32 v33, 0xffff0000, v33
	s_add_i32 s50, s50, 1
	s_sub_i32 s36, s36, 64
	s_waitcnt lgkmcnt(0)
	v_mfma_f32_16x16x32_bf16 v[30:33], v[46:49], v[2:5], v[30:33]
	ds_read2_b64 v[46:49], v54 offset0:96 offset1:100
	s_add_i32 s0, s0, 64
	s_cmp_eq_u32 s36, -1
	s_waitcnt lgkmcnt(0)
	v_mfma_f32_16x16x32_bf16 v[2:5], v[46:49], v[2:5], v[42:45]
	s_nop 2
	ds_read2_b64 v[42:45], v41 offset0:232 offset1:236
	s_waitcnt lgkmcnt(0)
	v_mfma_f32_16x16x32_bf16 v[42:45], v[42:45], v[6:9], v[30:33]
	s_nop 2
	ds_read2_b64 v[30:33], v54 offset0:104 offset1:108
	s_waitcnt lgkmcnt(0)
	v_mfma_f32_16x16x32_bf16 v[30:33], v[30:33], v[6:9], v[2:5]
	s_nop 2
	v_add_u32_e32 v2, s51, v39
	v_ashrrev_i32_e32 v3, 31, v2
	v_lshlrev_b64 v[2:3], 9, v[2:3]
	v_lshl_add_u64 v[2:3], v[36:37], 0, v[2:3]
	v_cvt_pk_bf16_f32 v4, v18, v18
	global_store_short v[2:3], v4, off
	v_cvt_pk_bf16_f32 v4, v19, v19
	v_lshl_add_u64 v[2:3], v[2:3], 0, s[28:29]
	global_store_short v[2:3], v4, off
	v_cvt_pk_bf16_f32 v4, v20, v20
	v_lshl_add_u64 v[2:3], v[2:3], 0, s[28:29]
	global_store_short v[2:3], v4, off
	v_cvt_pk_bf16_f32 v4, v21, v21
	v_lshl_add_u64 v[2:3], v[2:3], 0, s[28:29]
	global_store_short v[2:3], v4, off
	v_cvt_pk_bf16_f32 v4, v26, v26
	v_lshl_add_u64 v[2:3], v[2:3], 0, s[48:49]
	global_store_short v[2:3], v4, off
	v_cvt_pk_bf16_f32 v4, v27, v27
	v_lshl_add_u64 v[2:3], v[2:3], 0, s[28:29]
	global_store_short v[2:3], v4, off
	v_cvt_pk_bf16_f32 v4, v28, v28
	v_lshl_add_u64 v[2:3], v[2:3], 0, s[28:29]
	global_store_short v[2:3], v4, off
	v_cvt_pk_bf16_f32 v4, v29, v29
	v_lshl_add_u64 v[2:3], v[2:3], 0, s[28:29]
	global_store_short v[2:3], v4, off
	v_cvt_pk_bf16_f32 v4, v50, v50
	v_lshl_add_u64 v[2:3], v[2:3], 0, s[48:49]
	global_store_short v[2:3], v4, off
	v_cvt_pk_bf16_f32 v4, v51, v51
	v_lshl_add_u64 v[2:3], v[2:3], 0, s[28:29]
	global_store_short v[2:3], v4, off
	v_cvt_pk_bf16_f32 v4, v52, v52
	v_lshl_add_u64 v[2:3], v[2:3], 0, s[28:29]
	global_store_short v[2:3], v4, off
	v_cvt_pk_bf16_f32 v4, v53, v53
	v_lshl_add_u64 v[2:3], v[2:3], 0, s[28:29]
	global_store_short v[2:3], v4, off
	v_cvt_pk_bf16_f32 v4, v42, v42
	v_lshl_add_u64 v[2:3], v[2:3], 0, s[48:49]
	global_store_short v[2:3], v4, off
	v_cvt_pk_bf16_f32 v4, v43, v43
	v_lshl_add_u64 v[2:3], v[2:3], 0, s[28:29]
	global_store_short v[2:3], v4, off
	v_cvt_pk_bf16_f32 v4, v44, v44
	v_lshl_add_u64 v[2:3], v[2:3], 0, s[28:29]
	global_store_short v[2:3], v4, off
	v_bfe_u32 v4, v45, 16, 1
	v_add3_u32 v4, v45, v4, s81
	v_lshl_add_u64 v[2:3], v[2:3], 0, s[28:29]
	global_store_short_d16_hi v[2:3], v4, off
	s_barrier
	s_cbranch_scc1 .LBB0_1890

; #define LAS __attribute__((address_space(3)))
; __device__ __forceinline__ unsigned pk2(float lo, float hi) { return f2bf(lo) | (f2bf(hi) << 16); }
; template <int L>
; __device__ __forceinline__ void hyena_unit(CArgs& a, int l, int c, LAS unsigned char* lds) {
;     ...
;     } else {
;         static_assert(L == 256, "hyena_unit");
; #pragma unroll
;         for (int i = 0; i < 8; ++i)
; #pragma unroll
;             for (int j = 0; j < NTW; ++j) acc[j] = __builtin_amdgcn_mfma_f32_16x16x32_bf16(*(const LAS bf16x8*)(ap + (4 * i - 2 * j) * 16), zc[i], acc[j], 0, 0, 0);
;     }
; #pragma unroll
;     for (int j = 0; j < NTW; ++j) *(u32x2*)(YT + 16 * (w * NTW + j) + 4 * kg) = (u32x2){pk2(acc[j][0], acc[j][1]), pk2(acc[j][2], acc[j][3])};
.LBB0_2094:
	s_or_b64 exec, exec, s[14:15]
	v_sub_u32_e32 v39, v34, v39
	v_sub_u32_e32 v40, 0, v38
	v_lshlrev_b32_e32 v39, 1, v39
	v_and_b32_e32 v40, 7, v40
	v_and_b32_e32 v38, 0xffffffc0, v38
	v_and_b32_e32 v39, -16, v39
	v_mul_u32_u24_e32 v40, 0x440, v40
	v_sub_u32_e32 v38, v39, v38
	v_add3_u32 v46, 0, v40, v38
	s_waitcnt lgkmcnt(0)
	s_barrier
	ds_read_b128 v[38:41], v46 offset:480
	ds_read_b128 v[42:45], v46 offset:512
	s_waitcnt vmcnt(7) lgkmcnt(0)
	v_mfma_f32_16x16x32_bf16 v[42:45], v[42:45], v[30:33], 0
	v_mfma_f32_16x16x32_bf16 v[30:33], v[38:41], v[30:33], 0
	ds_read_b128 v[38:41], v46 offset:576
	s_waitcnt vmcnt(6) lgkmcnt(0)
	v_mfma_f32_16x16x32_bf16 v[38:41], v[38:41], v[26:29], v[42:45]
	s_nop 3
	ds_read_b128 v[42:45], v46 offset:544
	s_waitcnt lgkmcnt(0)
	v_mfma_f32_16x16x32_bf16 v[26:29], v[42:45], v[26:29], v[30:33]
	s_nop 2
	ds_read_b128 v[30:33], v46 offset:640
	s_waitcnt vmcnt(5) lgkmcnt(0)
	v_mfma_f32_16x16x32_bf16 v[30:33], v[30:33], v[22:25], v[38:41]
	s_nop 2
	ds_read_b128 v[38:41], v46 offset:608
	s_waitcnt lgkmcnt(0)
	v_mfma_f32_16x16x32_bf16 v[22:25], v[38:41], v[22:25], v[26:29]
	s_nop 2
	ds_read_b128 v[26:29], v46 offset:704
	s_waitcnt vmcnt(4) lgkmcnt(0)
	v_mfma_f32_16x16x32_bf16 v[26:29], v[26:29], v[18:21], v[30:33]
	s_nop 2
	ds_read_b128 v[30:33], v46 offset:672
	s_waitcnt lgkmcnt(0)
	v_mfma_f32_16x16x32_bf16 v[18:21], v[30:33], v[18:21], v[22:25]
	s_nop 2
	ds_read_b128 v[22:25], v46 offset:768
	s_waitcnt vmcnt(3) lgkmcnt(0)
	v_mfma_f32_16x16x32_bf16 v[22:25], v[22:25], v[14:17], v[26:29]
	s_nop 2
	ds_read_b128 v[26:29], v46 offset:736
	s_waitcnt lgkmcnt(0)
	v_mfma_f32_16x16x32_bf16 v[14:17], v[26:29], v[14:17], v[18:21]
	s_nop 2
	ds_read_b128 v[18:21], v46 offset:832
	s_waitcnt vmcnt(2) lgkmcnt(0)
	v_mfma_f32_16x16x32_bf16 v[18:21], v[18:21], v[10:13], v[22:25]
	s_nop 2
	ds_read_b128 v[22:25], v46 offset:800
	s_waitcnt lgkmcnt(0)
	v_mfma_f32_16x16x32_bf16 v[10:13], v[22:25], v[10:13], v[14:17]
	s_nop 2
	ds_read_b128 v[14:17], v46 offset:896
	s_waitcnt vmcnt(1) lgkmcnt(0)
	v_mfma_f32_16x16x32_bf16 v[14:17], v[14:17], v[6:9], v[18:21]
	s_nop 2
	ds_read_b128 v[18:21], v46 offset:864
	s_waitcnt lgkmcnt(0)
	v_mfma_f32_16x16x32_bf16 v[6:9], v[18:21], v[6:9], v[10:13]
	s_nop 2
	ds_read_b128 v[10:13], v46 offset:960
	s_waitcnt vmcnt(0) lgkmcnt(0)
	v_mfma_f32_16x16x32_bf16 v[10:13], v[10:13], v[2:5], v[14:17]
	s_nop 2
	ds_read_b128 v[14:17], v46 offset:928
	s_waitcnt lgkmcnt(0)
	v_mfma_f32_16x16x32_bf16 v[2:5], v[14:17], v[2:5], v[6:9]
	s_nop 2
	v_lshlrev_b32_e32 v8, 5, v1
	v_cvt_pk_bf16_f32 v10, v10, v11
	v_cvt_pk_bf16_f32 v11, v12, v13
	s_nop 1
	v_cvt_pk_bf16_f32 v2, v2, v3
	v_bfe_u32 v1, v4, 16, 1
	v_lshl_add_u64 v[6:7], v[36:37], 1, s[6:7]
	v_add3_u32 v1, v4, v1, s81
	v_bfe_u32 v3, v5, 16, 1
	v_lshl_add_u64 v[6:7], v[6:7], 0, v[34:35]
	v_ashrrev_i32_e32 v9, 31, v8
	v_lshrrev_b32_e32 v1, 16, v1
	v_add3_u32 v3, v5, v3, s81
	v_lshl_add_u64 v[6:7], v[8:9], 1, v[6:7]
	v_and_or_b32 v3, v3, s80, v1
	global_store_dwordx2 v[6:7], v[10:11], off
	global_store_dwordx2 v[6:7], v[2:3], off offset:32
	s_barrier
	s_branch .LBB0_2061

; #define LAS __attribute__((address_space(3)))
; template <int L>
; __device__ __forceinline__ void hyena_unit(CArgs& a, int l, int c, LAS unsigned char* lds) {
;     ...
;         bf16x8 zn[8], A[16];
; #pragma unroll
;         for (int j = 2; j < 16; ++j) A[j] = *(const LAS bf16x8*)(ap - 32 * j);
; #pragma unroll 1
;         for (int ib = 0; ib < 8; ++ib) {
;             const bf16* zq = zp + 256 * (ib < 7 ? ib + 1 : 7);
; #pragma unroll
;             for (int ii = 0; ii < 8; ++ii) zn[ii] = *(const bf16x8*)(zq + 32 * ii);
; #pragma unroll
;             for (int ii = 0; ii < 8; ++ii) {
;                 A[(16 - 2 * ii) & 15] = *(const LAS bf16x8*)(ap + 64 * ii);
;                 A[(17 - 2 * ii) & 15] = *(const LAS bf16x8*)(ap + 64 * ii - 32);
; #pragma unroll
;                 for (int jj = 0; jj < 16; ++jj) { const int j = (jj + 2) & 15; acc[j] = __builtin_amdgcn_mfma_f32_16x16x32_bf16(A[(j + 16 - 2 * ii) & 15], zc[ii], acc[j], 0, 0, 0); }
;             }
;             ap += 512;
; #pragma unroll
;             for (int ii = 0; ii < 8; ++ii) zc[ii] = zn[ii];
;         }
.LBB0_2257:
	s_waitcnt vmcnt(1) lgkmcnt(1)
	s_nop 0
	v_mfma_f32_16x16x32_bf16 v[44:47], v[56:59], v[30:33], v[44:47]
	s_cmpk_lg_i32 s14, 0x800
	s_cselect_b32 s78, s14, 0x700
	s_addk_i32 s14, 0x100
	v_mfma_f32_16x16x32_bf16 v[36:39], v[80:83], v[30:33], v[36:39]
	s_cmpk_lg_i32 s14, 0x900
	v_mfma_f32_16x16x32_bf16 v[44:47], v[80:83], v[26:29], v[44:47]
	v_mfma_f32_16x16x32_bf16 v[136:139], v[88:91], v[30:33], v[136:139]
	v_mfma_f32_16x16x32_bf16 v[132:135], v[84:87], v[30:33], v[132:135]
	v_mfma_f32_16x16x32_bf16 v[128:131], v[104:107], v[30:33], v[128:131]
	v_mfma_f32_16x16x32_bf16 v[124:127], v[96:99], v[30:33], v[124:127]
	v_mfma_f32_16x16x32_bf16 v[48:51], v[112:115], v[30:33], v[48:51]
	v_mfma_f32_16x16x32_bf16 v[36:39], v[112:115], v[26:29], v[36:39]
	v_mfma_f32_16x16x32_bf16 v[44:47], v[112:115], v[22:25], v[44:47]
	v_subrev_u32_e32 v112, 32, v161
	s_waitcnt lgkmcnt(0)
	v_mfma_f32_16x16x32_bf16 v[52:55], v[60:63], v[30:33], v[52:55]
	v_mfma_f32_16x16x32_bf16 v[56:59], v[72:75], v[26:29], v[136:139]
	v_mfma_f32_16x16x32_bf16 v[60:63], v[68:71], v[26:29], v[132:135]
	s_nop 1
	ds_read_b128 v[136:139], v112
	ds_read_b128 v[132:135], v161
	v_mfma_f32_16x16x32_bf16 v[128:131], v[88:91], v[26:29], v[128:131]
	v_mfma_f32_16x16x32_bf16 v[124:127], v[84:87], v[26:29], v[124:127]
	v_mfma_f32_16x16x32_bf16 v[140:143], v[68:71], v[30:33], v[140:143]
	v_mfma_f32_16x16x32_bf16 v[40:43], v[76:79], v[30:33], v[40:43]
	v_mfma_f32_16x16x32_bf16 v[52:55], v[76:79], v[26:29], v[52:55]
	v_mfma_f32_16x16x32_bf16 v[76:79], v[72:75], v[22:25], v[128:131]
	v_mfma_f32_16x16x32_bf16 v[80:83], v[68:71], v[22:25], v[124:127]
	v_mfma_f32_16x16x32_bf16 v[144:147], v[72:75], v[30:33], v[144:147]
	s_waitcnt lgkmcnt(0)
	v_mfma_f32_16x16x32_bf16 v[124:127], v[132:135], v[22:25], v[56:59]
	v_mfma_f32_16x16x32_bf16 v[128:131], v[136:139], v[26:29], v[140:143]
	v_mfma_f32_16x16x32_bf16 v[140:143], v[136:139], v[22:25], v[60:63]
	s_nop 2
	ds_read_b128 v[60:63], v161 offset:64
	ds_read_b128 v[56:59], v161 offset:32
	v_mfma_f32_16x16x32_bf16 v[120:123], v[100:103], v[30:33], v[120:123]
	v_mfma_f32_16x16x32_bf16 v[92:95], v[108:111], v[30:33], v[92:95]
	v_mfma_f32_16x16x32_bf16 v[64:67], v[116:119], v[30:33], v[64:67]
	v_mfma_f32_16x16x32_bf16 v[40:43], v[116:119], v[26:29], v[40:43]
	v_mfma_f32_16x16x32_bf16 v[52:55], v[116:119], v[22:25], v[52:55]
	v_mfma_f32_16x16x32_bf16 v[112:115], v[132:135], v[30:33], v[148:151]
	v_mfma_f32_16x16x32_bf16 v[30:33], v[136:139], v[30:33], v[152:155]
	v_mfma_f32_16x16x32_bf16 v[76:79], v[132:135], v[18:21], v[76:79]
	v_mfma_f32_16x16x32_bf16 v[80:83], v[136:139], v[18:21], v[80:83]
	v_mfma_f32_16x16x32_bf16 v[116:119], v[132:135], v[26:29], v[144:147]
	v_mfma_f32_16x16x32_bf16 v[120:123], v[104:107], v[26:29], v[120:123]
	v_mfma_f32_16x16x32_bf16 v[92:95], v[96:99], v[26:29], v[92:95]
	v_mfma_f32_16x16x32_bf16 v[64:67], v[100:103], v[26:29], v[64:67]
	v_mfma_f32_16x16x32_bf16 v[48:51], v[108:111], v[26:29], v[48:51]
	v_mfma_f32_16x16x32_bf16 v[40:43], v[100:103], v[22:25], v[40:43]
	v_mfma_f32_16x16x32_bf16 v[52:55], v[100:103], v[18:21], v[52:55]
	s_waitcnt lgkmcnt(1)
	v_mfma_f32_16x16x32_bf16 v[100:103], v[60:63], v[26:29], v[112:115]
	v_mfma_f32_16x16x32_bf16 v[112:115], v[60:63], v[18:21], v[124:127]
	s_waitcnt lgkmcnt(0)
	v_mfma_f32_16x16x32_bf16 v[26:29], v[56:59], v[26:29], v[30:33]
	v_mfma_f32_16x16x32_bf16 v[30:33], v[56:59], v[22:25], v[128:131]
	v_mfma_f32_16x16x32_bf16 v[124:127], v[60:63], v[14:17], v[76:79]
	v_mfma_f32_16x16x32_bf16 v[128:131], v[56:59], v[14:17], v[80:83]
	s_nop 1
	ds_read_b128 v[76:79], v161 offset:128
	ds_read_b128 v[80:83], v161 offset:96
	v_mfma_f32_16x16x32_bf16 v[36:39], v[108:111], v[22:25], v[36:39]
	v_mfma_f32_16x16x32_bf16 v[44:47], v[108:111], v[18:21], v[44:47]
	v_mfma_f32_16x16x32_bf16 v[108:111], v[60:63], v[22:25], v[116:119]
	v_mfma_f32_16x16x32_bf16 v[116:119], v[56:59], v[18:21], v[140:143]
	v_mfma_f32_16x16x32_bf16 v[120:123], v[88:91], v[22:25], v[120:123]
	v_mfma_f32_16x16x32_bf16 v[92:95], v[84:87], v[22:25], v[92:95]
	v_mfma_f32_16x16x32_bf16 v[64:67], v[104:107], v[22:25], v[64:67]
	v_mfma_f32_16x16x32_bf16 v[48:51], v[96:99], v[22:25], v[48:51]
	v_mfma_f32_16x16x32_bf16 v[40:43], v[104:107], v[18:21], v[40:43]
	v_mfma_f32_16x16x32_bf16 v[36:39], v[96:99], v[18:21], v[36:39]
	v_mfma_f32_16x16x32_bf16 v[52:55], v[104:107], v[14:17], v[52:55]
	v_mfma_f32_16x16x32_bf16 v[44:47], v[96:99], v[14:17], v[44:47]
	s_waitcnt lgkmcnt(1)
	v_mfma_f32_16x16x32_bf16 v[96:99], v[76:79], v[22:25], v[100:103]
	v_mfma_f32_16x16x32_bf16 v[104:107], v[76:79], v[14:17], v[112:115]
	s_waitcnt lgkmcnt(0)
	v_mfma_f32_16x16x32_bf16 v[22:25], v[80:83], v[22:25], v[26:29]
	v_mfma_f32_16x16x32_bf16 v[26:29], v[80:83], v[18:21], v[30:33]
	v_mfma_f32_16x16x32_bf16 v[30:33], v[80:83], v[14:17], v[116:119]
	s_nop 2
	ds_read_b128 v[116:119], v161 offset:192
	ds_read_b128 v[112:115], v161 offset:160
	v_mfma_f32_16x16x32_bf16 v[100:103], v[76:79], v[18:21], v[108:111]
	v_mfma_f32_16x16x32_bf16 v[108:111], v[76:79], v[10:13], v[124:127]
	v_mfma_f32_16x16x32_bf16 v[124:127], v[80:83], v[10:13], v[128:131]
	v_mfma_f32_16x16x32_bf16 v[120:123], v[72:75], v[18:21], v[120:123]
	v_mfma_f32_16x16x32_bf16 v[92:95], v[68:71], v[18:21], v[92:95]
	v_mfma_f32_16x16x32_bf16 v[64:67], v[88:91], v[18:21], v[64:67]
	v_mfma_f32_16x16x32_bf16 v[48:51], v[84:87], v[18:21], v[48:51]
	v_mfma_f32_16x16x32_bf16 v[40:43], v[88:91], v[14:17], v[40:43]
	v_mfma_f32_16x16x32_bf16 v[36:39], v[84:87], v[14:17], v[36:39]
	v_mfma_f32_16x16x32_bf16 v[52:55], v[88:91], v[10:13], v[52:55]
	v_mfma_f32_16x16x32_bf16 v[44:47], v[84:87], v[10:13], v[44:47]
	s_waitcnt lgkmcnt(1)
; #define LAS __attribute__((address_space(3)))
; template <int L>
; __device__ __forceinline__ void hyena_unit(CArgs& a, int l, int c, LAS unsigned char* lds) {
;     ...
;         bf16x8 zn[8], A[16];
; #pragma unroll
;         for (int j = 2; j < 16; ++j) A[j] = *(const LAS bf16x8*)(ap - 32 * j);
; #pragma unroll 1
;         for (int ib = 0; ib < 8; ++ib) {
;             const bf16* zq = zp + 256 * (ib < 7 ? ib + 1 : 7);
; #pragma unroll
;             for (int ii = 0; ii < 8; ++ii) zn[ii] = *(const bf16x8*)(zq + 32 * ii);
; #pragma unroll
;             for (int ii = 0; ii < 8; ++ii) {
;                 A[(16 - 2 * ii) & 15] = *(const LAS bf16x8*)(ap + 64 * ii);
;                 A[(17 - 2 * ii) & 15] = *(const LAS bf16x8*)(ap + 64 * ii - 32);
; #pragma unroll
;                 for (int jj = 0; jj < 16; ++jj) { const int j = (jj + 2) & 15; acc[j] = __builtin_amdgcn_mfma_f32_16x16x32_bf16(A[(j + 16 - 2 * ii) & 15], zc[ii], acc[j], 0, 0, 0); }
;             }
;             ap += 512;
; #pragma unroll
;             for (int ii = 0; ii < 8; ++ii) zc[ii] = zn[ii];
;         }
	v_mfma_f32_16x16x32_bf16 v[84:87], v[116:119], v[18:21], v[96:99]
	v_mfma_f32_16x16x32_bf16 v[88:91], v[116:119], v[14:17], v[100:103]
	s_waitcnt lgkmcnt(0)
	v_mfma_f32_16x16x32_bf16 v[18:21], v[112:115], v[18:21], v[22:25]
	v_mfma_f32_16x16x32_bf16 v[22:25], v[112:115], v[14:17], v[26:29]
	v_mfma_f32_16x16x32_bf16 v[26:29], v[112:115], v[10:13], v[30:33]
	v_mfma_f32_16x16x32_bf16 v[30:33], v[116:119], v[6:9], v[108:111]
	ds_read_b128 v[100:103], v161 offset:256
	s_nop 1
	ds_read_b128 v[108:111], v161 offset:224
	v_mfma_f32_16x16x32_bf16 v[96:99], v[116:119], v[10:13], v[104:107]
	v_mfma_f32_16x16x32_bf16 v[104:107], v[112:115], v[6:9], v[124:127]
	v_mfma_f32_16x16x32_bf16 v[48:51], v[68:71], v[14:17], v[48:51]
	v_mfma_f32_16x16x32_bf16 v[36:39], v[68:71], v[10:13], v[36:39]
	v_mfma_f32_16x16x32_bf16 v[44:47], v[68:71], v[6:9], v[44:47]
	s_waitcnt lgkmcnt(1)
	v_mfma_f32_16x16x32_bf16 v[68:71], v[100:103], v[14:17], v[84:87]
	v_mfma_f32_16x16x32_bf16 v[84:87], v[100:103], v[6:9], v[96:99]
	s_waitcnt vmcnt(0) lgkmcnt(0)
	v_mfma_f32_16x16x32_bf16 v[124:127], v[108:111], v[2:5], v[104:107]
	s_nop 2
	ds_read_b128 v[104:107], v161 offset:320
	ds_read_b128 v[96:99], v161 offset:288
	v_mfma_f32_16x16x32_bf16 v[120:123], v[132:135], v[14:17], v[120:123]
	v_mfma_f32_16x16x32_bf16 v[92:95], v[136:139], v[14:17], v[92:95]
	v_mfma_f32_16x16x32_bf16 v[64:67], v[72:75], v[14:17], v[64:67]
	v_mfma_f32_16x16x32_bf16 v[14:17], v[108:111], v[14:17], v[18:21]
	v_mfma_f32_16x16x32_bf16 v[18:21], v[108:111], v[10:13], v[22:25]
	v_mfma_f32_16x16x32_bf16 v[22:25], v[108:111], v[6:9], v[26:29]
	s_waitcnt lgkmcnt(1)
	v_mfma_f32_16x16x32_bf16 v[26:29], v[104:107], v[10:13], v[68:71]
	s_nop 2
	v_lshl_add_u64 v[68:69], s[78:79], 1, v[158:159]
	v_mfma_f32_16x16x32_bf16 v[120:123], v[60:63], v[10:13], v[120:123]
	v_mfma_f32_16x16x32_bf16 v[92:95], v[56:59], v[10:13], v[92:95]
	v_mfma_f32_16x16x32_bf16 v[64:67], v[132:135], v[10:13], v[64:67]
	v_mfma_f32_16x16x32_bf16 v[48:51], v[136:139], v[10:13], v[48:51]
	v_mfma_f32_16x16x32_bf16 v[40:43], v[72:75], v[10:13], v[40:43]
	v_mfma_f32_16x16x32_bf16 v[52:55], v[72:75], v[6:9], v[52:55]
	v_mfma_f32_16x16x32_bf16 v[72:75], v[100:103], v[10:13], v[88:91]
	s_waitcnt lgkmcnt(0)
	v_mfma_f32_16x16x32_bf16 v[10:13], v[96:99], v[10:13], v[14:17]
	s_nop 2
	global_load_dwordx4 v[14:17], v[68:69], off
	v_mfma_f32_16x16x32_bf16 v[36:39], v[136:139], v[6:9], v[36:39]
	global_load_dwordx4 v[170:173], v[68:69], off offset:64
	global_load_dwordx4 v[174:177], v[68:69], off offset:128
	global_load_dwordx4 v[178:181], v[68:69], off offset:192
	v_mfma_f32_16x16x32_bf16 v[44:47], v[136:139], v[2:5], v[44:47]
	v_mfma_f32_16x16x32_bf16 v[136:139], v[104:107], v[2:5], v[84:87]
	ds_read_b128 v[88:91], v161 offset:384
	s_nop 1
	ds_read_b128 v[84:87], v161 offset:352
	global_load_dwordx4 v[182:185], v[68:69], off offset:256
	global_load_dwordx4 v[186:189], v[68:69], off offset:320
	global_load_dwordx4 v[202:205], v[68:69], off offset:384
	global_load_dwordx4 v[206:209], v[68:69], off offset:448
	v_mfma_f32_16x16x32_bf16 v[128:131], v[100:103], v[2:5], v[30:33]
	ds_read_b128 v[68:71], v161 offset:416
	v_mfma_f32_16x16x32_bf16 v[30:33], v[104:107], v[6:9], v[72:75]
	s_nop 2
	ds_read_b128 v[72:75], v161 offset:448
	v_mfma_f32_16x16x32_bf16 v[120:123], v[76:79], v[6:9], v[120:123]
	v_add_u32_e32 v161, 0x200, v161
	v_mfma_f32_16x16x32_bf16 v[92:95], v[80:83], v[6:9], v[92:95]
	v_mfma_f32_16x16x32_bf16 v[64:67], v[60:63], v[6:9], v[64:67]
	v_mfma_f32_16x16x32_bf16 v[48:51], v[56:59], v[6:9], v[48:51]
	v_mfma_f32_16x16x32_bf16 v[40:43], v[132:135], v[6:9], v[40:43]
	v_mfma_f32_16x16x32_bf16 v[52:55], v[132:135], v[2:5], v[52:55]
	v_mfma_f32_16x16x32_bf16 v[18:21], v[96:99], v[6:9], v[18:21]
	v_mfma_f32_16x16x32_bf16 v[132:135], v[96:99], v[2:5], v[22:25]
	s_waitcnt lgkmcnt(3)
	v_mfma_f32_16x16x32_bf16 v[22:25], v[88:91], v[6:9], v[26:29]
	s_waitcnt lgkmcnt(2)
	v_mfma_f32_16x16x32_bf16 v[6:9], v[84:87], v[6:9], v[10:13]
	s_waitcnt vmcnt(6)
	v_mov_b64_e32 v[26:27], v[170:171]
	v_mfma_f32_16x16x32_bf16 v[120:123], v[116:119], v[2:5], v[120:123]
	v_mov_b64_e32 v[28:29], v[172:173]
	s_waitcnt vmcnt(2)
	v_mov_b64_e32 v[10:11], v[186:187]
	v_mfma_f32_16x16x32_bf16 v[92:95], v[112:115], v[2:5], v[92:95]
	v_mov_b64_e32 v[12:13], v[188:189]
	v_mfma_f32_16x16x32_bf16 v[64:67], v[76:79], v[2:5], v[64:67]
	v_mfma_f32_16x16x32_bf16 v[48:51], v[80:83], v[2:5], v[48:51]
	v_mfma_f32_16x16x32_bf16 v[40:43], v[60:63], v[2:5], v[40:43]
	v_mfma_f32_16x16x32_bf16 v[36:39], v[56:59], v[2:5], v[36:39]
	v_mfma_f32_16x16x32_bf16 v[144:147], v[88:91], v[2:5], v[30:33]
	v_mfma_f32_16x16x32_bf16 v[140:143], v[84:87], v[2:5], v[18:21]
	s_nop 1
	v_mov_b64_e32 v[32:33], v[16:17]
	v_mov_b64_e32 v[30:31], v[14:15]
	v_mov_b64_e32 v[14:15], v[182:183]
	s_waitcnt lgkmcnt(0)
	v_mfma_f32_16x16x32_bf16 v[148:151], v[72:75], v[2:5], v[22:25]
	v_mov_b64_e32 v[18:19], v[178:179]
	v_mov_b64_e32 v[20:21], v[180:181]
	v_mov_b64_e32 v[16:17], v[184:185]
	v_mfma_f32_16x16x32_bf16 v[152:155], v[68:71], v[2:5], v[6:9]
	v_mov_b64_e32 v[22:23], v[174:175]
	s_waitcnt vmcnt(0)
	v_mov_b64_e32 v[2:3], v[206:207]
	v_mov_b64_e32 v[24:25], v[176:177]
	v_mov_b64_e32 v[6:7], v[202:203]
	v_mov_b64_e32 v[8:9], v[204:205]
	v_mov_b64_e32 v[4:5], v[208:209]
	s_cbranch_scc1 .LBB0_2257
; __device__ __forceinline__ unsigned pk2(float lo, float hi) { return f2bf(lo) | (f2bf(hi) << 16); }
; template <int L>
; __device__ __forceinline__ void hyena_unit(CArgs& a, int l, int c, LAS unsigned char* lds) {
;     ...
; #pragma unroll
;     for (int j = 0; j < NTW; ++j) *(u32x2*)(YT + 16 * (w * NTW + j) + 4 * kg) = (u32x2){pk2(acc[j][0], acc[j][1]), pk2(acc[j][2], acc[j][3])};
	v_lshlrev_b32_e32 v2, 8, v1
	v_cvt_pk_bf16_f32 v6, v148, v149
	v_lshl_add_u64 v[4:5], v[156:157], 0, v[34:35]
	v_cvt_pk_bf16_f32 v7, v150, v151
	v_ashrrev_i32_e32 v3, 31, v2
	v_lshl_add_u64 v[2:3], v[2:3], 1, v[4:5]
	s_mov_b64 s[14:15], 0x50400200
	v_lshl_add_u64 v[4:5], v[2:3], 0, s[14:15]
	s_mov_b32 s14, 0x50400000
	v_add_co_u32_e32 v2, vcc, s14, v2
	s_nop 0
	s_nop 0
	v_addc_co_u32_e32 v3, vcc, 0, v3, vcc
	global_store_dwordx2 v[2:3], v[6:7], off offset:512
	v_cvt_pk_bf16_f32 v2, v152, v153
	v_cvt_pk_bf16_f32 v3, v154, v155
	global_store_dwordx2 v[4:5], v[2:3], off offset:32
	v_cvt_pk_bf16_f32 v2, v144, v145
	v_cvt_pk_bf16_f32 v3, v146, v147
	global_store_dwordx2 v[4:5], v[2:3], off offset:64
	v_cvt_pk_bf16_f32 v2, v140, v141
	v_cvt_pk_bf16_f32 v3, v142, v143
	global_store_dwordx2 v[4:5], v[2:3], off offset:96
	v_cvt_pk_bf16_f32 v2, v136, v137
	v_cvt_pk_bf16_f32 v3, v138, v139
	global_store_dwordx2 v[4:5], v[2:3], off offset:128
	v_cvt_pk_bf16_f32 v2, v132, v133
	v_cvt_pk_bf16_f32 v3, v134, v135
	global_store_dwordx2 v[4:5], v[2:3], off offset:160
	v_cvt_pk_bf16_f32 v2, v128, v129
	v_cvt_pk_bf16_f32 v3, v130, v131
	global_store_dwordx2 v[4:5], v[2:3], off offset:192
	v_cvt_pk_bf16_f32 v2, v124, v125
	v_cvt_pk_bf16_f32 v3, v126, v127
	global_store_dwordx2 v[4:5], v[2:3], off offset:224
	v_cvt_pk_bf16_f32 v2, v120, v121
	v_cvt_pk_bf16_f32 v3, v122, v123
	global_store_dwordx2 v[4:5], v[2:3], off offset:256
	v_cvt_pk_bf16_f32 v2, v92, v93
	v_cvt_pk_bf16_f32 v3, v94, v95
	global_store_dwordx2 v[4:5], v[2:3], off offset:288
	v_cvt_pk_bf16_f32 v2, v64, v65
	v_cvt_pk_bf16_f32 v3, v66, v67
	global_store_dwordx2 v[4:5], v[2:3], off offset:320
	v_cvt_pk_bf16_f32 v2, v48, v49
	v_cvt_pk_bf16_f32 v3, v50, v51
	global_store_dwordx2 v[4:5], v[2:3], off offset:352
	v_cvt_pk_bf16_f32 v2, v40, v41
	v_cvt_pk_bf16_f32 v3, v42, v43
	global_store_dwordx2 v[4:5], v[2:3], off offset:384
	v_cvt_pk_bf16_f32 v2, v36, v37
	v_cvt_pk_bf16_f32 v3, v38, v39
	global_store_dwordx2 v[4:5], v[2:3], off offset:416
	v_cvt_pk_bf16_f32 v2, v52, v53
	v_cvt_pk_bf16_f32 v3, v54, v55
	global_store_dwordx2 v[4:5], v[2:3], off offset:448
	v_cvt_pk_bf16_f32 v2, v44, v45
	v_bfe_u32 v1, v46, 16, 1
	v_add3_u32 v1, v46, v1, s81
	v_bfe_u32 v3, v47, 16, 1
	v_lshrrev_b32_e32 v1, 16, v1
	v_add3_u32 v3, v47, v3, s81
	v_and_or_b32 v3, v3, s80, v1
	global_store_dwordx2 v[4:5], v[2:3], off offset:480
	s_barrier
	s_branch .LBB0_2061

; #define LAS __attribute__((address_space(3)))
; template <int L>
; __device__ __forceinline__ void hyena_unit(CArgs& a, int l, int c, LAS unsigned char* lds) {
;     ...
;         bf16x8 zn[8], A[16];
; #pragma unroll
;         for (int j = 2; j < 16; ++j) A[j] = *(const LAS bf16x8*)(ap - 32 * j);
; #pragma unroll 1
;         for (int ib = 0; ib < 8; ++ib) {
;             const bf16* zq = zp + 256 * (ib < 7 ? ib + 1 : 7);
; #pragma unroll
;             for (int ii = 0; ii < 8; ++ii) zn[ii] = *(const bf16x8*)(zq + 32 * ii);
; #pragma unroll
;             for (int ii = 0; ii < 8; ++ii) {
;                 A[(16 - 2 * ii) & 15] = *(const LAS bf16x8*)(ap + 64 * ii);
;                 A[(17 - 2 * ii) & 15] = *(const LAS bf16x8*)(ap + 64 * ii - 32);
; #pragma unroll
;                 for (int jj = 0; jj < 16; ++jj) { const int j = (jj + 2) & 15; acc[j] = __builtin_amdgcn_mfma_f32_16x16x32_bf16(A[(j + 16 - 2 * ii) & 15], zc[ii], acc[j], 0, 0, 0); }
;             }
;             ap += 512;
; #pragma unroll
;             for (int ii = 0; ii < 8; ++ii) zc[ii] = zn[ii];
;         }
.LBB0_2417:
	s_waitcnt vmcnt(1) lgkmcnt(1)
	s_nop 0
	v_mfma_f32_16x16x32_bf16 v[44:47], v[56:59], v[30:33], v[44:47]
	s_cmpk_lg_i32 s6, 0x800
	s_cselect_b32 s78, s6, 0x700
	s_addk_i32 s6, 0x100
	v_mfma_f32_16x16x32_bf16 v[36:39], v[80:83], v[30:33], v[36:39]
	s_cmpk_lg_i32 s6, 0x900
	v_mfma_f32_16x16x32_bf16 v[44:47], v[80:83], v[26:29], v[44:47]
	v_mfma_f32_16x16x32_bf16 v[136:139], v[88:91], v[30:33], v[136:139]
	v_mfma_f32_16x16x32_bf16 v[132:135], v[84:87], v[30:33], v[132:135]
	v_mfma_f32_16x16x32_bf16 v[128:131], v[104:107], v[30:33], v[128:131]
	v_mfma_f32_16x16x32_bf16 v[124:127], v[96:99], v[30:33], v[124:127]
	v_mfma_f32_16x16x32_bf16 v[48:51], v[112:115], v[30:33], v[48:51]
	v_mfma_f32_16x16x32_bf16 v[36:39], v[112:115], v[26:29], v[36:39]
	v_mfma_f32_16x16x32_bf16 v[44:47], v[112:115], v[22:25], v[44:47]
	v_subrev_u32_e32 v112, 32, v161
	s_waitcnt lgkmcnt(0)
	v_mfma_f32_16x16x32_bf16 v[52:55], v[60:63], v[30:33], v[52:55]
	v_mfma_f32_16x16x32_bf16 v[56:59], v[72:75], v[26:29], v[136:139]
	v_mfma_f32_16x16x32_bf16 v[60:63], v[68:71], v[26:29], v[132:135]
	s_nop 1
	ds_read_b128 v[136:139], v112
	ds_read_b128 v[132:135], v161
	v_mfma_f32_16x16x32_bf16 v[128:131], v[88:91], v[26:29], v[128:131]
	v_mfma_f32_16x16x32_bf16 v[124:127], v[84:87], v[26:29], v[124:127]
	v_mfma_f32_16x16x32_bf16 v[140:143], v[68:71], v[30:33], v[140:143]
	v_mfma_f32_16x16x32_bf16 v[40:43], v[76:79], v[30:33], v[40:43]
	v_mfma_f32_16x16x32_bf16 v[52:55], v[76:79], v[26:29], v[52:55]
	v_mfma_f32_16x16x32_bf16 v[76:79], v[72:75], v[22:25], v[128:131]
	v_mfma_f32_16x16x32_bf16 v[80:83], v[68:71], v[22:25], v[124:127]
	v_mfma_f32_16x16x32_bf16 v[144:147], v[72:75], v[30:33], v[144:147]
	s_waitcnt lgkmcnt(0)
	v_mfma_f32_16x16x32_bf16 v[124:127], v[132:135], v[22:25], v[56:59]
	v_mfma_f32_16x16x32_bf16 v[128:131], v[136:139], v[26:29], v[140:143]
	v_mfma_f32_16x16x32_bf16 v[140:143], v[136:139], v[22:25], v[60:63]
	s_nop 2
	ds_read_b128 v[60:63], v161 offset:64
	ds_read_b128 v[56:59], v161 offset:32
	v_mfma_f32_16x16x32_bf16 v[120:123], v[100:103], v[30:33], v[120:123]
	v_mfma_f32_16x16x32_bf16 v[92:95], v[108:111], v[30:33], v[92:95]
	v_mfma_f32_16x16x32_bf16 v[64:67], v[116:119], v[30:33], v[64:67]
	v_mfma_f32_16x16x32_bf16 v[40:43], v[116:119], v[26:29], v[40:43]
	v_mfma_f32_16x16x32_bf16 v[52:55], v[116:119], v[22:25], v[52:55]
	v_mfma_f32_16x16x32_bf16 v[112:115], v[132:135], v[30:33], v[148:151]
	v_mfma_f32_16x16x32_bf16 v[30:33], v[136:139], v[30:33], v[152:155]
	v_mfma_f32_16x16x32_bf16 v[76:79], v[132:135], v[18:21], v[76:79]
	v_mfma_f32_16x16x32_bf16 v[80:83], v[136:139], v[18:21], v[80:83]
	v_mfma_f32_16x16x32_bf16 v[116:119], v[132:135], v[26:29], v[144:147]
	v_mfma_f32_16x16x32_bf16 v[120:123], v[104:107], v[26:29], v[120:123]
	v_mfma_f32_16x16x32_bf16 v[92:95], v[96:99], v[26:29], v[92:95]
	v_mfma_f32_16x16x32_bf16 v[64:67], v[100:103], v[26:29], v[64:67]
	v_mfma_f32_16x16x32_bf16 v[48:51], v[108:111], v[26:29], v[48:51]
	v_mfma_f32_16x16x32_bf16 v[40:43], v[100:103], v[22:25], v[40:43]
	v_mfma_f32_16x16x32_bf16 v[52:55], v[100:103], v[18:21], v[52:55]
	s_waitcnt lgkmcnt(1)
	v_mfma_f32_16x16x32_bf16 v[100:103], v[60:63], v[26:29], v[112:115]
	v_mfma_f32_16x16x32_bf16 v[112:115], v[60:63], v[18:21], v[124:127]
	s_waitcnt lgkmcnt(0)
	v_mfma_f32_16x16x32_bf16 v[26:29], v[56:59], v[26:29], v[30:33]
	v_mfma_f32_16x16x32_bf16 v[30:33], v[56:59], v[22:25], v[128:131]
	v_mfma_f32_16x16x32_bf16 v[124:127], v[60:63], v[14:17], v[76:79]
	v_mfma_f32_16x16x32_bf16 v[128:131], v[56:59], v[14:17], v[80:83]
	s_nop 1
	ds_read_b128 v[76:79], v161 offset:128
	ds_read_b128 v[80:83], v161 offset:96
	v_mfma_f32_16x16x32_bf16 v[36:39], v[108:111], v[22:25], v[36:39]
	v_mfma_f32_16x16x32_bf16 v[44:47], v[108:111], v[18:21], v[44:47]
	v_mfma_f32_16x16x32_bf16 v[108:111], v[60:63], v[22:25], v[116:119]
	v_mfma_f32_16x16x32_bf16 v[116:119], v[56:59], v[18:21], v[140:143]
	v_mfma_f32_16x16x32_bf16 v[120:123], v[88:91], v[22:25], v[120:123]
	v_mfma_f32_16x16x32_bf16 v[92:95], v[84:87], v[22:25], v[92:95]
	v_mfma_f32_16x16x32_bf16 v[64:67], v[104:107], v[22:25], v[64:67]
	v_mfma_f32_16x16x32_bf16 v[48:51], v[96:99], v[22:25], v[48:51]
	v_mfma_f32_16x16x32_bf16 v[40:43], v[104:107], v[18:21], v[40:43]
	v_mfma_f32_16x16x32_bf16 v[36:39], v[96:99], v[18:21], v[36:39]
	v_mfma_f32_16x16x32_bf16 v[52:55], v[104:107], v[14:17], v[52:55]
	v_mfma_f32_16x16x32_bf16 v[44:47], v[96:99], v[14:17], v[44:47]
	s_waitcnt lgkmcnt(1)
	v_mfma_f32_16x16x32_bf16 v[96:99], v[76:79], v[22:25], v[100:103]
	v_mfma_f32_16x16x32_bf16 v[104:107], v[76:79], v[14:17], v[112:115]
	s_waitcnt lgkmcnt(0)
	v_mfma_f32_16x16x32_bf16 v[22:25], v[80:83], v[22:25], v[26:29]
	v_mfma_f32_16x16x32_bf16 v[26:29], v[80:83], v[18:21], v[30:33]
	v_mfma_f32_16x16x32_bf16 v[30:33], v[80:83], v[14:17], v[116:119]
	s_nop 2
	ds_read_b128 v[116:119], v161 offset:192
	ds_read_b128 v[112:115], v161 offset:160
	v_mfma_f32_16x16x32_bf16 v[100:103], v[76:79], v[18:21], v[108:111]
	v_mfma_f32_16x16x32_bf16 v[108:111], v[76:79], v[10:13], v[124:127]
	v_mfma_f32_16x16x32_bf16 v[124:127], v[80:83], v[10:13], v[128:131]
	v_mfma_f32_16x16x32_bf16 v[120:123], v[72:75], v[18:21], v[120:123]
	v_mfma_f32_16x16x32_bf16 v[92:95], v[68:71], v[18:21], v[92:95]
	v_mfma_f32_16x16x32_bf16 v[64:67], v[88:91], v[18:21], v[64:67]
	v_mfma_f32_16x16x32_bf16 v[48:51], v[84:87], v[18:21], v[48:51]
	v_mfma_f32_16x16x32_bf16 v[40:43], v[88:91], v[14:17], v[40:43]
	v_mfma_f32_16x16x32_bf16 v[36:39], v[84:87], v[14:17], v[36:39]
	v_mfma_f32_16x16x32_bf16 v[52:55], v[88:91], v[10:13], v[52:55]
	v_mfma_f32_16x16x32_bf16 v[44:47], v[84:87], v[10:13], v[44:47]
	s_waitcnt lgkmcnt(1)
; #define LAS __attribute__((address_space(3)))
; template <int L>
; __device__ __forceinline__ void hyena_unit(CArgs& a, int l, int c, LAS unsigned char* lds) {
;     ...
;         bf16x8 zn[8], A[16];
; #pragma unroll
;         for (int j = 2; j < 16; ++j) A[j] = *(const LAS bf16x8*)(ap - 32 * j);
; #pragma unroll 1
;         for (int ib = 0; ib < 8; ++ib) {
;             const bf16* zq = zp + 256 * (ib < 7 ? ib + 1 : 7);
; #pragma unroll
;             for (int ii = 0; ii < 8; ++ii) zn[ii] = *(const bf16x8*)(zq + 32 * ii);
; #pragma unroll
;             for (int ii = 0; ii < 8; ++ii) {
;                 A[(16 - 2 * ii) & 15] = *(const LAS bf16x8*)(ap + 64 * ii);
;                 A[(17 - 2 * ii) & 15] = *(const LAS bf16x8*)(ap + 64 * ii - 32);
; #pragma unroll
;                 for (int jj = 0; jj < 16; ++jj) { const int j = (jj + 2) & 15; acc[j] = __builtin_amdgcn_mfma_f32_16x16x32_bf16(A[(j + 16 - 2 * ii) & 15], zc[ii], acc[j], 0, 0, 0); }
;             }
;             ap += 512;
; #pragma unroll
;             for (int ii = 0; ii < 8; ++ii) zc[ii] = zn[ii];
;         }
	v_mfma_f32_16x16x32_bf16 v[84:87], v[116:119], v[18:21], v[96:99]
	v_mfma_f32_16x16x32_bf16 v[88:91], v[116:119], v[14:17], v[100:103]
	s_waitcnt lgkmcnt(0)
	v_mfma_f32_16x16x32_bf16 v[18:21], v[112:115], v[18:21], v[22:25]
	v_mfma_f32_16x16x32_bf16 v[22:25], v[112:115], v[14:17], v[26:29]
	v_mfma_f32_16x16x32_bf16 v[26:29], v[112:115], v[10:13], v[30:33]
	v_mfma_f32_16x16x32_bf16 v[30:33], v[116:119], v[6:9], v[108:111]
	ds_read_b128 v[100:103], v161 offset:256
	s_nop 1
	ds_read_b128 v[108:111], v161 offset:224
	v_mfma_f32_16x16x32_bf16 v[96:99], v[116:119], v[10:13], v[104:107]
	v_mfma_f32_16x16x32_bf16 v[104:107], v[112:115], v[6:9], v[124:127]
	v_mfma_f32_16x16x32_bf16 v[48:51], v[68:71], v[14:17], v[48:51]
	v_mfma_f32_16x16x32_bf16 v[36:39], v[68:71], v[10:13], v[36:39]
	v_mfma_f32_16x16x32_bf16 v[44:47], v[68:71], v[6:9], v[44:47]
	s_waitcnt lgkmcnt(1)
	v_mfma_f32_16x16x32_bf16 v[68:71], v[100:103], v[14:17], v[84:87]
	v_mfma_f32_16x16x32_bf16 v[84:87], v[100:103], v[6:9], v[96:99]
	s_waitcnt vmcnt(0) lgkmcnt(0)
	v_mfma_f32_16x16x32_bf16 v[124:127], v[108:111], v[2:5], v[104:107]
	s_nop 2
	ds_read_b128 v[104:107], v161 offset:320
	ds_read_b128 v[96:99], v161 offset:288
	v_mfma_f32_16x16x32_bf16 v[120:123], v[132:135], v[14:17], v[120:123]
	v_mfma_f32_16x16x32_bf16 v[92:95], v[136:139], v[14:17], v[92:95]
	v_mfma_f32_16x16x32_bf16 v[64:67], v[72:75], v[14:17], v[64:67]
	v_mfma_f32_16x16x32_bf16 v[14:17], v[108:111], v[14:17], v[18:21]
	v_mfma_f32_16x16x32_bf16 v[18:21], v[108:111], v[10:13], v[22:25]
	v_mfma_f32_16x16x32_bf16 v[22:25], v[108:111], v[6:9], v[26:29]
	s_waitcnt lgkmcnt(1)
	v_mfma_f32_16x16x32_bf16 v[26:29], v[104:107], v[10:13], v[68:71]
	s_nop 2
	v_lshl_add_u64 v[68:69], s[78:79], 1, v[158:159]
	v_mfma_f32_16x16x32_bf16 v[120:123], v[60:63], v[10:13], v[120:123]
	v_mfma_f32_16x16x32_bf16 v[92:95], v[56:59], v[10:13], v[92:95]
	v_mfma_f32_16x16x32_bf16 v[64:67], v[132:135], v[10:13], v[64:67]
	v_mfma_f32_16x16x32_bf16 v[48:51], v[136:139], v[10:13], v[48:51]
	v_mfma_f32_16x16x32_bf16 v[40:43], v[72:75], v[10:13], v[40:43]
	v_mfma_f32_16x16x32_bf16 v[52:55], v[72:75], v[6:9], v[52:55]
	v_mfma_f32_16x16x32_bf16 v[72:75], v[100:103], v[10:13], v[88:91]
	s_waitcnt lgkmcnt(0)
	v_mfma_f32_16x16x32_bf16 v[10:13], v[96:99], v[10:13], v[14:17]
	s_nop 2
	global_load_dwordx4 v[14:17], v[68:69], off
	v_mfma_f32_16x16x32_bf16 v[36:39], v[136:139], v[6:9], v[36:39]
	global_load_dwordx4 v[170:173], v[68:69], off offset:64
	global_load_dwordx4 v[174:177], v[68:69], off offset:128
	global_load_dwordx4 v[178:181], v[68:69], off offset:192
	v_mfma_f32_16x16x32_bf16 v[44:47], v[136:139], v[2:5], v[44:47]
	v_mfma_f32_16x16x32_bf16 v[136:139], v[104:107], v[2:5], v[84:87]
	ds_read_b128 v[88:91], v161 offset:384
	s_nop 1
	ds_read_b128 v[84:87], v161 offset:352
	global_load_dwordx4 v[182:185], v[68:69], off offset:256
	global_load_dwordx4 v[186:189], v[68:69], off offset:320
	global_load_dwordx4 v[202:205], v[68:69], off offset:384
	global_load_dwordx4 v[206:209], v[68:69], off offset:448
	v_mfma_f32_16x16x32_bf16 v[128:131], v[100:103], v[2:5], v[30:33]
	ds_read_b128 v[68:71], v161 offset:416
	v_mfma_f32_16x16x32_bf16 v[30:33], v[104:107], v[6:9], v[72:75]
	s_nop 2
	ds_read_b128 v[72:75], v161 offset:448
	v_mfma_f32_16x16x32_bf16 v[120:123], v[76:79], v[6:9], v[120:123]
	v_add_u32_e32 v161, 0x200, v161
	v_mfma_f32_16x16x32_bf16 v[92:95], v[80:83], v[6:9], v[92:95]
	v_mfma_f32_16x16x32_bf16 v[64:67], v[60:63], v[6:9], v[64:67]
	v_mfma_f32_16x16x32_bf16 v[48:51], v[56:59], v[6:9], v[48:51]
	v_mfma_f32_16x16x32_bf16 v[40:43], v[132:135], v[6:9], v[40:43]
	v_mfma_f32_16x16x32_bf16 v[52:55], v[132:135], v[2:5], v[52:55]
	v_mfma_f32_16x16x32_bf16 v[18:21], v[96:99], v[6:9], v[18:21]
	v_mfma_f32_16x16x32_bf16 v[132:135], v[96:99], v[2:5], v[22:25]
	s_waitcnt lgkmcnt(3)
	v_mfma_f32_16x16x32_bf16 v[22:25], v[88:91], v[6:9], v[26:29]
	s_waitcnt lgkmcnt(2)
	v_mfma_f32_16x16x32_bf16 v[6:9], v[84:87], v[6:9], v[10:13]
	s_waitcnt vmcnt(6)
	v_mov_b64_e32 v[26:27], v[170:171]
	v_mfma_f32_16x16x32_bf16 v[120:123], v[116:119], v[2:5], v[120:123]
	v_mov_b64_e32 v[28:29], v[172:173]
	s_waitcnt vmcnt(2)
	v_mov_b64_e32 v[10:11], v[186:187]
	v_mfma_f32_16x16x32_bf16 v[92:95], v[112:115], v[2:5], v[92:95]
	v_mov_b64_e32 v[12:13], v[188:189]
	v_mfma_f32_16x16x32_bf16 v[64:67], v[76:79], v[2:5], v[64:67]
	v_mfma_f32_16x16x32_bf16 v[48:51], v[80:83], v[2:5], v[48:51]
	v_mfma_f32_16x16x32_bf16 v[40:43], v[60:63], v[2:5], v[40:43]
	v_mfma_f32_16x16x32_bf16 v[36:39], v[56:59], v[2:5], v[36:39]
	v_mfma_f32_16x16x32_bf16 v[144:147], v[88:91], v[2:5], v[30:33]
	v_mfma_f32_16x16x32_bf16 v[140:143], v[84:87], v[2:5], v[18:21]
	s_nop 1
	v_mov_b64_e32 v[32:33], v[16:17]
	v_mov_b64_e32 v[30:31], v[14:15]
	v_mov_b64_e32 v[14:15], v[182:183]
	s_waitcnt lgkmcnt(0)
	v_mfma_f32_16x16x32_bf16 v[148:151], v[72:75], v[2:5], v[22:25]
	v_mov_b64_e32 v[18:19], v[178:179]
	v_mov_b64_e32 v[20:21], v[180:181]
	v_mov_b64_e32 v[16:17], v[184:185]
	v_mfma_f32_16x16x32_bf16 v[152:155], v[68:71], v[2:5], v[6:9]
	v_mov_b64_e32 v[22:23], v[174:175]
	s_waitcnt vmcnt(0)
	v_mov_b64_e32 v[2:3], v[206:207]
	v_mov_b64_e32 v[24:25], v[176:177]
	v_mov_b64_e32 v[6:7], v[202:203]
	v_mov_b64_e32 v[8:9], v[204:205]
	v_mov_b64_e32 v[4:5], v[208:209]
	s_cbranch_scc1 .LBB0_2417
; #define LAS __attribute__((address_space(3)))
; __device__ __forceinline__ unsigned pk2(float lo, float hi) { return f2bf(lo) | (f2bf(hi) << 16); }
; template <int L>
; __device__ __forceinline__ void hyena_unit(CArgs& a, int l, int c, LAS unsigned char* lds) {
;     ...
;     const float* kf = (const float*)(a.ws + WS_KUN) + ((size_t)((l * 2 + Lt) * 512 + c)) * 2048;
;     const float* kb = kf + (size_t)256 * 2048;
;     LAS float* red = (LAS float*)(lds + 8 * CST);
;     const bf16* Z = (const bf16*)(a.ws + WS_MIX + MX_ZT) + ((size_t)(c * 16 + fr)) * 2304 + SOFF;
;     const bf16* zp = Z + 8 * kg;
;     bf16x8 zc[8];
; #pragma unroll
;     for (int ii = 0; ii < 8; ++ii) zc[ii] = *(const bf16x8*)(zp + 32 * ii);
;     constexpr int NI = (2 * L + 16 + 511) / 512;
;     float gv[NI];
;     float s = 0.f;
; #pragma unroll
;     for (int q = 0; q < NI; ++q) {
;         const int idx = tid + 512 * q, ic = min(max(idx, 1), 2 * L - 1);
;         const float v = *(ic <= L ? kf + (L - ic) : kb + (ic - L));
;         gv[q] = (idx >= 1 && idx < 2 * L) ? v : 0.f;
;         s += fabsf(gv[q]);
;     }
;     s = wave_sum(s);
;     if (lane == 0) red[w] = s;
;     __syncthreads();
;     ...
; #pragma unroll
;     for (int j = 0; j < NTW; ++j) *(u32x2*)(YT + 16 * (w * NTW + j) + 4 * kg) = (u32x2){pk2(acc[j][0], acc[j][1]), pk2(acc[j][2], acc[j][3])};
	v_lshlrev_b32_e32 v2, 8, v1
	v_cvt_pk_bf16_f32 v6, v148, v149
	v_lshl_add_u64 v[4:5], v[156:157], 0, v[34:35]
	v_cvt_pk_bf16_f32 v7, v150, v151
	v_ashrrev_i32_e32 v3, 31, v2
	v_lshl_add_u64 v[2:3], v[2:3], 1, v[4:5]
	s_mov_b64 s[6:7], 0x50400200
	v_lshl_add_u64 v[4:5], v[2:3], 0, s[6:7]
	s_mov_b32 s6, 0x50400000
	v_add_co_u32_e32 v2, vcc, s6, v2
	s_nop 0
	s_nop 0
	v_addc_co_u32_e32 v3, vcc, 0, v3, vcc
	global_store_dwordx2 v[2:3], v[6:7], off offset:512
	v_cvt_pk_bf16_f32 v2, v152, v153
	v_cvt_pk_bf16_f32 v3, v154, v155
	global_store_dwordx2 v[4:5], v[2:3], off offset:32
	v_cvt_pk_bf16_f32 v2, v144, v145
	v_cvt_pk_bf16_f32 v3, v146, v147
	global_store_dwordx2 v[4:5], v[2:3], off offset:64
	v_cvt_pk_bf16_f32 v2, v140, v141
	v_cvt_pk_bf16_f32 v3, v142, v143
	global_store_dwordx2 v[4:5], v[2:3], off offset:96
	v_cvt_pk_bf16_f32 v2, v136, v137
	v_cvt_pk_bf16_f32 v3, v138, v139
	global_store_dwordx2 v[4:5], v[2:3], off offset:128
	v_cvt_pk_bf16_f32 v2, v132, v133
	v_cvt_pk_bf16_f32 v3, v134, v135
	global_store_dwordx2 v[4:5], v[2:3], off offset:160
	v_cvt_pk_bf16_f32 v2, v128, v129
	v_cvt_pk_bf16_f32 v3, v130, v131
	global_store_dwordx2 v[4:5], v[2:3], off offset:192
	v_cvt_pk_bf16_f32 v2, v124, v125
	v_cvt_pk_bf16_f32 v3, v126, v127
	global_store_dwordx2 v[4:5], v[2:3], off offset:224
	v_cvt_pk_bf16_f32 v2, v120, v121
	v_cvt_pk_bf16_f32 v3, v122, v123
	global_store_dwordx2 v[4:5], v[2:3], off offset:256
	v_cvt_pk_bf16_f32 v2, v92, v93
	v_cvt_pk_bf16_f32 v3, v94, v95
	global_store_dwordx2 v[4:5], v[2:3], off offset:288
	v_cvt_pk_bf16_f32 v2, v64, v65
	v_cvt_pk_bf16_f32 v3, v66, v67
	global_store_dwordx2 v[4:5], v[2:3], off offset:320
	v_cvt_pk_bf16_f32 v2, v48, v49
	v_cvt_pk_bf16_f32 v3, v50, v51
	global_store_dwordx2 v[4:5], v[2:3], off offset:352
	v_cvt_pk_bf16_f32 v2, v40, v41
	v_cvt_pk_bf16_f32 v3, v42, v43
	global_store_dwordx2 v[4:5], v[2:3], off offset:384
	v_cvt_pk_bf16_f32 v2, v36, v37
	v_cvt_pk_bf16_f32 v3, v38, v39
	global_store_dwordx2 v[4:5], v[2:3], off offset:416
	v_cvt_pk_bf16_f32 v2, v52, v53
	v_cvt_pk_bf16_f32 v3, v54, v55
	global_store_dwordx2 v[4:5], v[2:3], off offset:448
	v_cvt_pk_bf16_f32 v2, v44, v45
	v_bfe_u32 v1, v46, 16, 1
	v_add3_u32 v1, v46, v1, s81
	v_bfe_u32 v3, v47, 16, 1
	v_readlane_b32 s10, v250, 58
	v_lshrrev_b32_e32 v1, 16, v1
	v_add3_u32 v3, v47, v3, s81
	v_readlane_b32 s11, v250, 59
	v_and_or_b32 v3, v3, s80, v1
	s_mov_b64 s[6:7], 0
	s_andn2_b64 vcc, exec, s[10:11]
	s_mov_b64 s[14:15], 0
	global_store_dwordx2 v[4:5], v[2:3], off offset:480
	s_barrier
	s_cbranch_vccnz .LBB0_2494
	v_readlane_b32 s9, v252, 21
	s_add_i32 s10, s8, s9
	v_mov_b32_e32 v38, v0
	s_ashr_i32 s11, s10, 31
	s_lshl_b64 s[10:11], s[10:11], 13
	v_and_b32_e32 v39, 15, v38
	v_readlane_b32 s9, v252, 22
	s_add_u32 s26, s2, 0x4f000000
	s_addc_u32 s27, s3, 0
	v_or_b32_e32 v1, s9, v39
	s_movk_i32 s9, 0x900
	v_mad_u64_u32 v[36:37], s[14:15], v1, s9, 0
	v_lshl_add_u64 v[2:3], v[36:37], 1, s[26:27]
	v_and_b32_e32 v34, 48, v38
	s_add_u32 s10, s0, s10
	v_med3_i32 v1, v38, 1, v197
	v_lshl_add_u64 v[2:3], v[2:3], 0, v[34:35]
	s_addc_u32 s11, s1, s11
	v_sub_u32_e32 v34, 0x100, v1
	v_lshl_add_u64 v[4:5], v[34:35], 2, s[10:11]
	v_lshlrev_b32_e32 v34, 2, v1
	v_lshl_add_u64 v[6:7], s[10:11], 0, v[34:35]
	s_mov_b64 s[14:15], 0x1ffc00
	s_movk_i32 s9, 0x101
	v_lshl_add_u64 v[6:7], v[6:7], 0, s[14:15]
	v_cmp_gt_i32_e32 vcc, s9, v38
	v_add_u32_e32 v40, 0x200, v38
	v_med3_i32 v1, v40, 1, v197
	v_cndmask_b32_e32 v5, v7, v5, vcc
	v_cndmask_b32_e32 v4, v6, v4, vcc
	global_load_dword v41, v[4:5], off
	v_sub_u32_e32 v34, 0x100, v1
	v_lshl_add_u64 v[4:5], v[34:35], 2, s[10:11]
	v_lshlrev_b32_e32 v34, 2, v1
	v_lshl_add_u64 v[6:7], s[10:11], 0, v[34:35]
	s_movk_i32 s9, 0xff01
	v_lshl_add_u64 v[6:7], v[6:7], 0, s[14:15]
	v_cmp_gt_i32_e32 vcc, s9, v38
	v_add_u32_e32 v34, -1, v38
	s_movk_i32 s9, 0x1ff
	v_cndmask_b32_e32 v5, v7, v5, vcc
	v_cndmask_b32_e32 v4, v6, v4, vcc
	global_load_dword v42, v[4:5], off
	global_load_dwordx4 v[30:33], v[2:3], off
	global_load_dwordx4 v[26:29], v[2:3], off offset:64
	global_load_dwordx4 v[22:25], v[2:3], off offset:128
	global_load_dwordx4 v[18:21], v[2:3], off offset:192
	global_load_dwordx4 v[14:17], v[2:3], off offset:256
	global_load_dwordx4 v[10:13], v[2:3], off offset:320
	global_load_dwordx4 v[6:9], v[2:3], off offset:384
	s_nop 0
	global_load_dwordx4 v[2:5], v[2:3], off offset:448
	v_cmp_gt_u32_e32 vcc, s9, v34
	v_and_b32_e32 v43, 63, v38
	v_ashrrev_i32_e32 v1, 6, v38
	s_waitcnt vmcnt(9)
	v_cndmask_b32_e32 v34, 0, v41, vcc
	v_cmp_lt_u32_e32 vcc, s30, v38
	s_waitcnt vmcnt(8)
	s_nop 0
	v_cndmask_b32_e32 v41, 0, v42, vcc
	v_add_f32_e64 v42, |v34|, |v41|
	v_cmp_eq_u32_e32 vcc, 0, v43
	s_nop 0
	v_add_f32_dpp v42, v42, v42 quad_perm:[1,0,3,2] row_mask:0xf bank_mask:0xf bound_ctrl:1
	s_nop 1
	v_add_f32_dpp v42, v42, v42 quad_perm:[2,3,0,1] row_mask:0xf bank_mask:0xf bound_ctrl:1
	s_nop 1
	v_add_f32_dpp v42, v42, v42 row_half_mirror row_mask:0xf bank_mask:0xf bound_ctrl:1
	s_nop 1
	v_add_f32_dpp v42, v42, v42 row_mirror row_mask:0xf bank_mask:0xf bound_ctrl:1
	s_nop 0
	v_readlane_b32 s28, v42, 0
	v_readlane_b32 s9, v42, 16
	v_readlane_b32 s29, v42, 32
	v_readlane_b32 s10, v42, 48
	s_and_saveexec_b64 s[14:15], vcc
	s_cbranch_execz .LBB0_2421
	v_mov_b32_e32 v42, s9
	v_mov_b32_e32 v43, s10
	v_pk_add_f32 v[42:43], s[28:29], v[42:43]
	v_lshl_add_u32 v44, v1, 2, 0
	v_add_f32_e32 v42, v42, v43
	ds_write_b32 v44, v42 offset:8704

; #define LAS __attribute__((address_space(3)))
; __device__ __forceinline__ unsigned pk2(float lo, float hi) { return f2bf(lo) | (f2bf(hi) << 16); }
; template <int L>
; __device__ __forceinline__ void hyena_unit(CArgs& a, int l, int c, LAS unsigned char* lds) {
;     ...
;     const float* kf = (const float*)(a.ws + WS_KUN) + ((size_t)((l * 2 + Lt) * 512 + c)) * 2048;
;     const float* kb = kf + (size_t)256 * 2048;
;     LAS float* red = (LAS float*)(lds + 8 * CST);
;     const bf16* Z = (const bf16*)(a.ws + WS_MIX + MX_ZT) + ((size_t)(c * 16 + fr)) * 2304 + SOFF;
;     const bf16* zp = Z + 8 * kg;
;     bf16x8 zc[8];
; #pragma unroll
;     for (int ii = 0; ii < 8; ++ii) zc[ii] = *(const bf16x8*)(zp + 32 * ii);
;     constexpr int NI = (2 * L + 16 + 511) / 512;
;     float gv[NI];
;     float s = 0.f;
; #pragma unroll
;     for (int q = 0; q < NI; ++q) {
;         const int idx = tid + 512 * q, ic = min(max(idx, 1), 2 * L - 1);
;         const float v = *(ic <= L ? kf + (L - ic) : kb + (ic - L));
;         gv[q] = (idx >= 1 && idx < 2 * L) ? v : 0.f;
;         s += fabsf(gv[q]);
;     }
;     s = wave_sum(s);
;     if (lane == 0) red[w] = s;
;     __syncthreads();
;     ...
;     } else {
;         static_assert(L == 256, "hyena_unit");
; #pragma unroll
;         for (int i = 0; i < 8; ++i)
; #pragma unroll
;             for (int j = 0; j < NTW; ++j) acc[j] = __builtin_amdgcn_mfma_f32_16x16x32_bf16(*(const LAS bf16x8*)(ap + (4 * i - 2 * j) * 16), zc[i], acc[j], 0, 0, 0);
;     }
; #pragma unroll
;     for (int j = 0; j < NTW; ++j) *(u32x2*)(YT + 16 * (w * NTW + j) + 4 * kg) = (u32x2){pk2(acc[j][0], acc[j][1]), pk2(acc[j][2], acc[j][3])};
.LBB0_2457:
	s_or_b64 exec, exec, s[14:15]
	v_sub_u32_e32 v39, v34, v39
	v_sub_u32_e32 v40, 0, v38
	v_lshlrev_b32_e32 v39, 1, v39
	v_and_b32_e32 v40, 7, v40
	v_and_b32_e32 v38, 0xffffffc0, v38
	v_and_b32_e32 v39, -16, v39
	v_mul_u32_u24_e32 v40, 0x440, v40
	v_sub_u32_e32 v38, v39, v38
	v_add3_u32 v46, 0, v40, v38
	s_waitcnt lgkmcnt(0)
	s_barrier
	ds_read_b128 v[38:41], v46 offset:480
	ds_read_b128 v[42:45], v46 offset:512
	s_waitcnt vmcnt(7) lgkmcnt(0)
	v_mfma_f32_16x16x32_bf16 v[42:45], v[42:45], v[30:33], 0
	s_add_u32 s14, s2, 0x50400000
	s_addc_u32 s15, s3, 0
	v_readlane_b32 s9, v252, 23
	v_mfma_f32_16x16x32_bf16 v[30:33], v[38:41], v[30:33], 0
	ds_read_b128 v[38:41], v46 offset:576
	s_add_i32 s8, s8, s9
	v_readlane_b32 s10, v252, 24
	s_waitcnt vmcnt(6) lgkmcnt(0)
	v_mfma_f32_16x16x32_bf16 v[38:41], v[38:41], v[26:29], v[42:45]
	s_nop 2
	ds_read_b128 v[42:45], v46 offset:544
	s_ashr_i32 s9, s8, 31
	s_lshl_b64 s[8:9], s[8:9], 13
	s_waitcnt lgkmcnt(0)
	v_mfma_f32_16x16x32_bf16 v[26:29], v[42:45], v[26:29], v[30:33]
	s_nop 2
	ds_read_b128 v[30:33], v46 offset:640
	s_add_u32 s0, s0, s8
	s_addc_u32 s1, s1, s9
	s_waitcnt vmcnt(5) lgkmcnt(0)
	v_mfma_f32_16x16x32_bf16 v[30:33], v[30:33], v[22:25], v[38:41]
	s_nop 2
	ds_read_b128 v[38:41], v46 offset:608
	s_movk_i32 s8, 0x101
	s_waitcnt lgkmcnt(0)
	v_mfma_f32_16x16x32_bf16 v[22:25], v[38:41], v[22:25], v[26:29]
	s_nop 2
	ds_read_b128 v[26:29], v46 offset:704
	s_waitcnt vmcnt(4) lgkmcnt(0)
	v_mfma_f32_16x16x32_bf16 v[26:29], v[26:29], v[18:21], v[30:33]
	s_nop 2
	ds_read_b128 v[30:33], v46 offset:672
	s_waitcnt lgkmcnt(0)
	v_mfma_f32_16x16x32_bf16 v[18:21], v[30:33], v[18:21], v[22:25]
	s_nop 2
	ds_read_b128 v[22:25], v46 offset:768
	s_waitcnt vmcnt(3) lgkmcnt(0)
	v_mfma_f32_16x16x32_bf16 v[22:25], v[22:25], v[14:17], v[26:29]
	s_nop 2
	ds_read_b128 v[26:29], v46 offset:736
	s_waitcnt lgkmcnt(0)
	v_mfma_f32_16x16x32_bf16 v[14:17], v[26:29], v[14:17], v[18:21]
	s_nop 2
	ds_read_b128 v[18:21], v46 offset:832
	s_waitcnt vmcnt(2) lgkmcnt(0)
	v_mfma_f32_16x16x32_bf16 v[18:21], v[18:21], v[10:13], v[22:25]
	s_nop 2
	ds_read_b128 v[22:25], v46 offset:800
	s_waitcnt lgkmcnt(0)
	v_mfma_f32_16x16x32_bf16 v[10:13], v[22:25], v[10:13], v[14:17]
	s_nop 2
	ds_read_b128 v[14:17], v46 offset:896
	s_waitcnt vmcnt(1) lgkmcnt(0)
	v_mfma_f32_16x16x32_bf16 v[14:17], v[14:17], v[6:9], v[18:21]
	s_nop 2
	ds_read_b128 v[18:21], v46 offset:864
	s_waitcnt lgkmcnt(0)
	v_mfma_f32_16x16x32_bf16 v[6:9], v[18:21], v[6:9], v[10:13]
	s_nop 2
	ds_read_b128 v[10:13], v46 offset:960
	s_waitcnt vmcnt(0) lgkmcnt(0)
	v_mfma_f32_16x16x32_bf16 v[10:13], v[10:13], v[2:5], v[14:17]
	s_nop 2
	ds_read_b128 v[14:17], v46 offset:928
	s_waitcnt lgkmcnt(0)
	v_mfma_f32_16x16x32_bf16 v[2:5], v[14:17], v[2:5], v[6:9]
	s_nop 2
	v_lshlrev_b32_e32 v8, 5, v1
	v_cvt_pk_bf16_f32 v10, v10, v11
	v_cvt_pk_bf16_f32 v11, v12, v13
	s_nop 1
	v_cvt_pk_bf16_f32 v2, v2, v3
	v_lshl_add_u64 v[6:7], v[36:37], 1, s[14:15]
	v_lshl_add_u64 v[6:7], v[6:7], 0, v[34:35]
	v_ashrrev_i32_e32 v9, 31, v8
	v_lshl_add_u64 v[6:7], v[8:9], 1, v[6:7]
	v_cvt_pk_bf16_f32 v3, v4, v5
	v_mov_b32_e32 v1, v0
	global_store_dwordx2 v[6:7], v[10:11], off
	global_store_dwordx2 v[6:7], v[2:3], off offset:32
	s_barrier
	s_nop 0
	v_and_b32_e32 v38, 15, v1
	v_or_b32_e32 v2, s10, v38
	s_movk_i32 s10, 0x900
	v_mad_u64_u32 v[36:37], s[10:11], v2, s10, 0
	v_lshl_add_u64 v[2:3], v[36:37], 1, s[26:27]
	v_and_b32_e32 v34, 48, v1
	v_med3_i32 v39, v1, 1, v197
	v_lshl_add_u64 v[2:3], v[2:3], 0, v[34:35]
	v_sub_u32_e32 v34, 0x100, v39
	v_lshl_add_u64 v[40:41], v[34:35], 2, s[0:1]
	v_lshlrev_b32_e32 v34, 2, v39
	v_lshl_add_u64 v[42:43], s[0:1], 0, v[34:35]
	s_mov_b64 s[10:11], 0x1ffc00
	v_cmp_gt_i32_e32 vcc, s8, v1
	v_lshl_add_u64 v[42:43], v[42:43], 0, s[10:11]
	global_load_dwordx4 v[30:33], v[2:3], off
	global_load_dwordx4 v[26:29], v[2:3], off offset:64
	global_load_dwordx4 v[22:25], v[2:3], off offset:128
	global_load_dwordx4 v[18:21], v[2:3], off offset:192
	global_load_dwordx4 v[14:17], v[2:3], off offset:256
	global_load_dwordx4 v[10:13], v[2:3], off offset:320
	global_load_dwordx4 v[6:9], v[2:3], off offset:384
	s_nop 0
	global_load_dwordx4 v[2:5], v[2:3], off offset:448
	v_cndmask_b32_e32 v41, v43, v41, vcc
	v_cndmask_b32_e32 v40, v42, v40, vcc
	global_load_dword v34, v[40:41], off
	v_add_u32_e32 v39, -1, v1
	s_movk_i32 s8, 0x1ff
	v_add_u32_e32 v40, 0x200, v1
	v_cmp_gt_u32_e32 vcc, s8, v39
	v_med3_i32 v39, v40, 1, v197
	s_movk_i32 s8, 0xff01
	v_and_b32_e32 v48, 63, v1
	s_waitcnt vmcnt(0)
	v_cndmask_b32_e32 v42, 0, v34, vcc
	v_sub_u32_e32 v34, 0x100, v39
	v_lshl_add_u64 v[44:45], v[34:35], 2, s[0:1]
	v_lshlrev_b32_e32 v34, 2, v39
	v_lshl_add_u64 v[46:47], s[0:1], 0, v[34:35]
	v_cmp_gt_i32_e32 vcc, s8, v1
	v_lshl_add_u64 v[46:47], v[46:47], 0, s[10:11]
	v_ashrrev_i32_e32 v39, 6, v1
	v_cndmask_b32_e32 v45, v47, v45, vcc
	v_cndmask_b32_e32 v44, v46, v44, vcc
	global_load_dword v34, v[44:45], off
	v_cmp_lt_u32_e32 vcc, s30, v1
	s_waitcnt vmcnt(0)
	s_nop 0
	v_cndmask_b32_e32 v41, 0, v34, vcc
	v_add_f32_e64 v34, |v42|, |v41|
	v_cmp_eq_u32_e32 vcc, 0, v48
	s_nop 0
	v_add_f32_dpp v34, v34, v34 quad_perm:[1,0,3,2] row_mask:0xf bank_mask:0xf bound_ctrl:1
	s_nop 1
	v_add_f32_dpp v34, v34, v34 quad_perm:[2,3,0,1] row_mask:0xf bank_mask:0xf bound_ctrl:1
	s_nop 1
	v_add_f32_dpp v34, v34, v34 row_half_mirror row_mask:0xf bank_mask:0xf bound_ctrl:1
	s_nop 1
	v_add_f32_dpp v34, v34, v34 row_mirror row_mask:0xf bank_mask:0xf bound_ctrl:1
	s_nop 0
	v_readlane_b32 s26, v34, 0
	v_readlane_b32 s0, v34, 16
	v_readlane_b32 s27, v34, 32
	v_readlane_b32 s1, v34, 48
	s_and_saveexec_b64 s[28:29], vcc
	s_cbranch_execz .LBB0_2459
	v_mov_b32_e32 v44, s0
	v_mov_b32_e32 v45, s1
	v_pk_add_f32 v[44:45], s[26:27], v[44:45]
	v_lshl_add_u32 v34, v39, 2, 0
	v_add_f32_e32 v43, v44, v45
	ds_write_b32 v34, v43 offset:8704

; #define LAS __attribute__((address_space(3)))
; __device__ __forceinline__ unsigned pk2(float lo, float hi) { return f2bf(lo) | (f2bf(hi) << 16); }
; template <int L>
; __device__ __forceinline__ void hyena_unit(CArgs& a, int l, int c, LAS unsigned char* lds) {
;     ...
;     } else {
;         static_assert(L == 256, "hyena_unit");
; #pragma unroll
;         for (int i = 0; i < 8; ++i)
; #pragma unroll
;             for (int j = 0; j < NTW; ++j) acc[j] = __builtin_amdgcn_mfma_f32_16x16x32_bf16(*(const LAS bf16x8*)(ap + (4 * i - 2 * j) * 16), zc[i], acc[j], 0, 0, 0);
;     }
; #pragma unroll
;     for (int j = 0; j < NTW; ++j) *(u32x2*)(YT + 16 * (w * NTW + j) + 4 * kg) = (u32x2){pk2(acc[j][0], acc[j][1]), pk2(acc[j][2], acc[j][3])};
.LBB0_2493:
	s_or_b64 exec, exec, s[26:27]
	v_sub_u32_e32 v38, v34, v38
	v_sub_u32_e32 v40, 0, v1
	v_lshlrev_b32_e32 v38, 1, v38
	v_and_b32_e32 v40, 7, v40
	v_and_b32_e32 v1, 0xffffffc0, v1
	v_and_b32_e32 v38, -16, v38
	v_mul_u32_u24_e32 v40, 0x440, v40
	v_sub_u32_e32 v1, v38, v1
	v_add3_u32 v1, 0, v40, v1
	s_waitcnt lgkmcnt(0)
	s_barrier
	ds_read_b128 v[40:43], v1 offset:480
	ds_read_b128 v[44:47], v1 offset:512
	s_waitcnt lgkmcnt(0)
	v_mfma_f32_16x16x32_bf16 v[44:47], v[44:47], v[30:33], 0
	v_mfma_f32_16x16x32_bf16 v[30:33], v[40:43], v[30:33], 0
	ds_read_b128 v[40:43], v1 offset:576
	s_waitcnt lgkmcnt(0)
	v_mfma_f32_16x16x32_bf16 v[40:43], v[40:43], v[26:29], v[44:47]
	s_nop 3
	ds_read_b128 v[44:47], v1 offset:544
	s_waitcnt lgkmcnt(0)
	v_mfma_f32_16x16x32_bf16 v[26:29], v[44:47], v[26:29], v[30:33]
	s_nop 2
	ds_read_b128 v[30:33], v1 offset:640
	s_waitcnt lgkmcnt(0)
	v_mfma_f32_16x16x32_bf16 v[30:33], v[30:33], v[22:25], v[40:43]
	s_nop 2
	ds_read_b128 v[40:43], v1 offset:608
	s_waitcnt lgkmcnt(0)
	v_mfma_f32_16x16x32_bf16 v[22:25], v[40:43], v[22:25], v[26:29]
	s_nop 2
	ds_read_b128 v[26:29], v1 offset:704
	s_waitcnt lgkmcnt(0)
	v_mfma_f32_16x16x32_bf16 v[26:29], v[26:29], v[18:21], v[30:33]
	s_nop 2
	ds_read_b128 v[30:33], v1 offset:672
	s_waitcnt lgkmcnt(0)
	v_mfma_f32_16x16x32_bf16 v[18:21], v[30:33], v[18:21], v[22:25]
	s_nop 2
	ds_read_b128 v[22:25], v1 offset:768
	s_waitcnt lgkmcnt(0)
	v_mfma_f32_16x16x32_bf16 v[22:25], v[22:25], v[14:17], v[26:29]
	s_nop 2
	ds_read_b128 v[26:29], v1 offset:736
	s_waitcnt lgkmcnt(0)
	v_mfma_f32_16x16x32_bf16 v[14:17], v[26:29], v[14:17], v[18:21]
	s_nop 2
	ds_read_b128 v[18:21], v1 offset:832
	s_waitcnt lgkmcnt(0)
	v_mfma_f32_16x16x32_bf16 v[18:21], v[18:21], v[10:13], v[22:25]
	s_nop 2
	ds_read_b128 v[22:25], v1 offset:800
	s_waitcnt lgkmcnt(0)
	v_mfma_f32_16x16x32_bf16 v[10:13], v[22:25], v[10:13], v[14:17]
	s_nop 2
	ds_read_b128 v[14:17], v1 offset:896
	s_waitcnt lgkmcnt(0)
	v_mfma_f32_16x16x32_bf16 v[14:17], v[14:17], v[6:9], v[18:21]
	s_nop 2
	ds_read_b128 v[18:21], v1 offset:864
	s_waitcnt lgkmcnt(0)
	v_mfma_f32_16x16x32_bf16 v[6:9], v[18:21], v[6:9], v[10:13]
	s_nop 2
	ds_read_b128 v[10:13], v1 offset:960
	s_waitcnt lgkmcnt(0)
	v_mfma_f32_16x16x32_bf16 v[10:13], v[10:13], v[2:5], v[14:17]
	s_nop 2
	ds_read_b128 v[14:17], v1 offset:928
	s_nop 3
	s_waitcnt lgkmcnt(0)
	v_mfma_f32_16x16x32_bf16 v[2:5], v[14:17], v[2:5], v[6:9]
	s_nop 1
	v_cvt_pk_bf16_f32 v10, v10, v11
	v_cvt_pk_bf16_f32 v11, v12, v13
	s_nop 3
	v_cvt_pk_bf16_f32 v2, v2, v3
	v_bfe_u32 v1, v4, 16, 1
	v_lshl_add_u64 v[6:7], v[36:37], 1, s[14:15]
	v_lshlrev_b32_e32 v8, 5, v39
	v_add3_u32 v1, v4, v1, s81
	v_bfe_u32 v3, v5, 16, 1
	v_lshl_add_u64 v[6:7], v[6:7], 0, v[34:35]
	v_ashrrev_i32_e32 v9, 31, v8
	v_lshrrev_b32_e32 v1, 16, v1
	v_add3_u32 v3, v5, v3, s81
	v_lshl_add_u64 v[6:7], v[8:9], 1, v[6:7]
	v_and_or_b32 v3, v3, s80, v1
	global_store_dwordx2 v[6:7], v[10:11], off
	global_store_dwordx2 v[6:7], v[2:3], off offset:32
	s_barrier
	s_mov_b64 s[14:15], -1

; #define LAS __attribute__((address_space(3)))
; template <int L>
; __device__ __forceinline__ void hyena_unit(CArgs& a, int l, int c, LAS unsigned char* lds) {
;     ...
;         bf16x8 zn[8], A[16];
; #pragma unroll
;         for (int j = 2; j < 16; ++j) A[j] = *(const LAS bf16x8*)(ap - 32 * j);
; #pragma unroll 1
;         for (int ib = 0; ib < 8; ++ib) {
;             const bf16* zq = zp + 256 * (ib < 7 ? ib + 1 : 7);
; #pragma unroll
;             for (int ii = 0; ii < 8; ++ii) zn[ii] = *(const bf16x8*)(zq + 32 * ii);
; #pragma unroll
;             for (int ii = 0; ii < 8; ++ii) {
;                 A[(16 - 2 * ii) & 15] = *(const LAS bf16x8*)(ap + 64 * ii);
;                 A[(17 - 2 * ii) & 15] = *(const LAS bf16x8*)(ap + 64 * ii - 32);
; #pragma unroll
;                 for (int jj = 0; jj < 16; ++jj) { const int j = (jj + 2) & 15; acc[j] = __builtin_amdgcn_mfma_f32_16x16x32_bf16(A[(j + 16 - 2 * ii) & 15], zc[ii], acc[j], 0, 0, 0); }
;             }
;             ap += 512;
; #pragma unroll
;             for (int ii = 0; ii < 8; ++ii) zc[ii] = zn[ii];
;         }
.LBB0_2649:
	s_waitcnt vmcnt(1) lgkmcnt(1)
	s_nop 0
	v_mfma_f32_16x16x32_bf16 v[44:47], v[56:59], v[30:33], v[44:47]
	s_cmpk_lg_i32 s0, 0x800
	s_cselect_b32 s78, s0, 0x700
	s_addk_i32 s0, 0x100
	v_mfma_f32_16x16x32_bf16 v[36:39], v[80:83], v[30:33], v[36:39]
	s_cmpk_lg_i32 s0, 0x900
	v_mfma_f32_16x16x32_bf16 v[44:47], v[80:83], v[26:29], v[44:47]
	v_mfma_f32_16x16x32_bf16 v[136:139], v[88:91], v[30:33], v[136:139]
	v_mfma_f32_16x16x32_bf16 v[132:135], v[84:87], v[30:33], v[132:135]
	v_mfma_f32_16x16x32_bf16 v[128:131], v[104:107], v[30:33], v[128:131]
	v_mfma_f32_16x16x32_bf16 v[124:127], v[96:99], v[30:33], v[124:127]
	v_mfma_f32_16x16x32_bf16 v[48:51], v[112:115], v[30:33], v[48:51]
	v_mfma_f32_16x16x32_bf16 v[36:39], v[112:115], v[26:29], v[36:39]
	v_mfma_f32_16x16x32_bf16 v[44:47], v[112:115], v[22:25], v[44:47]
	v_subrev_u32_e32 v112, 32, v161
	s_waitcnt lgkmcnt(0)
	v_mfma_f32_16x16x32_bf16 v[52:55], v[60:63], v[30:33], v[52:55]
	v_mfma_f32_16x16x32_bf16 v[56:59], v[72:75], v[26:29], v[136:139]
	v_mfma_f32_16x16x32_bf16 v[60:63], v[68:71], v[26:29], v[132:135]
	s_nop 1
	ds_read_b128 v[136:139], v112
	ds_read_b128 v[132:135], v161
	v_mfma_f32_16x16x32_bf16 v[128:131], v[88:91], v[26:29], v[128:131]
	v_mfma_f32_16x16x32_bf16 v[124:127], v[84:87], v[26:29], v[124:127]
	v_mfma_f32_16x16x32_bf16 v[140:143], v[68:71], v[30:33], v[140:143]
	v_mfma_f32_16x16x32_bf16 v[40:43], v[76:79], v[30:33], v[40:43]
	v_mfma_f32_16x16x32_bf16 v[52:55], v[76:79], v[26:29], v[52:55]
	v_mfma_f32_16x16x32_bf16 v[76:79], v[72:75], v[22:25], v[128:131]
	v_mfma_f32_16x16x32_bf16 v[80:83], v[68:71], v[22:25], v[124:127]
	v_mfma_f32_16x16x32_bf16 v[144:147], v[72:75], v[30:33], v[144:147]
	s_waitcnt lgkmcnt(0)
	v_mfma_f32_16x16x32_bf16 v[124:127], v[132:135], v[22:25], v[56:59]
	v_mfma_f32_16x16x32_bf16 v[128:131], v[136:139], v[26:29], v[140:143]
	v_mfma_f32_16x16x32_bf16 v[140:143], v[136:139], v[22:25], v[60:63]
	s_nop 2
	ds_read_b128 v[60:63], v161 offset:64
	ds_read_b128 v[56:59], v161 offset:32
	v_mfma_f32_16x16x32_bf16 v[120:123], v[100:103], v[30:33], v[120:123]
	v_mfma_f32_16x16x32_bf16 v[92:95], v[108:111], v[30:33], v[92:95]
	v_mfma_f32_16x16x32_bf16 v[64:67], v[116:119], v[30:33], v[64:67]
	v_mfma_f32_16x16x32_bf16 v[40:43], v[116:119], v[26:29], v[40:43]
	v_mfma_f32_16x16x32_bf16 v[52:55], v[116:119], v[22:25], v[52:55]
	v_mfma_f32_16x16x32_bf16 v[112:115], v[132:135], v[30:33], v[148:151]
	v_mfma_f32_16x16x32_bf16 v[30:33], v[136:139], v[30:33], v[152:155]
	v_mfma_f32_16x16x32_bf16 v[76:79], v[132:135], v[18:21], v[76:79]
	v_mfma_f32_16x16x32_bf16 v[80:83], v[136:139], v[18:21], v[80:83]
	v_mfma_f32_16x16x32_bf16 v[116:119], v[132:135], v[26:29], v[144:147]
	v_mfma_f32_16x16x32_bf16 v[120:123], v[104:107], v[26:29], v[120:123]
	v_mfma_f32_16x16x32_bf16 v[92:95], v[96:99], v[26:29], v[92:95]
	v_mfma_f32_16x16x32_bf16 v[64:67], v[100:103], v[26:29], v[64:67]
	v_mfma_f32_16x16x32_bf16 v[48:51], v[108:111], v[26:29], v[48:51]
	v_mfma_f32_16x16x32_bf16 v[40:43], v[100:103], v[22:25], v[40:43]
	v_mfma_f32_16x16x32_bf16 v[52:55], v[100:103], v[18:21], v[52:55]
	s_waitcnt lgkmcnt(1)
	v_mfma_f32_16x16x32_bf16 v[100:103], v[60:63], v[26:29], v[112:115]
	v_mfma_f32_16x16x32_bf16 v[112:115], v[60:63], v[18:21], v[124:127]
	s_waitcnt lgkmcnt(0)
	v_mfma_f32_16x16x32_bf16 v[26:29], v[56:59], v[26:29], v[30:33]
	v_mfma_f32_16x16x32_bf16 v[30:33], v[56:59], v[22:25], v[128:131]
	v_mfma_f32_16x16x32_bf16 v[124:127], v[60:63], v[14:17], v[76:79]
	v_mfma_f32_16x16x32_bf16 v[128:131], v[56:59], v[14:17], v[80:83]
	s_nop 1
	ds_read_b128 v[76:79], v161 offset:128
	ds_read_b128 v[80:83], v161 offset:96
	v_mfma_f32_16x16x32_bf16 v[36:39], v[108:111], v[22:25], v[36:39]
	v_mfma_f32_16x16x32_bf16 v[44:47], v[108:111], v[18:21], v[44:47]
	v_mfma_f32_16x16x32_bf16 v[108:111], v[60:63], v[22:25], v[116:119]
	v_mfma_f32_16x16x32_bf16 v[116:119], v[56:59], v[18:21], v[140:143]
	v_mfma_f32_16x16x32_bf16 v[120:123], v[88:91], v[22:25], v[120:123]
	v_mfma_f32_16x16x32_bf16 v[92:95], v[84:87], v[22:25], v[92:95]
	v_mfma_f32_16x16x32_bf16 v[64:67], v[104:107], v[22:25], v[64:67]
	v_mfma_f32_16x16x32_bf16 v[48:51], v[96:99], v[22:25], v[48:51]
	v_mfma_f32_16x16x32_bf16 v[40:43], v[104:107], v[18:21], v[40:43]
	v_mfma_f32_16x16x32_bf16 v[36:39], v[96:99], v[18:21], v[36:39]
	v_mfma_f32_16x16x32_bf16 v[52:55], v[104:107], v[14:17], v[52:55]
	v_mfma_f32_16x16x32_bf16 v[44:47], v[96:99], v[14:17], v[44:47]
	s_waitcnt lgkmcnt(1)
	v_mfma_f32_16x16x32_bf16 v[96:99], v[76:79], v[22:25], v[100:103]
	v_mfma_f32_16x16x32_bf16 v[104:107], v[76:79], v[14:17], v[112:115]
	s_waitcnt lgkmcnt(0)
	v_mfma_f32_16x16x32_bf16 v[22:25], v[80:83], v[22:25], v[26:29]
	v_mfma_f32_16x16x32_bf16 v[26:29], v[80:83], v[18:21], v[30:33]
	v_mfma_f32_16x16x32_bf16 v[30:33], v[80:83], v[14:17], v[116:119]
	s_nop 2
	ds_read_b128 v[116:119], v161 offset:192
	ds_read_b128 v[112:115], v161 offset:160
	v_mfma_f32_16x16x32_bf16 v[100:103], v[76:79], v[18:21], v[108:111]
	v_mfma_f32_16x16x32_bf16 v[108:111], v[76:79], v[10:13], v[124:127]
	v_mfma_f32_16x16x32_bf16 v[124:127], v[80:83], v[10:13], v[128:131]
	v_mfma_f32_16x16x32_bf16 v[120:123], v[72:75], v[18:21], v[120:123]
	v_mfma_f32_16x16x32_bf16 v[92:95], v[68:71], v[18:21], v[92:95]
	v_mfma_f32_16x16x32_bf16 v[64:67], v[88:91], v[18:21], v[64:67]
	v_mfma_f32_16x16x32_bf16 v[48:51], v[84:87], v[18:21], v[48:51]
	v_mfma_f32_16x16x32_bf16 v[40:43], v[88:91], v[14:17], v[40:43]
	v_mfma_f32_16x16x32_bf16 v[36:39], v[84:87], v[14:17], v[36:39]
	v_mfma_f32_16x16x32_bf16 v[52:55], v[88:91], v[10:13], v[52:55]
	v_mfma_f32_16x16x32_bf16 v[44:47], v[84:87], v[10:13], v[44:47]
	s_waitcnt lgkmcnt(1)
; #define LAS __attribute__((address_space(3)))
; template <int L>
; __device__ __forceinline__ void hyena_unit(CArgs& a, int l, int c, LAS unsigned char* lds) {
;     ...
;         bf16x8 zn[8], A[16];
; #pragma unroll
;         for (int j = 2; j < 16; ++j) A[j] = *(const LAS bf16x8*)(ap - 32 * j);
; #pragma unroll 1
;         for (int ib = 0; ib < 8; ++ib) {
;             const bf16* zq = zp + 256 * (ib < 7 ? ib + 1 : 7);
; #pragma unroll
;             for (int ii = 0; ii < 8; ++ii) zn[ii] = *(const bf16x8*)(zq + 32 * ii);
; #pragma unroll
;             for (int ii = 0; ii < 8; ++ii) {
;                 A[(16 - 2 * ii) & 15] = *(const LAS bf16x8*)(ap + 64 * ii);
;                 A[(17 - 2 * ii) & 15] = *(const LAS bf16x8*)(ap + 64 * ii - 32);
; #pragma unroll
;                 for (int jj = 0; jj < 16; ++jj) { const int j = (jj + 2) & 15; acc[j] = __builtin_amdgcn_mfma_f32_16x16x32_bf16(A[(j + 16 - 2 * ii) & 15], zc[ii], acc[j], 0, 0, 0); }
;             }
;             ap += 512;
; #pragma unroll
;             for (int ii = 0; ii < 8; ++ii) zc[ii] = zn[ii];
;         }
	v_mfma_f32_16x16x32_bf16 v[84:87], v[116:119], v[18:21], v[96:99]
	v_mfma_f32_16x16x32_bf16 v[88:91], v[116:119], v[14:17], v[100:103]
	s_waitcnt lgkmcnt(0)
	v_mfma_f32_16x16x32_bf16 v[18:21], v[112:115], v[18:21], v[22:25]
	v_mfma_f32_16x16x32_bf16 v[22:25], v[112:115], v[14:17], v[26:29]
	v_mfma_f32_16x16x32_bf16 v[26:29], v[112:115], v[10:13], v[30:33]
	v_mfma_f32_16x16x32_bf16 v[30:33], v[116:119], v[6:9], v[108:111]
	ds_read_b128 v[100:103], v161 offset:256
	s_nop 1
	ds_read_b128 v[108:111], v161 offset:224
	v_mfma_f32_16x16x32_bf16 v[96:99], v[116:119], v[10:13], v[104:107]
	v_mfma_f32_16x16x32_bf16 v[104:107], v[112:115], v[6:9], v[124:127]
	v_mfma_f32_16x16x32_bf16 v[48:51], v[68:71], v[14:17], v[48:51]
	v_mfma_f32_16x16x32_bf16 v[36:39], v[68:71], v[10:13], v[36:39]
	v_mfma_f32_16x16x32_bf16 v[44:47], v[68:71], v[6:9], v[44:47]
	s_waitcnt lgkmcnt(1)
	v_mfma_f32_16x16x32_bf16 v[68:71], v[100:103], v[14:17], v[84:87]
	v_mfma_f32_16x16x32_bf16 v[84:87], v[100:103], v[6:9], v[96:99]
	s_waitcnt vmcnt(0) lgkmcnt(0)
	v_mfma_f32_16x16x32_bf16 v[124:127], v[108:111], v[2:5], v[104:107]
	s_nop 2
	ds_read_b128 v[104:107], v161 offset:320
	ds_read_b128 v[96:99], v161 offset:288
	v_mfma_f32_16x16x32_bf16 v[120:123], v[132:135], v[14:17], v[120:123]
	v_mfma_f32_16x16x32_bf16 v[92:95], v[136:139], v[14:17], v[92:95]
	v_mfma_f32_16x16x32_bf16 v[64:67], v[72:75], v[14:17], v[64:67]
	v_mfma_f32_16x16x32_bf16 v[14:17], v[108:111], v[14:17], v[18:21]
	v_mfma_f32_16x16x32_bf16 v[18:21], v[108:111], v[10:13], v[22:25]
	v_mfma_f32_16x16x32_bf16 v[22:25], v[108:111], v[6:9], v[26:29]
	s_waitcnt lgkmcnt(1)
	v_mfma_f32_16x16x32_bf16 v[26:29], v[104:107], v[10:13], v[68:71]
	s_nop 2
	v_lshl_add_u64 v[68:69], s[78:79], 1, v[158:159]
	v_mfma_f32_16x16x32_bf16 v[120:123], v[60:63], v[10:13], v[120:123]
	v_mfma_f32_16x16x32_bf16 v[92:95], v[56:59], v[10:13], v[92:95]
	v_mfma_f32_16x16x32_bf16 v[64:67], v[132:135], v[10:13], v[64:67]
	v_mfma_f32_16x16x32_bf16 v[48:51], v[136:139], v[10:13], v[48:51]
	v_mfma_f32_16x16x32_bf16 v[40:43], v[72:75], v[10:13], v[40:43]
	v_mfma_f32_16x16x32_bf16 v[52:55], v[72:75], v[6:9], v[52:55]
	v_mfma_f32_16x16x32_bf16 v[72:75], v[100:103], v[10:13], v[88:91]
	s_waitcnt lgkmcnt(0)
	v_mfma_f32_16x16x32_bf16 v[10:13], v[96:99], v[10:13], v[14:17]
	s_nop 2
	global_load_dwordx4 v[14:17], v[68:69], off
	v_mfma_f32_16x16x32_bf16 v[36:39], v[136:139], v[6:9], v[36:39]
	global_load_dwordx4 v[170:173], v[68:69], off offset:64
	global_load_dwordx4 v[174:177], v[68:69], off offset:128
	global_load_dwordx4 v[178:181], v[68:69], off offset:192
	v_mfma_f32_16x16x32_bf16 v[44:47], v[136:139], v[2:5], v[44:47]
	v_mfma_f32_16x16x32_bf16 v[136:139], v[104:107], v[2:5], v[84:87]
	ds_read_b128 v[88:91], v161 offset:384
	s_nop 1
	ds_read_b128 v[84:87], v161 offset:352
	global_load_dwordx4 v[182:185], v[68:69], off offset:256
	global_load_dwordx4 v[186:189], v[68:69], off offset:320
	global_load_dwordx4 v[202:205], v[68:69], off offset:384
	global_load_dwordx4 v[206:209], v[68:69], off offset:448
	v_mfma_f32_16x16x32_bf16 v[128:131], v[100:103], v[2:5], v[30:33]
	ds_read_b128 v[68:71], v161 offset:416
	v_mfma_f32_16x16x32_bf16 v[30:33], v[104:107], v[6:9], v[72:75]
	s_nop 2
	ds_read_b128 v[72:75], v161 offset:448
	v_mfma_f32_16x16x32_bf16 v[120:123], v[76:79], v[6:9], v[120:123]
	v_add_u32_e32 v161, 0x200, v161
	v_mfma_f32_16x16x32_bf16 v[92:95], v[80:83], v[6:9], v[92:95]
	v_mfma_f32_16x16x32_bf16 v[64:67], v[60:63], v[6:9], v[64:67]
	v_mfma_f32_16x16x32_bf16 v[48:51], v[56:59], v[6:9], v[48:51]
	v_mfma_f32_16x16x32_bf16 v[40:43], v[132:135], v[6:9], v[40:43]
	v_mfma_f32_16x16x32_bf16 v[52:55], v[132:135], v[2:5], v[52:55]
	v_mfma_f32_16x16x32_bf16 v[18:21], v[96:99], v[6:9], v[18:21]
	v_mfma_f32_16x16x32_bf16 v[132:135], v[96:99], v[2:5], v[22:25]
	s_waitcnt lgkmcnt(3)
	v_mfma_f32_16x16x32_bf16 v[22:25], v[88:91], v[6:9], v[26:29]
	s_waitcnt lgkmcnt(2)
	v_mfma_f32_16x16x32_bf16 v[6:9], v[84:87], v[6:9], v[10:13]
	s_waitcnt vmcnt(6)
	v_mov_b64_e32 v[26:27], v[170:171]
	v_mfma_f32_16x16x32_bf16 v[120:123], v[116:119], v[2:5], v[120:123]
	v_mov_b64_e32 v[28:29], v[172:173]
	s_waitcnt vmcnt(2)
	v_mov_b64_e32 v[10:11], v[186:187]
	v_mfma_f32_16x16x32_bf16 v[92:95], v[112:115], v[2:5], v[92:95]
	v_mov_b64_e32 v[12:13], v[188:189]
	v_mfma_f32_16x16x32_bf16 v[64:67], v[76:79], v[2:5], v[64:67]
	v_mfma_f32_16x16x32_bf16 v[48:51], v[80:83], v[2:5], v[48:51]
	v_mfma_f32_16x16x32_bf16 v[40:43], v[60:63], v[2:5], v[40:43]
	v_mfma_f32_16x16x32_bf16 v[36:39], v[56:59], v[2:5], v[36:39]
	v_mfma_f32_16x16x32_bf16 v[144:147], v[88:91], v[2:5], v[30:33]
	v_mfma_f32_16x16x32_bf16 v[140:143], v[84:87], v[2:5], v[18:21]
	s_nop 1
	v_mov_b64_e32 v[32:33], v[16:17]
	v_mov_b64_e32 v[30:31], v[14:15]
	v_mov_b64_e32 v[14:15], v[182:183]
	s_waitcnt lgkmcnt(0)
	v_mfma_f32_16x16x32_bf16 v[148:151], v[72:75], v[2:5], v[22:25]
	v_mov_b64_e32 v[18:19], v[178:179]
	v_mov_b64_e32 v[20:21], v[180:181]
	v_mov_b64_e32 v[16:17], v[184:185]
	v_mfma_f32_16x16x32_bf16 v[152:155], v[68:71], v[2:5], v[6:9]
	v_mov_b64_e32 v[22:23], v[174:175]
	s_waitcnt vmcnt(0)
	v_mov_b64_e32 v[2:3], v[206:207]
	v_mov_b64_e32 v[24:25], v[176:177]
	v_mov_b64_e32 v[6:7], v[202:203]
	v_mov_b64_e32 v[8:9], v[204:205]
	v_mov_b64_e32 v[4:5], v[208:209]
	s_cbranch_scc1 .LBB0_2649
; __device__ __forceinline__ unsigned pk2(float lo, float hi) { return f2bf(lo) | (f2bf(hi) << 16); }
; template <int L>
; __device__ __forceinline__ void hyena_unit(CArgs& a, int l, int c, LAS unsigned char* lds) {
;     ...
; #pragma unroll
;     for (int j = 0; j < NTW; ++j) *(u32x2*)(YT + 16 * (w * NTW + j) + 4 * kg) = (u32x2){pk2(acc[j][0], acc[j][1]), pk2(acc[j][2], acc[j][3])};
	v_lshlrev_b32_e32 v2, 8, v1
	v_cvt_pk_bf16_f32 v6, v148, v149
	v_lshl_add_u64 v[4:5], v[156:157], 0, v[34:35]
	v_cvt_pk_bf16_f32 v7, v150, v151
	v_ashrrev_i32_e32 v3, 31, v2
	v_lshl_add_u64 v[2:3], v[2:3], 1, v[4:5]
	s_mov_b64 s[0:1], 0x50400200
	v_lshl_add_u64 v[4:5], v[2:3], 0, s[0:1]
	s_mov_b32 s0, 0x50400000
	v_add_co_u32_e32 v2, vcc, s0, v2
	s_nop 0
	s_nop 0
	v_addc_co_u32_e32 v3, vcc, 0, v3, vcc
	global_store_dwordx2 v[2:3], v[6:7], off offset:512
	v_cvt_pk_bf16_f32 v2, v152, v153
	v_cvt_pk_bf16_f32 v3, v154, v155
	global_store_dwordx2 v[4:5], v[2:3], off offset:32
	v_cvt_pk_bf16_f32 v2, v144, v145
	v_cvt_pk_bf16_f32 v3, v146, v147
	global_store_dwordx2 v[4:5], v[2:3], off offset:64
	v_cvt_pk_bf16_f32 v2, v140, v141
	v_cvt_pk_bf16_f32 v3, v142, v143
	global_store_dwordx2 v[4:5], v[2:3], off offset:96
	v_cvt_pk_bf16_f32 v2, v136, v137
	v_cvt_pk_bf16_f32 v3, v138, v139
	global_store_dwordx2 v[4:5], v[2:3], off offset:128
	v_cvt_pk_bf16_f32 v2, v132, v133
	v_cvt_pk_bf16_f32 v3, v134, v135
	global_store_dwordx2 v[4:5], v[2:3], off offset:160
	v_cvt_pk_bf16_f32 v2, v128, v129
	v_cvt_pk_bf16_f32 v3, v130, v131
	global_store_dwordx2 v[4:5], v[2:3], off offset:192
	v_cvt_pk_bf16_f32 v2, v124, v125
	v_cvt_pk_bf16_f32 v3, v126, v127
	global_store_dwordx2 v[4:5], v[2:3], off offset:224
	v_cvt_pk_bf16_f32 v2, v120, v121
	v_cvt_pk_bf16_f32 v3, v122, v123
	global_store_dwordx2 v[4:5], v[2:3], off offset:256
	v_cvt_pk_bf16_f32 v2, v92, v93
	v_cvt_pk_bf16_f32 v3, v94, v95
	global_store_dwordx2 v[4:5], v[2:3], off offset:288
	v_cvt_pk_bf16_f32 v2, v64, v65
	v_cvt_pk_bf16_f32 v3, v66, v67
	global_store_dwordx2 v[4:5], v[2:3], off offset:320
	v_cvt_pk_bf16_f32 v2, v48, v49
	v_cvt_pk_bf16_f32 v3, v50, v51
	global_store_dwordx2 v[4:5], v[2:3], off offset:352
	v_cvt_pk_bf16_f32 v2, v40, v41
	v_cvt_pk_bf16_f32 v3, v42, v43
	global_store_dwordx2 v[4:5], v[2:3], off offset:384
	v_cvt_pk_bf16_f32 v2, v36, v37
	v_cvt_pk_bf16_f32 v3, v38, v39
	global_store_dwordx2 v[4:5], v[2:3], off offset:416
	v_cvt_pk_bf16_f32 v2, v52, v53
	v_cvt_pk_bf16_f32 v3, v54, v55
	global_store_dwordx2 v[4:5], v[2:3], off offset:448
	v_cvt_pk_bf16_f32 v2, v44, v45
	v_bfe_u32 v1, v46, 16, 1
	v_add3_u32 v1, v46, v1, s81
	v_bfe_u32 v3, v47, 16, 1
	v_lshrrev_b32_e32 v1, 16, v1
	v_add3_u32 v3, v47, v3, s81
	v_and_or_b32 v3, v3, s80, v1
	s_mov_b64 s[14:15], -1
	global_store_dwordx2 v[4:5], v[2:3], off offset:480
	s_barrier

; #define LAS __attribute__((address_space(3)))
; __device__ __forceinline__ float lo_bf(unsigned w) { return __uint_as_float(w << 16); }
; __device__ __forceinline__ float hi_bf(unsigned w) { return __uint_as_float(w & 0xffff0000u); }
; __device__ __forceinline__ f32x4 bf4(u32x2 v) { return (f32x4){lo_bf(v.x), hi_bf(v.x), lo_bf(v.y), hi_bf(v.y)}; }
; __device__ __forceinline__ void ph_post_hyena(CArgs& a, int l, LAS unsigned char* lds, int bid, int nblk) {
;     ...
;         { const int ch = tid & 255, half = tid >> 8;
;           const bf16* srcp = YT + ((size_t)(ch * 16 + c.b)) * 2304 + soff + c.t0 + half * 32;
;           u32x4 v8[4];
; #pragma unroll
;           for (int j = 0; j < 4; ++j) v8[j] = *(const u32x4*)(srcp + 8 * j);
; #pragma unroll
;           for (int j = 0; j < 4; ++j) { LAS float* d = yt + (half * 32 + 8 * j) * 260 + ch;
;               d[0] = lo_bf(v8[j].x); d[260] = hi_bf(v8[j].x); d[2 * 260] = lo_bf(v8[j].y); d[3 * 260] = hi_bf(v8[j].y); d[4 * 260] = lo_bf(v8[j].z); d[5 * 260] = hi_bf(v8[j].z); d[6 * 260] = lo_bf(v8[j].w); d[7 * 260] = hi_bf(v8[j].w); } }
;         __syncthreads();
;         const int tb = c.t0 + tg * 8;
;         const bf16* pb = P + (size_t)(c.row0 + tg * 8) * D_INP;
;         f32x4 x0[10], x1[10], vv[10];
; #pragma unroll
;         for (int r = 0; r < 10; ++r) { const int t = tb + r - 1, tc = min(max(t, c.lo), c.hi - 1); const float ok = (t == tc) ? 1.f : 0.f; const bf16* p = pb + (ptrdiff_t)(tc - tb) * D_INP;
;             x0[r] = ok * bf4(*(const u32x2*)(p + HY0 + c4));
;             x1[r] = ok * bf4(*(const u32x2*)(p + HY0 + 256 + c4)); vv[r] = ok * bf4(*(const u32x2*)(p + HY0 + 512 + c4)); }
.LBB0_2754:
	v_add_u32_e32 v62, s7, v1
	v_mov_b64_e32 v[60:61], s[4:5]
	s_movk_i32 s7, 0x1200
	v_mad_i64_i32 v[60:61], s[16:17], v62, s7, v[60:61]
	s_lshl_b32 s78, s14, 1
	v_lshl_add_u64 v[60:61], v[60:61], 0, s[78:79]
	s_mov_b32 s7, s79
	v_lshl_add_u64 v[60:61], s[6:7], 1, v[60:61]
	v_lshl_add_u64 v[60:61], v[56:57], 1, v[60:61]
	global_load_dwordx4 v[66:69], v[60:61], off
	global_load_dwordx4 v[70:73], v[60:61], off offset:16
	global_load_dwordx4 v[74:77], v[60:61], off offset:32
	global_load_dwordx4 v[78:81], v[60:61], off offset:48
	v_add_u32_e32 v64, s6, v188
	v_add_u32_e32 v65, -1, v64
	v_max_i32_e32 v61, s9, v65
	v_add_u32_e32 v60, s10, v188
	v_mov_b64_e32 v[62:63], s[2:3]
	v_mad_i64_i32 v[62:63], s[6:7], v60, s65, v[62:63]
	v_or_b32_e32 v111, 2, v64
	v_or_b32_e32 v112, 3, v64
	v_or_b32_e32 v115, 5, v64
	v_or_b32_e32 v206, 6, v64
	v_or_b32_e32 v208, 7, v64
	v_add_u32_e32 v210, 8, v64
	s_add_i32 s0, s0, s68
	s_waitcnt vmcnt(3)
	v_lshlrev_b32_e32 v82, 16, v66
	s_waitcnt vmcnt(2)
	v_lshlrev_b32_e32 v89, 16, v73
	v_and_b32_e32 v66, 0xffff0000, v66
	v_lshlrev_b32_e32 v83, 16, v67
	v_and_b32_e32 v67, 0xffff0000, v67
	v_lshlrev_b32_e32 v84, 16, v68
	v_and_b32_e32 v68, 0xffff0000, v68
	v_lshlrev_b32_e32 v85, 16, v69
	v_and_b32_e32 v69, 0xffff0000, v69
	v_lshlrev_b32_e32 v86, 16, v70
	v_and_b32_e32 v70, 0xffff0000, v70
	v_lshlrev_b32_e32 v87, 16, v71
	v_and_b32_e32 v71, 0xffff0000, v71
	v_lshlrev_b32_e32 v88, 16, v72
	v_and_b32_e32 v72, 0xffff0000, v72
	v_and_b32_e32 v73, 0xffff0000, v73
	s_waitcnt vmcnt(1)
	v_lshlrev_b32_e32 v90, 16, v74
	v_and_b32_e32 v74, 0xffff0000, v74
	v_lshlrev_b32_e32 v91, 16, v75
	v_and_b32_e32 v75, 0xffff0000, v75
	v_lshlrev_b32_e32 v92, 16, v76
	v_and_b32_e32 v76, 0xffff0000, v76
	v_lshlrev_b32_e32 v93, 16, v77
	v_and_b32_e32 v77, 0xffff0000, v77
	s_waitcnt vmcnt(0)
	v_lshlrev_b32_e32 v94, 16, v78
	v_and_b32_e32 v78, 0xffff0000, v78
	v_lshlrev_b32_e32 v95, 16, v79
	v_and_b32_e32 v79, 0xffff0000, v79
	v_lshlrev_b32_e32 v96, 16, v80
	v_and_b32_e32 v80, 0xffff0000, v80
	v_lshlrev_b32_e32 v97, 16, v81
	v_and_b32_e32 v81, 0xffff0000, v81
	ds_write_b32 v189, v82
	ds_write_b32 v189, v66 offset:1040
	ds_write_b32 v189, v83 offset:2080
	ds_write_b32 v189, v67 offset:3120
	ds_write_b32 v189, v84 offset:4160
	ds_write_b32 v189, v68 offset:5200
	ds_write_b32 v189, v85 offset:6240
	ds_write_b32 v189, v69 offset:7280
	ds_write_b32 v189, v86 offset:8320
	ds_write_b32 v189, v70 offset:9360
	ds_write_b32 v189, v87 offset:10400
	ds_write_b32 v189, v71 offset:11440
	ds_write_b32 v189, v88 offset:12480
	ds_write_b32 v189, v72 offset:13520
	ds_write_b32 v189, v89 offset:14560
	ds_write_b32 v189, v73 offset:15600
	ds_write_b32 v189, v90 offset:16640
	ds_write_b32 v189, v74 offset:17680
	ds_write_b32 v189, v91 offset:18720
	ds_write_b32 v189, v75 offset:19760
	ds_write_b32 v189, v92 offset:20800
	ds_write_b32 v189, v76 offset:21840
	ds_write_b32 v189, v93 offset:22880
	ds_write_b32 v189, v77 offset:23920
	ds_write_b32 v189, v94 offset:24960
	ds_write_b32 v189, v78 offset:26000
	ds_write_b32 v189, v95 offset:27040
	ds_write_b32 v189, v79 offset:28080
	ds_write_b32 v189, v96 offset:29120
	ds_write_b32 v189, v80 offset:30160
	ds_write_b32 v189, v97 offset:31200
	ds_write_b32 v189, v81 offset:32240
	v_min_u32_e32 v89, s8, v61
	v_sub_u32_e32 v61, v89, v64
	v_mad_i64_i32 v[66:67], s[6:7], v61, s65, v[62:63]
	v_lshl_add_u64 v[66:67], v[66:67], 0, v[34:35]
	s_waitcnt lgkmcnt(0)
	s_barrier
	global_load_dwordx2 v[68:69], v[66:67], off
	global_load_dwordx2 v[70:71], v[66:67], off offset:512
	s_nop 0
	global_load_dwordx2 v[66:67], v[66:67], off offset:1024
	v_max_i32_e32 v61, s9, v64
	v_min_u32_e32 v88, s8, v61
	v_sub_u32_e32 v61, v88, v64
	v_mad_i64_i32 v[72:73], s[6:7], v61, s65, v[62:63]
	v_lshl_add_u64 v[72:73], v[72:73], 0, v[34:35]
	global_load_dwordx2 v[74:75], v[72:73], off
	global_load_dwordx2 v[76:77], v[72:73], off offset:512
	s_nop 0
	global_load_dwordx2 v[72:73], v[72:73], off offset:1024
	v_or_b32_e32 v91, 1, v64
	v_max_i32_e32 v61, s9, v91
	v_min_u32_e32 v110, s8, v61
	v_sub_u32_e32 v61, v110, v64
	v_mad_i64_i32 v[78:79], s[6:7], v61, s65, v[62:63]
	v_lshl_add_u64 v[78:79], v[78:79], 0, v[34:35]
	v_max_i32_e32 v84, s9, v111
	global_load_dwordx2 v[80:81], v[78:79], off
	global_load_dwordx2 v[82:83], v[78:79], off offset:512
	v_min_u32_e32 v113, s8, v84
	v_sub_u32_e32 v84, v113, v64
	v_mad_i64_i32 v[84:85], s[6:7], v84, s65, v[62:63]
	global_load_dwordx2 v[78:79], v[78:79], off offset:1024
	v_lshl_add_u64 v[84:85], v[84:85], 0, v[34:35]
	global_load_dwordx2 v[86:87], v[84:85], off
	global_load_dwordx2 v[92:93], v[84:85], off offset:512
	v_max_i32_e32 v90, s9, v112
	v_cmp_eq_u32_e32 vcc, v88, v64
	v_min_u32_e32 v114, s8, v90
	v_ashrrev_i32_e32 v61, 31, v60
	v_cndmask_b32_e64 v88, 0, 1.0, vcc
	v_cmp_eq_u32_e32 vcc, v65, v89
	v_sub_u32_e32 v65, v114, v64
	v_mad_i64_i32 v[94:95], s[6:7], v65, s65, v[62:63]
	v_lshl_add_u64 v[94:95], v[94:95], 0, v[34:35]
	global_load_dwordx2 v[84:85], v[84:85], off offset:1024
	s_nop 0
	global_load_dwordx2 v[96:97], v[94:95], off
	v_cndmask_b32_e64 v90, 0, 1.0, vcc
	v_cmp_eq_u32_e32 vcc, v91, v110
	v_or_b32_e32 v65, 4, v64
	v_lshlrev_b64 v[60:61], 11, v[60:61]
	v_lshl_add_u64 v[60:61], v[58:59], 0, v[60:61]
	s_waitcnt vmcnt(12)
	v_lshlrev_b32_e32 v98, 16, v68
	v_and_b32_e32 v99, 0xffff0000, v68
	v_lshlrev_b32_e32 v68, 16, v69
	v_and_b32_e32 v69, 0xffff0000, v69
	v_pk_mul_f32 v[184:185], v[90:91], v[68:69] op_sel_hi:[0,1]
	global_load_dwordx2 v[68:69], v[94:95], off offset:512
	s_waitcnt vmcnt(11)
	v_lshlrev_b32_e32 v102, 16, v66
	v_and_b32_e32 v103, 0xffff0000, v66
	v_lshlrev_b32_e32 v66, 16, v67
	v_and_b32_e32 v67, 0xffff0000, v67
	s_waitcnt vmcnt(8)
; __device__ __forceinline__ f32x4 bf4(u32x2 v) { return (f32x4){lo_bf(v.x), hi_bf(v.x), lo_bf(v.y), hi_bf(v.y)}; }
; __device__ __forceinline__ void ph_post_hyena(CArgs& a, int l, LAS unsigned char* lds, int bid, int nblk) {
;     ...
;         const int tb = c.t0 + tg * 8;
;         const bf16* pb = P + (size_t)(c.row0 + tg * 8) * D_INP;
;         f32x4 x0[10], x1[10], vv[10];
; #pragma unroll
;         for (int r = 0; r < 10; ++r) { const int t = tb + r - 1, tc = min(max(t, c.lo), c.hi - 1); const float ok = (t == tc) ? 1.f : 0.f; const bf16* p = pb + (ptrdiff_t)(tc - tb) * D_INP;
;             x0[r] = ok * bf4(*(const u32x2*)(p + HY0 + c4));
;             x1[r] = ok * bf4(*(const u32x2*)(p + HY0 + 256 + c4)); vv[r] = ok * bf4(*(const u32x2*)(p + HY0 + 512 + c4)); }
	v_lshlrev_b32_e32 v108, 16, v72
	v_pk_mul_f32 v[176:177], v[90:91], v[66:67] op_sel_hi:[0,1]
	v_and_b32_e32 v109, 0xffff0000, v72
	v_lshlrev_b32_e32 v66, 16, v73
	v_and_b32_e32 v67, 0xffff0000, v73
	global_load_dwordx2 v[72:73], v[94:95], off offset:1024
	v_lshlrev_b32_e32 v100, 16, v70
	v_and_b32_e32 v101, 0xffff0000, v70
	v_lshlrev_b32_e32 v70, 16, v71
	v_and_b32_e32 v71, 0xffff0000, v71
	v_lshlrev_b32_e32 v104, 16, v74
	v_and_b32_e32 v105, 0xffff0000, v74
	v_lshlrev_b32_e32 v74, 16, v75
	v_and_b32_e32 v75, 0xffff0000, v75
	v_pk_mul_f32 v[180:181], v[90:91], v[70:71] op_sel_hi:[0,1]
	v_pk_mul_f32 v[152:153], v[88:89], v[74:75] op_sel_hi:[0,1]
	v_pk_mul_f32 v[156:157], v[88:89], v[66:67] op_sel_hi:[0,1]
	v_cndmask_b32_e64 v66, 0, 1.0, vcc
	s_waitcnt vmcnt(8)
	v_lshlrev_b32_e32 v70, 16, v80
	v_and_b32_e32 v71, 0xffff0000, v80
	v_lshlrev_b32_e32 v74, 16, v81
	v_and_b32_e32 v75, 0xffff0000, v81
	v_pk_mul_f32 v[138:139], v[66:67], v[70:71] op_sel_hi:[0,1]
	v_pk_mul_f32 v[140:141], v[66:67], v[74:75] op_sel_hi:[0,1]
	s_waitcnt vmcnt(7)
	v_lshlrev_b32_e32 v70, 16, v82
	v_and_b32_e32 v71, 0xffff0000, v82
	v_lshlrev_b32_e32 v74, 16, v83
	v_and_b32_e32 v75, 0xffff0000, v83
	v_pk_mul_f32 v[134:135], v[66:67], v[70:71] op_sel_hi:[0,1]
	v_pk_mul_f32 v[136:137], v[66:67], v[74:75] op_sel_hi:[0,1]
	v_max_i32_e32 v67, s9, v65
	v_lshlrev_b32_e32 v106, 16, v76
	v_and_b32_e32 v107, 0xffff0000, v76
	v_lshlrev_b32_e32 v76, 16, v77
	v_and_b32_e32 v77, 0xffff0000, v77
	v_pk_mul_f32 v[178:179], v[90:91], v[102:103] op_sel_hi:[0,1]
	v_min_u32_e32 v102, s8, v67
	v_pk_mul_f32 v[144:145], v[88:89], v[76:77] op_sel_hi:[0,1]
	v_sub_u32_e32 v67, v102, v64
	s_waitcnt vmcnt(6)
	v_lshlrev_b32_e32 v76, 16, v78
	v_and_b32_e32 v77, 0xffff0000, v78
	v_lshlrev_b32_e32 v78, 16, v79
	v_and_b32_e32 v79, 0xffff0000, v79
	v_cmp_eq_u32_e32 vcc, v111, v113
	v_pk_mul_f32 v[158:159], v[66:67], v[76:77] op_sel_hi:[0,1]
	v_pk_mul_f32 v[160:161], v[66:67], v[78:79] op_sel_hi:[0,1]
	v_cndmask_b32_e64 v66, 0, 1.0, vcc
	s_waitcnt vmcnt(5)
	v_lshlrev_b32_e32 v78, 16, v87
	v_and_b32_e32 v79, 0xffff0000, v87
	v_lshlrev_b32_e32 v76, 16, v86
	v_and_b32_e32 v77, 0xffff0000, v86
	v_pk_mul_f32 v[82:83], v[66:67], v[78:79] op_sel_hi:[0,1]
	s_waitcnt vmcnt(4)
	v_lshlrev_b32_e32 v78, 16, v92
	v_and_b32_e32 v79, 0xffff0000, v92
	v_lshlrev_b32_e32 v86, 16, v93
	v_and_b32_e32 v87, 0xffff0000, v93
	v_pk_mul_f32 v[186:187], v[90:91], v[98:99] op_sel_hi:[0,1]
	v_pk_mul_f32 v[182:183], v[90:91], v[100:101] op_sel_hi:[0,1]
	v_mad_i64_i32 v[70:71], s[6:7], v67, s65, v[62:63]
	v_pk_mul_f32 v[80:81], v[66:67], v[76:77] op_sel_hi:[0,1]
	v_pk_mul_f32 v[90:91], v[66:67], v[78:79] op_sel_hi:[0,1]
	v_pk_mul_f32 v[92:93], v[66:67], v[86:87] op_sel_hi:[0,1]
	v_max_i32_e32 v67, s9, v115
	v_min_u32_e32 v116, s8, v67
	s_waitcnt vmcnt(3)
	v_lshlrev_b32_e32 v78, 16, v84
	v_sub_u32_e32 v67, v116, v64
	v_and_b32_e32 v79, 0xffff0000, v84
	v_pk_mul_f32 v[142:143], v[88:89], v[106:107] op_sel_hi:[0,1]
	v_pk_mul_f32 v[106:107], v[66:67], v[78:79] op_sel_hi:[0,1]
	v_max_i32_e32 v79, s9, v206
	v_mad_i64_i32 v[86:87], s[6:7], v67, s65, v[62:63]
	v_lshlrev_b32_e32 v84, 16, v85
	v_and_b32_e32 v85, 0xffff0000, v85
	v_cmp_eq_u32_e32 vcc, v112, v114
	v_min_u32_e32 v207, s8, v79
	v_pk_mul_f32 v[154:155], v[88:89], v[108:109] op_sel_hi:[0,1]
	v_lshl_add_u64 v[70:71], v[70:71], 0, v[34:35]
	v_lshl_add_u64 v[86:87], v[86:87], 0, v[34:35]
	v_pk_mul_f32 v[108:109], v[66:67], v[84:85] op_sel_hi:[0,1]
	v_cndmask_b32_e64 v78, 0, 1.0, vcc
	s_waitcnt vmcnt(2)
	v_lshlrev_b32_e32 v84, 16, v96
	v_and_b32_e32 v85, 0xffff0000, v96
	v_sub_u32_e32 v79, v207, v64
	v_pk_mul_f32 v[150:151], v[88:89], v[104:105] op_sel_hi:[0,1]
	global_load_dwordx2 v[76:77], v[70:71], off offset:512
	global_load_dwordx2 v[88:89], v[86:87], off
	v_pk_mul_f32 v[110:111], v[78:79], v[84:85] op_sel_hi:[0,1]
	s_waitcnt vmcnt(3)
	v_lshlrev_b32_e32 v84, 16, v68
	v_and_b32_e32 v85, 0xffff0000, v68
	v_lshlrev_b32_e32 v68, 16, v69
	v_and_b32_e32 v69, 0xffff0000, v69
	v_pk_mul_f32 v[132:133], v[78:79], v[68:69] op_sel_hi:[0,1]
	v_max_i32_e32 v69, s9, v208
	v_cmp_eq_u32_e32 vcc, v65, v102
	v_max_i32_e32 v65, s9, v210
	v_min_u32_e32 v209, s8, v69
	v_min_u32_e32 v211, s8, v65
	v_sub_u32_e32 v69, v209, v64
	v_sub_u32_e32 v64, v211, v64
	v_lshlrev_b32_e32 v94, 16, v97
	v_mad_i64_i32 v[98:99], s[6:7], v79, s65, v[62:63]
	v_and_b32_e32 v95, 0xffff0000, v97
	v_mad_i64_i32 v[96:97], s[6:7], v69, s65, v[62:63]
	v_mad_i64_i32 v[62:63], s[6:7], v64, s65, v[62:63]
	v_lshl_add_u64 v[62:63], v[62:63], 0, v[34:35]
	global_load_dwordx2 v[74:75], v[70:71], off
	global_load_dwordx2 v[102:103], v[62:63], off
	global_load_dwordx2 v[104:105], v[62:63], off offset:512
	global_load_dwordx2 v[204:205], v[62:63], off offset:1024
	global_load_dwordx2 v[66:67], v[86:87], off offset:512
	v_lshl_add_u64 v[98:99], v[98:99], 0, v[34:35]
	global_load_dwordx2 v[70:71], v[70:71], off offset:1024
	v_lshl_add_u64 v[96:97], v[96:97], 0, v[34:35]
	global_load_dwordx2 v[100:101], v[98:99], off
	v_pk_mul_f32 v[112:113], v[78:79], v[94:95] op_sel_hi:[0,1]
	global_load_dwordx2 v[94:95], v[98:99], off offset:512
	v_pk_mul_f32 v[130:131], v[78:79], v[84:85] op_sel_hi:[0,1]
	global_load_dwordx2 v[84:85], v[98:99], off offset:1024
	s_waitcnt vmcnt(11)
	v_lshlrev_b32_e32 v68, 16, v72
	global_load_dwordx2 v[98:99], v[96:97], off
	v_and_b32_e32 v69, 0xffff0000, v72
	global_load_dwordx2 v[86:87], v[86:87], off offset:1024
	v_lshlrev_b32_e32 v72, 16, v73
	v_and_b32_e32 v73, 0xffff0000, v73
	v_pk_mul_f32 v[172:173], v[78:79], v[68:69] op_sel_hi:[0,1]
	v_pk_mul_f32 v[174:175], v[78:79], v[72:73] op_sel_hi:[0,1]
	global_load_dwordx2 v[78:79], v[96:97], off offset:512
	v_cndmask_b32_e64 v68, 0, 1.0, vcc
	global_load_dwordx2 v[96:97], v[96:97], off offset:1024
	v_cmp_eq_u32_e32 vcc, v115, v116
	s_movk_i32 s6, 0x1000
	s_waitcnt vmcnt(14)
; #define LAS __attribute__((address_space(3)))
; __device__ __forceinline__ f32x4 bf4(u32x2 v) { return (f32x4){lo_bf(v.x), hi_bf(v.x), lo_bf(v.y), hi_bf(v.y)}; }
; __device__ __forceinline__ void ph_post_hyena(CArgs& a, int l, LAS unsigned char* lds, int bid, int nblk) {
;     ...
;         for (int r = 0; r < 10; ++r) { const int t = tb + r - 1, tc = min(max(t, c.lo), c.hi - 1); const float ok = (t == tc) ? 1.f : 0.f; const bf16* p = pb + (ptrdiff_t)(tc - tb) * D_INP;
;             x0[r] = ok * bf4(*(const u32x2*)(p + HY0 + c4));
;             x1[r] = ok * bf4(*(const u32x2*)(p + HY0 + 256 + c4)); vv[r] = ok * bf4(*(const u32x2*)(p + HY0 + 512 + c4)); }
; #pragma unroll
;         for (int tt = 0; tt < 8; ++tt) {
;             const f32x4 u0 = w0[0] * x0[tt] + w0[1] * x0[tt + 1] + w0[2] * x0[tt + 2] + b0;
;             const f32x4 xx = wx[0] * x1[tt] + wx[1] * x1[tt + 1] + wx[2] * x1[tt + 2] + bx, v2 = wv[0] * vv[tt] + wv[1] * vv[tt + 1] + wv[2] * vv[tt + 2] + bv, z = xx * v2;
;             const f32x4 y = *(const LAS f32x4*)(yt + (tg * 8 + tt) * 260 + c4);
;             const f32x4 o = (y + z * hd) * u0;
	v_lshlrev_b32_e32 v64, 16, v76
	v_and_b32_e32 v65, 0xffff0000, v76
	v_pk_mul_f32 v[146:147], v[68:69], v[64:65] op_sel_hi:[0,1]
	s_waitcnt vmcnt(12)
	v_lshlrev_b32_e32 v72, 16, v74
	v_and_b32_e32 v73, 0xffff0000, v74
	v_lshlrev_b32_e32 v74, 16, v75
	v_and_b32_e32 v75, 0xffff0000, v75
	v_pk_mul_f32 v[126:127], v[68:69], v[72:73] op_sel_hi:[0,1]
	v_lshlrev_b32_e32 v72, 16, v77
	s_waitcnt vmcnt(7)
	v_lshlrev_b32_e32 v64, 16, v70
	v_and_b32_e32 v65, 0xffff0000, v70
	v_lshlrev_b32_e32 v62, 16, v71
	v_and_b32_e32 v63, 0xffff0000, v71
	v_pk_mul_f32 v[162:163], v[68:69], v[64:65] op_sel_hi:[0,1]
	v_pk_mul_f32 v[170:171], v[68:69], v[62:63] op_sel_hi:[0,1]
	v_cndmask_b32_e64 v62, 0, 1.0, vcc
	v_lshlrev_b32_e32 v64, 16, v88
	v_and_b32_e32 v65, 0xffff0000, v88
	v_and_b32_e32 v73, 0xffff0000, v77
	v_pk_mul_f32 v[122:123], v[62:63], v[64:65] op_sel_hi:[0,1]
	v_lshlrev_b32_e32 v64, 16, v66
	v_and_b32_e32 v65, 0xffff0000, v66
	v_lshlrev_b32_e32 v66, 16, v67
	v_and_b32_e32 v67, 0xffff0000, v67
	v_pk_mul_f32 v[128:129], v[68:69], v[74:75] op_sel_hi:[0,1]
	v_pk_mul_f32 v[148:149], v[68:69], v[72:73] op_sel_hi:[0,1]
	v_lshlrev_b32_e32 v68, 16, v89
	v_and_b32_e32 v69, 0xffff0000, v89
	v_pk_mul_f32 v[118:119], v[62:63], v[64:65] op_sel_hi:[0,1]
	v_pk_mul_f32 v[120:121], v[62:63], v[66:67] op_sel_hi:[0,1]
	s_waitcnt vmcnt(2)
	v_lshlrev_b32_e32 v64, 16, v86
	v_and_b32_e32 v65, 0xffff0000, v86
	v_lshlrev_b32_e32 v66, 16, v87
	v_and_b32_e32 v67, 0xffff0000, v87
	v_cmp_eq_u32_e32 vcc, v206, v207
	v_pk_mul_f32 v[124:125], v[62:63], v[68:69] op_sel_hi:[0,1]
	v_pk_mul_f32 v[114:115], v[62:63], v[64:65] op_sel_hi:[0,1]
	v_pk_mul_f32 v[116:117], v[62:63], v[66:67] op_sel_hi:[0,1]
	v_cndmask_b32_e64 v64, 0, 1.0, vcc
	v_lshlrev_b32_e32 v62, 16, v100
	v_and_b32_e32 v63, 0xffff0000, v100
	v_lshlrev_b32_e32 v66, 16, v101
	v_and_b32_e32 v67, 0xffff0000, v101
	v_pk_mul_f32 v[70:71], v[64:65], v[62:63] op_sel_hi:[0,1]
	v_lshlrev_b32_e32 v62, 16, v94
	v_and_b32_e32 v63, 0xffff0000, v94
	v_pk_mul_f32 v[72:73], v[64:65], v[66:67] op_sel_hi:[0,1]
	v_lshlrev_b32_e32 v68, 16, v95
	v_and_b32_e32 v69, 0xffff0000, v95
	v_pk_mul_f32 v[66:67], v[64:65], v[62:63] op_sel_hi:[0,1]
	v_lshlrev_b32_e32 v62, 16, v84
	v_and_b32_e32 v63, 0xffff0000, v84
	v_lshlrev_b32_e32 v74, 16, v85
	v_and_b32_e32 v75, 0xffff0000, v85
	v_cmp_eq_u32_e32 vcc, v208, v209
	v_pk_mul_f32 v[68:69], v[64:65], v[68:69] op_sel_hi:[0,1]
	v_pk_mul_f32 v[62:63], v[64:65], v[62:63] op_sel_hi:[0,1]
	v_pk_mul_f32 v[64:65], v[64:65], v[74:75] op_sel_hi:[0,1]
	v_cndmask_b32_e64 v94, 0, 1.0, vcc
	v_lshlrev_b32_e32 v74, 16, v98
	v_and_b32_e32 v75, 0xffff0000, v98
	v_lshlrev_b32_e32 v76, 16, v99
	v_and_b32_e32 v77, 0xffff0000, v99
	v_pk_mul_f32 v[84:85], v[94:95], v[74:75] op_sel_hi:[0,1]
	s_waitcnt vmcnt(1)
	v_lshlrev_b32_e32 v74, 16, v78
	v_and_b32_e32 v75, 0xffff0000, v78
	v_lshlrev_b32_e32 v78, 16, v79
	v_and_b32_e32 v79, 0xffff0000, v79
	v_cmp_eq_u32_e32 vcc, v210, v211
	v_pk_mul_f32 v[88:89], v[94:95], v[76:77] op_sel_hi:[0,1]
	v_pk_mul_f32 v[76:77], v[94:95], v[74:75] op_sel_hi:[0,1]
	v_pk_mul_f32 v[86:87], v[94:95], v[78:79] op_sel_hi:[0,1]
	s_waitcnt vmcnt(0)
	v_lshlrev_b32_e32 v74, 16, v96
	v_and_b32_e32 v75, 0xffff0000, v96
	v_lshlrev_b32_e32 v78, 16, v97
	v_and_b32_e32 v79, 0xffff0000, v97
	v_cndmask_b32_e64 v206, 0, 1.0, vcc
	v_lshlrev_b32_e32 v96, 16, v103
	v_and_b32_e32 v97, 0xffff0000, v103
	v_pk_mul_f32 v[74:75], v[94:95], v[74:75] op_sel_hi:[0,1]
	v_pk_mul_f32 v[78:79], v[94:95], v[78:79] op_sel_hi:[0,1]
	v_lshlrev_b32_e32 v94, 16, v102
	v_and_b32_e32 v95, 0xffff0000, v102
	v_pk_mul_f32 v[102:103], v[206:207], v[96:97] op_sel_hi:[0,1]
	v_lshlrev_b32_e32 v96, 16, v105
	v_and_b32_e32 v97, 0xffff0000, v105
	v_pk_mul_f32 v[98:99], v[206:207], v[94:95] op_sel_hi:[0,1]
	v_lshlrev_b32_e32 v94, 16, v104
	v_and_b32_e32 v95, 0xffff0000, v104
	v_pk_mul_f32 v[100:101], v[206:207], v[96:97] op_sel_hi:[0,1]
	v_lshlrev_b32_e32 v96, 16, v204
	v_and_b32_e32 v97, 0xffff0000, v204
	v_lshlrev_b32_e32 v104, 16, v205
	v_and_b32_e32 v105, 0xffff0000, v205
	v_pk_mul_f32 v[94:95], v[206:207], v[94:95] op_sel_hi:[0,1]
	v_pk_mul_f32 v[96:97], v[206:207], v[96:97] op_sel_hi:[0,1]
	v_pk_mul_f32 v[104:105], v[206:207], v[104:105] op_sel_hi:[0,1]
	v_pk_mul_f32 v[204:205], v[16:17], v[152:153]
	v_pk_mul_f32 v[206:207], v[14:15], v[150:151]
	v_pk_fma_f32 v[184:185], v[4:5], v[184:185], v[204:205]
	v_pk_fma_f32 v[186:187], v[2:3], v[186:187], v[206:207]
	v_pk_mul_f32 v[204:205], v[20:21], v[144:145]
	v_pk_mul_f32 v[206:207], v[18:19], v[142:143]
	v_pk_fma_f32 v[180:181], v[8:9], v[180:181], v[204:205]
	v_pk_fma_f32 v[182:183], v[6:7], v[182:183], v[206:207]
	v_pk_mul_f32 v[204:205], v[24:25], v[156:157]
	v_pk_mul_f32 v[206:207], v[22:23], v[154:155]
	v_pk_fma_f32 v[176:177], v[12:13], v[176:177], v[204:205]
	v_pk_fma_f32 v[178:179], v[10:11], v[178:179], v[206:207]
	v_pk_fma_f32 v[204:205], v[38:39], v[160:161], v[176:177]
	v_pk_fma_f32 v[176:177], v[36:37], v[158:159], v[178:179]
	v_pk_fma_f32 v[182:183], v[30:31], v[134:135], v[182:183]
	v_pk_add_f32 v[206:207], v[48:49], v[176:177]
	ds_read_b128 v[176:179], v202
	v_pk_fma_f32 v[180:181], v[32:33], v[136:137], v[180:181]
	v_pk_add_f32 v[182:183], v[44:45], v[182:183]
	v_pk_fma_f32 v[186:187], v[26:27], v[138:139], v[186:187]
	v_pk_add_f32 v[180:181], v[46:47], v[180:181]
	v_pk_add_f32 v[204:205], v[50:51], v[204:205]
	v_pk_mul_f32 v[206:207], v[182:183], v[206:207]
	v_pk_fma_f32 v[184:185], v[28:29], v[140:141], v[184:185]
	v_pk_add_f32 v[186:187], v[40:41], v[186:187]
	v_pk_mul_f32 v[204:205], v[180:181], v[204:205]
	ds_read_b128 v[180:183], v202 offset:1040
	s_waitcnt lgkmcnt(1)
; #define LAS __attribute__((address_space(3)))
; __device__ __forceinline__ unsigned pk2(float lo, float hi) { return f2bf(lo) | (f2bf(hi) << 16); }
; __device__ __forceinline__ void ph_post_hyena(CArgs& a, int l, LAS unsigned char* lds, int bid, int nblk) {
;     ...
;         for (int tt = 0; tt < 8; ++tt) {
;             const f32x4 u0 = w0[0] * x0[tt] + w0[1] * x0[tt + 1] + w0[2] * x0[tt + 2] + b0;
;             const f32x4 xx = wx[0] * x1[tt] + wx[1] * x1[tt + 1] + wx[2] * x1[tt + 2] + bx, v2 = wv[0] * vv[tt] + wv[1] * vv[tt + 1] + wv[2] * vv[tt + 2] + bv, z = xx * v2;
;             const f32x4 y = *(const LAS f32x4*)(yt + (tg * 8 + tt) * 260 + c4);
;             const f32x4 o = (y + z * hd) * u0;
;             u32x2 oo; oo.x = pk2(o[0], o[1]); oo.y = pk2(o[2], o[3]); *(u32x2*)(YMIX + (size_t)(c.row0 + tg * 8 + tt) * D + c4) = oo;
	v_pk_fma_f32 v[176:177], v[52:53], v[206:207], v[176:177]
	v_pk_add_f32 v[184:185], v[42:43], v[184:185]
	v_pk_fma_f32 v[178:179], v[54:55], v[204:205], v[178:179]
	v_pk_mul_f32 v[176:177], v[186:187], v[176:177]
	v_pk_mul_f32 v[178:179], v[184:185], v[178:179]
	v_bfe_u32 v184, v176, 16, 1
	v_add3_u32 v176, v176, v184, s81
	v_bfe_u32 v184, v177, 16, 1
	v_lshrrev_b32_e32 v176, 16, v176
	v_add3_u32 v177, v177, v184, s81
	v_and_or_b32 v176, v177, s80, v176
	v_cvt_pk_bf16_f32 v177, v178, v179
	v_pk_mul_f32 v[178:179], v[14:15], v[138:139]
	global_store_dwordx2 v[60:61], v[176:177], off
	v_pk_fma_f32 v[150:151], v[2:3], v[150:151], v[178:179]
	v_pk_mul_f32 v[178:179], v[18:19], v[134:135]
	v_pk_mul_f32 v[176:177], v[16:17], v[140:141]
	v_pk_fma_f32 v[142:143], v[6:7], v[142:143], v[178:179]
	v_pk_mul_f32 v[178:179], v[22:23], v[158:159]
	v_pk_fma_f32 v[152:153], v[4:5], v[152:153], v[176:177]
	v_pk_fma_f32 v[154:155], v[10:11], v[154:155], v[178:179]
	v_pk_mul_f32 v[176:177], v[20:21], v[136:137]
	v_pk_fma_f32 v[142:143], v[30:31], v[90:91], v[142:143]
	v_pk_fma_f32 v[154:155], v[36:37], v[106:107], v[154:155]
	v_pk_fma_f32 v[144:145], v[8:9], v[144:145], v[176:177]
	v_pk_add_f32 v[142:143], v[44:45], v[142:143]
	v_pk_mul_f32 v[176:177], v[24:25], v[160:161]
	v_pk_add_f32 v[154:155], v[48:49], v[154:155]
	v_pk_fma_f32 v[150:151], v[26:27], v[80:81], v[150:151]
	v_pk_fma_f32 v[156:157], v[12:13], v[156:157], v[176:177]
	v_pk_mul_f32 v[142:143], v[142:143], v[154:155]
	v_pk_add_f32 v[150:151], v[40:41], v[150:151]
	v_pk_fma_f32 v[144:145], v[32:33], v[92:93], v[144:145]
	v_pk_fma_f32 v[156:157], v[38:39], v[108:109], v[156:157]
	s_waitcnt lgkmcnt(0)
	v_pk_fma_f32 v[142:143], v[52:53], v[142:143], v[180:181]
	v_pk_add_f32 v[144:145], v[46:47], v[144:145]
	v_pk_add_f32 v[156:157], v[50:51], v[156:157]
	v_pk_mul_f32 v[142:143], v[150:151], v[142:143]
	v_pk_fma_f32 v[152:153], v[28:29], v[82:83], v[152:153]
	v_pk_mul_f32 v[144:145], v[144:145], v[156:157]
	v_pk_add_f32 v[152:153], v[42:43], v[152:153]
	v_pk_fma_f32 v[144:145], v[54:55], v[144:145], v[182:183]
	v_pk_mul_f32 v[144:145], v[152:153], v[144:145]
	v_cvt_pk_bf16_f32 v142, v142, v143
	v_cvt_pk_bf16_f32 v143, v144, v145
	global_store_dwordx2 v[60:61], v[142:143], off offset:2048
	v_pk_mul_f32 v[142:143], v[16:17], v[82:83]
	v_pk_mul_f32 v[144:145], v[14:15], v[80:81]
	v_pk_fma_f32 v[140:141], v[4:5], v[140:141], v[142:143]
	v_pk_fma_f32 v[138:139], v[2:3], v[138:139], v[144:145]
	v_pk_fma_f32 v[140:141], v[28:29], v[112:113], v[140:141]
	v_pk_fma_f32 v[138:139], v[26:27], v[110:111], v[138:139]
	v_pk_add_f32 v[144:145], v[42:43], v[140:141]
	v_pk_add_f32 v[142:143], v[40:41], v[138:139]
	v_pk_mul_f32 v[138:139], v[20:21], v[92:93]
	v_pk_mul_f32 v[140:141], v[18:19], v[90:91]
	v_pk_fma_f32 v[136:137], v[8:9], v[136:137], v[138:139]
	v_pk_fma_f32 v[134:135], v[6:7], v[134:135], v[140:141]
	v_pk_fma_f32 v[136:137], v[32:33], v[132:133], v[136:137]
	v_pk_fma_f32 v[134:135], v[30:31], v[130:131], v[134:135]
	v_pk_add_f32 v[140:141], v[46:47], v[136:137]
	v_pk_add_f32 v[138:139], v[44:45], v[134:135]
	v_pk_mul_f32 v[134:135], v[24:25], v[108:109]
	v_pk_mul_f32 v[136:137], v[22:23], v[106:107]
	v_pk_fma_f32 v[134:135], v[12:13], v[160:161], v[134:135]
	v_pk_fma_f32 v[136:137], v[10:11], v[158:159], v[136:137]
	v_pk_fma_f32 v[150:151], v[38:39], v[174:175], v[134:135]
	v_pk_fma_f32 v[134:135], v[36:37], v[172:173], v[136:137]
	v_pk_add_f32 v[150:151], v[50:51], v[150:151]
	v_pk_add_f32 v[152:153], v[48:49], v[134:135]
	ds_read_b128 v[134:137], v202 offset:2080
	v_pk_mul_f32 v[152:153], v[138:139], v[152:153]
	v_pk_mul_f32 v[150:151], v[140:141], v[150:151]
	ds_read_b128 v[138:141], v202 offset:3120
	s_waitcnt lgkmcnt(1)
	v_pk_fma_f32 v[134:135], v[52:53], v[152:153], v[134:135]
	s_nop 0
	v_pk_mul_f32 v[134:135], v[142:143], v[134:135]
	v_pk_fma_f32 v[136:137], v[54:55], v[150:151], v[136:137]
	v_pk_mul_f32 v[136:137], v[144:145], v[136:137]
	v_cvt_pk_bf16_f32 v134, v134, v135
	v_cvt_pk_bf16_f32 v135, v136, v137
	v_add_co_u32_e32 v136, vcc, s6, v60
	s_movk_i32 s6, 0x2000
	s_nop 0
	v_addc_co_u32_e32 v137, vcc, 0, v61, vcc
	v_pk_mul_f32 v[144:145], v[14:15], v[110:111]
	v_add_co_u32_e32 v142, vcc, s6, v60
	v_pk_fma_f32 v[80:81], v[2:3], v[80:81], v[144:145]
	v_pk_mul_f32 v[144:145], v[18:19], v[130:131]
	v_addc_co_u32_e32 v143, vcc, 0, v61, vcc
	v_pk_fma_f32 v[90:91], v[6:7], v[90:91], v[144:145]
	v_pk_mul_f32 v[144:145], v[22:23], v[172:173]
	global_store_dwordx2 v[142:143], v[134:135], off offset:-4096
	v_pk_mul_f32 v[134:135], v[16:17], v[112:113]
	v_pk_fma_f32 v[106:107], v[10:11], v[106:107], v[144:145]
	v_pk_fma_f32 v[82:83], v[4:5], v[82:83], v[134:135]
	v_pk_mul_f32 v[134:135], v[20:21], v[132:133]
	v_pk_fma_f32 v[90:91], v[30:31], v[146:147], v[90:91]
	v_pk_fma_f32 v[106:107], v[36:37], v[162:163], v[106:107]
	v_pk_fma_f32 v[92:93], v[8:9], v[92:93], v[134:135]
	v_pk_add_f32 v[90:91], v[44:45], v[90:91]
	v_pk_mul_f32 v[134:135], v[24:25], v[174:175]
	v_pk_add_f32 v[106:107], v[48:49], v[106:107]
	v_pk_fma_f32 v[80:81], v[26:27], v[126:127], v[80:81]
	v_pk_fma_f32 v[108:109], v[12:13], v[108:109], v[134:135]
	v_pk_mul_f32 v[90:91], v[90:91], v[106:107]
	v_pk_add_f32 v[80:81], v[40:41], v[80:81]
	v_pk_fma_f32 v[92:93], v[32:33], v[148:149], v[92:93]
	v_pk_fma_f32 v[108:109], v[38:39], v[170:171], v[108:109]
	s_waitcnt lgkmcnt(0)
; #define LAS __attribute__((address_space(3)))
; __device__ __forceinline__ unsigned pk2(float lo, float hi) { return f2bf(lo) | (f2bf(hi) << 16); }
; __device__ __forceinline__ void ph_post_hyena(CArgs& a, int l, LAS unsigned char* lds, int bid, int nblk) {
;     ...
;         for (int tt = 0; tt < 8; ++tt) {
;             const f32x4 u0 = w0[0] * x0[tt] + w0[1] * x0[tt + 1] + w0[2] * x0[tt + 2] + b0;
;             const f32x4 xx = wx[0] * x1[tt] + wx[1] * x1[tt + 1] + wx[2] * x1[tt + 2] + bx, v2 = wv[0] * vv[tt] + wv[1] * vv[tt + 1] + wv[2] * vv[tt + 2] + bv, z = xx * v2;
;             const f32x4 y = *(const LAS f32x4*)(yt + (tg * 8 + tt) * 260 + c4);
;             const f32x4 o = (y + z * hd) * u0;
;             u32x2 oo; oo.x = pk2(o[0], o[1]); oo.y = pk2(o[2], o[3]); *(u32x2*)(YMIX + (size_t)(c.row0 + tg * 8 + tt) * D + c4) = oo;
	v_pk_fma_f32 v[90:91], v[52:53], v[90:91], v[138:139]
	v_pk_add_f32 v[92:93], v[46:47], v[92:93]
	v_pk_add_f32 v[108:109], v[50:51], v[108:109]
	v_pk_mul_f32 v[80:81], v[80:81], v[90:91]
	v_pk_fma_f32 v[82:83], v[28:29], v[128:129], v[82:83]
	v_pk_mul_f32 v[92:93], v[92:93], v[108:109]
	v_pk_add_f32 v[82:83], v[42:43], v[82:83]
	v_pk_fma_f32 v[92:93], v[54:55], v[92:93], v[140:141]
	v_pk_mul_f32 v[82:83], v[82:83], v[92:93]
	v_cvt_pk_bf16_f32 v80, v80, v81
	v_cvt_pk_bf16_f32 v81, v82, v83
	global_store_dwordx2 v[136:137], v[80:81], off offset:2048
	v_pk_mul_f32 v[80:81], v[16:17], v[128:129]
	v_pk_mul_f32 v[82:83], v[14:15], v[126:127]
	v_pk_fma_f32 v[80:81], v[4:5], v[112:113], v[80:81]
	v_pk_fma_f32 v[82:83], v[2:3], v[110:111], v[82:83]
	v_pk_fma_f32 v[80:81], v[28:29], v[124:125], v[80:81]
	v_pk_fma_f32 v[82:83], v[26:27], v[122:123], v[82:83]
	v_pk_add_f32 v[108:109], v[42:43], v[80:81]
	v_pk_add_f32 v[106:107], v[40:41], v[82:83]
	v_pk_mul_f32 v[80:81], v[20:21], v[148:149]
	v_pk_mul_f32 v[82:83], v[18:19], v[146:147]
	v_pk_fma_f32 v[80:81], v[8:9], v[132:133], v[80:81]
	v_pk_fma_f32 v[82:83], v[6:7], v[130:131], v[82:83]
	v_pk_fma_f32 v[80:81], v[32:33], v[120:121], v[80:81]
	v_pk_fma_f32 v[82:83], v[30:31], v[118:119], v[82:83]
	v_pk_add_f32 v[92:93], v[46:47], v[80:81]
	v_pk_add_f32 v[90:91], v[44:45], v[82:83]
	v_pk_mul_f32 v[80:81], v[24:25], v[170:171]
	v_pk_mul_f32 v[82:83], v[22:23], v[162:163]
	v_pk_fma_f32 v[80:81], v[12:13], v[174:175], v[80:81]
	v_pk_fma_f32 v[82:83], v[10:11], v[172:173], v[82:83]
	v_pk_fma_f32 v[110:111], v[38:39], v[116:117], v[80:81]
	v_pk_fma_f32 v[80:81], v[36:37], v[114:115], v[82:83]
	v_pk_add_f32 v[110:111], v[50:51], v[110:111]
	v_pk_add_f32 v[112:113], v[48:49], v[80:81]
	ds_read_b128 v[80:83], v202 offset:4160
	v_pk_mul_f32 v[112:113], v[90:91], v[112:113]
	v_pk_mul_f32 v[110:111], v[92:93], v[110:111]
	ds_read_b128 v[90:93], v202 offset:5200
	s_movk_i32 s6, 0x3000
	s_waitcnt lgkmcnt(1)
	v_pk_fma_f32 v[80:81], v[52:53], v[112:113], v[80:81]
	v_pk_fma_f32 v[82:83], v[54:55], v[110:111], v[82:83]
	v_pk_mul_f32 v[80:81], v[106:107], v[80:81]
	v_pk_mul_f32 v[82:83], v[108:109], v[82:83]
	v_cvt_pk_bf16_f32 v80, v80, v81
	v_pk_mul_f32 v[108:109], v[18:19], v[118:119]
	v_pk_mul_f32 v[112:113], v[22:23], v[114:115]
	v_pk_fma_f32 v[108:109], v[6:7], v[146:147], v[108:109]
	v_pk_fma_f32 v[112:113], v[10:11], v[162:163], v[112:113]
	v_cvt_pk_bf16_f32 v81, v82, v83
	v_pk_mul_f32 v[82:83], v[14:15], v[122:123]
	v_pk_fma_f32 v[108:109], v[30:31], v[66:67], v[108:109]
	v_pk_fma_f32 v[112:113], v[36:37], v[62:63], v[112:113]
	v_pk_fma_f32 v[82:83], v[2:3], v[126:127], v[82:83]
	v_pk_mul_f32 v[106:107], v[20:21], v[120:121]
	v_pk_add_f32 v[108:109], v[44:45], v[108:109]
	v_pk_mul_f32 v[110:111], v[24:25], v[116:117]
	v_pk_add_f32 v[112:113], v[48:49], v[112:113]
	v_pk_fma_f32 v[82:83], v[26:27], v[70:71], v[82:83]
	v_pk_fma_f32 v[106:107], v[8:9], v[148:149], v[106:107]
	v_pk_fma_f32 v[110:111], v[12:13], v[170:171], v[110:111]
	v_pk_mul_f32 v[108:109], v[108:109], v[112:113]
	global_store_dwordx2 v[142:143], v[80:81], off
	v_pk_mul_f32 v[80:81], v[16:17], v[124:125]
	v_pk_add_f32 v[82:83], v[40:41], v[82:83]
	v_pk_fma_f32 v[106:107], v[32:33], v[68:69], v[106:107]
	v_pk_fma_f32 v[110:111], v[38:39], v[64:65], v[110:111]
	s_waitcnt lgkmcnt(0)
; #define LAS __attribute__((address_space(3)))
; __device__ __forceinline__ unsigned pk2(float lo, float hi) { return f2bf(lo) | (f2bf(hi) << 16); }
; __device__ __forceinline__ void ph_post_hyena(CArgs& a, int l, LAS unsigned char* lds, int bid, int nblk) {
;     ...
;         for (int tt = 0; tt < 8; ++tt) {
;             const f32x4 u0 = w0[0] * x0[tt] + w0[1] * x0[tt + 1] + w0[2] * x0[tt + 2] + b0;
;             const f32x4 xx = wx[0] * x1[tt] + wx[1] * x1[tt + 1] + wx[2] * x1[tt + 2] + bx, v2 = wv[0] * vv[tt] + wv[1] * vv[tt + 1] + wv[2] * vv[tt + 2] + bv, z = xx * v2;
;             const f32x4 y = *(const LAS f32x4*)(yt + (tg * 8 + tt) * 260 + c4);
;             const f32x4 o = (y + z * hd) * u0;
;             u32x2 oo; oo.x = pk2(o[0], o[1]); oo.y = pk2(o[2], o[3]); *(u32x2*)(YMIX + (size_t)(c.row0 + tg * 8 + tt) * D + c4) = oo;
;         }
;         __syncthreads();
	v_pk_fma_f32 v[90:91], v[52:53], v[108:109], v[90:91]
	v_pk_fma_f32 v[80:81], v[4:5], v[128:129], v[80:81]
	v_pk_add_f32 v[106:107], v[46:47], v[106:107]
	v_pk_add_f32 v[110:111], v[50:51], v[110:111]
	v_pk_mul_f32 v[82:83], v[82:83], v[90:91]
	v_pk_fma_f32 v[80:81], v[28:29], v[72:73], v[80:81]
	v_pk_mul_f32 v[106:107], v[106:107], v[110:111]
	v_pk_add_f32 v[80:81], v[42:43], v[80:81]
	v_pk_fma_f32 v[92:93], v[54:55], v[106:107], v[92:93]
	v_pk_mul_f32 v[80:81], v[80:81], v[92:93]
	v_cvt_pk_bf16_f32 v82, v82, v83
	v_cvt_pk_bf16_f32 v83, v80, v81
	global_store_dwordx2 v[142:143], v[82:83], off offset:2048
	v_pk_mul_f32 v[80:81], v[16:17], v[72:73]
	v_pk_mul_f32 v[82:83], v[14:15], v[70:71]
	v_pk_fma_f32 v[80:81], v[4:5], v[124:125], v[80:81]
	v_pk_fma_f32 v[82:83], v[2:3], v[122:123], v[82:83]
	v_pk_fma_f32 v[80:81], v[28:29], v[88:89], v[80:81]
	v_pk_fma_f32 v[82:83], v[26:27], v[84:85], v[82:83]
	v_pk_add_f32 v[108:109], v[42:43], v[80:81]
	v_pk_add_f32 v[106:107], v[40:41], v[82:83]
	v_pk_mul_f32 v[80:81], v[20:21], v[68:69]
	v_pk_mul_f32 v[82:83], v[18:19], v[66:67]
	v_pk_fma_f32 v[80:81], v[8:9], v[120:121], v[80:81]
	v_pk_fma_f32 v[82:83], v[6:7], v[118:119], v[82:83]
	v_pk_fma_f32 v[80:81], v[32:33], v[86:87], v[80:81]
	v_pk_fma_f32 v[82:83], v[30:31], v[76:77], v[82:83]
	v_pk_add_f32 v[92:93], v[46:47], v[80:81]
	v_pk_add_f32 v[90:91], v[44:45], v[82:83]
	v_pk_mul_f32 v[80:81], v[24:25], v[64:65]
	v_pk_mul_f32 v[82:83], v[22:23], v[62:63]
	v_pk_fma_f32 v[80:81], v[12:13], v[116:117], v[80:81]
	v_pk_fma_f32 v[82:83], v[10:11], v[114:115], v[82:83]
	v_pk_fma_f32 v[110:111], v[38:39], v[78:79], v[80:81]
	v_pk_fma_f32 v[80:81], v[36:37], v[74:75], v[82:83]
	v_pk_add_f32 v[110:111], v[50:51], v[110:111]
	v_pk_add_f32 v[112:113], v[48:49], v[80:81]
	ds_read_b128 v[80:83], v202 offset:6240
	v_pk_mul_f32 v[112:113], v[90:91], v[112:113]
	v_pk_mul_f32 v[110:111], v[92:93], v[110:111]
	ds_read_b128 v[90:93], v203
	v_add_co_u32_e32 v60, vcc, s6, v60
	s_waitcnt lgkmcnt(1)
	v_pk_fma_f32 v[80:81], v[52:53], v[112:113], v[80:81]
	v_pk_fma_f32 v[82:83], v[54:55], v[110:111], v[82:83]
	v_pk_mul_f32 v[80:81], v[106:107], v[80:81]
	v_pk_mul_f32 v[82:83], v[108:109], v[82:83]
	v_bfe_u32 v106, v80, 16, 1
	v_add3_u32 v80, v80, v106, s81
	v_bfe_u32 v106, v81, 16, 1
	v_lshrrev_b32_e32 v80, 16, v80
	v_add3_u32 v81, v81, v106, s81
	v_and_or_b32 v80, v81, s80, v80
	v_pk_mul_f32 v[76:77], v[18:19], v[76:77]
	v_pk_mul_f32 v[74:75], v[22:23], v[74:75]
	v_cvt_pk_bf16_f32 v81, v82, v83
	v_addc_co_u32_e32 v61, vcc, 0, v61, vcc
	v_pk_fma_f32 v[66:67], v[6:7], v[66:67], v[76:77]
	v_pk_fma_f32 v[62:63], v[10:11], v[62:63], v[74:75]
	global_store_dwordx2 v[60:61], v[80:81], off
	v_pk_mul_f32 v[80:81], v[16:17], v[88:89]
	v_pk_mul_f32 v[82:83], v[14:15], v[84:85]
	v_pk_fma_f32 v[66:67], v[30:31], v[94:95], v[66:67]
	v_pk_fma_f32 v[62:63], v[36:37], v[96:97], v[62:63]
	v_pk_fma_f32 v[70:71], v[2:3], v[70:71], v[82:83]
	v_pk_fma_f32 v[72:73], v[4:5], v[72:73], v[80:81]
	v_pk_mul_f32 v[80:81], v[20:21], v[86:87]
	v_pk_add_f32 v[66:67], v[44:45], v[66:67]
	v_pk_mul_f32 v[76:77], v[24:25], v[78:79]
	v_pk_add_f32 v[62:63], v[48:49], v[62:63]
	v_pk_fma_f32 v[70:71], v[26:27], v[98:99], v[70:71]
	v_pk_fma_f32 v[68:69], v[8:9], v[68:69], v[80:81]
	v_pk_fma_f32 v[64:65], v[12:13], v[64:65], v[76:77]
	v_pk_mul_f32 v[62:63], v[66:67], v[62:63]
	v_pk_add_f32 v[70:71], v[40:41], v[70:71]
	v_pk_fma_f32 v[68:69], v[32:33], v[100:101], v[68:69]
	v_pk_fma_f32 v[64:65], v[38:39], v[104:105], v[64:65]
	s_waitcnt lgkmcnt(0)
	v_pk_fma_f32 v[62:63], v[52:53], v[62:63], v[90:91]
	v_pk_add_f32 v[68:69], v[46:47], v[68:69]
	v_pk_add_f32 v[64:65], v[50:51], v[64:65]
	v_pk_mul_f32 v[62:63], v[70:71], v[62:63]
	v_pk_fma_f32 v[72:73], v[28:29], v[102:103], v[72:73]
	v_pk_mul_f32 v[64:65], v[68:69], v[64:65]
	v_bfe_u32 v66, v62, 16, 1
	v_pk_add_f32 v[72:73], v[42:43], v[72:73]
	v_pk_fma_f32 v[64:65], v[54:55], v[64:65], v[92:93]
	v_add3_u32 v62, v62, v66, s81
	v_bfe_u32 v66, v63, 16, 1
	v_pk_mul_f32 v[64:65], v[72:73], v[64:65]
	v_lshrrev_b32_e32 v62, 16, v62
	v_add3_u32 v63, v63, v66, s81
	v_and_or_b32 v62, v63, s80, v62
	v_bfe_u32 v63, v64, 16, 1
	v_add3_u32 v63, v64, v63, s81
	v_bfe_u32 v64, v65, 16, 1
	v_readlane_b32 s6, v252, 57
	v_lshrrev_b32_e32 v63, 16, v63
	v_add3_u32 v64, v65, v64, s81
	s_add_i32 s1, s1, s6
	v_and_or_b32 v63, v64, s80, v63
	s_cmpk_lt_i32 s0, 0x240
	global_store_dwordx2 v[60:61], v[62:63], off offset:2048
	s_barrier
	s_cbranch_scc0 .LBB0_2759

; #define LAS __attribute__((address_space(3)))
; __device__ __forceinline__ float lo_bf(unsigned w) { return __uint_as_float(w << 16); }
; __device__ __forceinline__ float hi_bf(unsigned w) { return __uint_as_float(w & 0xffff0000u); }
; __device__ __forceinline__ void ph_ln1_route(CArgs& a, int l, LAS unsigned char* lds, int bid, int nblk) {
;     ...
;             const int row = base + 2 * w + t;
;             f32x4 v[4]; float s = 0.f;
; #pragma unroll
;             for (int j = 0; j < 4; ++j) { const int c0 = j * 256 + 4 * lane; const f32x4 g1 = *(const LAS f32x4*)(mods + c0);
;                 const f32x4 xin = (l == 0) ? __builtin_bit_cast(f32x4, xw[t][j]) : (f32x4){lo_bf(xw[t][j].x), hi_bf(xw[t][j].x), lo_bf(xw[t][j].y), hi_bf(xw[t][j].y)};
;                 v[j] = DN_ALPHA * xin + g1 * (f32x4){lo_bf(tv[t][j].x), hi_bf(tv[t][j].x), lo_bf(tv[t][j].y), hi_bf(tv[t][j].y)}; s += (v[j][0] + v[j][1]) + (v[j][2] + v[j][3]); }
;             const float mean = wave_sum(s) * (1.f / D); float s2 = 0.f;
; #pragma unroll
;             for (int j = 0; j < 4; ++j) { v[j] = v[j] - mean; s2 += (v[j][0] * v[j][0] + v[j][1] * v[j][1]) + (v[j][2] * v[j][2] + v[j][3] * v[j][3]); }
;             const float rstd = rsqrtf(wave_sum(s2) * (1.f / D) + LN_EPS);
.LBB0_2926:
	s_waitcnt vmcnt(0)
	v_add_u32_e32 v34, 0, v149
	v_add_u32_e32 v101, 0x1c200, v34
	ds_read_b128 v[102:105], v101
	s_waitcnt vmcnt(28)
	v_lshlrev_b32_e32 v34, 16, v14
	v_and_b32_e32 v100, 0xffff0000, v14
	v_lshlrev_b32_e32 v106, 16, v15
	v_and_b32_e32 v107, 0xffff0000, v15
	s_waitcnt vmcnt(24)
	v_lshlrev_b32_e32 v140, 16, v112
	v_and_b32_e32 v141, 0xffff0000, v112
	v_lshlrev_b32_e32 v142, 16, v113
	v_and_b32_e32 v143, 0xffff0000, v113
	v_cndmask_b32_e64 v107, v107, v17, s[42:43]
	v_cndmask_b32_e64 v106, v106, v16, s[42:43]
	v_cndmask_b32_e64 v139, v100, v15, s[42:43]
	s_waitcnt lgkmcnt(0)
	v_cndmask_b32_e64 v138, v34, v14, s[42:43]
	s_waitcnt lgkmcnt(0)
	v_pk_mul_f32 v[104:105], v[104:105], v[142:143]
	v_pk_mul_f32 v[102:103], v[102:103], v[140:141]
	s_mov_b32 s56, 0x3fd744fd
	v_pk_fma_f32 v[140:141], v[138:139], s[56:57], v[102:103] op_sel_hi:[1,0,1]
	v_pk_fma_f32 v[142:143], v[106:107], s[56:57], v[104:105] op_sel_hi:[1,0,1]
	v_mov_b32_e32 v104, v140
	v_pk_mov_b32 v[102:103], v[140:141], v[142:143] op_sel:[1,0]
	v_mov_b32_e32 v105, v143
	v_pk_add_f32 v[102:103], v[102:103], v[104:105]
	v_and_b32_e32 v138, 0xffff0000, v2
	v_add_f32_e32 v34, v102, v103
	ds_read_b128 v[102:105], v101 offset:1024
	v_add_f32_e32 v182, 0, v34
	v_lshlrev_b32_e32 v34, 16, v2
	v_lshlrev_b32_e32 v106, 16, v3
	v_and_b32_e32 v107, 0xffff0000, v3
	s_waitcnt vmcnt(23)
	v_lshlrev_b32_e32 v144, 16, v114
	v_and_b32_e32 v145, 0xffff0000, v114
	v_lshlrev_b32_e32 v146, 16, v115
	v_and_b32_e32 v147, 0xffff0000, v115
	v_cndmask_b32_e64 v107, v107, v5, s[42:43]
	v_cndmask_b32_e64 v106, v106, v4, s[42:43]
	v_cndmask_b32_e64 v139, v138, v3, s[42:43]
	v_cndmask_b32_e64 v138, v34, v2, s[42:43]
	s_waitcnt lgkmcnt(0)
	v_pk_mul_f32 v[104:105], v[104:105], v[146:147]
	v_pk_mul_f32 v[102:103], v[102:103], v[144:145]
	v_pk_fma_f32 v[146:147], v[106:107], s[56:57], v[104:105] op_sel_hi:[1,0,1]
	v_pk_fma_f32 v[144:145], v[138:139], s[56:57], v[102:103] op_sel_hi:[1,0,1]
	v_mov_b32_e32 v105, v147
	v_pk_mov_b32 v[102:103], v[144:145], v[146:147] op_sel:[1,0]
	v_mov_b32_e32 v104, v144
	v_pk_add_f32 v[102:103], v[102:103], v[104:105]
	v_lshlrev_b32_e32 v34, 16, v6
	v_pk_add_f32 v[184:185], v[102:103], v[102:103] op_sel:[0,1] op_sel_hi:[1,0]
	ds_read_b128 v[102:105], v101 offset:2048
	v_and_b32_e32 v106, 0xffff0000, v6
	v_lshlrev_b32_e32 v181, 16, v7
	v_and_b32_e32 v107, 0xffff0000, v7
	s_waitcnt vmcnt(22)
	v_lshlrev_b32_e32 v186, 16, v116
	v_and_b32_e32 v187, 0xffff0000, v116
	v_lshlrev_b32_e32 v188, 16, v117
	v_and_b32_e32 v189, 0xffff0000, v117
	v_cndmask_b32_e64 v139, v106, v7, s[42:43]
	v_cndmask_b32_e64 v138, v34, v6, s[42:43]
	v_cndmask_b32_e64 v107, v107, v9, s[42:43]
	v_cndmask_b32_e64 v106, v181, v8, s[42:43]
	s_waitcnt lgkmcnt(0)
	v_pk_mul_f32 v[104:105], v[104:105], v[188:189]
	v_pk_mul_f32 v[102:103], v[102:103], v[186:187]
	v_pk_fma_f32 v[106:107], v[106:107], s[56:57], v[104:105] op_sel_hi:[1,0,1]
	v_pk_fma_f32 v[138:139], v[138:139], s[56:57], v[102:103] op_sel_hi:[1,0,1]
	ds_read_b128 v[102:105], v101 offset:3072
	v_lshlrev_b32_e32 v34, 16, v10
	v_and_b32_e32 v181, 0xffff0000, v10
	v_lshlrev_b32_e32 v183, 16, v11
	v_and_b32_e32 v185, 0xffff0000, v11
	s_waitcnt vmcnt(21)
	v_lshlrev_b32_e32 v206, 16, v118
	v_and_b32_e32 v207, 0xffff0000, v118
	v_lshlrev_b32_e32 v208, 16, v119
	v_and_b32_e32 v209, 0xffff0000, v119
	v_cndmask_b32_e64 v203, v181, v11, s[42:43]
	v_cndmask_b32_e64 v202, v34, v10, s[42:43]
	v_cndmask_b32_e64 v205, v185, v13, s[42:43]
	v_cndmask_b32_e64 v204, v183, v12, s[42:43]
	s_waitcnt lgkmcnt(0)
	v_pk_mul_f32 v[104:105], v[104:105], v[208:209]
	v_pk_mul_f32 v[206:207], v[102:103], v[206:207]
	v_pk_fma_f32 v[102:103], v[204:205], s[56:57], v[104:105] op_sel_hi:[1,0,1]
	v_pk_fma_f32 v[104:105], v[202:203], s[56:57], v[206:207] op_sel_hi:[1,0,1]
	v_add_f32_e32 v186, v138, v139
	v_add_f32_e32 v188, v106, v107
	v_mov_b32_e32 v183, v104
	v_mov_b32_e32 v185, v105
	v_mov_b32_e32 v187, v102
	v_mov_b32_e32 v189, v103
	v_pk_add_f32 v[182:183], v[182:183], v[184:185]
	v_pk_add_f32 v[184:185], v[186:187], v[188:189]
	s_add_i32 s34, s8, s10
	v_pk_add_f32 v[182:183], v[182:183], v[184:185]
	s_ashr_i32 s35, s34, 31
	v_add_f32_e32 v34, v182, v183
	s_mov_b32 s54, 0x800000
	s_add_i32 s8, s8, s36
	v_add_f32_dpp v34, v34, v34 quad_perm:[1,0,3,2] row_mask:0xf bank_mask:0xf bound_ctrl:1
	v_mov_b32_e32 v100, 0
	s_nop 0
	v_add_f32_dpp v34, v34, v34 quad_perm:[2,3,0,1] row_mask:0xf bank_mask:0xf bound_ctrl:1
	s_nop 1
	v_add_f32_dpp v34, v34, v34 row_half_mirror row_mask:0xf bank_mask:0xf bound_ctrl:1
	s_nop 1
	v_add_f32_dpp v34, v34, v34 row_mirror row_mask:0xf bank_mask:0xf bound_ctrl:1
	s_nop 0
	v_readlane_b32 s17, v34, 16
	v_readlane_b32 s20, v34, 48
	v_readlane_b32 s18, v34, 0
	v_readlane_b32 s19, v34, 32
	v_mov_b32_e32 v182, s17
	v_mov_b32_e32 v183, s20
	v_pk_add_f32 v[182:183], s[18:19], v[182:183]
	s_nop 0
	v_add_f32_e32 v181, v182, v183
	v_fmamk_f32 v141, v181, 0xba800000, v141
	v_fmac_f32_e32 v140, 0xba800000, v181
	v_fmamk_f32 v143, v181, 0xba800000, v143
	v_fmac_f32_e32 v142, 0xba800000, v181
	v_pk_mul_f32 v[182:183], v[142:143], v[142:143]
	v_pk_mul_f32 v[184:185], v[140:141], v[140:141]
	v_fmamk_f32 v145, v181, 0xba800000, v145
	v_pk_mov_b32 v[186:187], v[184:185], v[182:183] op_sel:[1,0]
	v_mov_b32_e32 v185, v183
	v_fmac_f32_e32 v144, 0xba800000, v181
	v_fmamk_f32 v147, v181, 0xba800000, v147
	v_fmac_f32_e32 v146, 0xba800000, v181
	v_pk_add_f32 v[182:183], v[186:187], v[184:185]
	v_pk_mul_f32 v[184:185], v[146:147], v[146:147]
	v_pk_mul_f32 v[186:187], v[144:145], v[144:145]
	v_fmac_f32_e32 v138, 0xba800000, v181
	v_pk_mov_b32 v[188:189], v[186:187], v[184:185] op_sel:[1,0]
; #define LAS __attribute__((address_space(3)))
; __device__ __forceinline__ unsigned pk2(float lo, float hi) { return f2bf(lo) | (f2bf(hi) << 16); }
; __device__ __forceinline__ unsigned pk4_fp8(float a, float b, float c, float d) { int r = __builtin_amdgcn_cvt_pk_fp8_f32(a, b, 0, false); return (unsigned)__builtin_amdgcn_cvt_pk_fp8_f32(c, d, r, true); }
; __device__ __forceinline__ void ph_ln1_route(CArgs& a, int l, LAS unsigned char* lds, int bid, int nblk) {
;     ...
;             const float mean = wave_sum(s) * (1.f / D); float s2 = 0.f;
; #pragma unroll
;             for (int j = 0; j < 4; ++j) { v[j] = v[j] - mean; s2 += (v[j][0] * v[j][0] + v[j][1] * v[j][1]) + (v[j][2] * v[j][2] + v[j][3] * v[j][3]); }
;             const float rstd = rsqrtf(wave_sum(s2) * (1.f / D) + LN_EPS);
; #pragma unroll
;             for (int j = 0; j < 4; ++j) { const int c0 = j * 256 + 4 * lane; const f32x4 g = *(const LAS f32x4*)(lgb + c0), bb = *(const LAS f32x4*)(lgb + 1024 + c0), sh = *(const LAS f32x4*)(mods + 1024 + c0), sc = *(const LAS f32x4*)(mods + 2048 + c0);
;                 const f32x4 xn = v[j] * rstd * g + bb; *(u32x2*)(X + (size_t)row * D + c0) = (u32x2){pk2(xn[0], xn[1]), pk2(xn[2], xn[3])};
;                 const f32x4 hh = xn * (1.f + sc) + sh;
;                 *(unsigned*)(a.ws + WS_HB8 + (size_t)row * D + c0) = pk4_fp8(4.f * hh[0], 4.f * hh[1], 4.f * hh[2], 4.f * hh[3]);
;                 *(LAS f32x4*)(hrow + (2 * w + t) * 1028 + c0) = hh; }
	v_mov_b32_e32 v187, v185
	v_fmamk_f32 v139, v181, 0xba800000, v139
	v_fmac_f32_e32 v106, 0xba800000, v181
	v_mul_f32_e32 v34, v138, v138
	v_pk_add_f32 v[184:185], v[188:189], v[186:187]
	v_fmamk_f32 v107, v181, 0xba800000, v107
	v_pk_fma_f32 v[186:187], v[138:139], v[138:139], v[34:35] op_sel_hi:[1,1,0]
	v_mul_f32_e32 v34, v106, v106
	v_pk_add_f32 v[182:183], v[182:183], v[182:183] op_sel_hi:[0,1]
	v_pk_add_f32 v[184:185], v[184:185], v[184:185] op_sel_hi:[0,1]
	v_pk_fma_f32 v[188:189], v[106:107], v[106:107], v[34:35] op_sel_hi:[1,1,0]
	v_fmamk_f32 v103, v181, 0xba800000, v103
	v_fmac_f32_e32 v102, 0xba800000, v181
	v_fmamk_f32 v105, v181, 0xba800000, v105
	v_fmac_f32_e32 v104, 0xba800000, v181
	v_mul_f32_e32 v186, v104, v104
	v_mul_f32_e32 v188, v105, v105
	v_mul_f32_e32 v182, v102, v102
	v_mul_f32_e32 v184, v103, v103
	v_pk_add_f32 v[186:187], v[186:187], v[188:189]
	v_pk_add_f32 v[182:183], v[182:183], v[184:185]
	s_nop 0
	v_pk_add_f32 v[182:183], v[186:187], v[182:183]
	s_nop 0
	v_add_f32_e32 v34, v182, v183
	s_nop 1
	v_add_f32_dpp v34, v34, v34 quad_perm:[1,0,3,2] row_mask:0xf bank_mask:0xf bound_ctrl:1
	s_nop 1
	v_add_f32_dpp v34, v34, v34 quad_perm:[2,3,0,1] row_mask:0xf bank_mask:0xf bound_ctrl:1
	s_nop 1
	v_add_f32_dpp v34, v34, v34 row_half_mirror row_mask:0xf bank_mask:0xf bound_ctrl:1
	s_nop 1
	v_add_f32_dpp v34, v34, v34 row_mirror row_mask:0xf bank_mask:0xf bound_ctrl:1
	s_nop 0
	v_readlane_b32 s17, v34, 16
	v_readlane_b32 s20, v34, 48
	v_readlane_b32 s18, v34, 0
	v_readlane_b32 s19, v34, 32
	v_mov_b32_e32 v182, s17
	v_mov_b32_e32 v183, s20
	v_pk_add_f32 v[182:183], s[18:19], v[182:183]
	s_lshl_b64 s[18:19], s[34:35], 10
	v_add_f32_e32 v34, v182, v183
	v_fmamk_f32 v34, v34, 0x3a800000, v190
	v_cmp_gt_f32_e32 vcc, s21, v34
	v_mul_f32_e32 v181, 0x4b800000, v34
	ds_read_b128 v[182:185], v154
	ds_read_b128 v[186:189], v155
	ds_read_b128 v[202:205], v156
	ds_read_b128 v[206:209], v157
	v_cndmask_b32_e32 v34, v34, v181, vcc
	v_rsq_f32_e32 v34, v34
	s_lshl_b64 s[20:21], s[34:35], 11
	v_mul_f32_e32 v181, 0x45800000, v34
	v_cndmask_b32_e32 v34, v34, v181, vcc
	v_pk_mul_f32 v[140:141], v[140:141], v[34:35] op_sel_hi:[1,0]
	v_pk_mul_f32 v[142:143], v[142:143], v[34:35] op_sel_hi:[1,0]
	s_waitcnt lgkmcnt(2)
	v_pk_fma_f32 v[182:183], v[182:183], v[140:141], v[186:187]
	v_pk_fma_f32 v[142:143], v[184:185], v[142:143], v[188:189]
	v_cvt_pk_bf16_f32 v184, v182, v183
	v_cvt_pk_bf16_f32 v185, v142, v143
	v_lshl_add_u64 v[140:141], v[122:123], 0, s[20:21]
	s_waitcnt lgkmcnt(0)
	v_pk_add_f32 v[186:187], v[206:207], 1.0 op_sel_hi:[1,0]
	global_store_dwordx2 v[140:141], v[184:185], off
	v_pk_add_f32 v[184:185], v[208:209], 1.0 op_sel_hi:[1,0]
	v_pk_fma_f32 v[182:183], v[186:187], v[182:183], v[202:203]
	v_pk_fma_f32 v[184:185], v[184:185], v[142:143], v[204:205]
	v_mul_f32_e32 v142, 4.0, v182
	v_mul_f32_e32 v143, 4.0, v183
	v_mov_b32_e32 v187, v35
	v_cvt_pk_fp8_f32 v187, v142, v143
	v_mul_f32_e32 v181, 4.0, v184
	v_mul_f32_e32 v186, 4.0, v185
	v_lshl_add_u64 v[142:143], v[128:129], 0, s[18:19]
	v_cvt_pk_fp8_f32 v187, v181, v186 op_sel:[0,0,1]
	ds_write_b128 v158, v[182:185]
	v_pk_mul_f32 v[144:145], v[144:145], v[34:35] op_sel_hi:[1,0]
	v_pk_mul_f32 v[146:147], v[146:147], v[34:35] op_sel_hi:[1,0]
	global_store_dword v[142:143], v187, off
	ds_read_b128 v[182:185], v159
	ds_read_b128 v[186:189], v160
	ds_read_b128 v[202:205], v161
	ds_read_b128 v[206:209], v162
	v_pk_mul_f32 v[138:139], v[138:139], v[34:35] op_sel_hi:[1,0]
	v_pk_mul_f32 v[106:107], v[106:107], v[34:35] op_sel_hi:[1,0]
	s_waitcnt lgkmcnt(2)
	v_pk_fma_f32 v[144:145], v[182:183], v[144:145], v[186:187]
	v_pk_fma_f32 v[146:147], v[184:185], v[146:147], v[188:189]
	v_cvt_pk_bf16_f32 v182, v144, v145
	v_cvt_pk_bf16_f32 v183, v146, v147
	s_waitcnt lgkmcnt(0)
	v_pk_add_f32 v[184:185], v[206:207], 1.0 op_sel_hi:[1,0]
	global_store_dwordx2 v[140:141], v[182:183], off offset:512
	v_pk_add_f32 v[182:183], v[208:209], 1.0 op_sel_hi:[1,0]
	v_pk_fma_f32 v[144:145], v[144:145], v[184:185], v[202:203]
	v_pk_fma_f32 v[146:147], v[146:147], v[182:183], v[204:205]
	v_mul_f32_e32 v181, 4.0, v144
	v_mul_f32_e32 v182, 4.0, v145
	v_mov_b32_e32 v185, v35
	v_cvt_pk_fp8_f32 v185, v181, v182
	v_mul_f32_e32 v183, 4.0, v146
	v_mul_f32_e32 v184, 4.0, v147
	ds_write_b128 v158, v[144:147] offset:1024
	v_cvt_pk_fp8_f32 v185, v183, v184 op_sel:[0,0,1]
	v_mov_b32_e32 v181, v35
	v_pk_mul_f32 v[104:105], v[104:105], v[34:35] op_sel_hi:[1,0]
	v_pk_mul_f32 v[102:103], v[102:103], v[34:35] op_sel_hi:[1,0]
	global_store_dword v[142:143], v185, off offset:256
	ds_read_b128 v[144:147], v163
	ds_read_b128 v[182:185], v170
	ds_read_b128 v[186:189], v171
	ds_read_b128 v[202:205], v172
	s_waitcnt vmcnt(21)
	v_lshlrev_b32_e32 v206, 16, v136
	v_and_b32_e32 v207, 0xffff0000, v136
	s_waitcnt lgkmcnt(2)
	v_pk_fma_f32 v[138:139], v[138:139], v[144:145], v[182:183]
	v_pk_fma_f32 v[106:107], v[106:107], v[146:147], v[184:185]
	v_cvt_pk_bf16_f32 v144, v138, v139
	v_cvt_pk_bf16_f32 v145, v106, v107
	global_store_dwordx2 v[140:141], v[144:145], off offset:1024
	s_waitcnt lgkmcnt(0)
	v_pk_add_f32 v[144:145], v[204:205], 1.0 op_sel_hi:[1,0]
	v_pk_add_f32 v[182:183], v[202:203], 1.0 op_sel_hi:[1,0]
	v_pk_fma_f32 v[146:147], v[106:107], v[144:145], v[188:189]
	v_pk_fma_f32 v[144:145], v[138:139], v[182:183], v[186:187]
	v_mul_f32_e32 v138, 4.0, v146
	v_mul_f32_e32 v106, 4.0, v144
	v_mul_f32_e32 v107, 4.0, v145
	v_cvt_pk_fp8_f32 v181, v106, v107
	v_mul_f32_e32 v139, 4.0, v147
	ds_write_b128 v158, v[144:147] offset:2048
	v_lshlrev_b32_e32 v208, 16, v137
	v_cvt_pk_fp8_f32 v181, v138, v139 op_sel:[0,0,1]
	v_and_b32_e32 v209, 0xffff0000, v137
	global_store_dword v[142:143], v181, off offset:512
	ds_read_b128 v[144:147], v173
	ds_read_b128 v[182:185], v174
	ds_read_b128 v[186:189], v175
	ds_read_b128 v[202:205], v176
	v_lshlrev_b32_e32 v181, 16, v93
	s_waitcnt lgkmcnt(2)
; #define LAS __attribute__((address_space(3)))
; __device__ __forceinline__ unsigned pk2(float lo, float hi) { return f2bf(lo) | (f2bf(hi) << 16); }
; __device__ __forceinline__ unsigned pk4_fp8(float a, float b, float c, float d) { int r = __builtin_amdgcn_cvt_pk_fp8_f32(a, b, 0, false); return (unsigned)__builtin_amdgcn_cvt_pk_fp8_f32(c, d, r, true); }
; __device__ __forceinline__ float lo_bf(unsigned w) { return __uint_as_float(w << 16); }
; __device__ __forceinline__ float hi_bf(unsigned w) { return __uint_as_float(w & 0xffff0000u); }
; __device__ __forceinline__ void ph_ln1_route(CArgs& a, int l, LAS unsigned char* lds, int bid, int nblk) {
;     ...
;             const int row = base + 2 * w + t;
;             f32x4 v[4]; float s = 0.f;
; #pragma unroll
;             for (int j = 0; j < 4; ++j) { const int c0 = j * 256 + 4 * lane; const f32x4 g1 = *(const LAS f32x4*)(mods + c0);
;                 const f32x4 xin = (l == 0) ? __builtin_bit_cast(f32x4, xw[t][j]) : (f32x4){lo_bf(xw[t][j].x), hi_bf(xw[t][j].x), lo_bf(xw[t][j].y), hi_bf(xw[t][j].y)};
;                 v[j] = DN_ALPHA * xin + g1 * (f32x4){lo_bf(tv[t][j].x), hi_bf(tv[t][j].x), lo_bf(tv[t][j].y), hi_bf(tv[t][j].y)}; s += (v[j][0] + v[j][1]) + (v[j][2] + v[j][3]); }
;             const float mean = wave_sum(s) * (1.f / D); float s2 = 0.f;
;     ...
;             for (int j = 0; j < 4; ++j) { const int c0 = j * 256 + 4 * lane; const f32x4 g = *(const LAS f32x4*)(lgb + c0), bb = *(const LAS f32x4*)(lgb + 1024 + c0), sh = *(const LAS f32x4*)(mods + 1024 + c0), sc = *(const LAS f32x4*)(mods + 2048 + c0);
;                 const f32x4 xn = v[j] * rstd * g + bb; *(u32x2*)(X + (size_t)row * D + c0) = (u32x2){pk2(xn[0], xn[1]), pk2(xn[2], xn[3])};
;                 const f32x4 hh = xn * (1.f + sc) + sh;
;                 *(unsigned*)(a.ws + WS_HB8 + (size_t)row * D + c0) = pk4_fp8(4.f * hh[0], 4.f * hh[1], 4.f * hh[2], 4.f * hh[3]);
;                 *(LAS f32x4*)(hrow + (2 * w + t) * 1028 + c0) = hh; }
	v_pk_fma_f32 v[106:107], v[104:105], v[144:145], v[182:183]
	s_nop 0
	v_pk_fma_f32 v[102:103], v[102:103], v[146:147], v[184:185]
	v_cvt_pk_bf16_f32 v104, v106, v107
	v_cvt_pk_bf16_f32 v105, v102, v103
	global_store_dwordx2 v[140:141], v[104:105], off offset:1536
	s_waitcnt lgkmcnt(0)
	v_pk_add_f32 v[104:105], v[204:205], 1.0 op_sel_hi:[1,0]
	v_pk_add_f32 v[138:139], v[202:203], 1.0 op_sel_hi:[1,0]
	v_pk_fma_f32 v[104:105], v[102:103], v[104:105], v[188:189]
	v_pk_fma_f32 v[102:103], v[106:107], v[138:139], v[186:187]
	v_mov_b32_e32 v139, v35
	v_mul_f32_e32 v34, 4.0, v102
	v_mul_f32_e32 v106, 4.0, v103
	v_cvt_pk_fp8_f32 v139, v34, v106
	v_mul_f32_e32 v107, 4.0, v104
	v_mul_f32_e32 v138, 4.0, v105
	ds_write_b128 v158, v[102:105] offset:3072
	v_cvt_pk_fp8_f32 v139, v107, v138 op_sel:[0,0,1]
	ds_read_b128 v[102:105], v101
	v_lshlrev_b32_e32 v34, 16, v30
	v_and_b32_e32 v138, 0xffff0000, v30
	global_store_dword v[142:143], v139, off offset:768
	v_lshlrev_b32_e32 v106, 16, v31
	v_and_b32_e32 v107, 0xffff0000, v31
	v_lshlrev_b32_e32 v140, 16, v130
	v_and_b32_e32 v141, 0xffff0000, v130
	v_lshlrev_b32_e32 v142, 16, v131
	v_and_b32_e32 v143, 0xffff0000, v131
	v_cndmask_b32_e64 v107, v107, v33, s[42:43]
	v_cndmask_b32_e64 v106, v106, v32, s[42:43]
	v_cndmask_b32_e64 v139, v138, v31, s[42:43]
	v_cndmask_b32_e64 v138, v34, v30, s[42:43]
	s_waitcnt lgkmcnt(0)
	v_pk_mul_f32 v[104:105], v[104:105], v[142:143]
	v_pk_mul_f32 v[102:103], v[102:103], v[140:141]
	v_pk_fma_f32 v[142:143], v[106:107], s[56:57], v[104:105] op_sel_hi:[1,0,1]
	v_pk_fma_f32 v[140:141], v[138:139], s[56:57], v[102:103] op_sel_hi:[1,0,1]
	v_mov_b32_e32 v105, v143
	v_pk_mov_b32 v[102:103], v[140:141], v[142:143] op_sel:[1,0]
	v_mov_b32_e32 v104, v140
	v_pk_add_f32 v[102:103], v[102:103], v[104:105]
	v_and_b32_e32 v138, 0xffff0000, v64
	v_add_f32_e32 v34, v102, v103
	ds_read_b128 v[102:105], v101 offset:1024
	v_add_f32_e32 v182, 0, v34
	v_lshlrev_b32_e32 v34, 16, v64
	v_lshlrev_b32_e32 v106, 16, v65
	v_and_b32_e32 v107, 0xffff0000, v65
	v_lshlrev_b32_e32 v144, 16, v132
	v_and_b32_e32 v145, 0xffff0000, v132
	v_lshlrev_b32_e32 v146, 16, v133
	v_and_b32_e32 v147, 0xffff0000, v133
	v_cndmask_b32_e64 v107, v107, v67, s[42:43]
	v_cndmask_b32_e64 v106, v106, v66, s[42:43]
	v_cndmask_b32_e64 v139, v138, v65, s[42:43]
	v_cndmask_b32_e64 v138, v34, v64, s[42:43]
	s_waitcnt lgkmcnt(0)
	v_pk_mul_f32 v[104:105], v[104:105], v[146:147]
	v_pk_mul_f32 v[102:103], v[102:103], v[144:145]
	v_pk_fma_f32 v[146:147], v[106:107], s[56:57], v[104:105] op_sel_hi:[1,0,1]
	v_pk_fma_f32 v[144:145], v[138:139], s[56:57], v[102:103] op_sel_hi:[1,0,1]
	v_mov_b32_e32 v105, v147
	v_pk_mov_b32 v[102:103], v[144:145], v[146:147] op_sel:[1,0]
	v_mov_b32_e32 v104, v144
	v_pk_add_f32 v[102:103], v[102:103], v[104:105]
	v_lshlrev_b32_e32 v34, 16, v92
	v_pk_add_f32 v[184:185], v[102:103], v[102:103] op_sel:[0,1] op_sel_hi:[1,0]
	ds_read_b128 v[102:105], v101 offset:2048
	v_and_b32_e32 v106, 0xffff0000, v92
	v_and_b32_e32 v107, 0xffff0000, v93
	v_lshlrev_b32_e32 v186, 16, v134
	v_and_b32_e32 v187, 0xffff0000, v134
	v_lshlrev_b32_e32 v188, 16, v135
	v_and_b32_e32 v189, 0xffff0000, v135
	v_cndmask_b32_e64 v139, v106, v93, s[42:43]
	v_cndmask_b32_e64 v138, v34, v92, s[42:43]
	v_cndmask_b32_e64 v107, v107, v95, s[42:43]
	v_cndmask_b32_e64 v106, v181, v94, s[42:43]
	s_waitcnt lgkmcnt(0)
	v_pk_mul_f32 v[104:105], v[104:105], v[188:189]
	v_pk_mul_f32 v[102:103], v[102:103], v[186:187]
	v_pk_fma_f32 v[106:107], v[106:107], s[56:57], v[104:105] op_sel_hi:[1,0,1]
	v_pk_fma_f32 v[138:139], v[138:139], s[56:57], v[102:103] op_sel_hi:[1,0,1]
	ds_read_b128 v[102:105], v101 offset:3072
	v_lshlrev_b32_e32 v34, 16, v96
	v_and_b32_e32 v101, 0xffff0000, v96
	v_lshlrev_b32_e32 v181, 16, v97
	v_and_b32_e32 v183, 0xffff0000, v97
	v_cndmask_b32_e64 v203, v101, v97, s[42:43]
	v_cndmask_b32_e64 v202, v34, v96, s[42:43]
	v_cndmask_b32_e64 v205, v183, v99, s[42:43]
	v_cndmask_b32_e64 v204, v181, v98, s[42:43]
	s_waitcnt lgkmcnt(0)
	v_pk_mul_f32 v[104:105], v[104:105], v[208:209]
	v_pk_mul_f32 v[206:207], v[102:103], v[206:207]
	v_pk_fma_f32 v[102:103], v[204:205], s[56:57], v[104:105] op_sel_hi:[1,0,1]
	v_pk_fma_f32 v[104:105], v[202:203], s[56:57], v[206:207] op_sel_hi:[1,0,1]
	v_add_f32_e32 v186, v138, v139
	v_add_f32_e32 v188, v106, v107
	v_mov_b32_e32 v183, v104
	v_mov_b32_e32 v185, v105
	v_mov_b32_e32 v187, v102
	v_mov_b32_e32 v189, v103
	v_pk_add_f32 v[182:183], v[182:183], v[184:185]
	v_pk_add_f32 v[184:185], v[186:187], v[188:189]
	s_nop 0
	v_pk_add_f32 v[182:183], v[182:183], v[184:185]
	s_nop 0
	v_add_f32_e32 v34, v182, v183
	s_nop 1
	v_add_f32_dpp v34, v34, v34 quad_perm:[1,0,3,2] row_mask:0xf bank_mask:0xf bound_ctrl:1
	s_nop 1
	v_add_f32_dpp v34, v34, v34 quad_perm:[2,3,0,1] row_mask:0xf bank_mask:0xf bound_ctrl:1
	s_nop 1
	v_add_f32_dpp v34, v34, v34 row_half_mirror row_mask:0xf bank_mask:0xf bound_ctrl:1
	s_nop 1
	v_add_f32_dpp v34, v34, v34 row_mirror row_mask:0xf bank_mask:0xf bound_ctrl:1
	s_nop 0
	v_readlane_b32 s17, v34, 16
	v_readlane_b32 s20, v34, 48
	v_readlane_b32 s18, v34, 0
	v_readlane_b32 s19, v34, 32
	v_mov_b32_e32 v182, s17
	v_mov_b32_e32 v183, s20
	v_pk_add_f32 v[182:183], s[18:19], v[182:183]
	s_or_b32 s18, s34, 1
	v_add_f32_e32 v101, v182, v183
	v_fmamk_f32 v141, v101, 0xba800000, v141
	v_fmac_f32_e32 v140, 0xba800000, v101
	v_fmamk_f32 v143, v101, 0xba800000, v143
	v_fmac_f32_e32 v142, 0xba800000, v101
	v_pk_mul_f32 v[182:183], v[142:143], v[142:143]
	v_pk_mul_f32 v[184:185], v[140:141], v[140:141]
	v_fmamk_f32 v145, v101, 0xba800000, v145
	v_pk_mov_b32 v[186:187], v[184:185], v[182:183] op_sel:[1,0]
	v_mov_b32_e32 v185, v183
; #define LAS __attribute__((address_space(3)))
; __device__ __forceinline__ unsigned pk2(float lo, float hi) { return f2bf(lo) | (f2bf(hi) << 16); }
; __device__ __forceinline__ unsigned pk4_fp8(float a, float b, float c, float d) { int r = __builtin_amdgcn_cvt_pk_fp8_f32(a, b, 0, false); return (unsigned)__builtin_amdgcn_cvt_pk_fp8_f32(c, d, r, true); }
; __device__ __forceinline__ void ph_ln1_route(CArgs& a, int l, LAS unsigned char* lds, int bid, int nblk) {
;     ...
; #pragma unroll
;             for (int j = 0; j < 4; ++j) { v[j] = v[j] - mean; s2 += (v[j][0] * v[j][0] + v[j][1] * v[j][1]) + (v[j][2] * v[j][2] + v[j][3] * v[j][3]); }
;             const float rstd = rsqrtf(wave_sum(s2) * (1.f / D) + LN_EPS);
; #pragma unroll
;             for (int j = 0; j < 4; ++j) { const int c0 = j * 256 + 4 * lane; const f32x4 g = *(const LAS f32x4*)(lgb + c0), bb = *(const LAS f32x4*)(lgb + 1024 + c0), sh = *(const LAS f32x4*)(mods + 1024 + c0), sc = *(const LAS f32x4*)(mods + 2048 + c0);
;                 const f32x4 xn = v[j] * rstd * g + bb; *(u32x2*)(X + (size_t)row * D + c0) = (u32x2){pk2(xn[0], xn[1]), pk2(xn[2], xn[3])};
;                 const f32x4 hh = xn * (1.f + sc) + sh;
;                 *(unsigned*)(a.ws + WS_HB8 + (size_t)row * D + c0) = pk4_fp8(4.f * hh[0], 4.f * hh[1], 4.f * hh[2], 4.f * hh[3]);
;                 *(LAS f32x4*)(hrow + (2 * w + t) * 1028 + c0) = hh; }
	v_fmac_f32_e32 v144, 0xba800000, v101
	v_fmamk_f32 v147, v101, 0xba800000, v147
	v_fmac_f32_e32 v146, 0xba800000, v101
	v_pk_add_f32 v[182:183], v[186:187], v[184:185]
	v_pk_mul_f32 v[184:185], v[146:147], v[146:147]
	v_pk_mul_f32 v[186:187], v[144:145], v[144:145]
	v_fmac_f32_e32 v138, 0xba800000, v101
	v_pk_mov_b32 v[188:189], v[186:187], v[184:185] op_sel:[1,0]
	v_mov_b32_e32 v187, v185
	v_fmamk_f32 v139, v101, 0xba800000, v139
	v_fmac_f32_e32 v106, 0xba800000, v101
	v_mul_f32_e32 v34, v138, v138
	v_pk_add_f32 v[184:185], v[188:189], v[186:187]
	v_fmamk_f32 v107, v101, 0xba800000, v107
	v_pk_fma_f32 v[186:187], v[138:139], v[138:139], v[34:35] op_sel_hi:[1,1,0]
	v_mul_f32_e32 v34, v106, v106
	v_pk_add_f32 v[182:183], v[182:183], v[182:183] op_sel_hi:[0,1]
	v_pk_add_f32 v[184:185], v[184:185], v[184:185] op_sel_hi:[0,1]
	v_pk_fma_f32 v[188:189], v[106:107], v[106:107], v[34:35] op_sel_hi:[1,1,0]
	v_fmamk_f32 v103, v101, 0xba800000, v103
	v_fmac_f32_e32 v102, 0xba800000, v101
	v_fmamk_f32 v105, v101, 0xba800000, v105
	v_fmac_f32_e32 v104, 0xba800000, v101
	v_mul_f32_e32 v186, v104, v104
	v_mul_f32_e32 v188, v105, v105
	v_mul_f32_e32 v182, v102, v102
	v_mul_f32_e32 v184, v103, v103
	v_pk_add_f32 v[186:187], v[186:187], v[188:189]
	v_pk_add_f32 v[182:183], v[182:183], v[184:185]
	s_nop 0
	v_pk_add_f32 v[182:183], v[186:187], v[182:183]
	s_nop 0
	v_add_f32_e32 v34, v182, v183
	s_nop 1
	v_add_f32_dpp v34, v34, v34 quad_perm:[1,0,3,2] row_mask:0xf bank_mask:0xf bound_ctrl:1
	s_nop 1
	v_add_f32_dpp v34, v34, v34 quad_perm:[2,3,0,1] row_mask:0xf bank_mask:0xf bound_ctrl:1
	s_nop 1
	v_add_f32_dpp v34, v34, v34 row_half_mirror row_mask:0xf bank_mask:0xf bound_ctrl:1
	s_nop 1
	v_add_f32_dpp v34, v34, v34 row_mirror row_mask:0xf bank_mask:0xf bound_ctrl:1
	s_nop 0
	v_readlane_b32 s17, v34, 16
	v_readlane_b32 s19, v34, 48
	v_readlane_b32 s20, v34, 0
	v_readlane_b32 s21, v34, 32
	v_mov_b32_e32 v182, s17
	v_mov_b32_e32 v183, s19
	v_pk_add_f32 v[182:183], s[20:21], v[182:183]
	s_ashr_i32 s19, s18, 31
	v_add_f32_e32 v34, v182, v183
	v_fmamk_f32 v34, v34, 0x3a800000, v190
	v_cmp_gt_f32_e32 vcc, s54, v34
	v_mul_f32_e32 v101, 0x4b800000, v34
	ds_read_b128 v[182:185], v154
	ds_read_b128 v[186:189], v155
	ds_read_b128 v[202:205], v156
	ds_read_b128 v[206:209], v157
	v_cndmask_b32_e32 v34, v34, v101, vcc
	v_rsq_f32_e32 v34, v34
	s_lshl_b64 s[20:21], s[18:19], 10
	s_lshl_b64 s[18:19], s[18:19], 11
	s_cmp_lt_i32 s8, 0x9000
	v_mul_f32_e32 v101, 0x45800000, v34
	v_cndmask_b32_e32 v34, v34, v101, vcc
	v_pk_mul_f32 v[140:141], v[140:141], v[34:35] op_sel_hi:[1,0]
	v_pk_mul_f32 v[142:143], v[142:143], v[34:35] op_sel_hi:[1,0]
	s_waitcnt lgkmcnt(2)
	v_pk_fma_f32 v[140:141], v[182:183], v[140:141], v[186:187]
	v_pk_fma_f32 v[184:185], v[184:185], v[142:143], v[188:189]
	v_cvt_pk_bf16_f32 v182, v140, v141
	v_cvt_pk_bf16_f32 v183, v184, v185
	v_lshl_add_u64 v[142:143], v[122:123], 0, s[18:19]
	global_store_dwordx2 v[142:143], v[182:183], off
	s_waitcnt lgkmcnt(0)
	v_pk_add_f32 v[182:183], v[208:209], 1.0 op_sel_hi:[1,0]
	v_pk_add_f32 v[186:187], v[206:207], 1.0 op_sel_hi:[1,0]
	v_pk_fma_f32 v[184:185], v[182:183], v[184:185], v[204:205]
	v_pk_fma_f32 v[182:183], v[186:187], v[140:141], v[202:203]
	v_mov_b32_e32 v186, v35
	v_mul_f32_e32 v101, 4.0, v182
	v_mul_f32_e32 v140, 4.0, v183
	v_cvt_pk_fp8_f32 v186, v101, v140
	v_mul_f32_e32 v141, 4.0, v184
	v_mul_f32_e32 v181, 4.0, v185
	ds_write_b128 v158, v[182:185] offset:4112
	v_cvt_pk_fp8_f32 v186, v141, v181 op_sel:[0,0,1]
	v_lshl_add_u64 v[140:141], v[128:129], 0, s[20:21]
	v_pk_mul_f32 v[144:145], v[144:145], v[34:35] op_sel_hi:[1,0]
	v_pk_mul_f32 v[146:147], v[146:147], v[34:35] op_sel_hi:[1,0]
	global_store_dword v[140:141], v186, off
	ds_read_b128 v[182:185], v159
	ds_read_b128 v[186:189], v160
	ds_read_b128 v[202:205], v161
	ds_read_b128 v[206:209], v162
	v_pk_mul_f32 v[138:139], v[138:139], v[34:35] op_sel_hi:[1,0]
	v_pk_mul_f32 v[106:107], v[106:107], v[34:35] op_sel_hi:[1,0]
	s_waitcnt lgkmcnt(2)
; #define LAS __attribute__((address_space(3)))
; __device__ __forceinline__ unsigned pk2(float lo, float hi) { return f2bf(lo) | (f2bf(hi) << 16); }
; __device__ __forceinline__ unsigned pk4_fp8(float a, float b, float c, float d) { int r = __builtin_amdgcn_cvt_pk_fp8_f32(a, b, 0, false); return (unsigned)__builtin_amdgcn_cvt_pk_fp8_f32(c, d, r, true); }
; __device__ __forceinline__ void ph_ln1_route(CArgs& a, int l, LAS unsigned char* lds, int bid, int nblk) {
;     ...
;             for (int j = 0; j < 4; ++j) { const int c0 = j * 256 + 4 * lane; const f32x4 g = *(const LAS f32x4*)(lgb + c0), bb = *(const LAS f32x4*)(lgb + 1024 + c0), sh = *(const LAS f32x4*)(mods + 1024 + c0), sc = *(const LAS f32x4*)(mods + 2048 + c0);
;                 const f32x4 xn = v[j] * rstd * g + bb; *(u32x2*)(X + (size_t)row * D + c0) = (u32x2){pk2(xn[0], xn[1]), pk2(xn[2], xn[3])};
;                 const f32x4 hh = xn * (1.f + sc) + sh;
;                 *(unsigned*)(a.ws + WS_HB8 + (size_t)row * D + c0) = pk4_fp8(4.f * hh[0], 4.f * hh[1], 4.f * hh[2], 4.f * hh[3]);
;                 *(LAS f32x4*)(hrow + (2 * w + t) * 1028 + c0) = hh; }
;         }
;         __syncthreads();
;         f32x4 mnext[2] = {(f32x4){0.f, 0.f, 0.f, 0.f}, (f32x4){0.f, 0.f, 0.f, 0.f}};
;         const bool more = base + nblk * 16 < NTOK;
;         if (more) { const float* mvn = MOD + (size_t)mod_vec(base + nblk * 16) * 6144 + 2048; mnext[0] = *(const f32x4*)(mvn + 4 * tid); if (tid < 256) mnext[1] = *(const f32x4*)(mvn + 2048 + 4 * tid); }
;         if (more) LN1_FETCH(base + nblk * 16);
	v_pk_fma_f32 v[144:145], v[182:183], v[144:145], v[186:187]
	v_pk_fma_f32 v[146:147], v[184:185], v[146:147], v[188:189]
	v_cvt_pk_bf16_f32 v182, v144, v145
	s_waitcnt lgkmcnt(0)
	v_pk_add_f32 v[184:185], v[206:207], 1.0 op_sel_hi:[1,0]
	v_pk_fma_f32 v[144:145], v[144:145], v[184:185], v[202:203]
	v_cvt_pk_bf16_f32 v183, v146, v147
	v_mul_f32_e32 v101, 4.0, v144
	v_mul_f32_e32 v181, 4.0, v145
	v_mov_b32_e32 v184, v35
	v_cvt_pk_fp8_f32 v184, v101, v181
	global_store_dwordx2 v[142:143], v[182:183], off offset:512
	v_pk_add_f32 v[182:183], v[208:209], 1.0 op_sel_hi:[1,0]
	v_pk_mul_f32 v[104:105], v[104:105], v[34:35] op_sel_hi:[1,0]
	v_pk_fma_f32 v[146:147], v[146:147], v[182:183], v[204:205]
	ds_write_b128 v158, v[144:147] offset:5136
	v_mul_f32_e32 v182, 4.0, v146
	v_mul_f32_e32 v183, 4.0, v147
	v_cvt_pk_fp8_f32 v184, v182, v183 op_sel:[0,0,1]
	v_pk_mul_f32 v[102:103], v[102:103], v[34:35] op_sel_hi:[1,0]
	s_cselect_b64 s[56:57], -1, 0
	s_cmp_gt_i32 s8, 0x8fff
	global_store_dword v[140:141], v184, off offset:256
	ds_read_b128 v[144:147], v163
	ds_read_b128 v[182:185], v170
	ds_read_b128 v[186:189], v171
	ds_read_b128 v[202:205], v172
	s_cselect_b64 s[34:35], -1, 0
	s_and_b64 vcc, exec, s[34:35]
	s_waitcnt lgkmcnt(2)
	v_pk_fma_f32 v[138:139], v[138:139], v[144:145], v[182:183]
	v_pk_fma_f32 v[106:107], v[106:107], v[146:147], v[184:185]
	v_cvt_pk_bf16_f32 v144, v138, v139
	v_cvt_pk_bf16_f32 v145, v106, v107
	global_store_dwordx2 v[142:143], v[144:145], off offset:1024
	s_waitcnt lgkmcnt(0)
	v_pk_add_f32 v[144:145], v[204:205], 1.0 op_sel_hi:[1,0]
	v_pk_add_f32 v[182:183], v[202:203], 1.0 op_sel_hi:[1,0]
	v_pk_fma_f32 v[146:147], v[106:107], v[144:145], v[188:189]
	v_pk_fma_f32 v[144:145], v[138:139], v[182:183], v[186:187]
	v_mov_b32_e32 v139, v35
	v_mul_f32_e32 v101, 4.0, v144
	v_mul_f32_e32 v106, 4.0, v145
	v_cvt_pk_fp8_f32 v139, v101, v106
	v_mul_f32_e32 v107, 4.0, v146
	v_mul_f32_e32 v138, 4.0, v147
	ds_write_b128 v158, v[144:147] offset:6160
	v_cvt_pk_fp8_f32 v139, v107, v138 op_sel:[0,0,1]
	global_store_dword v[140:141], v139, off offset:512
	ds_read_b128 v[144:147], v173
	ds_read_b128 v[182:185], v174
	ds_read_b128 v[186:189], v175
	ds_read_b128 v[202:205], v176
	s_waitcnt lgkmcnt(2)
	v_pk_fma_f32 v[106:107], v[104:105], v[144:145], v[182:183]
	s_nop 0
	v_pk_fma_f32 v[102:103], v[102:103], v[146:147], v[184:185]
	v_cvt_pk_bf16_f32 v104, v106, v107
	v_cvt_pk_bf16_f32 v105, v102, v103
	global_store_dwordx2 v[142:143], v[104:105], off offset:1536
	s_waitcnt lgkmcnt(0)
	v_pk_add_f32 v[104:105], v[204:205], 1.0 op_sel_hi:[1,0]
	v_pk_add_f32 v[138:139], v[202:203], 1.0 op_sel_hi:[1,0]
	v_pk_fma_f32 v[104:105], v[102:103], v[104:105], v[188:189]
	v_pk_fma_f32 v[102:103], v[106:107], v[138:139], v[186:187]
	v_mov_b32_e32 v138, v35
	v_mul_f32_e32 v34, 4.0, v102
	v_mul_f32_e32 v101, 4.0, v103
	v_cvt_pk_fp8_f32 v138, v34, v101
	v_mul_f32_e32 v106, 4.0, v104
	v_mul_f32_e32 v107, 4.0, v105
	ds_write_b128 v158, v[102:105] offset:7184
	v_cvt_pk_fp8_f32 v138, v106, v107 op_sel:[0,0,1]
	v_mov_b32_e32 v101, 0
	v_mov_b32_e32 v102, 0
	v_mov_b32_e32 v103, 0
	v_mov_b32_e32 v104, 0
	v_mov_b32_e32 v105, 0
	v_mov_b32_e32 v106, 0
	v_mov_b32_e32 v107, 0
	global_store_dword v[140:141], v138, off offset:768
	s_waitcnt lgkmcnt(0)
	s_barrier
	s_cbranch_vccnz .LBB0_2930
	s_add_i32 s17, s8, 0xfffff000
	s_lshr_b32 s17, s17, 11
	s_cmpk_gt_i32 s8, 0xfff
	s_cselect_b32 s17, s17, 16
	s_mul_hi_u32 s19, s17, 0x6000
	s_mulk_i32 s17, 0x6000
	s_add_u32 s18, s0, s17
	s_addc_u32 s19, s1, s19
	v_lshl_add_u64 v[138:139], v[108:109], 2, s[18:19]
	v_add_co_u32_e32 v100, vcc, 0x2000, v138
	v_mov_b32_e32 v107, 0
	s_nop 0
	v_addc_co_u32_e32 v101, vcc, 0, v139, vcc
	global_load_dwordx4 v[100:103], v[100:101], off
	v_mov_b32_e32 v106, 0
	v_mov_b32_e32 v105, 0
	v_mov_b32_e32 v104, 0
	s_and_saveexec_b64 s[54:55], s[40:41]
	s_cbranch_execz .LBB0_2929
	v_add_co_u32_e32 v104, vcc, 0x4000, v138
	s_nop 1
	v_addc_co_u32_e32 v105, vcc, 0, v139, vcc
	global_load_dwordx4 v[104:107], v[104:105], off

; __device__ __forceinline__ unsigned pk2(float lo, float hi) { return f2bf(lo) | (f2bf(hi) << 16); }
; __device__ __forceinline__ void ph_ln2(CArgs& a, int l, LAS unsigned char* lds, int gw, int ngw) {
;     ...
;             for (int j = 0; j < 4; ++j) { const int c0 = j * 256 + 4 * lane;
;                 const f32x4 xn = v[j] * rstd * lgv[j] + lbv[j];
;                 if (lastl) *(f32x4*)(a.out + (size_t)(row - NTOK_C) * D + c0) = xn;
;                 else { *(u32x2*)(X + (size_t)row * D + c0) = (u32x2){pk2(xn[0], xn[1]), pk2(xn[2], xn[3])}; const f32x4 hh = xn * (1.f + scv[j]) + shv[j];
;                     u32x2 o; o.x = pk2(hh[0], hh[1]); o.y = pk2(hh[2], hh[3]); *(u32x2*)(HB + (size_t)row * D + c0) = o; } }
.LBB0_3309:
	s_andn2_b64 vcc, exec, s[28:29]
	s_cbranch_vccnz .LBB0_3311
	v_cvt_pk_bf16_f32 v140, v88, v89
	v_pk_fma_f32 v[88:89], v[114:115], v[88:89], v[64:65]
	v_cvt_pk_bf16_f32 v141, v90, v91
	v_pk_fma_f32 v[90:91], v[116:117], v[90:91], v[66:67]
	v_cvt_pk_bf16_f32 v88, v88, v89
	v_bfe_u32 v34, v90, 16, 1
	s_mov_b32 s18, 0xf6fff200
	v_add3_u32 v34, v90, v34, s81
	v_bfe_u32 v89, v91, 16, 1
	s_mov_b32 s19, -1
	v_lshrrev_b32_e32 v34, 16, v34
	v_add3_u32 v89, v91, v89, s81
	v_lshl_add_u64 v[138:139], v[100:101], 0, s[18:19]
	v_and_or_b32 v89, v89, s80, v34
	global_store_dwordx2 v[138:139], v[140:141], off
	global_store_dwordx2 v[100:101], v[88:89], off offset:-3584

; __device__ __forceinline__ unsigned pk2(float lo, float hi) { return f2bf(lo) | (f2bf(hi) << 16); }
; __device__ __forceinline__ void ph_ln2(CArgs& a, int l, LAS unsigned char* lds, int gw, int ngw) {
;     ...
;             for (int j = 0; j < 4; ++j) { const int c0 = j * 256 + 4 * lane;
;                 const f32x4 xn = v[j] * rstd * lgv[j] + lbv[j];
;                 if (lastl) *(f32x4*)(a.out + (size_t)(row - NTOK_C) * D + c0) = xn;
;                 else { *(u32x2*)(X + (size_t)row * D + c0) = (u32x2){pk2(xn[0], xn[1]), pk2(xn[2], xn[3])}; const f32x4 hh = xn * (1.f + scv[j]) + shv[j];
;                     u32x2 o; o.x = pk2(hh[0], hh[1]); o.y = pk2(hh[2], hh[3]); *(u32x2*)(HB + (size_t)row * D + c0) = o; } }
.LBB0_3313:
	s_andn2_b64 vcc, exec, s[28:29]
	s_cbranch_vccnz .LBB0_3315
	v_cvt_pk_bf16_f32 v136, v88, v89
	v_pk_fma_f32 v[88:89], v[106:107], v[88:89], v[52:53]
	v_cvt_pk_bf16_f32 v137, v90, v91
	v_pk_fma_f32 v[90:91], v[112:113], v[90:91], v[54:55]
	v_cvt_pk_bf16_f32 v88, v88, v89
	v_bfe_u32 v34, v90, 16, 1
	s_mov_b32 s18, 0xf6fff400
	v_add3_u32 v34, v90, v34, s81
	v_bfe_u32 v89, v91, 16, 1
	s_mov_b32 s19, -1
	v_lshrrev_b32_e32 v34, 16, v34
	v_add3_u32 v89, v91, v89, s81
	v_lshl_add_u64 v[132:133], v[100:101], 0, s[18:19]
	v_and_or_b32 v89, v89, s80, v34
	global_store_dwordx2 v[132:133], v[136:137], off
	global_store_dwordx2 v[100:101], v[88:89], off offset:-3072

; __device__ __forceinline__ unsigned pk2(float lo, float hi) { return f2bf(lo) | (f2bf(hi) << 16); }
; __device__ __forceinline__ void ph_ln2(CArgs& a, int l, LAS unsigned char* lds, int gw, int ngw) {
;     ...
;             for (int j = 0; j < 4; ++j) { const int c0 = j * 256 + 4 * lane;
;                 const f32x4 xn = v[j] * rstd * lgv[j] + lbv[j];
;                 if (lastl) *(f32x4*)(a.out + (size_t)(row - NTOK_C) * D + c0) = xn;
;                 else { *(u32x2*)(X + (size_t)row * D + c0) = (u32x2){pk2(xn[0], xn[1]), pk2(xn[2], xn[3])}; const f32x4 hh = xn * (1.f + scv[j]) + shv[j];
;                     u32x2 o; o.x = pk2(hh[0], hh[1]); o.y = pk2(hh[2], hh[3]); *(u32x2*)(HB + (size_t)row * D + c0) = o; } }
.LBB0_3317:
	s_andn2_b64 vcc, exec, s[28:29]
	s_cbranch_vccnz .LBB0_3319
	v_cvt_pk_bf16_f32 v132, v88, v89
	v_pk_fma_f32 v[88:89], v[108:109], v[88:89], v[60:61]
	v_cvt_pk_bf16_f32 v133, v90, v91
	v_pk_fma_f32 v[90:91], v[110:111], v[90:91], v[62:63]
	v_cvt_pk_bf16_f32 v88, v88, v89
	v_bfe_u32 v34, v90, 16, 1
	s_mov_b32 s18, 0xf6fff600
	v_add3_u32 v34, v90, v34, s81
	v_bfe_u32 v89, v91, 16, 1
	s_mov_b32 s19, -1
	v_lshrrev_b32_e32 v34, 16, v34
	v_add3_u32 v89, v91, v89, s81
	v_lshl_add_u64 v[130:131], v[100:101], 0, s[18:19]
	v_and_or_b32 v89, v89, s80, v34
	global_store_dwordx2 v[130:131], v[132:133], off
	global_store_dwordx2 v[100:101], v[88:89], off offset:-2560

; __device__ __forceinline__ unsigned pk2(float lo, float hi) { return f2bf(lo) | (f2bf(hi) << 16); }
; __device__ __forceinline__ void ph_ln2(CArgs& a, int l, LAS unsigned char* lds, int gw, int ngw) {
;     ...
;             for (int j = 0; j < 4; ++j) { const int c0 = j * 256 + 4 * lane;
;                 const f32x4 xn = v[j] * rstd * lgv[j] + lbv[j];
;                 if (lastl) *(f32x4*)(a.out + (size_t)(row - NTOK_C) * D + c0) = xn;
;                 else { *(u32x2*)(X + (size_t)row * D + c0) = (u32x2){pk2(xn[0], xn[1]), pk2(xn[2], xn[3])}; const f32x4 hh = xn * (1.f + scv[j]) + shv[j];
;                     u32x2 o; o.x = pk2(hh[0], hh[1]); o.y = pk2(hh[2], hh[3]); *(u32x2*)(HB + (size_t)row * D + c0) = o; } }
.LBB0_3321:
	s_andn2_b64 vcc, exec, s[28:29]
	s_cbranch_vccnz .LBB0_3323
	v_cvt_pk_bf16_f32 v128, v88, v89
	v_pk_fma_f32 v[88:89], v[102:103], v[88:89], v[48:49]
	v_cvt_pk_bf16_f32 v129, v90, v91
	v_pk_fma_f32 v[90:91], v[104:105], v[90:91], v[50:51]
	v_cvt_pk_bf16_f32 v88, v88, v89
	s_mov_b32 s18, 0xf6fff800
	s_mov_b32 s19, -1
	v_lshl_add_u64 v[126:127], v[100:101], 0, s[18:19]
	v_cvt_pk_bf16_f32 v89, v90, v91
	global_store_dwordx2 v[126:127], v[128:129], off
	global_store_dwordx2 v[100:101], v[88:89], off offset:-2048

; __device__ __forceinline__ unsigned pk2(float lo, float hi) { return f2bf(lo) | (f2bf(hi) << 16); }
; __device__ __forceinline__ void ph_ln2(CArgs& a, int l, LAS unsigned char* lds, int gw, int ngw) {
;     ...
;             for (int j = 0; j < 4; ++j) { const int c0 = j * 256 + 4 * lane;
;                 const f32x4 xn = v[j] * rstd * lgv[j] + lbv[j];
;                 if (lastl) *(f32x4*)(a.out + (size_t)(row - NTOK_C) * D + c0) = xn;
;                 else { *(u32x2*)(X + (size_t)row * D + c0) = (u32x2){pk2(xn[0], xn[1]), pk2(xn[2], xn[3])}; const f32x4 hh = xn * (1.f + scv[j]) + shv[j];
;                     u32x2 o; o.x = pk2(hh[0], hh[1]); o.y = pk2(hh[2], hh[3]); *(u32x2*)(HB + (size_t)row * D + c0) = o; } }
.LBB0_3325:
	s_andn2_b64 vcc, exec, s[26:27]
	s_cbranch_vccnz .LBB0_3327
	v_cvt_pk_bf16_f32 v88, v68, v69
	v_pk_fma_f32 v[64:65], v[114:115], v[68:69], v[64:65]
	v_cvt_pk_bf16_f32 v89, v70, v71
	v_pk_fma_f32 v[66:67], v[116:117], v[70:71], v[66:67]
	v_cvt_pk_bf16_f32 v64, v64, v65
	v_bfe_u32 v34, v66, 16, 1
	s_mov_b32 s18, 0xf6fffa00
	v_add3_u32 v34, v66, v34, s81
	v_bfe_u32 v65, v67, 16, 1
	s_mov_b32 s19, -1
	v_lshrrev_b32_e32 v34, 16, v34
	v_add3_u32 v65, v67, v65, s81
	v_lshl_add_u64 v[86:87], v[100:101], 0, s[18:19]
	v_and_or_b32 v65, v65, s80, v34
	global_store_dwordx2 v[86:87], v[88:89], off
	global_store_dwordx2 v[100:101], v[64:65], off offset:-1536

; __device__ __forceinline__ unsigned pk2(float lo, float hi) { return f2bf(lo) | (f2bf(hi) << 16); }
; __device__ __forceinline__ void ph_ln2(CArgs& a, int l, LAS unsigned char* lds, int gw, int ngw) {
;     ...
;             for (int j = 0; j < 4; ++j) { const int c0 = j * 256 + 4 * lane;
;                 const f32x4 xn = v[j] * rstd * lgv[j] + lbv[j];
;                 if (lastl) *(f32x4*)(a.out + (size_t)(row - NTOK_C) * D + c0) = xn;
;                 else { *(u32x2*)(X + (size_t)row * D + c0) = (u32x2){pk2(xn[0], xn[1]), pk2(xn[2], xn[3])}; const f32x4 hh = xn * (1.f + scv[j]) + shv[j];
;                     u32x2 o; o.x = pk2(hh[0], hh[1]); o.y = pk2(hh[2], hh[3]); *(u32x2*)(HB + (size_t)row * D + c0) = o; } }
.LBB0_3329:
	s_andn2_b64 vcc, exec, s[26:27]
	s_cbranch_vccnz .LBB0_3331
	v_cvt_pk_bf16_f32 v70, v64, v65
	v_pk_fma_f32 v[52:53], v[106:107], v[64:65], v[52:53]
	v_cvt_pk_bf16_f32 v71, v66, v67
	v_pk_fma_f32 v[54:55], v[112:113], v[66:67], v[54:55]
	v_cvt_pk_bf16_f32 v52, v52, v53
	v_bfe_u32 v34, v54, 16, 1
	s_mov_b32 s18, 0xf6fffc00
	v_add3_u32 v34, v54, v34, s81
	v_bfe_u32 v53, v55, 16, 1
	s_mov_b32 s19, -1
	v_lshrrev_b32_e32 v34, 16, v34
	v_add3_u32 v53, v55, v53, s81
	v_lshl_add_u64 v[68:69], v[100:101], 0, s[18:19]
	v_and_or_b32 v53, v53, s80, v34
	global_store_dwordx2 v[68:69], v[70:71], off
	global_store_dwordx2 v[100:101], v[52:53], off offset:-1024

; __device__ __forceinline__ unsigned pk2(float lo, float hi) { return f2bf(lo) | (f2bf(hi) << 16); }
; __device__ __forceinline__ void ph_ln2(CArgs& a, int l, LAS unsigned char* lds, int gw, int ngw) {
;     ...
;             for (int j = 0; j < 4; ++j) { const int c0 = j * 256 + 4 * lane;
;                 const f32x4 xn = v[j] * rstd * lgv[j] + lbv[j];
;                 if (lastl) *(f32x4*)(a.out + (size_t)(row - NTOK_C) * D + c0) = xn;
;                 else { *(u32x2*)(X + (size_t)row * D + c0) = (u32x2){pk2(xn[0], xn[1]), pk2(xn[2], xn[3])}; const f32x4 hh = xn * (1.f + scv[j]) + shv[j];
;                     u32x2 o; o.x = pk2(hh[0], hh[1]); o.y = pk2(hh[2], hh[3]); *(u32x2*)(HB + (size_t)row * D + c0) = o; } }
.LBB0_3333:
	s_andn2_b64 vcc, exec, s[26:27]
	s_cbranch_vccnz .LBB0_3335
	v_cvt_pk_bf16_f32 v66, v52, v53
	v_pk_fma_f32 v[52:53], v[108:109], v[52:53], v[60:61]
	v_cvt_pk_bf16_f32 v67, v54, v55
	v_pk_fma_f32 v[54:55], v[110:111], v[54:55], v[62:63]
	v_cvt_pk_bf16_f32 v52, v52, v53
	v_bfe_u32 v34, v54, 16, 1
	s_mov_b32 s18, 0xf6fffe00
	v_add3_u32 v34, v54, v34, s81
	v_bfe_u32 v53, v55, 16, 1
	s_mov_b32 s19, -1
	v_lshrrev_b32_e32 v34, 16, v34
	v_add3_u32 v53, v55, v53, s81
	v_lshl_add_u64 v[64:65], v[100:101], 0, s[18:19]
	v_and_or_b32 v53, v53, s80, v34
	global_store_dwordx2 v[64:65], v[66:67], off
	global_store_dwordx2 v[100:101], v[52:53], off offset:-512

; __device__ __forceinline__ unsigned pk2(float lo, float hi) { return f2bf(lo) | (f2bf(hi) << 16); }
; __device__ __forceinline__ void ph_ln2(CArgs& a, int l, LAS unsigned char* lds, int gw, int ngw) {
;     ...
;             for (int j = 0; j < 4; ++j) { const int c0 = j * 256 + 4 * lane;
;                 const f32x4 xn = v[j] * rstd * lgv[j] + lbv[j];
;                 if (lastl) *(f32x4*)(a.out + (size_t)(row - NTOK_C) * D + c0) = xn;
;                 else { *(u32x2*)(X + (size_t)row * D + c0) = (u32x2){pk2(xn[0], xn[1]), pk2(xn[2], xn[3])}; const f32x4 hh = xn * (1.f + scv[j]) + shv[j];
;                     u32x2 o; o.x = pk2(hh[0], hh[1]); o.y = pk2(hh[2], hh[3]); *(u32x2*)(HB + (size_t)row * D + c0) = o; } }
.LBB0_3337:
	s_andn2_b64 vcc, exec, s[26:27]
	s_cbranch_vccnz .LBB0_3298
	v_cvt_pk_bf16_f32 v62, v52, v53
	v_pk_fma_f32 v[48:49], v[102:103], v[52:53], v[48:49]
	v_cvt_pk_bf16_f32 v63, v54, v55
	v_pk_fma_f32 v[50:51], v[104:105], v[54:55], v[50:51]
	v_cvt_pk_bf16_f32 v48, v48, v49
	v_bfe_u32 v34, v50, 16, 1
	s_mov_b32 s14, 0xf7000000
	v_add3_u32 v34, v50, v34, s81
	v_bfe_u32 v49, v51, 16, 1
	s_mov_b32 s15, -1
	v_lshrrev_b32_e32 v34, 16, v34
	v_add3_u32 v49, v51, v49, s81
	v_lshl_add_u64 v[60:61], v[100:101], 0, s[14:15]
	v_and_or_b32 v49, v49, s80, v34
	global_store_dwordx2 v[60:61], v[62:63], off
	global_store_dwordx2 v[100:101], v[48:49], off
	s_branch .LBB0_3298
